# v21 + one LDS-DMA load (2nd half of next B(0,1) piece) moved from the first light load phase to the top of the following heavy one (TA balance 5+3), that phase's wait vmcnt(7); + combine index loads i
# speedup vs baseline: 1.0129x; 1.0039x over previous
;     __device__ __forceinline__ unsigned a_off(const Unit& u, const Gemm& g) const { return (unsigned)u.pm * (unsigned)(BM * 2) * (unsigned)g.K; }
;     __device__ __forceinline__ unsigned b_off(const Unit& u, const Gemm& g) const { return (unsigned)u.pn * (unsigned)(BM * 2) * (unsigned)g.K; }
;     __device__ __forceinline__ bool next(int i, Unit& u) const { return so.next(i, u); }
;     __device__ __forceinline__ unsigned a_off(const Unit& u, const Gemm& g) const { return (unsigned)u.pm * (unsigned)(BM * 2) * (unsigned)g.K; }
; template <class Epi, class Sched, bool ALIGN_EPI = false, bool SP2 = false, bool FP8 = false>
; __device__ __forceinline__ void gemm_phase(LAS unsigned char* lds, const Gemm g, const Sched& S, const Epi& E, int wbase) {
;     ...
;         const bool has_next = S.next(ui + 1, nxt);
;         const unsigned nA = has_next ? S.a_off(nxt, g) : cA, nB = has_next ? S.b_off(nxt, g) : cB;
;         const rsrc_t rAn = (Sched::TWO && has_next) ? (nxt.part ? rA1 : rA0) : rAc, rBn = (Sched::TWO && has_next) ? (nxt.part ? rB1 : rB0) : rBc;
;         float pre_[8] = {0.f, 0.f, 0.f, 0.f, 0.f, 0.f, 0.f, 0.f};
;         if constexpr (Epi::HAS_PRE) E.pre_load(pre_, cur, wr);
;         for (int t = 0; t < nt; t += 2) {
;             const bool last = (t == nt - 2);
;             const unsigned a1 = cA + (unsigned)(t + 1) * kstep;
;             const unsigned a2 = last ? nA : cA + (unsigned)(t + 2) * kstep, b2 = last ? nB : cB + (unsigned)(t + 2) * kstep; const rsrc_t rA2 = (Sched::TWO && last) ? rAn : rAc, rB2 = (Sched::TWO && last) ? rBn : rBc;
;     ...
;             if constexpr (SP2) {
;             PG8_LDB(B0, 0, 0); PG8_LDB(B1, 0, 1); PG8_SCHED; PG8_LDA(At, 0, 0); PG8_STAGE(PG8_SA(1, 1), rAc, a1 + hstep, voffA);
;             PG8_WAIT_V(8); PG8_WAIT_L(0); PG8_BAR; PG8_MMA(0, 0, At, B0); PG8_MMA(0, 1, At, B1); PG8_BAR; PG8_SCHED;
;             PG8_LDA(At, 0, 1); PG8_STAGE(PG8_SB(0, 0), rB2, b2, voffB); PG8_STAGE(PG8_SB(0, 1), rB2, b2 + hstep, voffB); PG8_STAGE(PG8_SA(0, 0), rA2, a2, voffA);
;             PG8_WAIT_V(8); PG8_WAIT_L(0); PG8_BAR; PG8_MMA(1, 0, At, B0); PG8_MMA(1, 1, At, B1); PG8_BAR; PG8_SCHED;
;             PG8_LDB(B0, 1, 0); PG8_LDB(B1, 1, 1); PG8_SCHED; PG8_LDA(At, 1, 0); PG8_STAGE(PG8_SA(0, 1), rA2, a2 + hstep, voffA);
;             PG8_WAIT_V(8); PG8_WAIT_L(0); PG8_BAR; PG8_MMA(0, 0, At, B0); PG8_MMA(0, 1, At, B1); PG8_BAR; PG8_SCHED;
.LBB0_256:
	s_lshl_b32 s82, s1, 18
	s_andn2_b64 vcc, exec, s[66:67]
	s_lshl_b32 s83, s21, 18
	s_cbranch_vccnz .LBB0_260
	s_and_b64 s[2:3], s[26:27], exec
	s_waitcnt vmcnt(37)
	s_waitcnt vmcnt(36)
	s_waitcnt vmcnt(35)
	s_waitcnt vmcnt(32)
	s_waitcnt vmcnt(31)
	s_waitcnt vmcnt(28)
	s_waitcnt vmcnt(27)
	s_waitcnt vmcnt(24)
	s_waitcnt vmcnt(23)
	s_waitcnt vmcnt(22)
	v_mov_b32_e32 v231, v164
	v_mov_b32_e32 v230, 0xff61b1e6
	v_mov_b32_e32 v175, v233
	s_cselect_b32 s2, s82, s29
	s_cselect_b32 s3, s83, s28
	s_add_i32 s16, s29, 0x80
	s_addk_i32 s28, 0x100
	s_mov_b32 s29, 0
	ds_read_b128 v[128:131], v252
	ds_read_b128 v[132:135], v252 offset:1024
	ds_read_b128 v[136:139], v252 offset:2048
	ds_read_b128 v[140:143], v252 offset:3072
	ds_read_b128 v[144:147], v225
	ds_read_b128 v[148:151], v225 offset:1024
	ds_read_b128 v[152:155], v225 offset:2048
	ds_read_b128 v[156:159], v225 offset:3072
	s_add_i32 s6, s16, 0x80
	s_cmp_eq_u32 s18, s29
	s_cselect_b32 s46, s2, s6
	s_cselect_b32 s31, s3, s28
	s_or_b32 s30, s46, 0x80
	s_add_i32 s6, s41, s16
	s_mov_b32 m0, s19
	ds_read_b128 v[176:179], v172
	ds_read_b128 v[180:183], v172 offset:1024
	ds_read_b128 v[184:187], v172 offset:2048
	ds_read_b128 v[188:191], v172 offset:3072
	ds_read_b128 v[194:197], v172 offset:4096
	ds_read_b128 v[198:201], v172 offset:5120
	ds_read_b128 v[202:205], v172 offset:6144
	ds_read_b128 v[206:209], v172 offset:7168
	buffer_load_dwordx4 v192, s[36:39], s6 offen lds
	s_mov_b32 m0, s20
	s_nop 0
	buffer_load_dwordx4 v223, s[36:39], s6 offen lds
	s_waitcnt vmcnt(8)
	s_waitcnt lgkmcnt(0)
	s_barrier
	s_setprio 1
	v_mfma_f32_16x16x128_f8f6f4 v[124:127], v[128:135], v[176:183], 0
	v_mfma_f32_16x16x128_f8f6f4 v[120:123], v[136:143], v[176:183], 0
	v_mfma_f32_16x16x128_f8f6f4 v[108:111], v[128:135], v[184:191], 0
	v_mfma_f32_16x16x128_f8f6f4 v[104:107], v[136:143], v[184:191], 0
	v_mfma_f32_16x16x128_f8f6f4 v[160:163], v[128:135], v[194:201], 0
	v_mfma_f32_16x16x128_f8f6f4 v[210:213], v[136:143], v[194:201], 0
	v_mfma_f32_16x16x128_f8f6f4 v[214:217], v[128:135], v[202:209], 0
	v_mfma_f32_16x16x128_f8f6f4 v[218:221], v[136:143], v[202:209], 0
	v_mfma_f32_16x16x128_f8f6f4 v[116:119], v[144:151], v[176:183], 0
	v_mfma_f32_16x16x128_f8f6f4 v[112:115], v[152:159], v[176:183], 0
	v_mfma_f32_16x16x128_f8f6f4 v[100:103], v[144:151], v[184:191], 0
	v_mfma_f32_16x16x128_f8f6f4 v[96:99], v[152:159], v[184:191], 0
	v_mfma_f32_16x16x128_f8f6f4 v[176:179], v[144:151], v[194:201], 0
	v_mfma_f32_16x16x128_f8f6f4 v[180:183], v[152:159], v[194:201], 0
	v_mfma_f32_16x16x128_f8f6f4 v[184:187], v[144:151], v[202:209], 0
	v_mfma_f32_16x16x128_f8f6f4 v[188:191], v[152:159], v[202:209], 0
	s_setprio 0
	s_barrier
	s_mov_b32 m0, s43
	s_mov_b32 s6, s38
	s_mov_b32 s7, s39
	s_nop 1
	buffer_load_dwordx4 v222, s[4:7], s31 offen lds
	s_mov_b32 m0, s44
	ds_read_b128 v[64:67], v172 offset:16384
	s_add_i32 s47, s31, s41
	buffer_load_dwordx4 v193, s[4:7], s31 offen lds
	s_mov_b32 m0, s45
	ds_read_b128 v[68:71], v172 offset:17408
	buffer_load_dwordx4 v222, s[4:7], s47 offen lds
	s_mov_b32 m0, s42
	ds_read_b128 v[72:75], v172 offset:18432
	buffer_load_dwordx4 v192, s[36:39], s46 offen lds
	s_mov_b32 m0, s53
	ds_read_b128 v[76:79], v172 offset:19456
	buffer_load_dwordx4 v223, s[36:39], s46 offen lds
	ds_read_b128 v[80:83], v172 offset:20480
	ds_read_b128 v[84:87], v172 offset:21504
	ds_read_b128 v[88:91], v172 offset:22528
	ds_read_b128 v[92:95], v172 offset:23552
	s_waitcnt vmcnt(7)
	s_waitcnt lgkmcnt(0)
	s_barrier
	s_setprio 1
	v_mfma_f32_16x16x128_f8f6f4 v[60:63], v[128:135], v[64:71], 0
	v_mfma_f32_16x16x128_f8f6f4 v[56:59], v[136:143], v[64:71], 0
	v_mfma_f32_16x16x128_f8f6f4 v[194:197], v[128:135], v[72:79], 0
	v_mfma_f32_16x16x128_f8f6f4 v[198:201], v[136:143], v[72:79], 0
	v_mfma_f32_16x16x128_f8f6f4 v[202:205], v[128:135], v[80:87], 0
	v_mfma_f32_16x16x128_f8f6f4 v[206:209], v[136:143], v[80:87], 0
	v_mfma_f32_16x16x128_f8f6f4 v[236:239], v[128:135], v[88:95], 0
	v_mfma_f32_16x16x128_f8f6f4 v[240:243], v[136:143], v[88:95], 0
	v_mfma_f32_16x16x128_f8f6f4 v[52:55], v[144:151], v[64:71], 0
	v_mfma_f32_16x16x128_f8f6f4 v[48:51], v[152:159], v[64:71], 0
	v_mfma_f32_16x16x128_f8f6f4 v[244:247], v[144:151], v[72:79], 0
	v_mfma_f32_16x16x128_f8f6f4 v[248:251], v[152:159], v[72:79], 0
	v_mfma_f32_16x16x128_f8f6f4 v[226:229], v[144:151], v[80:87], 0
	v_mfma_f32_16x16x128_f8f6f4 v[232:235], v[152:159], v[80:87], 0
	v_mfma_f32_16x16x128_f8f6f4 v[164:167], v[144:151], v[88:95], 0
	v_mfma_f32_16x16x128_f8f6f4 v[168:171], v[152:159], v[88:95], 0
	s_setprio 0
	s_barrier
	s_mov_b32 m0, s52
	s_nop 0
	buffer_load_dwordx4 v193, s[4:7], s47 offen lds
	s_nop 4
	ds_read_b128 v[0:3], v173
	ds_read_b128 v[4:7], v173 offset:1024
	ds_read_b128 v[16:19], v173 offset:2048
	ds_read_b128 v[20:23], v173 offset:3072
	ds_read_b128 v[128:131], v174
	ds_read_b128 v[132:135], v174 offset:1024
	ds_read_b128 v[136:139], v174 offset:2048
	ds_read_b128 v[140:143], v174 offset:3072
	s_add_i32 s46, s46, s41
	s_mov_b32 m0, s56
	ds_read_b128 v[8:11], v172 offset:32768
	ds_read_b128 v[12:15], v172 offset:33792
	ds_read_b128 v[24:27], v172 offset:34816
	ds_read_b128 v[28:31], v172 offset:35840
	ds_read_b128 v[32:35], v172 offset:36864
	ds_read_b128 v[36:39], v172 offset:37888
	ds_read_b128 v[40:43], v172 offset:38912
	ds_read_b128 v[44:47], v172 offset:39936
	buffer_load_dwordx4 v192, s[36:39], s46 offen lds
	s_mov_b32 m0, s57
	s_nop 0
	buffer_load_dwordx4 v223, s[36:39], s46 offen lds
	s_waitcnt vmcnt(8)
	s_waitcnt lgkmcnt(0)
	s_barrier
; #define PG8_STAGE(bufoff, rs_, soff_, voff) do { _Pragma("unroll") for (int _i = 0; _i < 2; ++_i) \
;         __builtin_amdgcn_raw_ptr_buffer_load_lds(rs_, (LAS void*)(lds + (bufoff) + ldsw + _i * 8192), 16, (int)(voff)[_i], (int)(soff_), 0, 0); } while (0)
; #define PG8_LDA(dst, b, h) do { _Pragma("unroll") for (int m = 0; m < 4; ++m) dst[m] = PG8_LD2(lds + PG8_SA(b, h) + aoff + m * 2048); } while (0)
; #define PG8_LDB(dst, b, h) do { _Pragma("unroll") for (int n = 0; n < 2; ++n) dst[n] = PG8_LD2(lds + PG8_SB(b, h) + boff + n * 2048); } while (0)
; #define PG8_WAIT_V(n) asm volatile("s_waitcnt vmcnt(" #n ")" ::: "memory")
; #define PG8_WAIT_L(n) asm volatile("s_waitcnt lgkmcnt(" #n ")" ::: "memory")
; #define PG8_BAR __builtin_amdgcn_s_barrier()
; #define PG8_SCHED __builtin_amdgcn_sched_barrier(0)
; template <class Epi, class Sched, bool ALIGN_EPI = false, bool SP2 = false, bool FP8 = false>
; __device__ __forceinline__ void gemm_phase(LAS unsigned char* lds, const Gemm g, const Sched& S, const Epi& E, int wbase) {
;     ...
;             if constexpr (SP2) {
;             PG8_LDB(B0, 0, 0); PG8_LDB(B1, 0, 1); PG8_SCHED; PG8_LDA(At, 0, 0); PG8_STAGE(PG8_SA(1, 1), rAc, a1 + hstep, voffA);
;             PG8_WAIT_V(8); PG8_WAIT_L(0); PG8_BAR; PG8_MMA(0, 0, At, B0); PG8_MMA(0, 1, At, B1); PG8_BAR; PG8_SCHED;
;     ...
;             PG8_WAIT_V(8); PG8_WAIT_L(0); PG8_BAR; PG8_MMA(0, 0, At, B0); PG8_MMA(0, 1, At, B1); PG8_BAR; PG8_SCHED;
;             PG8_LDA(At, 1, 1); PG8_STAGE(PG8_SB(1, 0), rB2, b3, voffB); PG8_STAGE(PG8_SB(1, 1), rB2, b3 + hstep, voffB); PG8_STAGE(PG8_SA(1, 0), rA2, a3, voffA);
;             PG8_WAIT_V(8); PG8_WAIT_L(0); PG8_BAR; PG8_MMA(1, 0, At, B0); PG8_MMA(1, 1, At, B1); PG8_BAR; PG8_SCHED;
	s_setprio 1
	v_mfma_f32_16x16x128_f8f6f4 v[124:127], v[0:7], v[8:15], v[124:127]
	v_mfma_f32_16x16x128_f8f6f4 v[120:123], v[16:23], v[8:15], v[120:123]
	v_mfma_f32_16x16x128_f8f6f4 v[108:111], v[0:7], v[24:31], v[108:111]
	v_mfma_f32_16x16x128_f8f6f4 v[104:107], v[16:23], v[24:31], v[104:107]
	v_mfma_f32_16x16x128_f8f6f4 v[92:95], v[0:7], v[32:39], v[160:163]
	v_mfma_f32_16x16x128_f8f6f4 v[88:91], v[16:23], v[32:39], v[210:213]
	v_mfma_f32_16x16x128_f8f6f4 v[76:79], v[0:7], v[40:47], v[214:217]
	v_mfma_f32_16x16x128_f8f6f4 v[72:75], v[16:23], v[40:47], v[218:221]
	v_mfma_f32_16x16x128_f8f6f4 v[116:119], v[128:135], v[8:15], v[116:119]
	v_mfma_f32_16x16x128_f8f6f4 v[112:115], v[136:143], v[8:15], v[112:115]
	v_mfma_f32_16x16x128_f8f6f4 v[100:103], v[128:135], v[24:31], v[100:103]
	v_mfma_f32_16x16x128_f8f6f4 v[96:99], v[136:143], v[24:31], v[96:99]
	v_mfma_f32_16x16x128_f8f6f4 v[84:87], v[128:135], v[32:39], v[176:179]
	v_mfma_f32_16x16x128_f8f6f4 v[80:83], v[136:143], v[32:39], v[180:183]
	v_mfma_f32_16x16x128_f8f6f4 v[68:71], v[128:135], v[40:47], v[184:187]
	v_mfma_f32_16x16x128_f8f6f4 v[64:67], v[136:143], v[40:47], v[188:191]
	s_setprio 0
	s_barrier
	s_mov_b32 m0, s58
	s_bitset1_b32 s31, 7
	buffer_load_dwordx4 v222, s[4:7], s31 offen lds
	s_mov_b32 m0, s59
	ds_read_b128 v[32:35], v172 offset:49152
	buffer_load_dwordx4 v193, s[4:7], s31 offen lds
	s_add_i32 s31, s31, s41
	s_mov_b32 m0, s65
	ds_read_b128 v[36:39], v172 offset:50176
	buffer_load_dwordx4 v222, s[4:7], s31 offen lds
	s_mov_b32 m0, s33
	ds_read_b128 v[144:147], v172 offset:51200
	buffer_load_dwordx4 v193, s[4:7], s31 offen lds
	s_mov_b32 m0, s12
	ds_read_b128 v[148:151], v172 offset:52224
	buffer_load_dwordx4 v192, s[36:39], s30 offen lds
	s_mov_b32 m0, s13
	ds_read_b128 v[152:155], v172 offset:53248
	buffer_load_dwordx4 v223, s[36:39], s30 offen lds
	ds_read_b128 v[156:159], v172 offset:54272
	ds_read_b128 v[176:179], v172 offset:55296
	ds_read_b128 v[180:183], v172 offset:56320
	s_waitcnt vmcnt(8)
	s_waitcnt lgkmcnt(0)
	s_barrier
	s_setprio 1
	v_mfma_f32_16x16x128_f8f6f4 v[60:63], v[0:7], v[32:39], v[60:63]
	v_mfma_f32_16x16x128_f8f6f4 v[56:59], v[16:23], v[32:39], v[56:59]
	v_mfma_f32_16x16x128_f8f6f4 v[44:47], v[0:7], v[144:151], v[194:197]
	v_mfma_f32_16x16x128_f8f6f4 v[40:43], v[16:23], v[144:151], v[198:201]
	v_mfma_f32_16x16x128_f8f6f4 v[28:31], v[0:7], v[152:159], v[202:205]
	v_mfma_f32_16x16x128_f8f6f4 v[24:27], v[16:23], v[152:159], v[206:209]
	v_mfma_f32_16x16x128_f8f6f4 v[12:15], v[0:7], v[176:183], v[236:239]
	v_mfma_f32_16x16x128_f8f6f4 v[8:11], v[16:23], v[176:183], v[240:243]
	v_mfma_f32_16x16x128_f8f6f4 v[52:55], v[128:135], v[32:39], v[52:55]
	v_mfma_f32_16x16x128_f8f6f4 v[48:51], v[136:143], v[32:39], v[48:51]
	v_mfma_f32_16x16x128_f8f6f4 v[36:39], v[128:135], v[144:151], v[244:247]
	v_mfma_f32_16x16x128_f8f6f4 v[32:35], v[136:143], v[144:151], v[248:251]
	v_mfma_f32_16x16x128_f8f6f4 v[20:23], v[128:135], v[152:159], v[226:229]
	v_mfma_f32_16x16x128_f8f6f4 v[16:19], v[136:143], v[152:159], v[232:235]
	v_mfma_f32_16x16x128_f8f6f4 v[4:7], v[128:135], v[176:183], v[164:167]
	v_mfma_f32_16x16x128_f8f6f4 v[0:3], v[136:143], v[176:183], v[168:171]
	s_setprio 0
	s_barrier
	s_add_i32 s29, s29, 2
	s_addk_i32 s16, 0x100
	s_addk_i32 s28, 0x100
	s_cmp_ge_i32 s29, s77
	s_cbranch_scc0 .LBB0_258
	s_branch .Lzp_after_258
.LBB0_258:
	ds_read_b128 v[128:131], v252
	ds_read_b128 v[132:135], v252 offset:1024
	ds_read_b128 v[136:139], v252 offset:2048
	ds_read_b128 v[140:143], v252 offset:3072
	ds_read_b128 v[144:147], v225
	ds_read_b128 v[148:151], v225 offset:1024
	ds_read_b128 v[152:155], v225 offset:2048
	ds_read_b128 v[156:159], v225 offset:3072
	s_add_i32 s6, s16, 0x80
	s_cmp_eq_u32 s18, s29
	s_cselect_b32 s46, s2, s6
	s_cselect_b32 s31, s3, s28
	s_or_b32 s30, s46, 0x80
	s_add_i32 s6, s41, s16
	s_mov_b32 m0, s19
	ds_read_b128 v[176:179], v172
	ds_read_b128 v[180:183], v172 offset:1024
	ds_read_b128 v[184:187], v172 offset:2048
	ds_read_b128 v[188:191], v172 offset:3072
	ds_read_b128 v[194:197], v172 offset:4096
	ds_read_b128 v[198:201], v172 offset:5120
	ds_read_b128 v[202:205], v172 offset:6144
	ds_read_b128 v[206:209], v172 offset:7168
	buffer_load_dwordx4 v192, s[36:39], s6 offen lds
	s_mov_b32 m0, s20
	s_nop 0
	buffer_load_dwordx4 v223, s[36:39], s6 offen lds
	s_waitcnt vmcnt(8)
	s_waitcnt lgkmcnt(0)
	s_barrier
	s_setprio 1
	v_mfma_f32_16x16x128_f8f6f4 v[124:127], v[128:135], v[176:183], v[124:127]
	v_mfma_f32_16x16x128_f8f6f4 v[120:123], v[136:143], v[176:183], v[120:123]
	v_mfma_f32_16x16x128_f8f6f4 v[108:111], v[128:135], v[184:191], v[108:111]
	v_mfma_f32_16x16x128_f8f6f4 v[104:107], v[136:143], v[184:191], v[104:107]
	v_mfma_f32_16x16x128_f8f6f4 v[160:163], v[128:135], v[194:201], v[92:95]
	v_mfma_f32_16x16x128_f8f6f4 v[210:213], v[136:143], v[194:201], v[88:91]
	v_mfma_f32_16x16x128_f8f6f4 v[214:217], v[128:135], v[202:209], v[76:79]
	v_mfma_f32_16x16x128_f8f6f4 v[218:221], v[136:143], v[202:209], v[72:75]
	v_mfma_f32_16x16x128_f8f6f4 v[116:119], v[144:151], v[176:183], v[116:119]
	v_mfma_f32_16x16x128_f8f6f4 v[112:115], v[152:159], v[176:183], v[112:115]
	v_mfma_f32_16x16x128_f8f6f4 v[100:103], v[144:151], v[184:191], v[100:103]
	v_mfma_f32_16x16x128_f8f6f4 v[96:99], v[152:159], v[184:191], v[96:99]
	v_mfma_f32_16x16x128_f8f6f4 v[176:179], v[144:151], v[194:201], v[84:87]
	v_mfma_f32_16x16x128_f8f6f4 v[180:183], v[152:159], v[194:201], v[80:83]
	v_mfma_f32_16x16x128_f8f6f4 v[184:187], v[144:151], v[202:209], v[68:71]
	v_mfma_f32_16x16x128_f8f6f4 v[188:191], v[152:159], v[202:209], v[64:67]
	s_setprio 0
	s_barrier
; #define PG8_STAGE(bufoff, rs_, soff_, voff) do { _Pragma("unroll") for (int _i = 0; _i < 2; ++_i) \
;         __builtin_amdgcn_raw_ptr_buffer_load_lds(rs_, (LAS void*)(lds + (bufoff) + ldsw + _i * 8192), 16, (int)(voff)[_i], (int)(soff_), 0, 0); } while (0)
; #define PG8_LDA(dst, b, h) do { _Pragma("unroll") for (int m = 0; m < 4; ++m) dst[m] = PG8_LD2(lds + PG8_SA(b, h) + aoff + m * 2048); } while (0)
; #define PG8_LDB(dst, b, h) do { _Pragma("unroll") for (int n = 0; n < 2; ++n) dst[n] = PG8_LD2(lds + PG8_SB(b, h) + boff + n * 2048); } while (0)
; #define PG8_WAIT_V(n) asm volatile("s_waitcnt vmcnt(" #n ")" ::: "memory")
; #define PG8_WAIT_L(n) asm volatile("s_waitcnt lgkmcnt(" #n ")" ::: "memory")
; #define PG8_BAR __builtin_amdgcn_s_barrier()
; #define PG8_SCHED __builtin_amdgcn_sched_barrier(0)
; template <class Epi, class Sched, bool ALIGN_EPI = false, bool SP2 = false, bool FP8 = false>
; __device__ __forceinline__ void gemm_phase(LAS unsigned char* lds, const Gemm g, const Sched& S, const Epi& E, int wbase) {
;     ...
;             PG8_LDA(At, 0, 1); PG8_STAGE(PG8_SB(0, 0), rB2, b2, voffB); PG8_STAGE(PG8_SB(0, 1), rB2, b2 + hstep, voffB); PG8_STAGE(PG8_SA(0, 0), rA2, a2, voffA);
;             PG8_WAIT_V(8); PG8_WAIT_L(0); PG8_BAR; PG8_MMA(1, 0, At, B0); PG8_MMA(1, 1, At, B1); PG8_BAR; PG8_SCHED;
;             PG8_LDB(B0, 1, 0); PG8_LDB(B1, 1, 1); PG8_SCHED; PG8_LDA(At, 1, 0); PG8_STAGE(PG8_SA(0, 1), rA2, a2 + hstep, voffA);
;             PG8_WAIT_V(8); PG8_WAIT_L(0); PG8_BAR; PG8_MMA(0, 0, At, B0); PG8_MMA(0, 1, At, B1); PG8_BAR; PG8_SCHED;
;             PG8_LDA(At, 1, 1); PG8_STAGE(PG8_SB(1, 0), rB2, b3, voffB); PG8_STAGE(PG8_SB(1, 1), rB2, b3 + hstep, voffB); PG8_STAGE(PG8_SA(1, 0), rA2, a3, voffA);
;             PG8_WAIT_V(8); PG8_WAIT_L(0); PG8_BAR; PG8_MMA(1, 0, At, B0); PG8_MMA(1, 1, At, B1); PG8_BAR; PG8_SCHED;
	s_mov_b32 m0, s43
	s_mov_b32 s6, s38
	s_mov_b32 s7, s39
	s_nop 1
	buffer_load_dwordx4 v222, s[4:7], s31 offen lds
	s_mov_b32 m0, s44
	ds_read_b128 v[64:67], v172 offset:16384
	s_add_i32 s47, s31, s41
	buffer_load_dwordx4 v193, s[4:7], s31 offen lds
	s_mov_b32 m0, s45
	ds_read_b128 v[68:71], v172 offset:17408
	buffer_load_dwordx4 v222, s[4:7], s47 offen lds
	s_mov_b32 m0, s42
	ds_read_b128 v[72:75], v172 offset:18432
	buffer_load_dwordx4 v192, s[36:39], s46 offen lds
	s_mov_b32 m0, s53
	ds_read_b128 v[76:79], v172 offset:19456
	buffer_load_dwordx4 v223, s[36:39], s46 offen lds
	ds_read_b128 v[80:83], v172 offset:20480
	ds_read_b128 v[84:87], v172 offset:21504
	ds_read_b128 v[88:91], v172 offset:22528
	ds_read_b128 v[92:95], v172 offset:23552
	s_waitcnt vmcnt(7)
	s_waitcnt lgkmcnt(0)
	s_barrier
	s_setprio 1
	v_mfma_f32_16x16x128_f8f6f4 v[60:63], v[128:135], v[64:71], v[60:63]
	v_mfma_f32_16x16x128_f8f6f4 v[56:59], v[136:143], v[64:71], v[56:59]
	v_mfma_f32_16x16x128_f8f6f4 v[194:197], v[128:135], v[72:79], v[44:47]
	v_mfma_f32_16x16x128_f8f6f4 v[198:201], v[136:143], v[72:79], v[40:43]
	v_mfma_f32_16x16x128_f8f6f4 v[202:205], v[128:135], v[80:87], v[28:31]
	v_mfma_f32_16x16x128_f8f6f4 v[206:209], v[136:143], v[80:87], v[24:27]
	v_mfma_f32_16x16x128_f8f6f4 v[236:239], v[128:135], v[88:95], v[12:15]
	v_mfma_f32_16x16x128_f8f6f4 v[240:243], v[136:143], v[88:95], v[8:11]
	v_mfma_f32_16x16x128_f8f6f4 v[52:55], v[144:151], v[64:71], v[52:55]
	v_mfma_f32_16x16x128_f8f6f4 v[48:51], v[152:159], v[64:71], v[48:51]
	v_mfma_f32_16x16x128_f8f6f4 v[244:247], v[144:151], v[72:79], v[36:39]
	v_mfma_f32_16x16x128_f8f6f4 v[248:251], v[152:159], v[72:79], v[32:35]
	v_mfma_f32_16x16x128_f8f6f4 v[226:229], v[144:151], v[80:87], v[20:23]
	v_mfma_f32_16x16x128_f8f6f4 v[232:235], v[152:159], v[80:87], v[16:19]
	v_mfma_f32_16x16x128_f8f6f4 v[164:167], v[144:151], v[88:95], v[4:7]
	v_mfma_f32_16x16x128_f8f6f4 v[168:171], v[152:159], v[88:95], v[0:3]
	s_setprio 0
	s_barrier
	s_mov_b32 m0, s52
	s_nop 0
	buffer_load_dwordx4 v193, s[4:7], s47 offen lds
	s_nop 4
	ds_read_b128 v[0:3], v173
	ds_read_b128 v[4:7], v173 offset:1024
	ds_read_b128 v[16:19], v173 offset:2048
	ds_read_b128 v[20:23], v173 offset:3072
	ds_read_b128 v[128:131], v174
	ds_read_b128 v[132:135], v174 offset:1024
	ds_read_b128 v[136:139], v174 offset:2048
	ds_read_b128 v[140:143], v174 offset:3072
	s_add_i32 s46, s46, s41
	s_mov_b32 m0, s56
	ds_read_b128 v[8:11], v172 offset:32768
	ds_read_b128 v[12:15], v172 offset:33792
	ds_read_b128 v[24:27], v172 offset:34816
	ds_read_b128 v[28:31], v172 offset:35840
	ds_read_b128 v[32:35], v172 offset:36864
	ds_read_b128 v[36:39], v172 offset:37888
	ds_read_b128 v[40:43], v172 offset:38912
	ds_read_b128 v[44:47], v172 offset:39936
	buffer_load_dwordx4 v192, s[36:39], s46 offen lds
	s_mov_b32 m0, s57
	s_nop 0
	buffer_load_dwordx4 v223, s[36:39], s46 offen lds
	s_waitcnt vmcnt(8)
	s_waitcnt lgkmcnt(0)
	s_barrier
	s_setprio 1
	v_mfma_f32_16x16x128_f8f6f4 v[124:127], v[0:7], v[8:15], v[124:127]
	v_mfma_f32_16x16x128_f8f6f4 v[120:123], v[16:23], v[8:15], v[120:123]
	v_mfma_f32_16x16x128_f8f6f4 v[108:111], v[0:7], v[24:31], v[108:111]
	v_mfma_f32_16x16x128_f8f6f4 v[104:107], v[16:23], v[24:31], v[104:107]
	v_mfma_f32_16x16x128_f8f6f4 v[92:95], v[0:7], v[32:39], v[160:163]
	v_mfma_f32_16x16x128_f8f6f4 v[88:91], v[16:23], v[32:39], v[210:213]
	v_mfma_f32_16x16x128_f8f6f4 v[76:79], v[0:7], v[40:47], v[214:217]
	v_mfma_f32_16x16x128_f8f6f4 v[72:75], v[16:23], v[40:47], v[218:221]
	v_mfma_f32_16x16x128_f8f6f4 v[116:119], v[128:135], v[8:15], v[116:119]
	v_mfma_f32_16x16x128_f8f6f4 v[112:115], v[136:143], v[8:15], v[112:115]
	v_mfma_f32_16x16x128_f8f6f4 v[100:103], v[128:135], v[24:31], v[100:103]
	v_mfma_f32_16x16x128_f8f6f4 v[96:99], v[136:143], v[24:31], v[96:99]
	v_mfma_f32_16x16x128_f8f6f4 v[84:87], v[128:135], v[32:39], v[176:179]
	v_mfma_f32_16x16x128_f8f6f4 v[80:83], v[136:143], v[32:39], v[180:183]
	v_mfma_f32_16x16x128_f8f6f4 v[68:71], v[128:135], v[40:47], v[184:187]
	v_mfma_f32_16x16x128_f8f6f4 v[64:67], v[136:143], v[40:47], v[188:191]
	s_setprio 0
	s_barrier
	s_mov_b32 m0, s58
	s_bitset1_b32 s31, 7
	buffer_load_dwordx4 v222, s[4:7], s31 offen lds
	s_mov_b32 m0, s59
	ds_read_b128 v[32:35], v172 offset:49152
	buffer_load_dwordx4 v193, s[4:7], s31 offen lds
	s_add_i32 s31, s31, s41
	s_mov_b32 m0, s65
	ds_read_b128 v[36:39], v172 offset:50176
	buffer_load_dwordx4 v222, s[4:7], s31 offen lds
	s_mov_b32 m0, s33
	ds_read_b128 v[144:147], v172 offset:51200
	buffer_load_dwordx4 v193, s[4:7], s31 offen lds
	s_mov_b32 m0, s12
	ds_read_b128 v[148:151], v172 offset:52224
	buffer_load_dwordx4 v192, s[36:39], s30 offen lds
	s_mov_b32 m0, s13
	ds_read_b128 v[152:155], v172 offset:53248
	buffer_load_dwordx4 v223, s[36:39], s30 offen lds
	ds_read_b128 v[156:159], v172 offset:54272
	ds_read_b128 v[176:179], v172 offset:55296
	ds_read_b128 v[180:183], v172 offset:56320
	s_waitcnt vmcnt(8)
	s_waitcnt lgkmcnt(0)
	s_barrier
	s_setprio 1
	v_mfma_f32_16x16x128_f8f6f4 v[60:63], v[0:7], v[32:39], v[60:63]
	v_mfma_f32_16x16x128_f8f6f4 v[56:59], v[16:23], v[32:39], v[56:59]
	v_mfma_f32_16x16x128_f8f6f4 v[44:47], v[0:7], v[144:151], v[194:197]
	v_mfma_f32_16x16x128_f8f6f4 v[40:43], v[16:23], v[144:151], v[198:201]
	v_mfma_f32_16x16x128_f8f6f4 v[28:31], v[0:7], v[152:159], v[202:205]
	v_mfma_f32_16x16x128_f8f6f4 v[24:27], v[16:23], v[152:159], v[206:209]
	v_mfma_f32_16x16x128_f8f6f4 v[12:15], v[0:7], v[176:183], v[236:239]
	v_mfma_f32_16x16x128_f8f6f4 v[8:11], v[16:23], v[176:183], v[240:243]
	v_mfma_f32_16x16x128_f8f6f4 v[52:55], v[128:135], v[32:39], v[52:55]
	v_mfma_f32_16x16x128_f8f6f4 v[48:51], v[136:143], v[32:39], v[48:51]
	v_mfma_f32_16x16x128_f8f6f4 v[36:39], v[128:135], v[144:151], v[244:247]
	v_mfma_f32_16x16x128_f8f6f4 v[32:35], v[136:143], v[144:151], v[248:251]
	v_mfma_f32_16x16x128_f8f6f4 v[20:23], v[128:135], v[152:159], v[226:229]
	v_mfma_f32_16x16x128_f8f6f4 v[16:19], v[136:143], v[152:159], v[232:235]
	v_mfma_f32_16x16x128_f8f6f4 v[4:7], v[128:135], v[176:183], v[164:167]
	v_mfma_f32_16x16x128_f8f6f4 v[0:3], v[136:143], v[176:183], v[168:171]
	s_setprio 0
	s_barrier
	s_add_i32 s29, s29, 2
	s_addk_i32 s16, 0x100
	s_addk_i32 s28, 0x100
	s_cmp_ge_i32 s29, s77
	s_cbranch_scc0 .LBB0_258

;     __device__ __forceinline__ unsigned a_off(const Unit& u, const Gemm& g) const { return (unsigned)u.pm * (unsigned)(BM * 2) * (unsigned)g.K; }
;     __device__ __forceinline__ unsigned b_off(const Unit& u, const Gemm& g) const { return (unsigned)u.pn * (unsigned)(BM * 2) * (unsigned)g.K; }
;     __device__ __forceinline__ bool next(int i, Unit& u) const { return so.next(i, u); }
;     __device__ __forceinline__ unsigned a_off(const Unit& u, const Gemm& g) const { return (unsigned)u.pm * (unsigned)(BM * 2) * (unsigned)g.K; }
;     __device__ __forceinline__ bool next(int i, Unit& u) const { const bool ok = so.next(i >> 1, u); u.part = i & 1; return ok; }
; template <class Epi, class Sched, bool ALIGN_EPI = false, bool SP2 = false, bool FP8 = false>
; __device__ __forceinline__ void gemm_phase(LAS unsigned char* lds, const Gemm g, const Sched& S, const Epi& E, int wbase) {
;     ...
;         const bool has_next = S.next(ui + 1, nxt);
;         const unsigned nA = has_next ? S.a_off(nxt, g) : cA, nB = has_next ? S.b_off(nxt, g) : cB;
;         const rsrc_t rAn = (Sched::TWO && has_next) ? (nxt.part ? rA1 : rA0) : rAc, rBn = (Sched::TWO && has_next) ? (nxt.part ? rB1 : rB0) : rBc;
;         float pre_[8] = {0.f, 0.f, 0.f, 0.f, 0.f, 0.f, 0.f, 0.f};
;         if constexpr (Epi::HAS_PRE) E.pre_load(pre_, cur, wr);
;         for (int t = 0; t < nt; t += 2) {
;             const bool last = (t == nt - 2);
;             const unsigned a1 = cA + (unsigned)(t + 1) * kstep;
;             const unsigned a2 = last ? nA : cA + (unsigned)(t + 2) * kstep, b2 = last ? nB : cB + (unsigned)(t + 2) * kstep; const rsrc_t rA2 = (Sched::TWO && last) ? rAn : rAc, rB2 = (Sched::TWO && last) ? rBn : rBc;
;             const unsigned a3 = a2 + kstep, b3 = b2 + kstep;
;             if (last && has_next) S.a_ready(nxt);
;             if constexpr (SP2) {
;             PG8_LDB(B0, 0, 0); PG8_LDB(B1, 0, 1); PG8_SCHED; PG8_LDA(At, 0, 0); PG8_STAGE(PG8_SA(1, 1), rAc, a1 + hstep, voffA);
;             PG8_WAIT_V(8); PG8_WAIT_L(0); PG8_BAR; PG8_MMA(0, 0, At, B0); PG8_MMA(0, 1, At, B1); PG8_BAR; PG8_SCHED;
;             PG8_LDA(At, 0, 1); PG8_STAGE(PG8_SB(0, 0), rB2, b2, voffB); PG8_STAGE(PG8_SB(0, 1), rB2, b2 + hstep, voffB); PG8_STAGE(PG8_SA(0, 0), rA2, a2, voffA);
;             PG8_WAIT_V(8); PG8_WAIT_L(0); PG8_BAR; PG8_MMA(1, 0, At, B0); PG8_MMA(1, 1, At, B1); PG8_BAR; PG8_SCHED;
.LBB0_350:
	s_lshl_b32 s20, s19, 19
	s_andn2_b64 vcc, exec, s[66:67]
	s_lshl_b32 s21, s18, 19
	s_cbranch_vccnz .LBB0_430
	s_and_b64 s[2:3], s[26:27], exec
	s_waitcnt vmcnt(37)
	s_waitcnt vmcnt(36)
	s_waitcnt vmcnt(35)
	s_waitcnt vmcnt(32)
	s_waitcnt vmcnt(31)
	s_waitcnt vmcnt(28)
	s_waitcnt vmcnt(27)
	s_waitcnt vmcnt(24)
	s_waitcnt vmcnt(23)
	s_waitcnt vmcnt(22)
	s_cselect_b32 s2, s20, s29
	s_cselect_b32 s3, s21, s28
	s_add_i32 s16, s29, 0x80
	s_addk_i32 s28, 0x100
	s_mov_b32 s29, 0
	v_add_u32_e32 v140, 0x10000, v170
	v_add_u32_e32 v156, 0x14000, v170
	ds_read_b128 v[128:131], v140
	ds_read_b128 v[132:135], v140 offset:1024
	ds_read_b128 v[136:139], v140 offset:2048
	ds_read_b128 v[140:143], v140 offset:3072
	ds_read_b128 v[144:147], v156
	ds_read_b128 v[148:151], v156 offset:1024
	ds_read_b128 v[152:155], v156 offset:2048
	ds_read_b128 v[156:159], v156 offset:3072
	s_add_i32 s6, s16, 0x80
	s_cmp_eq_u32 s12, s29
	s_cselect_b32 s46, s2, s6
	s_cselect_b32 s31, s3, s28
	s_or_b32 s30, s46, 0x80
	s_add_i32 s6, s33, s16
	s_mov_b32 m0, s13
	ds_read_b128 v[160:163], v171
	ds_read_b128 v[172:175], v171 offset:1024
	ds_read_b128 v[176:179], v171 offset:2048
	ds_read_b128 v[180:183], v171 offset:3072
	ds_read_b128 v[184:187], v171 offset:4096
	ds_read_b128 v[188:191], v171 offset:5120
	ds_read_b128 v[194:197], v171 offset:6144
	ds_read_b128 v[198:201], v171 offset:7168
	buffer_load_dwordx4 v164, s[36:39], s6 offen lds
	s_mov_b32 m0, s83
	s_nop 0
	buffer_load_dwordx4 v166, s[36:39], s6 offen lds
	s_waitcnt vmcnt(8)
	s_waitcnt lgkmcnt(0)
	s_barrier
	s_setprio 1
	v_mfma_f32_16x16x32_bf16 v[124:127], v[128:131], v[160:163], 0
	v_mfma_f32_16x16x32_bf16 v[120:123], v[136:139], v[160:163], 0
	v_mfma_f32_16x16x32_bf16 v[108:111], v[128:131], v[176:179], 0
	v_mfma_f32_16x16x32_bf16 v[104:107], v[136:139], v[176:179], 0
	v_mfma_f32_16x16x32_bf16 v[92:95], v[128:131], v[184:187], 0
	v_mfma_f32_16x16x32_bf16 v[88:91], v[136:139], v[184:187], 0
	v_mfma_f32_16x16x32_bf16 v[76:79], v[128:131], v[194:197], 0
	v_mfma_f32_16x16x32_bf16 v[72:75], v[136:139], v[194:197], 0
	v_mfma_f32_16x16x32_bf16 v[124:127], v[132:135], v[172:175], v[124:127]
	v_mfma_f32_16x16x32_bf16 v[120:123], v[140:143], v[172:175], v[120:123]
	v_mfma_f32_16x16x32_bf16 v[108:111], v[132:135], v[180:183], v[108:111]
	v_mfma_f32_16x16x32_bf16 v[104:107], v[140:143], v[180:183], v[104:107]
	v_mfma_f32_16x16x32_bf16 v[92:95], v[132:135], v[188:191], v[92:95]
	v_mfma_f32_16x16x32_bf16 v[88:91], v[140:143], v[188:191], v[88:91]
	v_mfma_f32_16x16x32_bf16 v[76:79], v[132:135], v[198:201], v[76:79]
	v_mfma_f32_16x16x32_bf16 v[72:75], v[140:143], v[198:201], v[72:75]
	v_mfma_f32_16x16x32_bf16 v[116:119], v[144:147], v[160:163], 0
	v_mfma_f32_16x16x32_bf16 v[112:115], v[152:155], v[160:163], 0
	v_mfma_f32_16x16x32_bf16 v[100:103], v[144:147], v[176:179], 0
	v_mfma_f32_16x16x32_bf16 v[96:99], v[152:155], v[176:179], 0
	v_mfma_f32_16x16x32_bf16 v[84:87], v[144:147], v[184:187], 0
	v_mfma_f32_16x16x32_bf16 v[80:83], v[152:155], v[184:187], 0
	v_mfma_f32_16x16x32_bf16 v[68:71], v[144:147], v[194:197], 0
	v_mfma_f32_16x16x32_bf16 v[64:67], v[152:155], v[194:197], 0
	v_mfma_f32_16x16x32_bf16 v[116:119], v[148:151], v[172:175], v[116:119]
	v_mfma_f32_16x16x32_bf16 v[112:115], v[156:159], v[172:175], v[112:115]
	v_mfma_f32_16x16x32_bf16 v[100:103], v[148:151], v[180:183], v[100:103]
	v_mfma_f32_16x16x32_bf16 v[96:99], v[156:159], v[180:183], v[96:99]
	v_mfma_f32_16x16x32_bf16 v[84:87], v[148:151], v[188:191], v[84:87]
	v_mfma_f32_16x16x32_bf16 v[80:83], v[156:159], v[188:191], v[80:83]
	v_mfma_f32_16x16x32_bf16 v[68:71], v[148:151], v[198:201], v[68:71]
	v_mfma_f32_16x16x32_bf16 v[64:67], v[156:159], v[198:201], v[64:67]
	s_setprio 0
	s_barrier
	s_mov_b32 m0, s42
	s_mov_b32 s6, s38
	s_mov_b32 s7, s39
	buffer_load_dwordx4 v165, s[4:7], s31 offen lds
	s_mov_b32 m0, s43
	ds_read_b128 v[160:163], v171 offset:16384
	s_add_i32 s47, s31, s33
	buffer_load_dwordx4 v167, s[4:7], s31 offen lds
	s_mov_b32 m0, s44
	ds_read_b128 v[172:175], v171 offset:17408
	buffer_load_dwordx4 v165, s[4:7], s47 offen lds
	s_mov_b32 m0, s41
	ds_read_b128 v[176:179], v171 offset:18432
	buffer_load_dwordx4 v164, s[36:39], s46 offen lds
	s_mov_b32 m0, s52
	ds_read_b128 v[180:183], v171 offset:19456
	buffer_load_dwordx4 v166, s[36:39], s46 offen lds
	ds_read_b128 v[184:187], v171 offset:20480
	ds_read_b128 v[188:191], v171 offset:21504
	ds_read_b128 v[194:197], v171 offset:22528
	ds_read_b128 v[198:201], v171 offset:23552
	s_waitcnt vmcnt(7)
	s_waitcnt lgkmcnt(0)
	s_barrier
	s_setprio 1
	v_mfma_f32_16x16x32_bf16 v[60:63], v[128:131], v[160:163], 0
	v_mfma_f32_16x16x32_bf16 v[56:59], v[136:139], v[160:163], 0
	v_mfma_f32_16x16x32_bf16 v[44:47], v[128:131], v[176:179], 0
	v_mfma_f32_16x16x32_bf16 v[40:43], v[136:139], v[176:179], 0
	v_mfma_f32_16x16x32_bf16 v[28:31], v[128:131], v[184:187], 0
	v_mfma_f32_16x16x32_bf16 v[24:27], v[136:139], v[184:187], 0
	v_mfma_f32_16x16x32_bf16 v[12:15], v[128:131], v[194:197], 0
	v_mfma_f32_16x16x32_bf16 v[8:11], v[136:139], v[194:197], 0
	v_mfma_f32_16x16x32_bf16 v[60:63], v[132:135], v[172:175], v[60:63]
	v_mfma_f32_16x16x32_bf16 v[56:59], v[140:143], v[172:175], v[56:59]
	v_mfma_f32_16x16x32_bf16 v[44:47], v[132:135], v[180:183], v[44:47]
	v_mfma_f32_16x16x32_bf16 v[40:43], v[140:143], v[180:183], v[40:43]
	v_mfma_f32_16x16x32_bf16 v[28:31], v[132:135], v[188:191], v[28:31]
	v_mfma_f32_16x16x32_bf16 v[24:27], v[140:143], v[188:191], v[24:27]
	v_mfma_f32_16x16x32_bf16 v[12:15], v[132:135], v[198:201], v[12:15]
	v_mfma_f32_16x16x32_bf16 v[8:11], v[140:143], v[198:201], v[8:11]
	v_mfma_f32_16x16x32_bf16 v[52:55], v[144:147], v[160:163], 0
	v_mfma_f32_16x16x32_bf16 v[48:51], v[152:155], v[160:163], 0
	v_mfma_f32_16x16x32_bf16 v[36:39], v[144:147], v[176:179], 0
	v_mfma_f32_16x16x32_bf16 v[32:35], v[152:155], v[176:179], 0
	v_mfma_f32_16x16x32_bf16 v[20:23], v[144:147], v[184:187], 0
	v_mfma_f32_16x16x32_bf16 v[16:19], v[152:155], v[184:187], 0
	v_mfma_f32_16x16x32_bf16 v[4:7], v[144:147], v[194:197], 0
	v_mfma_f32_16x16x32_bf16 v[0:3], v[152:155], v[194:197], 0
	v_mfma_f32_16x16x32_bf16 v[52:55], v[148:151], v[172:175], v[52:55]
	v_mfma_f32_16x16x32_bf16 v[48:51], v[156:159], v[172:175], v[48:51]
	v_mfma_f32_16x16x32_bf16 v[36:39], v[148:151], v[180:183], v[36:39]
	v_mfma_f32_16x16x32_bf16 v[32:35], v[156:159], v[180:183], v[32:35]
	v_mfma_f32_16x16x32_bf16 v[20:23], v[148:151], v[188:191], v[20:23]
	v_mfma_f32_16x16x32_bf16 v[16:19], v[156:159], v[188:191], v[16:19]
	v_mfma_f32_16x16x32_bf16 v[4:7], v[148:151], v[198:201], v[4:7]
	v_mfma_f32_16x16x32_bf16 v[0:3], v[156:159], v[198:201], v[0:3]
	s_setprio 0
	s_barrier
; #define PG8_STAGE(bufoff, rs_, soff_, voff) do { _Pragma("unroll") for (int _i = 0; _i < 2; ++_i) \
;         __builtin_amdgcn_raw_ptr_buffer_load_lds(rs_, (LAS void*)(lds + (bufoff) + ldsw + _i * 8192), 16, (int)(voff)[_i], (int)(soff_), 0, 0); } while (0)
; #define PG8_LDA(dst, b, h) do { _Pragma("unroll") for (int m = 0; m < 4; ++m) dst[m] = PG8_LD2(lds + PG8_SA(b, h) + aoff + m * 2048); } while (0)
; #define PG8_LDB(dst, b, h) do { _Pragma("unroll") for (int n = 0; n < 2; ++n) dst[n] = PG8_LD2(lds + PG8_SB(b, h) + boff + n * 2048); } while (0)
; #define PG8_WAIT_V(n) asm volatile("s_waitcnt vmcnt(" #n ")" ::: "memory")
; #define PG8_WAIT_L(n) asm volatile("s_waitcnt lgkmcnt(" #n ")" ::: "memory")
; #define PG8_BAR __builtin_amdgcn_s_barrier()
; #define PG8_SCHED __builtin_amdgcn_sched_barrier(0)
; template <class Epi, class Sched, bool ALIGN_EPI = false, bool SP2 = false, bool FP8 = false>
; __device__ __forceinline__ void gemm_phase(LAS unsigned char* lds, const Gemm g, const Sched& S, const Epi& E, int wbase) {
;     ...
;         for (int t = 0; t < nt; t += 2) {
;     ...
;             PG8_LDB(B0, 1, 0); PG8_LDB(B1, 1, 1); PG8_SCHED; PG8_LDA(At, 1, 0); PG8_STAGE(PG8_SA(0, 1), rA2, a2 + hstep, voffA);
;             PG8_WAIT_V(8); PG8_WAIT_L(0); PG8_BAR; PG8_MMA(0, 0, At, B0); PG8_MMA(0, 1, At, B1); PG8_BAR; PG8_SCHED;
;             PG8_LDA(At, 1, 1); PG8_STAGE(PG8_SB(1, 0), rB2, b3, voffB); PG8_STAGE(PG8_SB(1, 1), rB2, b3 + hstep, voffB); PG8_STAGE(PG8_SA(1, 0), rA2, a3, voffA);
;             PG8_WAIT_V(8); PG8_WAIT_L(0); PG8_BAR; PG8_MMA(1, 0, At, B0); PG8_MMA(1, 1, At, B1); PG8_BAR; PG8_SCHED;
	s_mov_b32 m0, s45
	s_nop 0
	buffer_load_dwordx4 v167, s[4:7], s47 offen lds
	v_add_u32_e32 v140, 0x18000, v170
	v_add_u32_e32 v156, 0x1c000, v170
	ds_read_b128 v[128:131], v140
	ds_read_b128 v[132:135], v140 offset:1024
	ds_read_b128 v[136:139], v140 offset:2048
	ds_read_b128 v[140:143], v140 offset:3072
	ds_read_b128 v[144:147], v156
	ds_read_b128 v[148:151], v156 offset:1024
	ds_read_b128 v[152:155], v156 offset:2048
	ds_read_b128 v[156:159], v156 offset:3072
	s_add_i32 s46, s46, s33
	s_mov_b32 m0, s53
	ds_read_b128 v[160:163], v171 offset:32768
	ds_read_b128 v[172:175], v171 offset:33792
	ds_read_b128 v[176:179], v171 offset:34816
	ds_read_b128 v[180:183], v171 offset:35840
	ds_read_b128 v[184:187], v171 offset:36864
	ds_read_b128 v[188:191], v171 offset:37888
	ds_read_b128 v[194:197], v171 offset:38912
	ds_read_b128 v[198:201], v171 offset:39936
	buffer_load_dwordx4 v164, s[36:39], s46 offen lds
	s_mov_b32 m0, s1
	s_nop 0
	buffer_load_dwordx4 v166, s[36:39], s46 offen lds
	s_waitcnt vmcnt(8)
	s_waitcnt lgkmcnt(0)
	s_barrier
	s_setprio 1
	v_mfma_f32_16x16x32_bf16 v[124:127], v[128:131], v[160:163], v[124:127]
	v_mfma_f32_16x16x32_bf16 v[120:123], v[136:139], v[160:163], v[120:123]
	v_mfma_f32_16x16x32_bf16 v[108:111], v[128:131], v[176:179], v[108:111]
	v_mfma_f32_16x16x32_bf16 v[104:107], v[136:139], v[176:179], v[104:107]
	v_mfma_f32_16x16x32_bf16 v[92:95], v[128:131], v[184:187], v[92:95]
	v_mfma_f32_16x16x32_bf16 v[88:91], v[136:139], v[184:187], v[88:91]
	v_mfma_f32_16x16x32_bf16 v[76:79], v[128:131], v[194:197], v[76:79]
	v_mfma_f32_16x16x32_bf16 v[72:75], v[136:139], v[194:197], v[72:75]
	v_mfma_f32_16x16x32_bf16 v[124:127], v[132:135], v[172:175], v[124:127]
	v_mfma_f32_16x16x32_bf16 v[120:123], v[140:143], v[172:175], v[120:123]
	v_mfma_f32_16x16x32_bf16 v[108:111], v[132:135], v[180:183], v[108:111]
	v_mfma_f32_16x16x32_bf16 v[104:107], v[140:143], v[180:183], v[104:107]
	v_mfma_f32_16x16x32_bf16 v[92:95], v[132:135], v[188:191], v[92:95]
	v_mfma_f32_16x16x32_bf16 v[88:91], v[140:143], v[188:191], v[88:91]
	v_mfma_f32_16x16x32_bf16 v[76:79], v[132:135], v[198:201], v[76:79]
	v_mfma_f32_16x16x32_bf16 v[72:75], v[140:143], v[198:201], v[72:75]
	v_mfma_f32_16x16x32_bf16 v[116:119], v[144:147], v[160:163], v[116:119]
	v_mfma_f32_16x16x32_bf16 v[112:115], v[152:155], v[160:163], v[112:115]
	v_mfma_f32_16x16x32_bf16 v[100:103], v[144:147], v[176:179], v[100:103]
	v_mfma_f32_16x16x32_bf16 v[96:99], v[152:155], v[176:179], v[96:99]
	v_mfma_f32_16x16x32_bf16 v[84:87], v[144:147], v[184:187], v[84:87]
	v_mfma_f32_16x16x32_bf16 v[80:83], v[152:155], v[184:187], v[80:83]
	v_mfma_f32_16x16x32_bf16 v[68:71], v[144:147], v[194:197], v[68:71]
	v_mfma_f32_16x16x32_bf16 v[64:67], v[152:155], v[194:197], v[64:67]
	v_mfma_f32_16x16x32_bf16 v[116:119], v[148:151], v[172:175], v[116:119]
	v_mfma_f32_16x16x32_bf16 v[112:115], v[156:159], v[172:175], v[112:115]
	v_mfma_f32_16x16x32_bf16 v[100:103], v[148:151], v[180:183], v[100:103]
	v_mfma_f32_16x16x32_bf16 v[96:99], v[156:159], v[180:183], v[96:99]
	v_mfma_f32_16x16x32_bf16 v[84:87], v[148:151], v[188:191], v[84:87]
	v_mfma_f32_16x16x32_bf16 v[80:83], v[156:159], v[188:191], v[80:83]
	v_mfma_f32_16x16x32_bf16 v[68:71], v[148:151], v[198:201], v[68:71]
	v_mfma_f32_16x16x32_bf16 v[64:67], v[156:159], v[198:201], v[64:67]
	s_setprio 0
	s_barrier
	s_mov_b32 m0, s56
	s_bitset1_b32 s31, 7
	buffer_load_dwordx4 v165, s[4:7], s31 offen lds
	s_mov_b32 m0, s57
	ds_read_b128 v[160:163], v171 offset:49152
	buffer_load_dwordx4 v167, s[4:7], s31 offen lds
	s_add_i32 s31, s31, s33
	s_mov_b32 m0, s65
	ds_read_b128 v[172:175], v171 offset:50176
	buffer_load_dwordx4 v165, s[4:7], s31 offen lds
	s_mov_b32 m0, s76
	ds_read_b128 v[176:179], v171 offset:51200
	buffer_load_dwordx4 v167, s[4:7], s31 offen lds
	s_mov_b32 m0, s58
	ds_read_b128 v[180:183], v171 offset:52224
	buffer_load_dwordx4 v164, s[36:39], s30 offen lds
	s_mov_b32 m0, s59
	ds_read_b128 v[184:187], v171 offset:53248
	buffer_load_dwordx4 v166, s[36:39], s30 offen lds
	ds_read_b128 v[188:191], v171 offset:54272
	ds_read_b128 v[194:197], v171 offset:55296
	ds_read_b128 v[198:201], v171 offset:56320
	s_waitcnt vmcnt(8)
	s_waitcnt lgkmcnt(0)
	s_barrier
	s_setprio 1
	v_mfma_f32_16x16x32_bf16 v[60:63], v[128:131], v[160:163], v[60:63]
	v_mfma_f32_16x16x32_bf16 v[56:59], v[136:139], v[160:163], v[56:59]
	v_mfma_f32_16x16x32_bf16 v[44:47], v[128:131], v[176:179], v[44:47]
	v_mfma_f32_16x16x32_bf16 v[40:43], v[136:139], v[176:179], v[40:43]
	v_mfma_f32_16x16x32_bf16 v[28:31], v[128:131], v[184:187], v[28:31]
	v_mfma_f32_16x16x32_bf16 v[24:27], v[136:139], v[184:187], v[24:27]
	v_mfma_f32_16x16x32_bf16 v[12:15], v[128:131], v[194:197], v[12:15]
	v_mfma_f32_16x16x32_bf16 v[8:11], v[136:139], v[194:197], v[8:11]
	v_mfma_f32_16x16x32_bf16 v[60:63], v[132:135], v[172:175], v[60:63]
	v_mfma_f32_16x16x32_bf16 v[56:59], v[140:143], v[172:175], v[56:59]
	v_mfma_f32_16x16x32_bf16 v[44:47], v[132:135], v[180:183], v[44:47]
	v_mfma_f32_16x16x32_bf16 v[40:43], v[140:143], v[180:183], v[40:43]
	v_mfma_f32_16x16x32_bf16 v[28:31], v[132:135], v[188:191], v[28:31]
	v_mfma_f32_16x16x32_bf16 v[24:27], v[140:143], v[188:191], v[24:27]
	v_mfma_f32_16x16x32_bf16 v[12:15], v[132:135], v[198:201], v[12:15]
	v_mfma_f32_16x16x32_bf16 v[8:11], v[140:143], v[198:201], v[8:11]
	v_mfma_f32_16x16x32_bf16 v[52:55], v[144:147], v[160:163], v[52:55]
	v_mfma_f32_16x16x32_bf16 v[48:51], v[152:155], v[160:163], v[48:51]
	v_mfma_f32_16x16x32_bf16 v[36:39], v[144:147], v[176:179], v[36:39]
	v_mfma_f32_16x16x32_bf16 v[32:35], v[152:155], v[176:179], v[32:35]
	v_mfma_f32_16x16x32_bf16 v[20:23], v[144:147], v[184:187], v[20:23]
	v_mfma_f32_16x16x32_bf16 v[16:19], v[152:155], v[184:187], v[16:19]
	v_mfma_f32_16x16x32_bf16 v[4:7], v[144:147], v[194:197], v[4:7]
	v_mfma_f32_16x16x32_bf16 v[0:3], v[152:155], v[194:197], v[0:3]
	v_mfma_f32_16x16x32_bf16 v[52:55], v[148:151], v[172:175], v[52:55]
	v_mfma_f32_16x16x32_bf16 v[48:51], v[156:159], v[172:175], v[48:51]
	v_mfma_f32_16x16x32_bf16 v[36:39], v[148:151], v[180:183], v[36:39]
	v_mfma_f32_16x16x32_bf16 v[32:35], v[156:159], v[180:183], v[32:35]
	v_mfma_f32_16x16x32_bf16 v[20:23], v[148:151], v[188:191], v[20:23]
	v_mfma_f32_16x16x32_bf16 v[16:19], v[156:159], v[188:191], v[16:19]
	v_mfma_f32_16x16x32_bf16 v[4:7], v[148:151], v[198:201], v[4:7]
	v_mfma_f32_16x16x32_bf16 v[0:3], v[156:159], v[198:201], v[0:3]
	s_setprio 0
	s_barrier
	s_add_i32 s29, s29, 2
	s_addk_i32 s16, 0x100
	s_addk_i32 s28, 0x100
	s_cmp_ge_i32 s29, s82
	s_cbranch_scc0 .LBB0_352
	s_branch .Lzp_after_352
; #define PG8_STAGE(bufoff, rs_, soff_, voff) do { _Pragma("unroll") for (int _i = 0; _i < 2; ++_i) \
;         __builtin_amdgcn_raw_ptr_buffer_load_lds(rs_, (LAS void*)(lds + (bufoff) + ldsw + _i * 8192), 16, (int)(voff)[_i], (int)(soff_), 0, 0); } while (0)
; #define PG8_LDA(dst, b, h) do { _Pragma("unroll") for (int m = 0; m < 4; ++m) dst[m] = PG8_LD2(lds + PG8_SA(b, h) + aoff + m * 2048); } while (0)
; #define PG8_LDB(dst, b, h) do { _Pragma("unroll") for (int n = 0; n < 2; ++n) dst[n] = PG8_LD2(lds + PG8_SB(b, h) + boff + n * 2048); } while (0)
; #define PG8_WAIT_V(n) asm volatile("s_waitcnt vmcnt(" #n ")" ::: "memory")
; #define PG8_WAIT_L(n) asm volatile("s_waitcnt lgkmcnt(" #n ")" ::: "memory")
; #define PG8_BAR __builtin_amdgcn_s_barrier()
; #define PG8_SCHED __builtin_amdgcn_sched_barrier(0)
; template <class Epi, class Sched, bool ALIGN_EPI = false, bool SP2 = false, bool FP8 = false>
; __device__ __forceinline__ void gemm_phase(LAS unsigned char* lds, const Gemm g, const Sched& S, const Epi& E, int wbase) {
;     ...
;             if constexpr (SP2) {
;             PG8_LDB(B0, 0, 0); PG8_LDB(B1, 0, 1); PG8_SCHED; PG8_LDA(At, 0, 0); PG8_STAGE(PG8_SA(1, 1), rAc, a1 + hstep, voffA);
;             PG8_WAIT_V(8); PG8_WAIT_L(0); PG8_BAR; PG8_MMA(0, 0, At, B0); PG8_MMA(0, 1, At, B1); PG8_BAR; PG8_SCHED;
;             PG8_LDA(At, 0, 1); PG8_STAGE(PG8_SB(0, 0), rB2, b2, voffB); PG8_STAGE(PG8_SB(0, 1), rB2, b2 + hstep, voffB); PG8_STAGE(PG8_SA(0, 0), rA2, a2, voffA);
;             PG8_WAIT_V(8); PG8_WAIT_L(0); PG8_BAR; PG8_MMA(1, 0, At, B0); PG8_MMA(1, 1, At, B1); PG8_BAR; PG8_SCHED;
.LBB0_352:
	v_add_u32_e32 v140, 0x10000, v170
	v_add_u32_e32 v156, 0x14000, v170
	ds_read_b128 v[128:131], v140
	ds_read_b128 v[132:135], v140 offset:1024
	ds_read_b128 v[136:139], v140 offset:2048
	ds_read_b128 v[140:143], v140 offset:3072
	ds_read_b128 v[144:147], v156
	ds_read_b128 v[148:151], v156 offset:1024
	ds_read_b128 v[152:155], v156 offset:2048
	ds_read_b128 v[156:159], v156 offset:3072
	s_add_i32 s6, s16, 0x80
	s_cmp_eq_u32 s12, s29
	s_cselect_b32 s46, s2, s6
	s_cselect_b32 s31, s3, s28
	s_or_b32 s30, s46, 0x80
	s_add_i32 s6, s33, s16
	s_mov_b32 m0, s13
	ds_read_b128 v[160:163], v171
	ds_read_b128 v[172:175], v171 offset:1024
	ds_read_b128 v[176:179], v171 offset:2048
	ds_read_b128 v[180:183], v171 offset:3072
	ds_read_b128 v[184:187], v171 offset:4096
	ds_read_b128 v[188:191], v171 offset:5120
	ds_read_b128 v[194:197], v171 offset:6144
	ds_read_b128 v[198:201], v171 offset:7168
	buffer_load_dwordx4 v164, s[36:39], s6 offen lds
	s_mov_b32 m0, s83
	s_nop 0
	buffer_load_dwordx4 v166, s[36:39], s6 offen lds
	s_waitcnt vmcnt(8)
	s_waitcnt lgkmcnt(0)
	s_barrier
	s_setprio 1
	v_mfma_f32_16x16x32_bf16 v[124:127], v[128:131], v[160:163], v[124:127]
	v_mfma_f32_16x16x32_bf16 v[120:123], v[136:139], v[160:163], v[120:123]
	v_mfma_f32_16x16x32_bf16 v[108:111], v[128:131], v[176:179], v[108:111]
	v_mfma_f32_16x16x32_bf16 v[104:107], v[136:139], v[176:179], v[104:107]
	v_mfma_f32_16x16x32_bf16 v[92:95], v[128:131], v[184:187], v[92:95]
	v_mfma_f32_16x16x32_bf16 v[88:91], v[136:139], v[184:187], v[88:91]
	v_mfma_f32_16x16x32_bf16 v[76:79], v[128:131], v[194:197], v[76:79]
	v_mfma_f32_16x16x32_bf16 v[72:75], v[136:139], v[194:197], v[72:75]
	v_mfma_f32_16x16x32_bf16 v[124:127], v[132:135], v[172:175], v[124:127]
	v_mfma_f32_16x16x32_bf16 v[120:123], v[140:143], v[172:175], v[120:123]
	v_mfma_f32_16x16x32_bf16 v[108:111], v[132:135], v[180:183], v[108:111]
	v_mfma_f32_16x16x32_bf16 v[104:107], v[140:143], v[180:183], v[104:107]
	v_mfma_f32_16x16x32_bf16 v[92:95], v[132:135], v[188:191], v[92:95]
	v_mfma_f32_16x16x32_bf16 v[88:91], v[140:143], v[188:191], v[88:91]
	v_mfma_f32_16x16x32_bf16 v[76:79], v[132:135], v[198:201], v[76:79]
	v_mfma_f32_16x16x32_bf16 v[72:75], v[140:143], v[198:201], v[72:75]
	v_mfma_f32_16x16x32_bf16 v[116:119], v[144:147], v[160:163], v[116:119]
	v_mfma_f32_16x16x32_bf16 v[112:115], v[152:155], v[160:163], v[112:115]
	v_mfma_f32_16x16x32_bf16 v[100:103], v[144:147], v[176:179], v[100:103]
	v_mfma_f32_16x16x32_bf16 v[96:99], v[152:155], v[176:179], v[96:99]
	v_mfma_f32_16x16x32_bf16 v[84:87], v[144:147], v[184:187], v[84:87]
	v_mfma_f32_16x16x32_bf16 v[80:83], v[152:155], v[184:187], v[80:83]
	v_mfma_f32_16x16x32_bf16 v[68:71], v[144:147], v[194:197], v[68:71]
	v_mfma_f32_16x16x32_bf16 v[64:67], v[152:155], v[194:197], v[64:67]
	v_mfma_f32_16x16x32_bf16 v[116:119], v[148:151], v[172:175], v[116:119]
	v_mfma_f32_16x16x32_bf16 v[112:115], v[156:159], v[172:175], v[112:115]
	v_mfma_f32_16x16x32_bf16 v[100:103], v[148:151], v[180:183], v[100:103]
	v_mfma_f32_16x16x32_bf16 v[96:99], v[156:159], v[180:183], v[96:99]
	v_mfma_f32_16x16x32_bf16 v[84:87], v[148:151], v[188:191], v[84:87]
	v_mfma_f32_16x16x32_bf16 v[80:83], v[156:159], v[188:191], v[80:83]
	v_mfma_f32_16x16x32_bf16 v[68:71], v[148:151], v[198:201], v[68:71]
	v_mfma_f32_16x16x32_bf16 v[64:67], v[156:159], v[198:201], v[64:67]
	s_setprio 0
	s_barrier
	s_mov_b32 m0, s42
	s_mov_b32 s6, s38
	s_mov_b32 s7, s39
	buffer_load_dwordx4 v165, s[4:7], s31 offen lds
	s_mov_b32 m0, s43
	ds_read_b128 v[160:163], v171 offset:16384
	s_add_i32 s47, s31, s33
	buffer_load_dwordx4 v167, s[4:7], s31 offen lds
	s_mov_b32 m0, s44
	ds_read_b128 v[172:175], v171 offset:17408
	buffer_load_dwordx4 v165, s[4:7], s47 offen lds
	s_mov_b32 m0, s41
	ds_read_b128 v[176:179], v171 offset:18432
	buffer_load_dwordx4 v164, s[36:39], s46 offen lds
	s_mov_b32 m0, s52
	ds_read_b128 v[180:183], v171 offset:19456
	buffer_load_dwordx4 v166, s[36:39], s46 offen lds
	ds_read_b128 v[184:187], v171 offset:20480
	ds_read_b128 v[188:191], v171 offset:21504
	ds_read_b128 v[194:197], v171 offset:22528
	ds_read_b128 v[198:201], v171 offset:23552
	s_waitcnt vmcnt(7)
	s_waitcnt lgkmcnt(0)
	s_barrier
	s_setprio 1
	v_mfma_f32_16x16x32_bf16 v[60:63], v[128:131], v[160:163], v[60:63]
	v_mfma_f32_16x16x32_bf16 v[56:59], v[136:139], v[160:163], v[56:59]
	v_mfma_f32_16x16x32_bf16 v[44:47], v[128:131], v[176:179], v[44:47]
	v_mfma_f32_16x16x32_bf16 v[40:43], v[136:139], v[176:179], v[40:43]
	v_mfma_f32_16x16x32_bf16 v[28:31], v[128:131], v[184:187], v[28:31]
	v_mfma_f32_16x16x32_bf16 v[24:27], v[136:139], v[184:187], v[24:27]
	v_mfma_f32_16x16x32_bf16 v[12:15], v[128:131], v[194:197], v[12:15]
	v_mfma_f32_16x16x32_bf16 v[8:11], v[136:139], v[194:197], v[8:11]
	v_mfma_f32_16x16x32_bf16 v[60:63], v[132:135], v[172:175], v[60:63]
	v_mfma_f32_16x16x32_bf16 v[56:59], v[140:143], v[172:175], v[56:59]
	v_mfma_f32_16x16x32_bf16 v[44:47], v[132:135], v[180:183], v[44:47]
	v_mfma_f32_16x16x32_bf16 v[40:43], v[140:143], v[180:183], v[40:43]
	v_mfma_f32_16x16x32_bf16 v[28:31], v[132:135], v[188:191], v[28:31]
	v_mfma_f32_16x16x32_bf16 v[24:27], v[140:143], v[188:191], v[24:27]
	v_mfma_f32_16x16x32_bf16 v[12:15], v[132:135], v[198:201], v[12:15]
	v_mfma_f32_16x16x32_bf16 v[8:11], v[140:143], v[198:201], v[8:11]
	v_mfma_f32_16x16x32_bf16 v[52:55], v[144:147], v[160:163], v[52:55]
	v_mfma_f32_16x16x32_bf16 v[48:51], v[152:155], v[160:163], v[48:51]
	v_mfma_f32_16x16x32_bf16 v[36:39], v[144:147], v[176:179], v[36:39]
	v_mfma_f32_16x16x32_bf16 v[32:35], v[152:155], v[176:179], v[32:35]
	v_mfma_f32_16x16x32_bf16 v[20:23], v[144:147], v[184:187], v[20:23]
	v_mfma_f32_16x16x32_bf16 v[16:19], v[152:155], v[184:187], v[16:19]
	v_mfma_f32_16x16x32_bf16 v[4:7], v[144:147], v[194:197], v[4:7]
	v_mfma_f32_16x16x32_bf16 v[0:3], v[152:155], v[194:197], v[0:3]
	v_mfma_f32_16x16x32_bf16 v[52:55], v[148:151], v[172:175], v[52:55]
	v_mfma_f32_16x16x32_bf16 v[48:51], v[156:159], v[172:175], v[48:51]
	v_mfma_f32_16x16x32_bf16 v[36:39], v[148:151], v[180:183], v[36:39]
	v_mfma_f32_16x16x32_bf16 v[32:35], v[156:159], v[180:183], v[32:35]
	v_mfma_f32_16x16x32_bf16 v[20:23], v[148:151], v[188:191], v[20:23]
	v_mfma_f32_16x16x32_bf16 v[16:19], v[156:159], v[188:191], v[16:19]
	v_mfma_f32_16x16x32_bf16 v[4:7], v[148:151], v[198:201], v[4:7]
	v_mfma_f32_16x16x32_bf16 v[0:3], v[156:159], v[198:201], v[0:3]
	s_setprio 0
	s_barrier
; #define PG8_STAGE(bufoff, rs_, soff_, voff) do { _Pragma("unroll") for (int _i = 0; _i < 2; ++_i) \
;         __builtin_amdgcn_raw_ptr_buffer_load_lds(rs_, (LAS void*)(lds + (bufoff) + ldsw + _i * 8192), 16, (int)(voff)[_i], (int)(soff_), 0, 0); } while (0)
; #define PG8_LDA(dst, b, h) do { _Pragma("unroll") for (int m = 0; m < 4; ++m) dst[m] = PG8_LD2(lds + PG8_SA(b, h) + aoff + m * 2048); } while (0)
; #define PG8_LDB(dst, b, h) do { _Pragma("unroll") for (int n = 0; n < 2; ++n) dst[n] = PG8_LD2(lds + PG8_SB(b, h) + boff + n * 2048); } while (0)
; #define PG8_WAIT_V(n) asm volatile("s_waitcnt vmcnt(" #n ")" ::: "memory")
; #define PG8_WAIT_L(n) asm volatile("s_waitcnt lgkmcnt(" #n ")" ::: "memory")
; #define PG8_BAR __builtin_amdgcn_s_barrier()
; #define PG8_SCHED __builtin_amdgcn_sched_barrier(0)
; template <class Epi, class Sched, bool ALIGN_EPI = false, bool SP2 = false, bool FP8 = false>
; __device__ __forceinline__ void gemm_phase(LAS unsigned char* lds, const Gemm g, const Sched& S, const Epi& E, int wbase) {
;     ...
;             PG8_LDB(B0, 1, 0); PG8_LDB(B1, 1, 1); PG8_SCHED; PG8_LDA(At, 1, 0); PG8_STAGE(PG8_SA(0, 1), rA2, a2 + hstep, voffA);
;             PG8_WAIT_V(8); PG8_WAIT_L(0); PG8_BAR; PG8_MMA(0, 0, At, B0); PG8_MMA(0, 1, At, B1); PG8_BAR; PG8_SCHED;
;             PG8_LDA(At, 1, 1); PG8_STAGE(PG8_SB(1, 0), rB2, b3, voffB); PG8_STAGE(PG8_SB(1, 1), rB2, b3 + hstep, voffB); PG8_STAGE(PG8_SA(1, 0), rA2, a3, voffA);
;             PG8_WAIT_V(8); PG8_WAIT_L(0); PG8_BAR; PG8_MMA(1, 0, At, B0); PG8_MMA(1, 1, At, B1); PG8_BAR; PG8_SCHED;
	s_mov_b32 m0, s45
	s_nop 0
	buffer_load_dwordx4 v167, s[4:7], s47 offen lds
	v_add_u32_e32 v140, 0x18000, v170
	v_add_u32_e32 v156, 0x1c000, v170
	ds_read_b128 v[128:131], v140
	ds_read_b128 v[132:135], v140 offset:1024
	ds_read_b128 v[136:139], v140 offset:2048
	ds_read_b128 v[140:143], v140 offset:3072
	ds_read_b128 v[144:147], v156
	ds_read_b128 v[148:151], v156 offset:1024
	ds_read_b128 v[152:155], v156 offset:2048
	ds_read_b128 v[156:159], v156 offset:3072
	s_add_i32 s46, s46, s33
	s_mov_b32 m0, s53
	ds_read_b128 v[160:163], v171 offset:32768
	ds_read_b128 v[172:175], v171 offset:33792
	ds_read_b128 v[176:179], v171 offset:34816
	ds_read_b128 v[180:183], v171 offset:35840
	ds_read_b128 v[184:187], v171 offset:36864
	ds_read_b128 v[188:191], v171 offset:37888
	ds_read_b128 v[194:197], v171 offset:38912
	ds_read_b128 v[198:201], v171 offset:39936
	buffer_load_dwordx4 v164, s[36:39], s46 offen lds
	s_mov_b32 m0, s1
	s_nop 0
	buffer_load_dwordx4 v166, s[36:39], s46 offen lds
	s_waitcnt vmcnt(8)
	s_waitcnt lgkmcnt(0)
	s_barrier
	s_setprio 1
	v_mfma_f32_16x16x32_bf16 v[124:127], v[128:131], v[160:163], v[124:127]
	v_mfma_f32_16x16x32_bf16 v[120:123], v[136:139], v[160:163], v[120:123]
	v_mfma_f32_16x16x32_bf16 v[108:111], v[128:131], v[176:179], v[108:111]
	v_mfma_f32_16x16x32_bf16 v[104:107], v[136:139], v[176:179], v[104:107]
	v_mfma_f32_16x16x32_bf16 v[92:95], v[128:131], v[184:187], v[92:95]
	v_mfma_f32_16x16x32_bf16 v[88:91], v[136:139], v[184:187], v[88:91]
	v_mfma_f32_16x16x32_bf16 v[76:79], v[128:131], v[194:197], v[76:79]
	v_mfma_f32_16x16x32_bf16 v[72:75], v[136:139], v[194:197], v[72:75]
	v_mfma_f32_16x16x32_bf16 v[124:127], v[132:135], v[172:175], v[124:127]
	v_mfma_f32_16x16x32_bf16 v[120:123], v[140:143], v[172:175], v[120:123]
	v_mfma_f32_16x16x32_bf16 v[108:111], v[132:135], v[180:183], v[108:111]
	v_mfma_f32_16x16x32_bf16 v[104:107], v[140:143], v[180:183], v[104:107]
	v_mfma_f32_16x16x32_bf16 v[92:95], v[132:135], v[188:191], v[92:95]
	v_mfma_f32_16x16x32_bf16 v[88:91], v[140:143], v[188:191], v[88:91]
	v_mfma_f32_16x16x32_bf16 v[76:79], v[132:135], v[198:201], v[76:79]
	v_mfma_f32_16x16x32_bf16 v[72:75], v[140:143], v[198:201], v[72:75]
	v_mfma_f32_16x16x32_bf16 v[116:119], v[144:147], v[160:163], v[116:119]
	v_mfma_f32_16x16x32_bf16 v[112:115], v[152:155], v[160:163], v[112:115]
	v_mfma_f32_16x16x32_bf16 v[100:103], v[144:147], v[176:179], v[100:103]
	v_mfma_f32_16x16x32_bf16 v[96:99], v[152:155], v[176:179], v[96:99]
	v_mfma_f32_16x16x32_bf16 v[84:87], v[144:147], v[184:187], v[84:87]
	v_mfma_f32_16x16x32_bf16 v[80:83], v[152:155], v[184:187], v[80:83]
	v_mfma_f32_16x16x32_bf16 v[68:71], v[144:147], v[194:197], v[68:71]
	v_mfma_f32_16x16x32_bf16 v[64:67], v[152:155], v[194:197], v[64:67]
	v_mfma_f32_16x16x32_bf16 v[116:119], v[148:151], v[172:175], v[116:119]
	v_mfma_f32_16x16x32_bf16 v[112:115], v[156:159], v[172:175], v[112:115]
	v_mfma_f32_16x16x32_bf16 v[100:103], v[148:151], v[180:183], v[100:103]
	v_mfma_f32_16x16x32_bf16 v[96:99], v[156:159], v[180:183], v[96:99]
	v_mfma_f32_16x16x32_bf16 v[84:87], v[148:151], v[188:191], v[84:87]
	v_mfma_f32_16x16x32_bf16 v[80:83], v[156:159], v[188:191], v[80:83]
	v_mfma_f32_16x16x32_bf16 v[68:71], v[148:151], v[198:201], v[68:71]
	v_mfma_f32_16x16x32_bf16 v[64:67], v[156:159], v[198:201], v[64:67]
	s_setprio 0
	s_barrier
	s_mov_b32 m0, s56
	s_bitset1_b32 s31, 7
	buffer_load_dwordx4 v165, s[4:7], s31 offen lds
	s_mov_b32 m0, s57
	ds_read_b128 v[160:163], v171 offset:49152
	buffer_load_dwordx4 v167, s[4:7], s31 offen lds
	s_add_i32 s31, s31, s33
	s_mov_b32 m0, s65
	ds_read_b128 v[172:175], v171 offset:50176
	buffer_load_dwordx4 v165, s[4:7], s31 offen lds
	s_mov_b32 m0, s76
	ds_read_b128 v[176:179], v171 offset:51200
	buffer_load_dwordx4 v167, s[4:7], s31 offen lds
	s_mov_b32 m0, s58
	ds_read_b128 v[180:183], v171 offset:52224
	buffer_load_dwordx4 v164, s[36:39], s30 offen lds
	s_mov_b32 m0, s59
	ds_read_b128 v[184:187], v171 offset:53248
	buffer_load_dwordx4 v166, s[36:39], s30 offen lds
	ds_read_b128 v[188:191], v171 offset:54272
	ds_read_b128 v[194:197], v171 offset:55296
	ds_read_b128 v[198:201], v171 offset:56320
	s_waitcnt vmcnt(8)
	s_waitcnt lgkmcnt(0)
	s_barrier
	s_setprio 1
	v_mfma_f32_16x16x32_bf16 v[60:63], v[128:131], v[160:163], v[60:63]
	v_mfma_f32_16x16x32_bf16 v[56:59], v[136:139], v[160:163], v[56:59]
	v_mfma_f32_16x16x32_bf16 v[44:47], v[128:131], v[176:179], v[44:47]
	v_mfma_f32_16x16x32_bf16 v[40:43], v[136:139], v[176:179], v[40:43]
	v_mfma_f32_16x16x32_bf16 v[28:31], v[128:131], v[184:187], v[28:31]
	v_mfma_f32_16x16x32_bf16 v[24:27], v[136:139], v[184:187], v[24:27]
	v_mfma_f32_16x16x32_bf16 v[12:15], v[128:131], v[194:197], v[12:15]
	v_mfma_f32_16x16x32_bf16 v[8:11], v[136:139], v[194:197], v[8:11]
	v_mfma_f32_16x16x32_bf16 v[60:63], v[132:135], v[172:175], v[60:63]
	v_mfma_f32_16x16x32_bf16 v[56:59], v[140:143], v[172:175], v[56:59]
	v_mfma_f32_16x16x32_bf16 v[44:47], v[132:135], v[180:183], v[44:47]
	v_mfma_f32_16x16x32_bf16 v[40:43], v[140:143], v[180:183], v[40:43]
	v_mfma_f32_16x16x32_bf16 v[28:31], v[132:135], v[188:191], v[28:31]
	v_mfma_f32_16x16x32_bf16 v[24:27], v[140:143], v[188:191], v[24:27]
	v_mfma_f32_16x16x32_bf16 v[12:15], v[132:135], v[198:201], v[12:15]
	v_mfma_f32_16x16x32_bf16 v[8:11], v[140:143], v[198:201], v[8:11]
	v_mfma_f32_16x16x32_bf16 v[52:55], v[144:147], v[160:163], v[52:55]
	v_mfma_f32_16x16x32_bf16 v[48:51], v[152:155], v[160:163], v[48:51]
	v_mfma_f32_16x16x32_bf16 v[36:39], v[144:147], v[176:179], v[36:39]
	v_mfma_f32_16x16x32_bf16 v[32:35], v[152:155], v[176:179], v[32:35]
	v_mfma_f32_16x16x32_bf16 v[20:23], v[144:147], v[184:187], v[20:23]
	v_mfma_f32_16x16x32_bf16 v[16:19], v[152:155], v[184:187], v[16:19]
	v_mfma_f32_16x16x32_bf16 v[4:7], v[144:147], v[194:197], v[4:7]
	v_mfma_f32_16x16x32_bf16 v[0:3], v[152:155], v[194:197], v[0:3]
	v_mfma_f32_16x16x32_bf16 v[52:55], v[148:151], v[172:175], v[52:55]
	v_mfma_f32_16x16x32_bf16 v[48:51], v[156:159], v[172:175], v[48:51]
	v_mfma_f32_16x16x32_bf16 v[36:39], v[148:151], v[180:183], v[36:39]
	v_mfma_f32_16x16x32_bf16 v[32:35], v[156:159], v[180:183], v[32:35]
	v_mfma_f32_16x16x32_bf16 v[20:23], v[148:151], v[188:191], v[20:23]
	v_mfma_f32_16x16x32_bf16 v[16:19], v[156:159], v[188:191], v[16:19]
	v_mfma_f32_16x16x32_bf16 v[4:7], v[148:151], v[198:201], v[4:7]
	v_mfma_f32_16x16x32_bf16 v[0:3], v[156:159], v[198:201], v[0:3]
	s_setprio 0
	s_barrier
	s_add_i32 s29, s29, 2
	s_addk_i32 s16, 0x100
	s_addk_i32 s28, 0x100
	s_cmp_ge_i32 s29, s82
	s_cbranch_scc0 .LBB0_352

; __device__ __forceinline__ int opaque_s(int x) { asm volatile("" : "+s"(x)); return x; }
; #define PG8_STAGE(bufoff, rs_, soff_, voff) do { _Pragma("unroll") for (int _i = 0; _i < 2; ++_i) \
;         __builtin_amdgcn_raw_ptr_buffer_load_lds(rs_, (LAS void*)(lds + (bufoff) + ldsw + _i * 8192), 16, (int)(voff)[_i], (int)(soff_), 0, 0); } while (0)
; #define PG8_LDA(dst, b, h) do { _Pragma("unroll") for (int m = 0; m < 4; ++m) dst[m] = PG8_LD2(lds + PG8_SA(b, h) + aoff + m * 2048); } while (0)
; #define PG8_LDB(dst, b, h) do { _Pragma("unroll") for (int n = 0; n < 2; ++n) dst[n] = PG8_LD2(lds + PG8_SB(b, h) + boff + n * 2048); } while (0)
; #define PG8_WAIT_V(n) asm volatile("s_waitcnt vmcnt(" #n ")" ::: "memory")
; #define PG8_WAIT_L(n) asm volatile("s_waitcnt lgkmcnt(" #n ")" ::: "memory")
; #define PG8_BAR __builtin_amdgcn_s_barrier()
; #define PG8_SCHED __builtin_amdgcn_sched_barrier(0)
; #define KWS (kargs()->ws)
; #define REP(id) for (int rep_ = 0; rep_ < ((DUP_ID == (id)) ? DUP_N : 1); ++rep_)
; template <class Epi, class Sched, bool ALIGN_EPI = false, bool SP2 = false, bool FP8 = false>
; __device__ __forceinline__ void gemm_phase(LAS unsigned char* lds, const Gemm g, const Sched& S, const Epi& E, int wbase) {
;     ...
;             if constexpr (SP2) {
;             PG8_LDB(B0, 0, 0); PG8_LDB(B1, 0, 1); PG8_SCHED; PG8_LDA(At, 0, 0); PG8_STAGE(PG8_SA(1, 1), rAc, a1 + hstep, voffA);
;             PG8_WAIT_V(8); PG8_WAIT_L(0); PG8_BAR; PG8_MMA(0, 0, At, B0); PG8_MMA(0, 1, At, B1); PG8_BAR; PG8_SCHED;
;             PG8_LDA(At, 0, 1); PG8_STAGE(PG8_SB(0, 0), rB2, b2, voffB); PG8_STAGE(PG8_SB(0, 1), rB2, b2 + hstep, voffB); PG8_STAGE(PG8_SA(0, 0), rA2, a2, voffA);
;             PG8_WAIT_V(8); PG8_WAIT_L(0); PG8_BAR; PG8_MMA(1, 0, At, B0); PG8_MMA(1, 1, At, B1); PG8_BAR; PG8_SCHED;
; __global__ void __launch_bounds__(512, 2) mega(Ptrs Pdummy) {
;     ...
;         REP(3) { unsigned char* ws = KWS; pg8::Gemm g{(const bf16*)(ws + WS_PB), (const bf16*)(ws + WS_WPP) + (size_t)l * DM * PLE, PLE, 0}; pg8::StaticOrder S; S.init(M, DM, opaque_s(G), opaque_s(c));
;           pg8::EpiStore16 E{(bf16*)(ws + WS_PP), DM, 1.f}; pg8::gemm_phase<pg8::EpiStore16, pg8::StaticOrder, true, true>(lds, g, S, E, wbase); }
.LBB0_448:
	s_lshl_b32 s48, s47, 17
	s_andn2_b64 vcc, exec, s[10:11]
	s_lshl_b32 s52, s46, 17
	s_cbranch_vccnz .LBB0_456
	s_and_b64 s[6:7], s[16:17], exec
	s_waitcnt vmcnt(37)
	s_waitcnt vmcnt(36)
	s_waitcnt vmcnt(35)
	s_waitcnt vmcnt(32)
	s_waitcnt vmcnt(31)
	s_waitcnt vmcnt(28)
	s_waitcnt vmcnt(27)
	s_waitcnt vmcnt(24)
	s_waitcnt vmcnt(23)
	s_waitcnt vmcnt(22)
	s_cselect_b32 s56, s48, s55
	s_cselect_b32 s57, s52, s54
	s_add_i32 s58, s55, 0x80
	s_add_i32 s59, s54, 0x100
	s_mov_b32 s60, 0
	v_add_u32_e32 v148, 0x10000, v138
	v_add_u32_e32 v164, 0x14000, v138
	ds_read_b128 v[128:131], v148
	ds_read_b128 v[140:143], v148 offset:1024
	ds_read_b128 v[144:147], v148 offset:2048
	ds_read_b128 v[148:151], v148 offset:3072
	ds_read_b128 v[152:155], v164
	ds_read_b128 v[156:159], v164 offset:1024
	ds_read_b128 v[160:163], v164 offset:2048
	ds_read_b128 v[164:167], v164 offset:3072
	s_add_i32 s6, s58, 0x80
	s_cmp_eq_u32 s42, s60
	s_cselect_b32 s61, s56, s6
	s_cselect_b32 s55, s57, s59
	s_or_b32 s54, s61, 0x80
	s_add_i32 s6, s19, s58
	s_mov_b32 m0, s43
	ds_read_b128 v[168:171], v139
	ds_read_b128 v[172:175], v139 offset:1024
	ds_read_b128 v[176:179], v139 offset:2048
	ds_read_b128 v[180:183], v139 offset:3072
	ds_read_b128 v[184:187], v139 offset:4096
	ds_read_b128 v[188:191], v139 offset:5120
	ds_read_b128 v[194:197], v139 offset:6144
	ds_read_b128 v[198:201], v139 offset:7168
	buffer_load_dwordx4 v132, s[36:39], s6 offen lds
	s_mov_b32 m0, s44
	s_nop 0
	buffer_load_dwordx4 v134, s[36:39], s6 offen lds
	s_waitcnt vmcnt(8)
	s_waitcnt lgkmcnt(0)
	s_barrier
	s_setprio 1
	v_mfma_f32_16x16x32_bf16 v[124:127], v[128:131], v[168:171], 0
	v_mfma_f32_16x16x32_bf16 v[120:123], v[144:147], v[168:171], 0
	v_mfma_f32_16x16x32_bf16 v[108:111], v[128:131], v[176:179], 0
	v_mfma_f32_16x16x32_bf16 v[104:107], v[144:147], v[176:179], 0
	v_mfma_f32_16x16x32_bf16 v[92:95], v[128:131], v[184:187], 0
	v_mfma_f32_16x16x32_bf16 v[88:91], v[144:147], v[184:187], 0
	v_mfma_f32_16x16x32_bf16 v[76:79], v[128:131], v[194:197], 0
	v_mfma_f32_16x16x32_bf16 v[72:75], v[144:147], v[194:197], 0
	v_mfma_f32_16x16x32_bf16 v[124:127], v[140:143], v[172:175], v[124:127]
	v_mfma_f32_16x16x32_bf16 v[120:123], v[148:151], v[172:175], v[120:123]
	v_mfma_f32_16x16x32_bf16 v[108:111], v[140:143], v[180:183], v[108:111]
	v_mfma_f32_16x16x32_bf16 v[104:107], v[148:151], v[180:183], v[104:107]
	v_mfma_f32_16x16x32_bf16 v[92:95], v[140:143], v[188:191], v[92:95]
	v_mfma_f32_16x16x32_bf16 v[88:91], v[148:151], v[188:191], v[88:91]
	v_mfma_f32_16x16x32_bf16 v[76:79], v[140:143], v[198:201], v[76:79]
	v_mfma_f32_16x16x32_bf16 v[72:75], v[148:151], v[198:201], v[72:75]
	v_mfma_f32_16x16x32_bf16 v[116:119], v[152:155], v[168:171], 0
	v_mfma_f32_16x16x32_bf16 v[112:115], v[160:163], v[168:171], 0
	v_mfma_f32_16x16x32_bf16 v[100:103], v[152:155], v[176:179], 0
	v_mfma_f32_16x16x32_bf16 v[96:99], v[160:163], v[176:179], 0
	v_mfma_f32_16x16x32_bf16 v[84:87], v[152:155], v[184:187], 0
	v_mfma_f32_16x16x32_bf16 v[80:83], v[160:163], v[184:187], 0
	v_mfma_f32_16x16x32_bf16 v[68:71], v[152:155], v[194:197], 0
	v_mfma_f32_16x16x32_bf16 v[64:67], v[160:163], v[194:197], 0
	v_mfma_f32_16x16x32_bf16 v[116:119], v[156:159], v[172:175], v[116:119]
	v_mfma_f32_16x16x32_bf16 v[112:115], v[164:167], v[172:175], v[112:115]
	v_mfma_f32_16x16x32_bf16 v[100:103], v[156:159], v[180:183], v[100:103]
	v_mfma_f32_16x16x32_bf16 v[96:99], v[164:167], v[180:183], v[96:99]
	v_mfma_f32_16x16x32_bf16 v[84:87], v[156:159], v[188:191], v[84:87]
	v_mfma_f32_16x16x32_bf16 v[80:83], v[164:167], v[188:191], v[80:83]
	v_mfma_f32_16x16x32_bf16 v[68:71], v[156:159], v[198:201], v[68:71]
	v_mfma_f32_16x16x32_bf16 v[64:67], v[164:167], v[198:201], v[64:67]
	s_setprio 0
	s_barrier
	s_mov_b32 m0, s21
	s_mov_b32 s6, s38
	s_mov_b32 s7, s39
	buffer_load_dwordx4 v133, s[4:7], s55 offen lds
	s_mov_b32 m0, s22
	ds_read_b128 v[168:171], v139 offset:16384
	s_add_i32 s62, s55, s19
	buffer_load_dwordx4 v135, s[4:7], s55 offen lds
	s_mov_b32 m0, s23
	ds_read_b128 v[172:175], v139 offset:17408
	buffer_load_dwordx4 v133, s[4:7], s62 offen lds
	s_mov_b32 m0, s20
	ds_read_b128 v[176:179], v139 offset:18432
	buffer_load_dwordx4 v132, s[36:39], s61 offen lds
	s_mov_b32 m0, s25
	ds_read_b128 v[180:183], v139 offset:19456
	buffer_load_dwordx4 v134, s[36:39], s61 offen lds
	ds_read_b128 v[184:187], v139 offset:20480
	ds_read_b128 v[188:191], v139 offset:21504
	ds_read_b128 v[194:197], v139 offset:22528
	ds_read_b128 v[198:201], v139 offset:23552
	s_waitcnt vmcnt(7)
	s_waitcnt lgkmcnt(0)
	s_barrier
	s_setprio 1
	v_mfma_f32_16x16x32_bf16 v[60:63], v[128:131], v[168:171], 0
	v_mfma_f32_16x16x32_bf16 v[56:59], v[144:147], v[168:171], 0
	v_mfma_f32_16x16x32_bf16 v[44:47], v[128:131], v[176:179], 0
	v_mfma_f32_16x16x32_bf16 v[40:43], v[144:147], v[176:179], 0
	v_mfma_f32_16x16x32_bf16 v[28:31], v[128:131], v[184:187], 0
	v_mfma_f32_16x16x32_bf16 v[24:27], v[144:147], v[184:187], 0
	v_mfma_f32_16x16x32_bf16 v[12:15], v[128:131], v[194:197], 0
	v_mfma_f32_16x16x32_bf16 v[8:11], v[144:147], v[194:197], 0
	v_mfma_f32_16x16x32_bf16 v[60:63], v[140:143], v[172:175], v[60:63]
	v_mfma_f32_16x16x32_bf16 v[56:59], v[148:151], v[172:175], v[56:59]
	v_mfma_f32_16x16x32_bf16 v[44:47], v[140:143], v[180:183], v[44:47]
	v_mfma_f32_16x16x32_bf16 v[40:43], v[148:151], v[180:183], v[40:43]
	v_mfma_f32_16x16x32_bf16 v[28:31], v[140:143], v[188:191], v[28:31]
	v_mfma_f32_16x16x32_bf16 v[24:27], v[148:151], v[188:191], v[24:27]
	v_mfma_f32_16x16x32_bf16 v[12:15], v[140:143], v[198:201], v[12:15]
	v_mfma_f32_16x16x32_bf16 v[8:11], v[148:151], v[198:201], v[8:11]
	v_mfma_f32_16x16x32_bf16 v[52:55], v[152:155], v[168:171], 0
	v_mfma_f32_16x16x32_bf16 v[48:51], v[160:163], v[168:171], 0
	v_mfma_f32_16x16x32_bf16 v[36:39], v[152:155], v[176:179], 0
	v_mfma_f32_16x16x32_bf16 v[32:35], v[160:163], v[176:179], 0
	v_mfma_f32_16x16x32_bf16 v[20:23], v[152:155], v[184:187], 0
	v_mfma_f32_16x16x32_bf16 v[16:19], v[160:163], v[184:187], 0
	v_mfma_f32_16x16x32_bf16 v[4:7], v[152:155], v[194:197], 0
	v_mfma_f32_16x16x32_bf16 v[0:3], v[160:163], v[194:197], 0
	v_mfma_f32_16x16x32_bf16 v[52:55], v[156:159], v[172:175], v[52:55]
	v_mfma_f32_16x16x32_bf16 v[48:51], v[164:167], v[172:175], v[48:51]
	v_mfma_f32_16x16x32_bf16 v[36:39], v[156:159], v[180:183], v[36:39]
	v_mfma_f32_16x16x32_bf16 v[32:35], v[164:167], v[180:183], v[32:35]
	v_mfma_f32_16x16x32_bf16 v[20:23], v[156:159], v[188:191], v[20:23]
	v_mfma_f32_16x16x32_bf16 v[16:19], v[164:167], v[188:191], v[16:19]
	v_mfma_f32_16x16x32_bf16 v[4:7], v[156:159], v[198:201], v[4:7]
	v_mfma_f32_16x16x32_bf16 v[0:3], v[164:167], v[198:201], v[0:3]
	s_setprio 0
	s_barrier
; #define PG8_STAGE(bufoff, rs_, soff_, voff) do { _Pragma("unroll") for (int _i = 0; _i < 2; ++_i) \
;         __builtin_amdgcn_raw_ptr_buffer_load_lds(rs_, (LAS void*)(lds + (bufoff) + ldsw + _i * 8192), 16, (int)(voff)[_i], (int)(soff_), 0, 0); } while (0)
; #define PG8_LDA(dst, b, h) do { _Pragma("unroll") for (int m = 0; m < 4; ++m) dst[m] = PG8_LD2(lds + PG8_SA(b, h) + aoff + m * 2048); } while (0)
; #define PG8_LDB(dst, b, h) do { _Pragma("unroll") for (int n = 0; n < 2; ++n) dst[n] = PG8_LD2(lds + PG8_SB(b, h) + boff + n * 2048); } while (0)
; #define PG8_WAIT_V(n) asm volatile("s_waitcnt vmcnt(" #n ")" ::: "memory")
; #define PG8_WAIT_L(n) asm volatile("s_waitcnt lgkmcnt(" #n ")" ::: "memory")
; #define PG8_BAR __builtin_amdgcn_s_barrier()
; #define PG8_SCHED __builtin_amdgcn_sched_barrier(0)
; template <class Epi, class Sched, bool ALIGN_EPI = false, bool SP2 = false, bool FP8 = false>
; __device__ __forceinline__ void gemm_phase(LAS unsigned char* lds, const Gemm g, const Sched& S, const Epi& E, int wbase) {
;     ...
;         for (int t = 0; t < nt; t += 2) {
;     ...
;             PG8_LDB(B0, 1, 0); PG8_LDB(B1, 1, 1); PG8_SCHED; PG8_LDA(At, 1, 0); PG8_STAGE(PG8_SA(0, 1), rA2, a2 + hstep, voffA);
;             PG8_WAIT_V(8); PG8_WAIT_L(0); PG8_BAR; PG8_MMA(0, 0, At, B0); PG8_MMA(0, 1, At, B1); PG8_BAR; PG8_SCHED;
;             PG8_LDA(At, 1, 1); PG8_STAGE(PG8_SB(1, 0), rB2, b3, voffB); PG8_STAGE(PG8_SB(1, 1), rB2, b3 + hstep, voffB); PG8_STAGE(PG8_SA(1, 0), rA2, a3, voffA);
;             PG8_WAIT_V(8); PG8_WAIT_L(0); PG8_BAR; PG8_MMA(1, 0, At, B0); PG8_MMA(1, 1, At, B1); PG8_BAR; PG8_SCHED;
	s_mov_b32 m0, s24
	s_nop 0
	buffer_load_dwordx4 v135, s[4:7], s62 offen lds
	v_add_u32_e32 v148, 0x18000, v138
	v_add_u32_e32 v164, 0x1c000, v138
	ds_read_b128 v[128:131], v148
	ds_read_b128 v[140:143], v148 offset:1024
	ds_read_b128 v[144:147], v148 offset:2048
	ds_read_b128 v[148:151], v148 offset:3072
	ds_read_b128 v[152:155], v164
	ds_read_b128 v[156:159], v164 offset:1024
	ds_read_b128 v[160:163], v164 offset:2048
	ds_read_b128 v[164:167], v164 offset:3072
	s_add_i32 s61, s61, s19
	s_mov_b32 m0, s26
	ds_read_b128 v[168:171], v139 offset:32768
	ds_read_b128 v[172:175], v139 offset:33792
	ds_read_b128 v[176:179], v139 offset:34816
	ds_read_b128 v[180:183], v139 offset:35840
	ds_read_b128 v[184:187], v139 offset:36864
	ds_read_b128 v[188:191], v139 offset:37888
	ds_read_b128 v[194:197], v139 offset:38912
	ds_read_b128 v[198:201], v139 offset:39936
	buffer_load_dwordx4 v132, s[36:39], s61 offen lds
	s_mov_b32 m0, s27
	s_nop 0
	buffer_load_dwordx4 v134, s[36:39], s61 offen lds
	s_waitcnt vmcnt(8)
	s_waitcnt lgkmcnt(0)
	s_barrier
	s_setprio 1
	v_mfma_f32_16x16x32_bf16 v[124:127], v[128:131], v[168:171], v[124:127]
	v_mfma_f32_16x16x32_bf16 v[120:123], v[144:147], v[168:171], v[120:123]
	v_mfma_f32_16x16x32_bf16 v[108:111], v[128:131], v[176:179], v[108:111]
	v_mfma_f32_16x16x32_bf16 v[104:107], v[144:147], v[176:179], v[104:107]
	v_mfma_f32_16x16x32_bf16 v[92:95], v[128:131], v[184:187], v[92:95]
	v_mfma_f32_16x16x32_bf16 v[88:91], v[144:147], v[184:187], v[88:91]
	v_mfma_f32_16x16x32_bf16 v[76:79], v[128:131], v[194:197], v[76:79]
	v_mfma_f32_16x16x32_bf16 v[72:75], v[144:147], v[194:197], v[72:75]
	v_mfma_f32_16x16x32_bf16 v[124:127], v[140:143], v[172:175], v[124:127]
	v_mfma_f32_16x16x32_bf16 v[120:123], v[148:151], v[172:175], v[120:123]
	v_mfma_f32_16x16x32_bf16 v[108:111], v[140:143], v[180:183], v[108:111]
	v_mfma_f32_16x16x32_bf16 v[104:107], v[148:151], v[180:183], v[104:107]
	v_mfma_f32_16x16x32_bf16 v[92:95], v[140:143], v[188:191], v[92:95]
	v_mfma_f32_16x16x32_bf16 v[88:91], v[148:151], v[188:191], v[88:91]
	v_mfma_f32_16x16x32_bf16 v[76:79], v[140:143], v[198:201], v[76:79]
	v_mfma_f32_16x16x32_bf16 v[72:75], v[148:151], v[198:201], v[72:75]
	v_mfma_f32_16x16x32_bf16 v[116:119], v[152:155], v[168:171], v[116:119]
	v_mfma_f32_16x16x32_bf16 v[112:115], v[160:163], v[168:171], v[112:115]
	v_mfma_f32_16x16x32_bf16 v[100:103], v[152:155], v[176:179], v[100:103]
	v_mfma_f32_16x16x32_bf16 v[96:99], v[160:163], v[176:179], v[96:99]
	v_mfma_f32_16x16x32_bf16 v[84:87], v[152:155], v[184:187], v[84:87]
	v_mfma_f32_16x16x32_bf16 v[80:83], v[160:163], v[184:187], v[80:83]
	v_mfma_f32_16x16x32_bf16 v[68:71], v[152:155], v[194:197], v[68:71]
	v_mfma_f32_16x16x32_bf16 v[64:67], v[160:163], v[194:197], v[64:67]
	v_mfma_f32_16x16x32_bf16 v[116:119], v[156:159], v[172:175], v[116:119]
	v_mfma_f32_16x16x32_bf16 v[112:115], v[164:167], v[172:175], v[112:115]
	v_mfma_f32_16x16x32_bf16 v[100:103], v[156:159], v[180:183], v[100:103]
	v_mfma_f32_16x16x32_bf16 v[96:99], v[164:167], v[180:183], v[96:99]
	v_mfma_f32_16x16x32_bf16 v[84:87], v[156:159], v[188:191], v[84:87]
	v_mfma_f32_16x16x32_bf16 v[80:83], v[164:167], v[188:191], v[80:83]
	v_mfma_f32_16x16x32_bf16 v[68:71], v[156:159], v[198:201], v[68:71]
	v_mfma_f32_16x16x32_bf16 v[64:67], v[164:167], v[198:201], v[64:67]
	s_setprio 0
	s_barrier
	s_mov_b32 m0, s28
	s_bitset1_b32 s55, 7
	buffer_load_dwordx4 v133, s[4:7], s55 offen lds
	s_mov_b32 m0, s29
	ds_read_b128 v[168:171], v139 offset:49152
	buffer_load_dwordx4 v135, s[4:7], s55 offen lds
	s_add_i32 s55, s55, s19
	s_mov_b32 m0, s33
	ds_read_b128 v[172:175], v139 offset:50176
	buffer_load_dwordx4 v133, s[4:7], s55 offen lds
	s_mov_b32 m0, s34
	ds_read_b128 v[176:179], v139 offset:51200
	buffer_load_dwordx4 v135, s[4:7], s55 offen lds
	s_mov_b32 m0, s30
	ds_read_b128 v[180:183], v139 offset:52224
	buffer_load_dwordx4 v132, s[36:39], s54 offen lds
	s_mov_b32 m0, s31
	ds_read_b128 v[184:187], v139 offset:53248
	buffer_load_dwordx4 v134, s[36:39], s54 offen lds
	ds_read_b128 v[188:191], v139 offset:54272
	ds_read_b128 v[194:197], v139 offset:55296
	ds_read_b128 v[198:201], v139 offset:56320
	s_waitcnt vmcnt(8)
	s_waitcnt lgkmcnt(0)
	s_barrier
	s_setprio 1
	v_mfma_f32_16x16x32_bf16 v[60:63], v[128:131], v[168:171], v[60:63]
	v_mfma_f32_16x16x32_bf16 v[56:59], v[144:147], v[168:171], v[56:59]
	v_mfma_f32_16x16x32_bf16 v[44:47], v[128:131], v[176:179], v[44:47]
	v_mfma_f32_16x16x32_bf16 v[40:43], v[144:147], v[176:179], v[40:43]
	v_mfma_f32_16x16x32_bf16 v[28:31], v[128:131], v[184:187], v[28:31]
	v_mfma_f32_16x16x32_bf16 v[24:27], v[144:147], v[184:187], v[24:27]
	v_mfma_f32_16x16x32_bf16 v[12:15], v[128:131], v[194:197], v[12:15]
	v_mfma_f32_16x16x32_bf16 v[8:11], v[144:147], v[194:197], v[8:11]
	v_mfma_f32_16x16x32_bf16 v[60:63], v[140:143], v[172:175], v[60:63]
	v_mfma_f32_16x16x32_bf16 v[56:59], v[148:151], v[172:175], v[56:59]
	v_mfma_f32_16x16x32_bf16 v[44:47], v[140:143], v[180:183], v[44:47]
	v_mfma_f32_16x16x32_bf16 v[40:43], v[148:151], v[180:183], v[40:43]
	v_mfma_f32_16x16x32_bf16 v[28:31], v[140:143], v[188:191], v[28:31]
	v_mfma_f32_16x16x32_bf16 v[24:27], v[148:151], v[188:191], v[24:27]
	v_mfma_f32_16x16x32_bf16 v[12:15], v[140:143], v[198:201], v[12:15]
	v_mfma_f32_16x16x32_bf16 v[8:11], v[148:151], v[198:201], v[8:11]
	v_mfma_f32_16x16x32_bf16 v[52:55], v[152:155], v[168:171], v[52:55]
	v_mfma_f32_16x16x32_bf16 v[48:51], v[160:163], v[168:171], v[48:51]
	v_mfma_f32_16x16x32_bf16 v[36:39], v[152:155], v[176:179], v[36:39]
	v_mfma_f32_16x16x32_bf16 v[32:35], v[160:163], v[176:179], v[32:35]
	v_mfma_f32_16x16x32_bf16 v[20:23], v[152:155], v[184:187], v[20:23]
	v_mfma_f32_16x16x32_bf16 v[16:19], v[160:163], v[184:187], v[16:19]
	v_mfma_f32_16x16x32_bf16 v[4:7], v[152:155], v[194:197], v[4:7]
	v_mfma_f32_16x16x32_bf16 v[0:3], v[160:163], v[194:197], v[0:3]
	v_mfma_f32_16x16x32_bf16 v[52:55], v[156:159], v[172:175], v[52:55]
	v_mfma_f32_16x16x32_bf16 v[48:51], v[164:167], v[172:175], v[48:51]
	v_mfma_f32_16x16x32_bf16 v[36:39], v[156:159], v[180:183], v[36:39]
	v_mfma_f32_16x16x32_bf16 v[32:35], v[164:167], v[180:183], v[32:35]
	v_mfma_f32_16x16x32_bf16 v[20:23], v[156:159], v[188:191], v[20:23]
	v_mfma_f32_16x16x32_bf16 v[16:19], v[164:167], v[188:191], v[16:19]
	v_mfma_f32_16x16x32_bf16 v[4:7], v[156:159], v[198:201], v[4:7]
	v_mfma_f32_16x16x32_bf16 v[0:3], v[164:167], v[198:201], v[0:3]
	s_setprio 0
	s_barrier
	s_add_i32 s60, s60, 2
	s_addk_i32 s58, 0x100
	s_addk_i32 s59, 0x100
	s_cmp_ge_i32 s60, s35
	s_cbranch_scc0 .LBB0_450
	s_branch .Lzp_after_450
; #define PG8_STAGE(bufoff, rs_, soff_, voff) do { _Pragma("unroll") for (int _i = 0; _i < 2; ++_i) \
;         __builtin_amdgcn_raw_ptr_buffer_load_lds(rs_, (LAS void*)(lds + (bufoff) + ldsw + _i * 8192), 16, (int)(voff)[_i], (int)(soff_), 0, 0); } while (0)
; #define PG8_LDA(dst, b, h) do { _Pragma("unroll") for (int m = 0; m < 4; ++m) dst[m] = PG8_LD2(lds + PG8_SA(b, h) + aoff + m * 2048); } while (0)
; #define PG8_LDB(dst, b, h) do { _Pragma("unroll") for (int n = 0; n < 2; ++n) dst[n] = PG8_LD2(lds + PG8_SB(b, h) + boff + n * 2048); } while (0)
; #define PG8_WAIT_V(n) asm volatile("s_waitcnt vmcnt(" #n ")" ::: "memory")
; #define PG8_WAIT_L(n) asm volatile("s_waitcnt lgkmcnt(" #n ")" ::: "memory")
; #define PG8_BAR __builtin_amdgcn_s_barrier()
; #define PG8_SCHED __builtin_amdgcn_sched_barrier(0)
; template <class Epi, class Sched, bool ALIGN_EPI = false, bool SP2 = false, bool FP8 = false>
; __device__ __forceinline__ void gemm_phase(LAS unsigned char* lds, const Gemm g, const Sched& S, const Epi& E, int wbase) {
;     ...
;             if constexpr (SP2) {
;             PG8_LDB(B0, 0, 0); PG8_LDB(B1, 0, 1); PG8_SCHED; PG8_LDA(At, 0, 0); PG8_STAGE(PG8_SA(1, 1), rAc, a1 + hstep, voffA);
;             PG8_WAIT_V(8); PG8_WAIT_L(0); PG8_BAR; PG8_MMA(0, 0, At, B0); PG8_MMA(0, 1, At, B1); PG8_BAR; PG8_SCHED;
;             PG8_LDA(At, 0, 1); PG8_STAGE(PG8_SB(0, 0), rB2, b2, voffB); PG8_STAGE(PG8_SB(0, 1), rB2, b2 + hstep, voffB); PG8_STAGE(PG8_SA(0, 0), rA2, a2, voffA);
;             PG8_WAIT_V(8); PG8_WAIT_L(0); PG8_BAR; PG8_MMA(1, 0, At, B0); PG8_MMA(1, 1, At, B1); PG8_BAR; PG8_SCHED;
.LBB0_450:
	v_add_u32_e32 v148, 0x10000, v138
	v_add_u32_e32 v164, 0x14000, v138
	ds_read_b128 v[128:131], v148
	ds_read_b128 v[140:143], v148 offset:1024
	ds_read_b128 v[144:147], v148 offset:2048
	ds_read_b128 v[148:151], v148 offset:3072
	ds_read_b128 v[152:155], v164
	ds_read_b128 v[156:159], v164 offset:1024
	ds_read_b128 v[160:163], v164 offset:2048
	ds_read_b128 v[164:167], v164 offset:3072
	s_add_i32 s6, s58, 0x80
	s_cmp_eq_u32 s42, s60
	s_cselect_b32 s61, s56, s6
	s_cselect_b32 s55, s57, s59
	s_or_b32 s54, s61, 0x80
	s_add_i32 s6, s19, s58
	s_mov_b32 m0, s43
	ds_read_b128 v[168:171], v139
	ds_read_b128 v[172:175], v139 offset:1024
	ds_read_b128 v[176:179], v139 offset:2048
	ds_read_b128 v[180:183], v139 offset:3072
	ds_read_b128 v[184:187], v139 offset:4096
	ds_read_b128 v[188:191], v139 offset:5120
	ds_read_b128 v[194:197], v139 offset:6144
	ds_read_b128 v[198:201], v139 offset:7168
	buffer_load_dwordx4 v132, s[36:39], s6 offen lds
	s_mov_b32 m0, s44
	s_nop 0
	buffer_load_dwordx4 v134, s[36:39], s6 offen lds
	s_waitcnt vmcnt(8)
	s_waitcnt lgkmcnt(0)
	s_barrier
	s_setprio 1
	v_mfma_f32_16x16x32_bf16 v[124:127], v[128:131], v[168:171], v[124:127]
	v_mfma_f32_16x16x32_bf16 v[120:123], v[144:147], v[168:171], v[120:123]
	v_mfma_f32_16x16x32_bf16 v[108:111], v[128:131], v[176:179], v[108:111]
	v_mfma_f32_16x16x32_bf16 v[104:107], v[144:147], v[176:179], v[104:107]
	v_mfma_f32_16x16x32_bf16 v[92:95], v[128:131], v[184:187], v[92:95]
	v_mfma_f32_16x16x32_bf16 v[88:91], v[144:147], v[184:187], v[88:91]
	v_mfma_f32_16x16x32_bf16 v[76:79], v[128:131], v[194:197], v[76:79]
	v_mfma_f32_16x16x32_bf16 v[72:75], v[144:147], v[194:197], v[72:75]
	v_mfma_f32_16x16x32_bf16 v[124:127], v[140:143], v[172:175], v[124:127]
	v_mfma_f32_16x16x32_bf16 v[120:123], v[148:151], v[172:175], v[120:123]
	v_mfma_f32_16x16x32_bf16 v[108:111], v[140:143], v[180:183], v[108:111]
	v_mfma_f32_16x16x32_bf16 v[104:107], v[148:151], v[180:183], v[104:107]
	v_mfma_f32_16x16x32_bf16 v[92:95], v[140:143], v[188:191], v[92:95]
	v_mfma_f32_16x16x32_bf16 v[88:91], v[148:151], v[188:191], v[88:91]
	v_mfma_f32_16x16x32_bf16 v[76:79], v[140:143], v[198:201], v[76:79]
	v_mfma_f32_16x16x32_bf16 v[72:75], v[148:151], v[198:201], v[72:75]
	v_mfma_f32_16x16x32_bf16 v[116:119], v[152:155], v[168:171], v[116:119]
	v_mfma_f32_16x16x32_bf16 v[112:115], v[160:163], v[168:171], v[112:115]
	v_mfma_f32_16x16x32_bf16 v[100:103], v[152:155], v[176:179], v[100:103]
	v_mfma_f32_16x16x32_bf16 v[96:99], v[160:163], v[176:179], v[96:99]
	v_mfma_f32_16x16x32_bf16 v[84:87], v[152:155], v[184:187], v[84:87]
	v_mfma_f32_16x16x32_bf16 v[80:83], v[160:163], v[184:187], v[80:83]
	v_mfma_f32_16x16x32_bf16 v[68:71], v[152:155], v[194:197], v[68:71]
	v_mfma_f32_16x16x32_bf16 v[64:67], v[160:163], v[194:197], v[64:67]
	v_mfma_f32_16x16x32_bf16 v[116:119], v[156:159], v[172:175], v[116:119]
	v_mfma_f32_16x16x32_bf16 v[112:115], v[164:167], v[172:175], v[112:115]
	v_mfma_f32_16x16x32_bf16 v[100:103], v[156:159], v[180:183], v[100:103]
	v_mfma_f32_16x16x32_bf16 v[96:99], v[164:167], v[180:183], v[96:99]
	v_mfma_f32_16x16x32_bf16 v[84:87], v[156:159], v[188:191], v[84:87]
	v_mfma_f32_16x16x32_bf16 v[80:83], v[164:167], v[188:191], v[80:83]
	v_mfma_f32_16x16x32_bf16 v[68:71], v[156:159], v[198:201], v[68:71]
	v_mfma_f32_16x16x32_bf16 v[64:67], v[164:167], v[198:201], v[64:67]
	s_setprio 0
	s_barrier
	s_mov_b32 m0, s21
	s_mov_b32 s6, s38
	s_mov_b32 s7, s39
	buffer_load_dwordx4 v133, s[4:7], s55 offen lds
	s_mov_b32 m0, s22
	ds_read_b128 v[168:171], v139 offset:16384
	s_add_i32 s62, s55, s19
	buffer_load_dwordx4 v135, s[4:7], s55 offen lds
	s_mov_b32 m0, s23
	ds_read_b128 v[172:175], v139 offset:17408
	buffer_load_dwordx4 v133, s[4:7], s62 offen lds
	s_mov_b32 m0, s20
	ds_read_b128 v[176:179], v139 offset:18432
	buffer_load_dwordx4 v132, s[36:39], s61 offen lds
	s_mov_b32 m0, s25
	ds_read_b128 v[180:183], v139 offset:19456
	buffer_load_dwordx4 v134, s[36:39], s61 offen lds
	ds_read_b128 v[184:187], v139 offset:20480
	ds_read_b128 v[188:191], v139 offset:21504
	ds_read_b128 v[194:197], v139 offset:22528
	ds_read_b128 v[198:201], v139 offset:23552
	s_waitcnt vmcnt(7)
	s_waitcnt lgkmcnt(0)
	s_barrier
	s_setprio 1
	v_mfma_f32_16x16x32_bf16 v[60:63], v[128:131], v[168:171], v[60:63]
	v_mfma_f32_16x16x32_bf16 v[56:59], v[144:147], v[168:171], v[56:59]
	v_mfma_f32_16x16x32_bf16 v[44:47], v[128:131], v[176:179], v[44:47]
	v_mfma_f32_16x16x32_bf16 v[40:43], v[144:147], v[176:179], v[40:43]
	v_mfma_f32_16x16x32_bf16 v[28:31], v[128:131], v[184:187], v[28:31]
	v_mfma_f32_16x16x32_bf16 v[24:27], v[144:147], v[184:187], v[24:27]
	v_mfma_f32_16x16x32_bf16 v[12:15], v[128:131], v[194:197], v[12:15]
	v_mfma_f32_16x16x32_bf16 v[8:11], v[144:147], v[194:197], v[8:11]
	v_mfma_f32_16x16x32_bf16 v[60:63], v[140:143], v[172:175], v[60:63]
	v_mfma_f32_16x16x32_bf16 v[56:59], v[148:151], v[172:175], v[56:59]
	v_mfma_f32_16x16x32_bf16 v[44:47], v[140:143], v[180:183], v[44:47]
	v_mfma_f32_16x16x32_bf16 v[40:43], v[148:151], v[180:183], v[40:43]
	v_mfma_f32_16x16x32_bf16 v[28:31], v[140:143], v[188:191], v[28:31]
	v_mfma_f32_16x16x32_bf16 v[24:27], v[148:151], v[188:191], v[24:27]
	v_mfma_f32_16x16x32_bf16 v[12:15], v[140:143], v[198:201], v[12:15]
	v_mfma_f32_16x16x32_bf16 v[8:11], v[148:151], v[198:201], v[8:11]
	v_mfma_f32_16x16x32_bf16 v[52:55], v[152:155], v[168:171], v[52:55]
	v_mfma_f32_16x16x32_bf16 v[48:51], v[160:163], v[168:171], v[48:51]
	v_mfma_f32_16x16x32_bf16 v[36:39], v[152:155], v[176:179], v[36:39]
	v_mfma_f32_16x16x32_bf16 v[32:35], v[160:163], v[176:179], v[32:35]
	v_mfma_f32_16x16x32_bf16 v[20:23], v[152:155], v[184:187], v[20:23]
	v_mfma_f32_16x16x32_bf16 v[16:19], v[160:163], v[184:187], v[16:19]
	v_mfma_f32_16x16x32_bf16 v[4:7], v[152:155], v[194:197], v[4:7]
	v_mfma_f32_16x16x32_bf16 v[0:3], v[160:163], v[194:197], v[0:3]
	v_mfma_f32_16x16x32_bf16 v[52:55], v[156:159], v[172:175], v[52:55]
	v_mfma_f32_16x16x32_bf16 v[48:51], v[164:167], v[172:175], v[48:51]
	v_mfma_f32_16x16x32_bf16 v[36:39], v[156:159], v[180:183], v[36:39]
	v_mfma_f32_16x16x32_bf16 v[32:35], v[164:167], v[180:183], v[32:35]
	v_mfma_f32_16x16x32_bf16 v[20:23], v[156:159], v[188:191], v[20:23]
	v_mfma_f32_16x16x32_bf16 v[16:19], v[164:167], v[188:191], v[16:19]
	v_mfma_f32_16x16x32_bf16 v[4:7], v[156:159], v[198:201], v[4:7]
	v_mfma_f32_16x16x32_bf16 v[0:3], v[164:167], v[198:201], v[0:3]
	s_setprio 0
	s_barrier
; #define PG8_STAGE(bufoff, rs_, soff_, voff) do { _Pragma("unroll") for (int _i = 0; _i < 2; ++_i) \
;         __builtin_amdgcn_raw_ptr_buffer_load_lds(rs_, (LAS void*)(lds + (bufoff) + ldsw + _i * 8192), 16, (int)(voff)[_i], (int)(soff_), 0, 0); } while (0)
; #define PG8_LDA(dst, b, h) do { _Pragma("unroll") for (int m = 0; m < 4; ++m) dst[m] = PG8_LD2(lds + PG8_SA(b, h) + aoff + m * 2048); } while (0)
; #define PG8_LDB(dst, b, h) do { _Pragma("unroll") for (int n = 0; n < 2; ++n) dst[n] = PG8_LD2(lds + PG8_SB(b, h) + boff + n * 2048); } while (0)
; #define PG8_WAIT_V(n) asm volatile("s_waitcnt vmcnt(" #n ")" ::: "memory")
; #define PG8_WAIT_L(n) asm volatile("s_waitcnt lgkmcnt(" #n ")" ::: "memory")
; #define PG8_BAR __builtin_amdgcn_s_barrier()
; #define PG8_SCHED __builtin_amdgcn_sched_barrier(0)
; template <class Epi, class Sched, bool ALIGN_EPI = false, bool SP2 = false, bool FP8 = false>
; __device__ __forceinline__ void gemm_phase(LAS unsigned char* lds, const Gemm g, const Sched& S, const Epi& E, int wbase) {
;     ...
;             PG8_LDB(B0, 1, 0); PG8_LDB(B1, 1, 1); PG8_SCHED; PG8_LDA(At, 1, 0); PG8_STAGE(PG8_SA(0, 1), rA2, a2 + hstep, voffA);
;             PG8_WAIT_V(8); PG8_WAIT_L(0); PG8_BAR; PG8_MMA(0, 0, At, B0); PG8_MMA(0, 1, At, B1); PG8_BAR; PG8_SCHED;
;             PG8_LDA(At, 1, 1); PG8_STAGE(PG8_SB(1, 0), rB2, b3, voffB); PG8_STAGE(PG8_SB(1, 1), rB2, b3 + hstep, voffB); PG8_STAGE(PG8_SA(1, 0), rA2, a3, voffA);
;             PG8_WAIT_V(8); PG8_WAIT_L(0); PG8_BAR; PG8_MMA(1, 0, At, B0); PG8_MMA(1, 1, At, B1); PG8_BAR; PG8_SCHED;
	s_mov_b32 m0, s24
	s_nop 0
	buffer_load_dwordx4 v135, s[4:7], s62 offen lds
	v_add_u32_e32 v148, 0x18000, v138
	v_add_u32_e32 v164, 0x1c000, v138
	ds_read_b128 v[128:131], v148
	ds_read_b128 v[140:143], v148 offset:1024
	ds_read_b128 v[144:147], v148 offset:2048
	ds_read_b128 v[148:151], v148 offset:3072
	ds_read_b128 v[152:155], v164
	ds_read_b128 v[156:159], v164 offset:1024
	ds_read_b128 v[160:163], v164 offset:2048
	ds_read_b128 v[164:167], v164 offset:3072
	s_add_i32 s61, s61, s19
	s_mov_b32 m0, s26
	ds_read_b128 v[168:171], v139 offset:32768
	ds_read_b128 v[172:175], v139 offset:33792
	ds_read_b128 v[176:179], v139 offset:34816
	ds_read_b128 v[180:183], v139 offset:35840
	ds_read_b128 v[184:187], v139 offset:36864
	ds_read_b128 v[188:191], v139 offset:37888
	ds_read_b128 v[194:197], v139 offset:38912
	ds_read_b128 v[198:201], v139 offset:39936
	buffer_load_dwordx4 v132, s[36:39], s61 offen lds
	s_mov_b32 m0, s27
	s_nop 0
	buffer_load_dwordx4 v134, s[36:39], s61 offen lds
	s_waitcnt vmcnt(8)
	s_waitcnt lgkmcnt(0)
	s_barrier
	s_setprio 1
	v_mfma_f32_16x16x32_bf16 v[124:127], v[128:131], v[168:171], v[124:127]
	v_mfma_f32_16x16x32_bf16 v[120:123], v[144:147], v[168:171], v[120:123]
	v_mfma_f32_16x16x32_bf16 v[108:111], v[128:131], v[176:179], v[108:111]
	v_mfma_f32_16x16x32_bf16 v[104:107], v[144:147], v[176:179], v[104:107]
	v_mfma_f32_16x16x32_bf16 v[92:95], v[128:131], v[184:187], v[92:95]
	v_mfma_f32_16x16x32_bf16 v[88:91], v[144:147], v[184:187], v[88:91]
	v_mfma_f32_16x16x32_bf16 v[76:79], v[128:131], v[194:197], v[76:79]
	v_mfma_f32_16x16x32_bf16 v[72:75], v[144:147], v[194:197], v[72:75]
	v_mfma_f32_16x16x32_bf16 v[124:127], v[140:143], v[172:175], v[124:127]
	v_mfma_f32_16x16x32_bf16 v[120:123], v[148:151], v[172:175], v[120:123]
	v_mfma_f32_16x16x32_bf16 v[108:111], v[140:143], v[180:183], v[108:111]
	v_mfma_f32_16x16x32_bf16 v[104:107], v[148:151], v[180:183], v[104:107]
	v_mfma_f32_16x16x32_bf16 v[92:95], v[140:143], v[188:191], v[92:95]
	v_mfma_f32_16x16x32_bf16 v[88:91], v[148:151], v[188:191], v[88:91]
	v_mfma_f32_16x16x32_bf16 v[76:79], v[140:143], v[198:201], v[76:79]
	v_mfma_f32_16x16x32_bf16 v[72:75], v[148:151], v[198:201], v[72:75]
	v_mfma_f32_16x16x32_bf16 v[116:119], v[152:155], v[168:171], v[116:119]
	v_mfma_f32_16x16x32_bf16 v[112:115], v[160:163], v[168:171], v[112:115]
	v_mfma_f32_16x16x32_bf16 v[100:103], v[152:155], v[176:179], v[100:103]
	v_mfma_f32_16x16x32_bf16 v[96:99], v[160:163], v[176:179], v[96:99]
	v_mfma_f32_16x16x32_bf16 v[84:87], v[152:155], v[184:187], v[84:87]
	v_mfma_f32_16x16x32_bf16 v[80:83], v[160:163], v[184:187], v[80:83]
	v_mfma_f32_16x16x32_bf16 v[68:71], v[152:155], v[194:197], v[68:71]
	v_mfma_f32_16x16x32_bf16 v[64:67], v[160:163], v[194:197], v[64:67]
	v_mfma_f32_16x16x32_bf16 v[116:119], v[156:159], v[172:175], v[116:119]
	v_mfma_f32_16x16x32_bf16 v[112:115], v[164:167], v[172:175], v[112:115]
	v_mfma_f32_16x16x32_bf16 v[100:103], v[156:159], v[180:183], v[100:103]
	v_mfma_f32_16x16x32_bf16 v[96:99], v[164:167], v[180:183], v[96:99]
	v_mfma_f32_16x16x32_bf16 v[84:87], v[156:159], v[188:191], v[84:87]
	v_mfma_f32_16x16x32_bf16 v[80:83], v[164:167], v[188:191], v[80:83]
	v_mfma_f32_16x16x32_bf16 v[68:71], v[156:159], v[198:201], v[68:71]
	v_mfma_f32_16x16x32_bf16 v[64:67], v[164:167], v[198:201], v[64:67]
	s_setprio 0
	s_barrier
	s_mov_b32 m0, s28
	s_bitset1_b32 s55, 7
	buffer_load_dwordx4 v133, s[4:7], s55 offen lds
	s_mov_b32 m0, s29
	ds_read_b128 v[168:171], v139 offset:49152
	buffer_load_dwordx4 v135, s[4:7], s55 offen lds
	s_add_i32 s55, s55, s19
	s_mov_b32 m0, s33
	ds_read_b128 v[172:175], v139 offset:50176
	buffer_load_dwordx4 v133, s[4:7], s55 offen lds
	s_mov_b32 m0, s34
	ds_read_b128 v[176:179], v139 offset:51200
	buffer_load_dwordx4 v135, s[4:7], s55 offen lds
	s_mov_b32 m0, s30
	ds_read_b128 v[180:183], v139 offset:52224
	buffer_load_dwordx4 v132, s[36:39], s54 offen lds
	s_mov_b32 m0, s31
	ds_read_b128 v[184:187], v139 offset:53248
	buffer_load_dwordx4 v134, s[36:39], s54 offen lds
	ds_read_b128 v[188:191], v139 offset:54272
	ds_read_b128 v[194:197], v139 offset:55296
	ds_read_b128 v[198:201], v139 offset:56320
	s_waitcnt vmcnt(8)
	s_waitcnt lgkmcnt(0)
	s_barrier
	s_setprio 1
	v_mfma_f32_16x16x32_bf16 v[60:63], v[128:131], v[168:171], v[60:63]
	v_mfma_f32_16x16x32_bf16 v[56:59], v[144:147], v[168:171], v[56:59]
	v_mfma_f32_16x16x32_bf16 v[44:47], v[128:131], v[176:179], v[44:47]
	v_mfma_f32_16x16x32_bf16 v[40:43], v[144:147], v[176:179], v[40:43]
	v_mfma_f32_16x16x32_bf16 v[28:31], v[128:131], v[184:187], v[28:31]
	v_mfma_f32_16x16x32_bf16 v[24:27], v[144:147], v[184:187], v[24:27]
	v_mfma_f32_16x16x32_bf16 v[12:15], v[128:131], v[194:197], v[12:15]
	v_mfma_f32_16x16x32_bf16 v[8:11], v[144:147], v[194:197], v[8:11]
	v_mfma_f32_16x16x32_bf16 v[60:63], v[140:143], v[172:175], v[60:63]
	v_mfma_f32_16x16x32_bf16 v[56:59], v[148:151], v[172:175], v[56:59]
	v_mfma_f32_16x16x32_bf16 v[44:47], v[140:143], v[180:183], v[44:47]
	v_mfma_f32_16x16x32_bf16 v[40:43], v[148:151], v[180:183], v[40:43]
	v_mfma_f32_16x16x32_bf16 v[28:31], v[140:143], v[188:191], v[28:31]
	v_mfma_f32_16x16x32_bf16 v[24:27], v[148:151], v[188:191], v[24:27]
	v_mfma_f32_16x16x32_bf16 v[12:15], v[140:143], v[198:201], v[12:15]
	v_mfma_f32_16x16x32_bf16 v[8:11], v[148:151], v[198:201], v[8:11]
	v_mfma_f32_16x16x32_bf16 v[52:55], v[152:155], v[168:171], v[52:55]
	v_mfma_f32_16x16x32_bf16 v[48:51], v[160:163], v[168:171], v[48:51]
	v_mfma_f32_16x16x32_bf16 v[36:39], v[152:155], v[176:179], v[36:39]
	v_mfma_f32_16x16x32_bf16 v[32:35], v[160:163], v[176:179], v[32:35]
	v_mfma_f32_16x16x32_bf16 v[20:23], v[152:155], v[184:187], v[20:23]
	v_mfma_f32_16x16x32_bf16 v[16:19], v[160:163], v[184:187], v[16:19]
	v_mfma_f32_16x16x32_bf16 v[4:7], v[152:155], v[194:197], v[4:7]
	v_mfma_f32_16x16x32_bf16 v[0:3], v[160:163], v[194:197], v[0:3]
	v_mfma_f32_16x16x32_bf16 v[52:55], v[156:159], v[172:175], v[52:55]
	v_mfma_f32_16x16x32_bf16 v[48:51], v[164:167], v[172:175], v[48:51]
	v_mfma_f32_16x16x32_bf16 v[36:39], v[156:159], v[180:183], v[36:39]
	v_mfma_f32_16x16x32_bf16 v[32:35], v[164:167], v[180:183], v[32:35]
	v_mfma_f32_16x16x32_bf16 v[20:23], v[156:159], v[188:191], v[20:23]
	v_mfma_f32_16x16x32_bf16 v[16:19], v[164:167], v[188:191], v[16:19]
	v_mfma_f32_16x16x32_bf16 v[4:7], v[156:159], v[198:201], v[4:7]
	v_mfma_f32_16x16x32_bf16 v[0:3], v[164:167], v[198:201], v[0:3]
	s_setprio 0
	s_barrier
	s_add_i32 s60, s60, 2
	s_addk_i32 s58, 0x100
	s_addk_i32 s59, 0x100
	s_cmp_ge_i32 s60, s35
	s_cbranch_scc0 .LBB0_450

; #define PG8_STAGE(bufoff, rs_, soff_, voff) do { _Pragma("unroll") for (int _i = 0; _i < 2; ++_i) \
;         __builtin_amdgcn_raw_ptr_buffer_load_lds(rs_, (LAS void*)(lds + (bufoff) + ldsw + _i * 8192), 16, (int)(voff)[_i], (int)(soff_), 0, 0); } while (0)
; #define PG8_LDA(dst, b, h) do { _Pragma("unroll") for (int m = 0; m < 4; ++m) dst[m] = PG8_LD2(lds + PG8_SA(b, h) + aoff + m * 2048); } while (0)
; #define PG8_LDB(dst, b, h) do { _Pragma("unroll") for (int n = 0; n < 2; ++n) dst[n] = PG8_LD2(lds + PG8_SB(b, h) + boff + n * 2048); } while (0)
; #define PG8_WAIT_V(n) asm volatile("s_waitcnt vmcnt(" #n ")" ::: "memory")
; #define PG8_WAIT_L(n) asm volatile("s_waitcnt lgkmcnt(" #n ")" ::: "memory")
; #define PG8_BAR __builtin_amdgcn_s_barrier()
; #define PG8_SCHED __builtin_amdgcn_sched_barrier(0)
; template <class Epi, class Sched, bool ALIGN_EPI = false, bool SP2 = false, bool FP8 = false>
; __device__ __forceinline__ void gemm_phase(LAS unsigned char* lds, const Gemm g, const Sched& S, const Epi& E, int wbase) {
;     ...
;             const unsigned a1 = cA + (unsigned)(t + 1) * kstep;
;             const unsigned a2 = last ? nA : cA + (unsigned)(t + 2) * kstep, b2 = last ? nB : cB + (unsigned)(t + 2) * kstep; const rsrc_t rA2 = (Sched::TWO && last) ? rAn : rAc, rB2 = (Sched::TWO && last) ? rBn : rBc;
;             const unsigned a3 = a2 + kstep, b3 = b2 + kstep;
;             if (last && has_next) S.a_ready(nxt);
;             if constexpr (SP2) {
;             PG8_LDB(B0, 0, 0); PG8_LDB(B1, 0, 1); PG8_SCHED; PG8_LDA(At, 0, 0); PG8_STAGE(PG8_SA(1, 1), rAc, a1 + hstep, voffA);
;             PG8_WAIT_V(8); PG8_WAIT_L(0); PG8_BAR; PG8_MMA(0, 0, At, B0); PG8_MMA(0, 1, At, B1); PG8_BAR; PG8_SCHED;
;             PG8_LDA(At, 0, 1); PG8_STAGE(PG8_SB(0, 0), rB2, b2, voffB); PG8_STAGE(PG8_SB(0, 1), rB2, b2 + hstep, voffB); PG8_STAGE(PG8_SA(0, 0), rA2, a2, voffA);
;             PG8_WAIT_V(8); PG8_WAIT_L(0); PG8_BAR; PG8_MMA(1, 0, At, B0); PG8_MMA(1, 1, At, B1); PG8_BAR; PG8_SCHED;
.LBB0_813:
	s_add_i32 s20, vcc_hi, 0x80
	v_add_u32_e32 v140, 0x10000, v240
	v_add_u32_e32 v156, 0x14000, v240
	s_cmp_eq_u32 s41, s78
	ds_read_b128 v[128:131], v140
	ds_read_b128 v[132:135], v140 offset:1024
	ds_read_b128 v[136:139], v140 offset:2048
	ds_read_b128 v[140:143], v140 offset:3072
	ds_read_b128 v[144:147], v156
	ds_read_b128 v[148:151], v156 offset:1024
	ds_read_b128 v[152:155], v156 offset:2048
	ds_read_b128 v[156:159], v156 offset:3072
	s_cselect_b64 s[16:17], -1, 0
	s_and_b64 s[18:19], s[16:17], exec
	s_cselect_b32 s68, s67, s20
	s_cselect_b32 s54, vcc_lo, s3
	s_and_b64 s[20:21], s[44:45], s[16:17]
	s_and_b64 s[16:17], s[20:21], exec
	s_cselect_b32 s18, s52, s14
	s_cselect_b32 s19, s53, s15
	s_cselect_b32 s17, s35, s13
	s_cselect_b32 s16, s34, s12
	s_or_b32 s55, s68, 0x80
	s_and_b64 s[20:21], s[20:21], exec
	s_cselect_b32 s23, s53, s31
	s_cselect_b32 s22, s52, s30
	s_cselect_b32 s21, s11, s59
	s_cselect_b32 s20, s10, s58
	s_add_i32 s69, s46, vcc_hi
	s_mov_b32 m0, s61
	ds_read_b128 v[160:163], v241
	ds_read_b128 v[164:167], v241 offset:1024
	ds_read_b128 v[168:171], v241 offset:2048
	ds_read_b128 v[172:175], v241 offset:3072
	ds_read_b128 v[176:179], v241 offset:4096
	ds_read_b128 v[180:183], v241 offset:5120
	ds_read_b128 v[184:187], v241 offset:6144
	ds_read_b128 v[188:191], v241 offset:7168
	buffer_load_dwordx4 v192, s[12:15], s69 offen lds
	s_mov_b32 m0, s62
	s_nop 0
	buffer_load_dwordx4 v236, s[12:15], s69 offen lds
	s_waitcnt vmcnt(8)
	s_waitcnt lgkmcnt(0)
	s_barrier
	s_setprio 1
	v_mfma_f32_16x16x128_f8f6f4 v[124:127], v[128:135], v[160:167], v[124:127]
	v_mfma_f32_16x16x128_f8f6f4 v[120:123], v[136:143], v[160:167], v[120:123]
	v_mfma_f32_16x16x128_f8f6f4 v[116:119], v[128:135], v[168:175], v[116:119]
	v_mfma_f32_16x16x128_f8f6f4 v[112:115], v[136:143], v[168:175], v[112:115]
	v_mfma_f32_16x16x128_f8f6f4 v[108:111], v[128:135], v[176:183], v[108:111]
	v_mfma_f32_16x16x128_f8f6f4 v[104:107], v[136:143], v[176:183], v[104:107]
	v_mfma_f32_16x16x128_f8f6f4 v[100:103], v[128:135], v[184:191], v[100:103]
	v_mfma_f32_16x16x128_f8f6f4 v[96:99], v[136:143], v[184:191], v[96:99]
	v_mfma_f32_16x16x128_f8f6f4 v[194:197], v[144:151], v[160:167], v[92:95]
	v_mfma_f32_16x16x128_f8f6f4 v[160:163], v[152:159], v[160:167], v[88:91]
	v_mfma_f32_16x16x128_f8f6f4 v[164:167], v[144:151], v[168:175], v[84:87]
	v_mfma_f32_16x16x128_f8f6f4 v[168:171], v[152:159], v[168:175], v[80:83]
	v_mfma_f32_16x16x128_f8f6f4 v[172:175], v[144:151], v[176:183], v[76:79]
	v_mfma_f32_16x16x128_f8f6f4 v[176:179], v[152:159], v[176:183], v[72:75]
	v_mfma_f32_16x16x128_f8f6f4 v[180:183], v[144:151], v[184:191], v[68:71]
	v_mfma_f32_16x16x128_f8f6f4 v[184:187], v[152:159], v[184:191], v[64:67]
	s_setprio 0
	s_barrier
	s_mov_b32 m0, s48
	s_nop 3
	buffer_load_dwordx4 v235, s[20:23], s54 offen lds
	s_mov_b32 m0, s56
	ds_read_b128 v[64:67], v241 offset:16384
	s_add_i32 s69, s54, s46
	buffer_load_dwordx4 v237, s[20:23], s54 offen lds
	s_mov_b32 m0, s57
	ds_read_b128 v[68:71], v241 offset:17408
	buffer_load_dwordx4 v235, s[20:23], s69 offen lds
	s_mov_b32 m0, s47
	ds_read_b128 v[72:75], v241 offset:18432
	buffer_load_dwordx4 v192, s[16:19], s68 offen lds
	s_mov_b32 m0, s76
	ds_read_b128 v[76:79], v241 offset:19456
	buffer_load_dwordx4 v236, s[16:19], s68 offen lds
	ds_read_b128 v[80:83], v241 offset:20480
	ds_read_b128 v[84:87], v241 offset:21504
	ds_read_b128 v[88:91], v241 offset:22528
	ds_read_b128 v[92:95], v241 offset:23552
	s_waitcnt vmcnt(7)
	s_waitcnt lgkmcnt(0)
	s_barrier
	s_setprio 1
	v_mfma_f32_16x16x128_f8f6f4 v[60:63], v[128:135], v[64:71], v[60:63]
	v_mfma_f32_16x16x128_f8f6f4 v[56:59], v[136:143], v[64:71], v[56:59]
	v_mfma_f32_16x16x128_f8f6f4 v[52:55], v[128:135], v[72:79], v[52:55]
	v_mfma_f32_16x16x128_f8f6f4 v[48:51], v[136:143], v[72:79], v[48:51]
	v_mfma_f32_16x16x128_f8f6f4 v[188:191], v[128:135], v[80:87], v[44:47]
	v_mfma_f32_16x16x128_f8f6f4 v[198:201], v[136:143], v[80:87], v[40:43]
	v_mfma_f32_16x16x128_f8f6f4 v[202:205], v[128:135], v[88:95], v[36:39]
	v_mfma_f32_16x16x128_f8f6f4 v[206:209], v[136:143], v[88:95], v[32:35]
	v_mfma_f32_16x16x128_f8f6f4 v[210:213], v[144:151], v[64:71], v[28:31]
	v_mfma_f32_16x16x128_f8f6f4 v[214:217], v[152:159], v[64:71], v[24:27]
	v_mfma_f32_16x16x128_f8f6f4 v[218:221], v[144:151], v[72:79], v[20:23]
	v_mfma_f32_16x16x128_f8f6f4 v[226:229], v[152:159], v[72:79], v[16:19]
	v_mfma_f32_16x16x128_f8f6f4 v[242:245], v[144:151], v[80:87], v[12:15]
	v_mfma_f32_16x16x128_f8f6f4 v[246:249], v[152:159], v[80:87], v[8:11]
	v_mfma_f32_16x16x128_f8f6f4 v[250:253], v[144:151], v[88:95], v[4:7]
	v_mfma_f32_16x16x128_f8f6f4 v[230:233], v[152:159], v[88:95], v[0:3]
	s_setprio 0
	s_barrier
; #define PG8_STAGE(bufoff, rs_, soff_, voff) do { _Pragma("unroll") for (int _i = 0; _i < 2; ++_i) \
;         __builtin_amdgcn_raw_ptr_buffer_load_lds(rs_, (LAS void*)(lds + (bufoff) + ldsw + _i * 8192), 16, (int)(voff)[_i], (int)(soff_), 0, 0); } while (0)
; #define PG8_LDA(dst, b, h) do { _Pragma("unroll") for (int m = 0; m < 4; ++m) dst[m] = PG8_LD2(lds + PG8_SA(b, h) + aoff + m * 2048); } while (0)
; #define PG8_LDB(dst, b, h) do { _Pragma("unroll") for (int n = 0; n < 2; ++n) dst[n] = PG8_LD2(lds + PG8_SB(b, h) + boff + n * 2048); } while (0)
; #define PG8_WAIT_V(n) asm volatile("s_waitcnt vmcnt(" #n ")" ::: "memory")
; #define PG8_WAIT_L(n) asm volatile("s_waitcnt lgkmcnt(" #n ")" ::: "memory")
; #define PG8_BAR __builtin_amdgcn_s_barrier()
; #define PG8_SCHED __builtin_amdgcn_sched_barrier(0)
; template <class Epi, class Sched, bool ALIGN_EPI = false, bool SP2 = false, bool FP8 = false>
; __device__ __forceinline__ void gemm_phase(LAS unsigned char* lds, const Gemm g, const Sched& S, const Epi& E, int wbase) {
;     ...
;             PG8_LDB(B0, 1, 0); PG8_LDB(B1, 1, 1); PG8_SCHED; PG8_LDA(At, 1, 0); PG8_STAGE(PG8_SA(0, 1), rA2, a2 + hstep, voffA);
;             PG8_WAIT_V(8); PG8_WAIT_L(0); PG8_BAR; PG8_MMA(0, 0, At, B0); PG8_MMA(0, 1, At, B1); PG8_BAR; PG8_SCHED;
;             PG8_LDA(At, 1, 1); PG8_STAGE(PG8_SB(1, 0), rB2, b3, voffB); PG8_STAGE(PG8_SB(1, 1), rB2, b3 + hstep, voffB); PG8_STAGE(PG8_SA(1, 0), rA2, a3, voffA);
;             PG8_WAIT_V(8); PG8_WAIT_L(0); PG8_BAR; PG8_MMA(1, 0, At, B0); PG8_MMA(1, 1, At, B1); PG8_BAR; PG8_SCHED;
	s_mov_b32 m0, s65
	s_nop 0
	buffer_load_dwordx4 v237, s[20:23], s69 offen lds
	s_nop 1
	v_add_u32_e32 v12, 0x18000, v240
	v_add_u32_e32 v16, 0x1c000, v240
	s_nop 0
	ds_read_b128 v[0:3], v12
	ds_read_b128 v[4:7], v12 offset:1024
	ds_read_b128 v[8:11], v12 offset:2048
	ds_read_b128 v[12:15], v12 offset:3072
	ds_read_b128 v[128:131], v16
	ds_read_b128 v[132:135], v16 offset:1024
	ds_read_b128 v[136:139], v16 offset:2048
	ds_read_b128 v[140:143], v16 offset:3072
	s_add_i32 s68, s68, s46
	s_mov_b32 m0, s77
	ds_read_b128 v[16:19], v241 offset:32768
	ds_read_b128 v[20:23], v241 offset:33792
	ds_read_b128 v[24:27], v241 offset:34816
	ds_read_b128 v[28:31], v241 offset:35840
	ds_read_b128 v[32:35], v241 offset:36864
	ds_read_b128 v[36:39], v241 offset:37888
	ds_read_b128 v[40:43], v241 offset:38912
	ds_read_b128 v[44:47], v241 offset:39936
	buffer_load_dwordx4 v192, s[16:19], s68 offen lds
	s_mov_b32 m0, s79
	s_nop 0
	buffer_load_dwordx4 v236, s[16:19], s68 offen lds
	s_waitcnt vmcnt(8)
	s_waitcnt lgkmcnt(0)
	s_barrier
	s_setprio 1
	v_mfma_f32_16x16x128_f8f6f4 v[124:127], v[0:7], v[16:23], v[124:127]
	v_mfma_f32_16x16x128_f8f6f4 v[120:123], v[8:15], v[16:23], v[120:123]
	v_mfma_f32_16x16x128_f8f6f4 v[116:119], v[0:7], v[24:31], v[116:119]
	v_mfma_f32_16x16x128_f8f6f4 v[112:115], v[8:15], v[24:31], v[112:115]
	v_mfma_f32_16x16x128_f8f6f4 v[108:111], v[0:7], v[32:39], v[108:111]
	v_mfma_f32_16x16x128_f8f6f4 v[104:107], v[8:15], v[32:39], v[104:107]
	v_mfma_f32_16x16x128_f8f6f4 v[100:103], v[0:7], v[40:47], v[100:103]
	v_mfma_f32_16x16x128_f8f6f4 v[96:99], v[8:15], v[40:47], v[96:99]
	v_mfma_f32_16x16x128_f8f6f4 v[92:95], v[128:135], v[16:23], v[194:197]
	v_mfma_f32_16x16x128_f8f6f4 v[88:91], v[136:143], v[16:23], v[160:163]
	v_mfma_f32_16x16x128_f8f6f4 v[84:87], v[128:135], v[24:31], v[164:167]
	v_mfma_f32_16x16x128_f8f6f4 v[80:83], v[136:143], v[24:31], v[168:171]
	v_mfma_f32_16x16x128_f8f6f4 v[76:79], v[128:135], v[32:39], v[172:175]
	v_mfma_f32_16x16x128_f8f6f4 v[72:75], v[136:143], v[32:39], v[176:179]
	v_mfma_f32_16x16x128_f8f6f4 v[68:71], v[128:135], v[40:47], v[180:183]
	v_mfma_f32_16x16x128_f8f6f4 v[64:67], v[136:143], v[40:47], v[184:187]
	s_setprio 0
	s_barrier
	s_mov_b32 m0, s84
	s_bitset1_b32 s54, 7
	buffer_load_dwordx4 v235, s[20:23], s54 offen lds
	s_mov_b32 m0, s85
	ds_read_b128 v[16:19], v241 offset:49152
	buffer_load_dwordx4 v237, s[20:23], s54 offen lds
	s_add_i32 s54, s54, s46
	s_mov_b32 m0, s96
	ds_read_b128 v[20:23], v241 offset:50176
	buffer_load_dwordx4 v235, s[20:23], s54 offen lds
	s_mov_b32 m0, s97
	ds_read_b128 v[144:147], v241 offset:51200
	buffer_load_dwordx4 v237, s[20:23], s54 offen lds
	s_mov_b32 m0, s94
	ds_read_b128 v[148:151], v241 offset:52224
	buffer_load_dwordx4 v192, s[16:19], s55 offen lds
	s_mov_b32 m0, s95
	ds_read_b128 v[152:155], v241 offset:53248
	buffer_load_dwordx4 v236, s[16:19], s55 offen lds
	ds_read_b128 v[156:159], v241 offset:54272
	ds_read_b128 v[160:163], v241 offset:55296
	ds_read_b128 v[164:167], v241 offset:56320
	s_waitcnt vmcnt(8)
	s_waitcnt lgkmcnt(0)
	s_barrier
	s_setprio 1
	v_mfma_f32_16x16x128_f8f6f4 v[60:63], v[0:7], v[16:23], v[60:63]
	v_mfma_f32_16x16x128_f8f6f4 v[56:59], v[8:15], v[16:23], v[56:59]
	v_mfma_f32_16x16x128_f8f6f4 v[52:55], v[0:7], v[144:151], v[52:55]
	v_mfma_f32_16x16x128_f8f6f4 v[48:51], v[8:15], v[144:151], v[48:51]
	v_mfma_f32_16x16x128_f8f6f4 v[44:47], v[0:7], v[152:159], v[188:191]
	v_mfma_f32_16x16x128_f8f6f4 v[40:43], v[8:15], v[152:159], v[198:201]
	v_mfma_f32_16x16x128_f8f6f4 v[36:39], v[0:7], v[160:167], v[202:205]
	v_mfma_f32_16x16x128_f8f6f4 v[32:35], v[8:15], v[160:167], v[206:209]
	v_mfma_f32_16x16x128_f8f6f4 v[28:31], v[128:135], v[16:23], v[210:213]
	v_mfma_f32_16x16x128_f8f6f4 v[24:27], v[136:143], v[16:23], v[214:217]
	v_mfma_f32_16x16x128_f8f6f4 v[20:23], v[128:135], v[144:151], v[218:221]
	v_mfma_f32_16x16x128_f8f6f4 v[16:19], v[136:143], v[144:151], v[226:229]
	v_mfma_f32_16x16x128_f8f6f4 v[12:15], v[128:135], v[152:159], v[242:245]
	v_mfma_f32_16x16x128_f8f6f4 v[8:11], v[136:143], v[152:159], v[246:249]
	v_mfma_f32_16x16x128_f8f6f4 v[4:7], v[128:135], v[160:167], v[250:253]
	v_mfma_f32_16x16x128_f8f6f4 v[0:3], v[136:143], v[160:167], v[230:233]
	s_setprio 0
	s_barrier
	s_add_i32 s78, s78, 2
	s_addk_i32 vcc_hi, 0x100
	s_addk_i32 s3, 0x100
	s_cmp_ge_i32 s78, s60
	s_cbranch_scc0 .LBB0_813
	v_readlane_b32 s68, v255, 22
	v_readlane_b32 s54, v255, 25
	v_readlane_b32 s69, v255, 23
	v_readlane_b32 s55, v255, 26
	v_mov_b32_e32 v230, v193
	v_mov_b32_e32 v231, v222

; #define PG8_STAGE(bufoff, rs_, soff_, voff) do { _Pragma("unroll") for (int _i = 0; _i < 2; ++_i) \
;         __builtin_amdgcn_raw_ptr_buffer_load_lds(rs_, (LAS void*)(lds + (bufoff) + ldsw + _i * 8192), 16, (int)(voff)[_i], (int)(soff_), 0, 0); } while (0)
; #define PG8_LDA(dst, b, h) do { _Pragma("unroll") for (int m = 0; m < 4; ++m) dst[m] = PG8_LD2(lds + PG8_SA(b, h) + aoff + m * 2048); } while (0)
; #define PG8_LDB(dst, b, h) do { _Pragma("unroll") for (int n = 0; n < 2; ++n) dst[n] = PG8_LD2(lds + PG8_SB(b, h) + boff + n * 2048); } while (0)
; #define PG8_WAIT_V(n) asm volatile("s_waitcnt vmcnt(" #n ")" ::: "memory")
; #define PG8_WAIT_L(n) asm volatile("s_waitcnt lgkmcnt(" #n ")" ::: "memory")
; #define PG8_BAR __builtin_amdgcn_s_barrier()
; #define PG8_SCHED __builtin_amdgcn_sched_barrier(0)
; template <class Epi, class Sched, bool ALIGN_EPI = false, bool SP2 = false, bool FP8 = false>
; __device__ __forceinline__ void gemm_phase(LAS unsigned char* lds, const Gemm g, const Sched& S, const Epi& E, int wbase) {
;     ...
;             const unsigned a1 = cA + (unsigned)(t + 1) * kstep;
;             const unsigned a2 = last ? nA : cA + (unsigned)(t + 2) * kstep, b2 = last ? nB : cB + (unsigned)(t + 2) * kstep; const rsrc_t rA2 = (Sched::TWO && last) ? rAn : rAc, rB2 = (Sched::TWO && last) ? rBn : rBc;
;             const unsigned a3 = a2 + kstep, b3 = b2 + kstep;
;             if (last && has_next) S.a_ready(nxt);
;             if constexpr (SP2) {
;             PG8_LDB(B0, 0, 0); PG8_LDB(B1, 0, 1); PG8_SCHED; PG8_LDA(At, 0, 0); PG8_STAGE(PG8_SA(1, 1), rAc, a1 + hstep, voffA);
;             PG8_WAIT_V(8); PG8_WAIT_L(0); PG8_BAR; PG8_MMA(0, 0, At, B0); PG8_MMA(0, 1, At, B1); PG8_BAR; PG8_SCHED;
;             PG8_LDA(At, 0, 1); PG8_STAGE(PG8_SB(0, 0), rB2, b2, voffB); PG8_STAGE(PG8_SB(0, 1), rB2, b2 + hstep, voffB); PG8_STAGE(PG8_SA(0, 0), rA2, a2, voffA);
;             PG8_WAIT_V(8); PG8_WAIT_L(0); PG8_BAR; PG8_MMA(1, 0, At, B0); PG8_MMA(1, 1, At, B1); PG8_BAR; PG8_SCHED;
.LBB0_847:
	s_add_i32 s20, vcc_lo, 0x80
	v_add_u32_e32 v140, 0x10000, v238
	v_add_u32_e32 v156, 0x14000, v238
	s_cmp_eq_u32 s88, s85
	ds_read_b128 v[128:131], v140
	ds_read_b128 v[132:135], v140 offset:1024
	ds_read_b128 v[136:139], v140 offset:2048
	ds_read_b128 v[140:143], v140 offset:3072
	ds_read_b128 v[144:147], v156
	ds_read_b128 v[148:151], v156 offset:1024
	ds_read_b128 v[152:155], v156 offset:2048
	ds_read_b128 v[156:159], v156 offset:3072
	s_cselect_b64 s[16:17], -1, 0
	s_and_b64 s[18:19], s[16:17], exec
	s_cselect_b32 s68, s67, s20
	s_cselect_b32 s54, s78, vcc_hi
	s_and_b64 s[20:21], s[58:59], s[16:17]
	s_and_b64 s[16:17], s[20:21], exec
	s_cselect_b32 s18, s30, s14
	s_cselect_b32 s19, s31, s15
	s_cselect_b32 s17, s35, s13
	s_cselect_b32 s16, s34, s12
	s_or_b32 s55, s68, 0x80
	s_and_b64 s[20:21], s[20:21], exec
	s_cselect_b32 s23, s31, s53
	s_cselect_b32 s22, s30, s52
	s_cselect_b32 s21, s45, s11
	s_cselect_b32 s20, s44, s10
	s_add_i32 s69, s41, vcc_lo
	s_mov_b32 m0, s89
	ds_read_b128 v[160:163], v239
	ds_read_b128 v[164:167], v239 offset:1024
	ds_read_b128 v[168:171], v239 offset:2048
	ds_read_b128 v[172:175], v239 offset:3072
	ds_read_b128 v[176:179], v239 offset:4096
	ds_read_b128 v[180:183], v239 offset:5120
	ds_read_b128 v[184:187], v239 offset:6144
	ds_read_b128 v[188:191], v239 offset:7168
	buffer_load_dwordx4 v192, s[12:15], s69 offen lds
	s_mov_b32 m0, s92
	s_nop 0
	buffer_load_dwordx4 v223, s[12:15], s69 offen lds
	s_waitcnt vmcnt(8)
	s_waitcnt lgkmcnt(0)
	s_barrier
	s_setprio 1
	v_mfma_f32_16x16x32_bf16 v[124:127], v[128:131], v[160:163], v[124:127]
	v_mfma_f32_16x16x32_bf16 v[120:123], v[136:139], v[160:163], v[120:123]
	v_mfma_f32_16x16x32_bf16 v[116:119], v[128:131], v[168:171], v[116:119]
	v_mfma_f32_16x16x32_bf16 v[112:115], v[136:139], v[168:171], v[112:115]
	v_mfma_f32_16x16x32_bf16 v[108:111], v[128:131], v[176:179], v[108:111]
	v_mfma_f32_16x16x32_bf16 v[104:107], v[136:139], v[176:179], v[104:107]
	v_mfma_f32_16x16x32_bf16 v[100:103], v[128:131], v[184:187], v[100:103]
	v_mfma_f32_16x16x32_bf16 v[96:99], v[136:139], v[184:187], v[96:99]
	v_mfma_f32_16x16x32_bf16 v[124:127], v[132:135], v[164:167], v[124:127]
	v_mfma_f32_16x16x32_bf16 v[120:123], v[140:143], v[164:167], v[120:123]
	v_mfma_f32_16x16x32_bf16 v[116:119], v[132:135], v[172:175], v[116:119]
	v_mfma_f32_16x16x32_bf16 v[112:115], v[140:143], v[172:175], v[112:115]
	v_mfma_f32_16x16x32_bf16 v[108:111], v[132:135], v[180:183], v[108:111]
	v_mfma_f32_16x16x32_bf16 v[104:107], v[140:143], v[180:183], v[104:107]
	v_mfma_f32_16x16x32_bf16 v[100:103], v[132:135], v[188:191], v[100:103]
	v_mfma_f32_16x16x32_bf16 v[96:99], v[140:143], v[188:191], v[96:99]
	v_mfma_f32_16x16x32_bf16 v[92:95], v[144:147], v[160:163], v[92:95]
	v_mfma_f32_16x16x32_bf16 v[88:91], v[152:155], v[160:163], v[88:91]
	v_mfma_f32_16x16x32_bf16 v[84:87], v[144:147], v[168:171], v[84:87]
	v_mfma_f32_16x16x32_bf16 v[80:83], v[152:155], v[168:171], v[80:83]
	v_mfma_f32_16x16x32_bf16 v[76:79], v[144:147], v[176:179], v[76:79]
	v_mfma_f32_16x16x32_bf16 v[72:75], v[152:155], v[176:179], v[72:75]
	v_mfma_f32_16x16x32_bf16 v[68:71], v[144:147], v[184:187], v[68:71]
	v_mfma_f32_16x16x32_bf16 v[64:67], v[152:155], v[184:187], v[64:67]
	v_mfma_f32_16x16x32_bf16 v[92:95], v[148:151], v[164:167], v[92:95]
	v_mfma_f32_16x16x32_bf16 v[88:91], v[156:159], v[164:167], v[88:91]
	v_mfma_f32_16x16x32_bf16 v[84:87], v[148:151], v[172:175], v[84:87]
	v_mfma_f32_16x16x32_bf16 v[80:83], v[156:159], v[172:175], v[80:83]
	v_mfma_f32_16x16x32_bf16 v[76:79], v[148:151], v[180:183], v[76:79]
	v_mfma_f32_16x16x32_bf16 v[72:75], v[156:159], v[180:183], v[72:75]
	v_mfma_f32_16x16x32_bf16 v[68:71], v[148:151], v[188:191], v[68:71]
	v_mfma_f32_16x16x32_bf16 v[64:67], v[156:159], v[188:191], v[64:67]
	s_setprio 0
	s_barrier
	s_mov_b32 m0, s43
	ds_read_b128 v[160:163], v239 offset:16384
	buffer_load_dwordx4 v222, s[20:23], s54 offen lds
	s_mov_b32 m0, s46
	ds_read_b128 v[164:167], v239 offset:17408
	s_add_i32 s69, s54, s41
	buffer_load_dwordx4 v235, s[20:23], s54 offen lds
	s_mov_b32 m0, s47
	ds_read_b128 v[168:171], v239 offset:18432
	buffer_load_dwordx4 v222, s[20:23], s69 offen lds
	s_mov_b32 m0, s42
	ds_read_b128 v[172:175], v239 offset:19456
	buffer_load_dwordx4 v192, s[16:19], s68 offen lds
	s_mov_b32 m0, s56
	ds_read_b128 v[176:179], v239 offset:20480
	buffer_load_dwordx4 v223, s[16:19], s68 offen lds
	ds_read_b128 v[180:183], v239 offset:21504
	ds_read_b128 v[184:187], v239 offset:22528
	ds_read_b128 v[188:191], v239 offset:23552
	s_waitcnt vmcnt(7)
	s_waitcnt lgkmcnt(0)
	s_barrier
; #define PG8_STAGE(bufoff, rs_, soff_, voff) do { _Pragma("unroll") for (int _i = 0; _i < 2; ++_i) \
;         __builtin_amdgcn_raw_ptr_buffer_load_lds(rs_, (LAS void*)(lds + (bufoff) + ldsw + _i * 8192), 16, (int)(voff)[_i], (int)(soff_), 0, 0); } while (0)
; #define PG8_LDA(dst, b, h) do { _Pragma("unroll") for (int m = 0; m < 4; ++m) dst[m] = PG8_LD2(lds + PG8_SA(b, h) + aoff + m * 2048); } while (0)
; #define PG8_LDB(dst, b, h) do { _Pragma("unroll") for (int n = 0; n < 2; ++n) dst[n] = PG8_LD2(lds + PG8_SB(b, h) + boff + n * 2048); } while (0)
; #define PG8_WAIT_V(n) asm volatile("s_waitcnt vmcnt(" #n ")" ::: "memory")
; #define PG8_WAIT_L(n) asm volatile("s_waitcnt lgkmcnt(" #n ")" ::: "memory")
; #define PG8_BAR __builtin_amdgcn_s_barrier()
; #define PG8_SCHED __builtin_amdgcn_sched_barrier(0)
; template <class Epi, class Sched, bool ALIGN_EPI = false, bool SP2 = false, bool FP8 = false>
; __device__ __forceinline__ void gemm_phase(LAS unsigned char* lds, const Gemm g, const Sched& S, const Epi& E, int wbase) {
;     ...
;             PG8_WAIT_V(8); PG8_WAIT_L(0); PG8_BAR; PG8_MMA(1, 0, At, B0); PG8_MMA(1, 1, At, B1); PG8_BAR; PG8_SCHED;
;             PG8_LDB(B0, 1, 0); PG8_LDB(B1, 1, 1); PG8_SCHED; PG8_LDA(At, 1, 0); PG8_STAGE(PG8_SA(0, 1), rA2, a2 + hstep, voffA);
;             PG8_WAIT_V(8); PG8_WAIT_L(0); PG8_BAR; PG8_MMA(0, 0, At, B0); PG8_MMA(0, 1, At, B1); PG8_BAR; PG8_SCHED;
	s_setprio 1
	v_mfma_f32_16x16x32_bf16 v[60:63], v[128:131], v[160:163], v[60:63]
	v_mfma_f32_16x16x32_bf16 v[56:59], v[136:139], v[160:163], v[56:59]
	v_mfma_f32_16x16x32_bf16 v[52:55], v[128:131], v[168:171], v[52:55]
	v_mfma_f32_16x16x32_bf16 v[48:51], v[136:139], v[168:171], v[48:51]
	v_mfma_f32_16x16x32_bf16 v[44:47], v[128:131], v[176:179], v[44:47]
	v_mfma_f32_16x16x32_bf16 v[40:43], v[136:139], v[176:179], v[40:43]
	v_mfma_f32_16x16x32_bf16 v[36:39], v[128:131], v[184:187], v[36:39]
	v_mfma_f32_16x16x32_bf16 v[32:35], v[136:139], v[184:187], v[32:35]
	v_mfma_f32_16x16x32_bf16 v[60:63], v[132:135], v[164:167], v[60:63]
	v_mfma_f32_16x16x32_bf16 v[56:59], v[140:143], v[164:167], v[56:59]
	v_mfma_f32_16x16x32_bf16 v[52:55], v[132:135], v[172:175], v[52:55]
	v_mfma_f32_16x16x32_bf16 v[48:51], v[140:143], v[172:175], v[48:51]
	v_mfma_f32_16x16x32_bf16 v[44:47], v[132:135], v[180:183], v[44:47]
	v_mfma_f32_16x16x32_bf16 v[40:43], v[140:143], v[180:183], v[40:43]
	v_mfma_f32_16x16x32_bf16 v[36:39], v[132:135], v[188:191], v[36:39]
	v_mfma_f32_16x16x32_bf16 v[32:35], v[140:143], v[188:191], v[32:35]
	v_mfma_f32_16x16x32_bf16 v[28:31], v[144:147], v[160:163], v[28:31]
	v_mfma_f32_16x16x32_bf16 v[24:27], v[152:155], v[160:163], v[24:27]
	v_mfma_f32_16x16x32_bf16 v[20:23], v[144:147], v[168:171], v[20:23]
	v_mfma_f32_16x16x32_bf16 v[16:19], v[152:155], v[168:171], v[16:19]
	v_mfma_f32_16x16x32_bf16 v[12:15], v[144:147], v[176:179], v[12:15]
	v_mfma_f32_16x16x32_bf16 v[8:11], v[152:155], v[176:179], v[8:11]
	v_mfma_f32_16x16x32_bf16 v[4:7], v[144:147], v[184:187], v[4:7]
	v_mfma_f32_16x16x32_bf16 v[0:3], v[152:155], v[184:187], v[0:3]
	v_mfma_f32_16x16x32_bf16 v[28:31], v[148:151], v[164:167], v[28:31]
	v_mfma_f32_16x16x32_bf16 v[24:27], v[156:159], v[164:167], v[24:27]
	v_mfma_f32_16x16x32_bf16 v[20:23], v[148:151], v[172:175], v[20:23]
	v_mfma_f32_16x16x32_bf16 v[16:19], v[156:159], v[172:175], v[16:19]
	v_mfma_f32_16x16x32_bf16 v[12:15], v[148:151], v[180:183], v[12:15]
	v_mfma_f32_16x16x32_bf16 v[8:11], v[156:159], v[180:183], v[8:11]
	v_mfma_f32_16x16x32_bf16 v[4:7], v[148:151], v[188:191], v[4:7]
	v_mfma_f32_16x16x32_bf16 v[0:3], v[156:159], v[188:191], v[0:3]
	s_setprio 0
	s_barrier
	s_mov_b32 m0, s48
	s_nop 0
	buffer_load_dwordx4 v235, s[20:23], s69 offen lds
	v_add_u32_e32 v140, 0x18000, v238
	v_add_u32_e32 v156, 0x1c000, v238
	ds_read_b128 v[128:131], v140
	ds_read_b128 v[132:135], v140 offset:1024
	ds_read_b128 v[136:139], v140 offset:2048
	ds_read_b128 v[140:143], v140 offset:3072
	ds_read_b128 v[144:147], v156
	ds_read_b128 v[148:151], v156 offset:1024
	ds_read_b128 v[152:155], v156 offset:2048
	ds_read_b128 v[156:159], v156 offset:3072
	s_add_i32 s68, s68, s41
	s_mov_b32 m0, s57
	ds_read_b128 v[160:163], v239 offset:32768
	ds_read_b128 v[164:167], v239 offset:33792
	ds_read_b128 v[168:171], v239 offset:34816
	ds_read_b128 v[172:175], v239 offset:35840
	ds_read_b128 v[176:179], v239 offset:36864
	ds_read_b128 v[180:183], v239 offset:37888
	ds_read_b128 v[184:187], v239 offset:38912
	ds_read_b128 v[188:191], v239 offset:39936
	buffer_load_dwordx4 v192, s[16:19], s68 offen lds
	s_mov_b32 m0, s60
	s_nop 0
	buffer_load_dwordx4 v223, s[16:19], s68 offen lds
	s_waitcnt vmcnt(8)
	s_waitcnt lgkmcnt(0)
	s_barrier
	s_setprio 1
	v_mfma_f32_16x16x32_bf16 v[124:127], v[128:131], v[160:163], v[124:127]
	v_mfma_f32_16x16x32_bf16 v[120:123], v[136:139], v[160:163], v[120:123]
	v_mfma_f32_16x16x32_bf16 v[116:119], v[128:131], v[168:171], v[116:119]
	v_mfma_f32_16x16x32_bf16 v[112:115], v[136:139], v[168:171], v[112:115]
	v_mfma_f32_16x16x32_bf16 v[108:111], v[128:131], v[176:179], v[108:111]
	v_mfma_f32_16x16x32_bf16 v[104:107], v[136:139], v[176:179], v[104:107]
	v_mfma_f32_16x16x32_bf16 v[100:103], v[128:131], v[184:187], v[100:103]
	v_mfma_f32_16x16x32_bf16 v[96:99], v[136:139], v[184:187], v[96:99]
	v_mfma_f32_16x16x32_bf16 v[124:127], v[132:135], v[164:167], v[124:127]
	v_mfma_f32_16x16x32_bf16 v[120:123], v[140:143], v[164:167], v[120:123]
	v_mfma_f32_16x16x32_bf16 v[116:119], v[132:135], v[172:175], v[116:119]
	v_mfma_f32_16x16x32_bf16 v[112:115], v[140:143], v[172:175], v[112:115]
	v_mfma_f32_16x16x32_bf16 v[108:111], v[132:135], v[180:183], v[108:111]
	v_mfma_f32_16x16x32_bf16 v[104:107], v[140:143], v[180:183], v[104:107]
	v_mfma_f32_16x16x32_bf16 v[100:103], v[132:135], v[188:191], v[100:103]
	v_mfma_f32_16x16x32_bf16 v[96:99], v[140:143], v[188:191], v[96:99]
	v_mfma_f32_16x16x32_bf16 v[92:95], v[144:147], v[160:163], v[92:95]
	v_mfma_f32_16x16x32_bf16 v[88:91], v[152:155], v[160:163], v[88:91]
	v_mfma_f32_16x16x32_bf16 v[84:87], v[144:147], v[168:171], v[84:87]
	v_mfma_f32_16x16x32_bf16 v[80:83], v[152:155], v[168:171], v[80:83]
	v_mfma_f32_16x16x32_bf16 v[76:79], v[144:147], v[176:179], v[76:79]
	v_mfma_f32_16x16x32_bf16 v[72:75], v[152:155], v[176:179], v[72:75]
	v_mfma_f32_16x16x32_bf16 v[68:71], v[144:147], v[184:187], v[68:71]
	v_mfma_f32_16x16x32_bf16 v[64:67], v[152:155], v[184:187], v[64:67]
	v_mfma_f32_16x16x32_bf16 v[92:95], v[148:151], v[164:167], v[92:95]
	v_mfma_f32_16x16x32_bf16 v[88:91], v[156:159], v[164:167], v[88:91]
	v_mfma_f32_16x16x32_bf16 v[84:87], v[148:151], v[172:175], v[84:87]
	v_mfma_f32_16x16x32_bf16 v[80:83], v[156:159], v[172:175], v[80:83]
	v_mfma_f32_16x16x32_bf16 v[76:79], v[148:151], v[180:183], v[76:79]
	v_mfma_f32_16x16x32_bf16 v[72:75], v[156:159], v[180:183], v[72:75]
	v_mfma_f32_16x16x32_bf16 v[68:71], v[148:151], v[188:191], v[68:71]
	v_mfma_f32_16x16x32_bf16 v[64:67], v[156:159], v[188:191], v[64:67]
	s_setprio 0
	s_barrier
; #define PG8_STAGE(bufoff, rs_, soff_, voff) do { _Pragma("unroll") for (int _i = 0; _i < 2; ++_i) \
;         __builtin_amdgcn_raw_ptr_buffer_load_lds(rs_, (LAS void*)(lds + (bufoff) + ldsw + _i * 8192), 16, (int)(voff)[_i], (int)(soff_), 0, 0); } while (0)
; #define PG8_LDA(dst, b, h) do { _Pragma("unroll") for (int m = 0; m < 4; ++m) dst[m] = PG8_LD2(lds + PG8_SA(b, h) + aoff + m * 2048); } while (0)
; #define PG8_WAIT_V(n) asm volatile("s_waitcnt vmcnt(" #n ")" ::: "memory")
; #define PG8_WAIT_L(n) asm volatile("s_waitcnt lgkmcnt(" #n ")" ::: "memory")
; #define PG8_BAR __builtin_amdgcn_s_barrier()
; #define PG8_SCHED __builtin_amdgcn_sched_barrier(0)
; template <class Epi, class Sched, bool ALIGN_EPI = false, bool SP2 = false, bool FP8 = false>
; __device__ __forceinline__ void gemm_phase(LAS unsigned char* lds, const Gemm g, const Sched& S, const Epi& E, int wbase) {
;     ...
;             PG8_LDA(At, 1, 1); PG8_STAGE(PG8_SB(1, 0), rB2, b3, voffB); PG8_STAGE(PG8_SB(1, 1), rB2, b3 + hstep, voffB); PG8_STAGE(PG8_SA(1, 0), rA2, a3, voffA);
;             PG8_WAIT_V(8); PG8_WAIT_L(0); PG8_BAR; PG8_MMA(1, 0, At, B0); PG8_MMA(1, 1, At, B1); PG8_BAR; PG8_SCHED;
	s_mov_b32 m0, s63
	s_bitset1_b32 s54, 7
	buffer_load_dwordx4 v222, s[20:23], s54 offen lds
	s_mov_b32 m0, s65
	ds_read_b128 v[160:163], v239 offset:49152
	buffer_load_dwordx4 v235, s[20:23], s54 offen lds
	s_add_i32 s54, s54, s41
	s_mov_b32 m0, s79
	ds_read_b128 v[164:167], v239 offset:50176
	buffer_load_dwordx4 v222, s[20:23], s54 offen lds
	s_mov_b32 m0, s80
	ds_read_b128 v[168:171], v239 offset:51200
	buffer_load_dwordx4 v235, s[20:23], s54 offen lds
	s_mov_b32 m0, s76
	ds_read_b128 v[172:175], v239 offset:52224
	buffer_load_dwordx4 v192, s[16:19], s55 offen lds
	s_mov_b32 m0, s77
	ds_read_b128 v[176:179], v239 offset:53248
	buffer_load_dwordx4 v223, s[16:19], s55 offen lds
	ds_read_b128 v[180:183], v239 offset:54272
	ds_read_b128 v[184:187], v239 offset:55296
	ds_read_b128 v[188:191], v239 offset:56320
	s_waitcnt vmcnt(8)
	s_waitcnt lgkmcnt(0)
	s_barrier
	s_setprio 1
	v_mfma_f32_16x16x32_bf16 v[60:63], v[128:131], v[160:163], v[60:63]
	v_mfma_f32_16x16x32_bf16 v[56:59], v[136:139], v[160:163], v[56:59]
	v_mfma_f32_16x16x32_bf16 v[52:55], v[128:131], v[168:171], v[52:55]
	v_mfma_f32_16x16x32_bf16 v[48:51], v[136:139], v[168:171], v[48:51]
	v_mfma_f32_16x16x32_bf16 v[44:47], v[128:131], v[176:179], v[44:47]
	v_mfma_f32_16x16x32_bf16 v[40:43], v[136:139], v[176:179], v[40:43]
	v_mfma_f32_16x16x32_bf16 v[36:39], v[128:131], v[184:187], v[36:39]
	v_mfma_f32_16x16x32_bf16 v[32:35], v[136:139], v[184:187], v[32:35]
	v_mfma_f32_16x16x32_bf16 v[60:63], v[132:135], v[164:167], v[60:63]
	v_mfma_f32_16x16x32_bf16 v[56:59], v[140:143], v[164:167], v[56:59]
	v_mfma_f32_16x16x32_bf16 v[52:55], v[132:135], v[172:175], v[52:55]
	v_mfma_f32_16x16x32_bf16 v[48:51], v[140:143], v[172:175], v[48:51]
	v_mfma_f32_16x16x32_bf16 v[44:47], v[132:135], v[180:183], v[44:47]
	v_mfma_f32_16x16x32_bf16 v[40:43], v[140:143], v[180:183], v[40:43]
	v_mfma_f32_16x16x32_bf16 v[36:39], v[132:135], v[188:191], v[36:39]
	v_mfma_f32_16x16x32_bf16 v[32:35], v[140:143], v[188:191], v[32:35]
	v_mfma_f32_16x16x32_bf16 v[28:31], v[144:147], v[160:163], v[28:31]
	v_mfma_f32_16x16x32_bf16 v[24:27], v[152:155], v[160:163], v[24:27]
	v_mfma_f32_16x16x32_bf16 v[20:23], v[144:147], v[168:171], v[20:23]
	v_mfma_f32_16x16x32_bf16 v[16:19], v[152:155], v[168:171], v[16:19]
	v_mfma_f32_16x16x32_bf16 v[12:15], v[144:147], v[176:179], v[12:15]
	v_mfma_f32_16x16x32_bf16 v[8:11], v[152:155], v[176:179], v[8:11]
	v_mfma_f32_16x16x32_bf16 v[4:7], v[144:147], v[184:187], v[4:7]
	v_mfma_f32_16x16x32_bf16 v[0:3], v[152:155], v[184:187], v[0:3]
	v_mfma_f32_16x16x32_bf16 v[28:31], v[148:151], v[164:167], v[28:31]
	v_mfma_f32_16x16x32_bf16 v[24:27], v[156:159], v[164:167], v[24:27]
	v_mfma_f32_16x16x32_bf16 v[20:23], v[148:151], v[172:175], v[20:23]
	v_mfma_f32_16x16x32_bf16 v[16:19], v[156:159], v[172:175], v[16:19]
	v_mfma_f32_16x16x32_bf16 v[12:15], v[148:151], v[180:183], v[12:15]
	v_mfma_f32_16x16x32_bf16 v[8:11], v[156:159], v[180:183], v[8:11]
	v_mfma_f32_16x16x32_bf16 v[4:7], v[148:151], v[188:191], v[4:7]
	v_mfma_f32_16x16x32_bf16 v[0:3], v[156:159], v[188:191], v[0:3]
	s_setprio 0
	s_barrier
	s_add_i32 s85, s85, 2
	s_addk_i32 vcc_lo, 0x100
	s_addk_i32 vcc_hi, 0x100
	s_cmp_ge_i32 s85, s81
	s_cbranch_scc0 .LBB0_847
	v_readlane_b32 s68, v255, 22
	v_readlane_b32 s54, v255, 25
	v_readlane_b32 s69, v255, 23
	v_readlane_b32 s55, v255, 26

; #define PG8_STAGE(bufoff, rs_, soff_, voff) do { _Pragma("unroll") for (int _i = 0; _i < 2; ++_i) \
;         __builtin_amdgcn_raw_ptr_buffer_load_lds(rs_, (LAS void*)(lds + (bufoff) + ldsw + _i * 8192), 16, (int)(voff)[_i], (int)(soff_), 0, 0); } while (0)
; #define PG8_LDA(dst, b, h) do { _Pragma("unroll") for (int m = 0; m < 4; ++m) dst[m] = PG8_LD2(lds + PG8_SA(b, h) + aoff + m * 2048); } while (0)
; #define PG8_LDB(dst, b, h) do { _Pragma("unroll") for (int n = 0; n < 2; ++n) dst[n] = PG8_LD2(lds + PG8_SB(b, h) + boff + n * 2048); } while (0)
; #define PG8_WAIT_V(n) asm volatile("s_waitcnt vmcnt(" #n ")" ::: "memory")
; #define PG8_WAIT_L(n) asm volatile("s_waitcnt lgkmcnt(" #n ")" ::: "memory")
; #define PG8_BAR __builtin_amdgcn_s_barrier()
; #define PG8_SCHED __builtin_amdgcn_sched_barrier(0)
; template <class Epi, class Sched, bool ALIGN_EPI = false, bool SP2 = false, bool FP8 = false>
; __device__ __forceinline__ void gemm_phase(LAS unsigned char* lds, const Gemm g, const Sched& S, const Epi& E, int wbase) {
;     ...
;         for (int t = 0; t < nt; t += 2) {
;             const bool last = (t == nt - 2);
;             const unsigned a1 = cA + (unsigned)(t + 1) * kstep;
;             const unsigned a2 = last ? nA : cA + (unsigned)(t + 2) * kstep, b2 = last ? nB : cB + (unsigned)(t + 2) * kstep; const rsrc_t rA2 = (Sched::TWO && last) ? rAn : rAc, rB2 = (Sched::TWO && last) ? rBn : rBc;
;             const unsigned a3 = a2 + kstep, b3 = b2 + kstep;
;             if (last && has_next) S.a_ready(nxt);
;             if constexpr (SP2) {
;             PG8_LDB(B0, 0, 0); PG8_LDB(B1, 0, 1); PG8_SCHED; PG8_LDA(At, 0, 0); PG8_STAGE(PG8_SA(1, 1), rAc, a1 + hstep, voffA);
;             PG8_WAIT_V(8); PG8_WAIT_L(0); PG8_BAR; PG8_MMA(0, 0, At, B0); PG8_MMA(0, 1, At, B1); PG8_BAR; PG8_SCHED;
;             PG8_LDA(At, 0, 1); PG8_STAGE(PG8_SB(0, 0), rB2, b2, voffB); PG8_STAGE(PG8_SB(0, 1), rB2, b2 + hstep, voffB); PG8_STAGE(PG8_SA(0, 0), rA2, a2, voffA);
;             PG8_WAIT_V(8); PG8_WAIT_L(0); PG8_BAR; PG8_MMA(1, 0, At, B0); PG8_MMA(1, 1, At, B1); PG8_BAR; PG8_SCHED;
;             PG8_LDB(B0, 1, 0); PG8_LDB(B1, 1, 1); PG8_SCHED; PG8_LDA(At, 1, 0); PG8_STAGE(PG8_SA(0, 1), rA2, a2 + hstep, voffA);
;             PG8_WAIT_V(8); PG8_WAIT_L(0); PG8_BAR; PG8_MMA(0, 0, At, B0); PG8_MMA(0, 1, At, B1); PG8_BAR; PG8_SCHED;
.LBB0_924:
	s_lshl_b32 s79, s77, 18
	s_andn2_b64 vcc, exec, s[22:23]
	s_lshl_b32 s80, s76, 18
	s_cbranch_vccnz .LBB0_928
	s_and_b64 s[2:3], s[26:27], exec
	s_waitcnt vmcnt(37)
	s_waitcnt vmcnt(36)
	s_waitcnt vmcnt(35)
	s_waitcnt vmcnt(32)
	s_waitcnt vmcnt(31)
	s_waitcnt vmcnt(28)
	s_waitcnt vmcnt(27)
	s_waitcnt vmcnt(24)
	s_waitcnt vmcnt(23)
	v_mov_b32_e32 v159, v233
	s_cselect_b32 s2, s79, s4
	s_cselect_b32 s3, s80, s5
	s_addk_i32 s4, 0x80
	s_addk_i32 s5, 0x100
	s_mov_b32 s11, 0
	s_waitcnt vmcnt(0)
	v_add_u32_e32 v120, 0x10000, v160
	ds_read_b128 v[132:135], v120
	ds_read_b128 v[136:139], v120 offset:1024
	ds_read_b128 v[140:143], v120 offset:2048
	ds_read_b128 v[144:147], v120 offset:3072
	v_add_u32_e32 v120, 0x14000, v160
	ds_read_b128 v[162:165], v120
	ds_read_b128 v[166:169], v120 offset:1024
	ds_read_b128 v[170:173], v120 offset:2048
	ds_read_b128 v[174:177], v120 offset:3072
	s_add_i32 s14, s4, 0x80
	s_cmp_eq_u32 s60, s11
	s_cselect_b32 s66, s2, s14
	s_cselect_b32 s55, s3, s5
	s_or_b32 s54, s66, 0x80
	s_add_i32 s14, s30, s4
	s_mov_b32 m0, s61
	ds_read_b128 v[178:181], v161
	ds_read_b128 v[182:185], v161 offset:1024
	ds_read_b128 v[194:197], v161 offset:2048
	ds_read_b128 v[198:201], v161 offset:3072
	ds_read_b128 v[202:205], v161 offset:4096
	ds_read_b128 v[206:209], v161 offset:5120
	ds_read_b128 v[210:213], v161 offset:6144
	ds_read_b128 v[214:217], v161 offset:7168
	buffer_load_dwordx4 v222, s[36:39], s14 offen lds
	s_mov_b32 m0, s62
	s_nop 0
	buffer_load_dwordx4 v156, s[36:39], s14 offen lds
	s_waitcnt vmcnt(8)
	s_waitcnt lgkmcnt(0)
	s_barrier
	s_setprio 1
	v_mfma_f32_16x16x128_f8f6f4 v[124:127], v[140:147], v[178:185], 0
	v_mfma_f32_16x16x128_f8f6f4 v[108:111], v[132:139], v[194:201], 0
	v_mfma_f32_16x16x128_f8f6f4 v[104:107], v[140:147], v[194:201], 0
	v_mfma_f32_16x16x128_f8f6f4 v[120:123], v[132:139], v[178:185], 0
	v_mfma_f32_16x16x128_f8f6f4 v[148:151], v[132:139], v[202:209], 0
	v_mfma_f32_16x16x128_f8f6f4 v[186:189], v[140:147], v[202:209], 0
	v_mfma_f32_16x16x128_f8f6f4 v[218:221], v[132:139], v[210:217], 0
	v_mfma_f32_16x16x128_f8f6f4 v[226:229], v[140:147], v[210:217], 0
	v_mfma_f32_16x16x128_f8f6f4 v[116:119], v[162:169], v[178:185], 0
	v_mfma_f32_16x16x128_f8f6f4 v[112:115], v[170:177], v[178:185], 0
	v_mfma_f32_16x16x128_f8f6f4 v[100:103], v[162:169], v[194:201], 0
	v_mfma_f32_16x16x128_f8f6f4 v[96:99], v[170:177], v[194:201], 0
	v_mfma_f32_16x16x128_f8f6f4 v[178:181], v[162:169], v[202:209], 0
	v_mfma_f32_16x16x128_f8f6f4 v[182:185], v[170:177], v[202:209], 0
	v_mfma_f32_16x16x128_f8f6f4 v[194:197], v[162:169], v[210:217], 0
	v_mfma_f32_16x16x128_f8f6f4 v[198:201], v[170:177], v[210:217], 0
	s_setprio 0
	s_barrier
	s_mov_b32 m0, s33
	s_mov_b32 s14, s38
	s_mov_b32 s15, s39
	s_nop 1
	buffer_load_dwordx4 v223, s[12:15], s55 offen lds
	s_mov_b32 m0, s34
	ds_read_b128 v[64:67], v161 offset:16384
	s_add_i32 s67, s55, s30
	buffer_load_dwordx4 v157, s[12:15], s55 offen lds
	s_mov_b32 m0, s35
	ds_read_b128 v[68:71], v161 offset:17408
	buffer_load_dwordx4 v223, s[12:15], s67 offen lds
	s_mov_b32 m0, s31
	ds_read_b128 v[72:75], v161 offset:18432
	buffer_load_dwordx4 v222, s[36:39], s66 offen lds
	s_mov_b32 m0, s42
	ds_read_b128 v[76:79], v161 offset:19456
	buffer_load_dwordx4 v156, s[36:39], s66 offen lds
	ds_read_b128 v[80:83], v161 offset:20480
	ds_read_b128 v[84:87], v161 offset:21504
	ds_read_b128 v[88:91], v161 offset:22528
	ds_read_b128 v[92:95], v161 offset:23552
	s_waitcnt vmcnt(7)
	s_waitcnt lgkmcnt(0)
	s_barrier
	s_setprio 1
	v_mfma_f32_16x16x128_f8f6f4 v[60:63], v[132:139], v[64:71], 0
	v_mfma_f32_16x16x128_f8f6f4 v[56:59], v[140:147], v[64:71], 0
	v_mfma_f32_16x16x128_f8f6f4 v[202:205], v[132:139], v[72:79], 0
	v_mfma_f32_16x16x128_f8f6f4 v[206:209], v[140:147], v[72:79], 0
	v_mfma_f32_16x16x128_f8f6f4 v[210:213], v[132:139], v[80:87], 0
	v_mfma_f32_16x16x128_f8f6f4 v[214:217], v[140:147], v[80:87], 0
	v_mfma_f32_16x16x128_f8f6f4 v[230:233], v[132:139], v[88:95], 0
	v_mfma_f32_16x16x128_f8f6f4 v[234:237], v[140:147], v[88:95], 0
	v_mfma_f32_16x16x128_f8f6f4 v[52:55], v[162:169], v[64:71], 0
	v_mfma_f32_16x16x128_f8f6f4 v[48:51], v[170:177], v[64:71], 0
	v_mfma_f32_16x16x128_f8f6f4 v[238:241], v[162:169], v[72:79], 0
	v_mfma_f32_16x16x128_f8f6f4 v[242:245], v[170:177], v[72:79], 0
	v_mfma_f32_16x16x128_f8f6f4 v[246:249], v[162:169], v[80:87], 0
	v_mfma_f32_16x16x128_f8f6f4 v[250:253], v[170:177], v[80:87], 0
	v_mfma_f32_16x16x128_f8f6f4 v[190:193], v[162:169], v[88:95], 0
	v_mfma_f32_16x16x128_f8f6f4 v[152:155], v[170:177], v[88:95], 0
	s_setprio 0
	s_barrier
	s_mov_b32 m0, s41
	s_nop 0
	buffer_load_dwordx4 v157, s[12:15], s67 offen lds
	v_add_u32_e32 v8, 0x18000, v160
	s_nop 3
	ds_read_b128 v[0:3], v8
	ds_read_b128 v[4:7], v8 offset:1024
	ds_read_b128 v[16:19], v8 offset:2048
	ds_read_b128 v[20:23], v8 offset:3072
	v_add_u32_e32 v8, 0x1c000, v160
	ds_read_b128 v[132:135], v8
	ds_read_b128 v[136:139], v8 offset:1024
	ds_read_b128 v[140:143], v8 offset:2048
	ds_read_b128 v[144:147], v8 offset:3072
	s_add_i32 s66, s66, s30
	s_mov_b32 m0, s43
	ds_read_b128 v[8:11], v161 offset:32768
	ds_read_b128 v[12:15], v161 offset:33792
	ds_read_b128 v[24:27], v161 offset:34816
	ds_read_b128 v[28:31], v161 offset:35840
	ds_read_b128 v[32:35], v161 offset:36864
	ds_read_b128 v[36:39], v161 offset:37888
	ds_read_b128 v[40:43], v161 offset:38912
	ds_read_b128 v[44:47], v161 offset:39936
	buffer_load_dwordx4 v222, s[36:39], s66 offen lds
	s_mov_b32 m0, s44
	s_nop 0
	buffer_load_dwordx4 v156, s[36:39], s66 offen lds
	s_waitcnt vmcnt(8)
	s_waitcnt lgkmcnt(0)
	s_barrier
; #define PG8_STAGE(bufoff, rs_, soff_, voff) do { _Pragma("unroll") for (int _i = 0; _i < 2; ++_i) \
;         __builtin_amdgcn_raw_ptr_buffer_load_lds(rs_, (LAS void*)(lds + (bufoff) + ldsw + _i * 8192), 16, (int)(voff)[_i], (int)(soff_), 0, 0); } while (0)
; #define PG8_LDA(dst, b, h) do { _Pragma("unroll") for (int m = 0; m < 4; ++m) dst[m] = PG8_LD2(lds + PG8_SA(b, h) + aoff + m * 2048); } while (0)
; #define PG8_LDB(dst, b, h) do { _Pragma("unroll") for (int n = 0; n < 2; ++n) dst[n] = PG8_LD2(lds + PG8_SB(b, h) + boff + n * 2048); } while (0)
; #define PG8_WAIT_V(n) asm volatile("s_waitcnt vmcnt(" #n ")" ::: "memory")
; #define PG8_WAIT_L(n) asm volatile("s_waitcnt lgkmcnt(" #n ")" ::: "memory")
; #define PG8_BAR __builtin_amdgcn_s_barrier()
; #define PG8_SCHED __builtin_amdgcn_sched_barrier(0)
; template <class Epi, class Sched, bool ALIGN_EPI = false, bool SP2 = false, bool FP8 = false>
; __device__ __forceinline__ void gemm_phase(LAS unsigned char* lds, const Gemm g, const Sched& S, const Epi& E, int wbase) {
;     ...
;             PG8_LDB(B0, 0, 0); PG8_LDB(B1, 0, 1); PG8_SCHED; PG8_LDA(At, 0, 0); PG8_STAGE(PG8_SA(1, 1), rAc, a1 + hstep, voffA);
;             PG8_WAIT_V(8); PG8_WAIT_L(0); PG8_BAR; PG8_MMA(0, 0, At, B0); PG8_MMA(0, 1, At, B1); PG8_BAR; PG8_SCHED;
;             PG8_LDA(At, 0, 1); PG8_STAGE(PG8_SB(0, 0), rB2, b2, voffB); PG8_STAGE(PG8_SB(0, 1), rB2, b2 + hstep, voffB); PG8_STAGE(PG8_SA(0, 0), rA2, a2, voffA);
;             PG8_WAIT_V(8); PG8_WAIT_L(0); PG8_BAR; PG8_MMA(1, 0, At, B0); PG8_MMA(1, 1, At, B1); PG8_BAR; PG8_SCHED;
;             PG8_LDB(B0, 1, 0); PG8_LDB(B1, 1, 1); PG8_SCHED; PG8_LDA(At, 1, 0); PG8_STAGE(PG8_SA(0, 1), rA2, a2 + hstep, voffA);
;             PG8_WAIT_V(8); PG8_WAIT_L(0); PG8_BAR; PG8_MMA(0, 0, At, B0); PG8_MMA(0, 1, At, B1); PG8_BAR; PG8_SCHED;
;             PG8_LDA(At, 1, 1); PG8_STAGE(PG8_SB(1, 0), rB2, b3, voffB); PG8_STAGE(PG8_SB(1, 1), rB2, b3 + hstep, voffB); PG8_STAGE(PG8_SA(1, 0), rA2, a3, voffA);
;             PG8_WAIT_V(8); PG8_WAIT_L(0); PG8_BAR; PG8_MMA(1, 0, At, B0); PG8_MMA(1, 1, At, B1); PG8_BAR; PG8_SCHED;
	s_setprio 1
	v_mfma_f32_16x16x128_f8f6f4 v[128:131], v[0:7], v[8:15], v[120:123]
	v_mfma_f32_16x16x128_f8f6f4 v[124:127], v[16:23], v[8:15], v[124:127]
	v_mfma_f32_16x16x128_f8f6f4 v[108:111], v[0:7], v[24:31], v[108:111]
	v_mfma_f32_16x16x128_f8f6f4 v[104:107], v[16:23], v[24:31], v[104:107]
	v_mfma_f32_16x16x128_f8f6f4 v[92:95], v[0:7], v[32:39], v[148:151]
	v_mfma_f32_16x16x128_f8f6f4 v[88:91], v[16:23], v[32:39], v[186:189]
	v_mfma_f32_16x16x128_f8f6f4 v[76:79], v[0:7], v[40:47], v[218:221]
	v_mfma_f32_16x16x128_f8f6f4 v[72:75], v[16:23], v[40:47], v[226:229]
	v_mfma_f32_16x16x128_f8f6f4 v[116:119], v[132:139], v[8:15], v[116:119]
	v_mfma_f32_16x16x128_f8f6f4 v[112:115], v[140:147], v[8:15], v[112:115]
	v_mfma_f32_16x16x128_f8f6f4 v[100:103], v[132:139], v[24:31], v[100:103]
	v_mfma_f32_16x16x128_f8f6f4 v[96:99], v[140:147], v[24:31], v[96:99]
	v_mfma_f32_16x16x128_f8f6f4 v[84:87], v[132:139], v[32:39], v[178:181]
	v_mfma_f32_16x16x128_f8f6f4 v[80:83], v[140:147], v[32:39], v[182:185]
	v_mfma_f32_16x16x128_f8f6f4 v[68:71], v[132:139], v[40:47], v[194:197]
	v_mfma_f32_16x16x128_f8f6f4 v[64:67], v[140:147], v[40:47], v[198:201]
	s_setprio 0
	s_barrier
	s_mov_b32 m0, s45
	s_bitset1_b32 s55, 7
	buffer_load_dwordx4 v223, s[12:15], s55 offen lds
	s_mov_b32 m0, s46
	ds_read_b128 v[32:35], v161 offset:49152
	buffer_load_dwordx4 v157, s[12:15], s55 offen lds
	s_add_i32 s55, s55, s30
	s_mov_b32 m0, s52
	ds_read_b128 v[36:39], v161 offset:50176
	buffer_load_dwordx4 v223, s[12:15], s55 offen lds
	s_mov_b32 m0, s53
	ds_read_b128 v[162:165], v161 offset:51200
	buffer_load_dwordx4 v157, s[12:15], s55 offen lds
	s_mov_b32 m0, s47
	ds_read_b128 v[166:169], v161 offset:52224
	buffer_load_dwordx4 v222, s[36:39], s54 offen lds
	s_mov_b32 m0, s48
	ds_read_b128 v[170:173], v161 offset:53248
	buffer_load_dwordx4 v156, s[36:39], s54 offen lds
	ds_read_b128 v[174:177], v161 offset:54272
	ds_read_b128 v[178:181], v161 offset:55296
	ds_read_b128 v[182:185], v161 offset:56320
	s_waitcnt vmcnt(8)
	s_waitcnt lgkmcnt(0)
	s_barrier
	s_setprio 1
	v_mfma_f32_16x16x128_f8f6f4 v[60:63], v[0:7], v[32:39], v[60:63]
	v_mfma_f32_16x16x128_f8f6f4 v[56:59], v[16:23], v[32:39], v[56:59]
	v_mfma_f32_16x16x128_f8f6f4 v[44:47], v[0:7], v[162:169], v[202:205]
	v_mfma_f32_16x16x128_f8f6f4 v[40:43], v[16:23], v[162:169], v[206:209]
	v_mfma_f32_16x16x128_f8f6f4 v[28:31], v[0:7], v[170:177], v[210:213]
	v_mfma_f32_16x16x128_f8f6f4 v[24:27], v[16:23], v[170:177], v[214:217]
	v_mfma_f32_16x16x128_f8f6f4 v[12:15], v[0:7], v[178:185], v[230:233]
	v_mfma_f32_16x16x128_f8f6f4 v[8:11], v[16:23], v[178:185], v[234:237]
	v_mfma_f32_16x16x128_f8f6f4 v[52:55], v[132:139], v[32:39], v[52:55]
	v_mfma_f32_16x16x128_f8f6f4 v[48:51], v[140:147], v[32:39], v[48:51]
	v_mfma_f32_16x16x128_f8f6f4 v[36:39], v[132:139], v[162:169], v[238:241]
	v_mfma_f32_16x16x128_f8f6f4 v[32:35], v[140:147], v[162:169], v[242:245]
	v_mfma_f32_16x16x128_f8f6f4 v[20:23], v[132:139], v[170:177], v[246:249]
	v_mfma_f32_16x16x128_f8f6f4 v[16:19], v[140:147], v[170:177], v[250:253]
	v_mfma_f32_16x16x128_f8f6f4 v[4:7], v[132:139], v[178:185], v[190:193]
	v_mfma_f32_16x16x128_f8f6f4 v[0:3], v[140:147], v[178:185], v[152:155]
	s_setprio 0
	s_barrier
	s_add_i32 s11, s11, 2
	s_addk_i32 s4, 0x100
	s_addk_i32 s5, 0x100
	s_cmp_ge_i32 s11, s58
	s_cbranch_scc0 .LBB0_926
	s_branch .Lzp_after_926
.LBB0_926:
	v_add_u32_e32 v120, 0x10000, v160
	ds_read_b128 v[132:135], v120
	ds_read_b128 v[136:139], v120 offset:1024
	ds_read_b128 v[140:143], v120 offset:2048
	ds_read_b128 v[144:147], v120 offset:3072
	v_add_u32_e32 v120, 0x14000, v160
	ds_read_b128 v[162:165], v120
	ds_read_b128 v[166:169], v120 offset:1024
	ds_read_b128 v[170:173], v120 offset:2048
	ds_read_b128 v[174:177], v120 offset:3072
	s_add_i32 s14, s4, 0x80
	s_cmp_eq_u32 s60, s11
	s_cselect_b32 s66, s2, s14
	s_cselect_b32 s55, s3, s5
	s_or_b32 s54, s66, 0x80
	s_add_i32 s14, s30, s4
	s_mov_b32 m0, s61
	ds_read_b128 v[178:181], v161
	ds_read_b128 v[182:185], v161 offset:1024
	ds_read_b128 v[194:197], v161 offset:2048
	ds_read_b128 v[198:201], v161 offset:3072
	ds_read_b128 v[202:205], v161 offset:4096
	ds_read_b128 v[206:209], v161 offset:5120
	ds_read_b128 v[210:213], v161 offset:6144
	ds_read_b128 v[214:217], v161 offset:7168
	buffer_load_dwordx4 v222, s[36:39], s14 offen lds
	s_mov_b32 m0, s62
	s_nop 0
	buffer_load_dwordx4 v156, s[36:39], s14 offen lds
	s_waitcnt vmcnt(8)
	s_waitcnt lgkmcnt(0)
	s_barrier
	s_setprio 1
	v_mfma_f32_16x16x128_f8f6f4 v[124:127], v[140:147], v[178:185], v[124:127]
	v_mfma_f32_16x16x128_f8f6f4 v[108:111], v[132:139], v[194:201], v[108:111]
	v_mfma_f32_16x16x128_f8f6f4 v[104:107], v[140:147], v[194:201], v[104:107]
	v_mfma_f32_16x16x128_f8f6f4 v[120:123], v[132:139], v[178:185], v[128:131]
	v_mfma_f32_16x16x128_f8f6f4 v[148:151], v[132:139], v[202:209], v[92:95]
	v_mfma_f32_16x16x128_f8f6f4 v[186:189], v[140:147], v[202:209], v[88:91]
	v_mfma_f32_16x16x128_f8f6f4 v[218:221], v[132:139], v[210:217], v[76:79]
	v_mfma_f32_16x16x128_f8f6f4 v[226:229], v[140:147], v[210:217], v[72:75]
	v_mfma_f32_16x16x128_f8f6f4 v[116:119], v[162:169], v[178:185], v[116:119]
	v_mfma_f32_16x16x128_f8f6f4 v[112:115], v[170:177], v[178:185], v[112:115]
	v_mfma_f32_16x16x128_f8f6f4 v[100:103], v[162:169], v[194:201], v[100:103]
	v_mfma_f32_16x16x128_f8f6f4 v[96:99], v[170:177], v[194:201], v[96:99]
	v_mfma_f32_16x16x128_f8f6f4 v[178:181], v[162:169], v[202:209], v[84:87]
	v_mfma_f32_16x16x128_f8f6f4 v[182:185], v[170:177], v[202:209], v[80:83]
	v_mfma_f32_16x16x128_f8f6f4 v[194:197], v[162:169], v[210:217], v[68:71]
	v_mfma_f32_16x16x128_f8f6f4 v[198:201], v[170:177], v[210:217], v[64:67]
	s_setprio 0
	s_barrier
; #define PG8_STAGE(bufoff, rs_, soff_, voff) do { _Pragma("unroll") for (int _i = 0; _i < 2; ++_i) \
;         __builtin_amdgcn_raw_ptr_buffer_load_lds(rs_, (LAS void*)(lds + (bufoff) + ldsw + _i * 8192), 16, (int)(voff)[_i], (int)(soff_), 0, 0); } while (0)
; #define PG8_LDA(dst, b, h) do { _Pragma("unroll") for (int m = 0; m < 4; ++m) dst[m] = PG8_LD2(lds + PG8_SA(b, h) + aoff + m * 2048); } while (0)
; #define PG8_LDB(dst, b, h) do { _Pragma("unroll") for (int n = 0; n < 2; ++n) dst[n] = PG8_LD2(lds + PG8_SB(b, h) + boff + n * 2048); } while (0)
; #define PG8_WAIT_V(n) asm volatile("s_waitcnt vmcnt(" #n ")" ::: "memory")
; #define PG8_WAIT_L(n) asm volatile("s_waitcnt lgkmcnt(" #n ")" ::: "memory")
; #define PG8_BAR __builtin_amdgcn_s_barrier()
; #define PG8_SCHED __builtin_amdgcn_sched_barrier(0)
; template <class Epi, class Sched, bool ALIGN_EPI = false, bool SP2 = false, bool FP8 = false>
; __device__ __forceinline__ void gemm_phase(LAS unsigned char* lds, const Gemm g, const Sched& S, const Epi& E, int wbase) {
;     ...
;             PG8_LDA(At, 0, 1); PG8_STAGE(PG8_SB(0, 0), rB2, b2, voffB); PG8_STAGE(PG8_SB(0, 1), rB2, b2 + hstep, voffB); PG8_STAGE(PG8_SA(0, 0), rA2, a2, voffA);
;             PG8_WAIT_V(8); PG8_WAIT_L(0); PG8_BAR; PG8_MMA(1, 0, At, B0); PG8_MMA(1, 1, At, B1); PG8_BAR; PG8_SCHED;
;             PG8_LDB(B0, 1, 0); PG8_LDB(B1, 1, 1); PG8_SCHED; PG8_LDA(At, 1, 0); PG8_STAGE(PG8_SA(0, 1), rA2, a2 + hstep, voffA);
;             PG8_WAIT_V(8); PG8_WAIT_L(0); PG8_BAR; PG8_MMA(0, 0, At, B0); PG8_MMA(0, 1, At, B1); PG8_BAR; PG8_SCHED;
;             PG8_LDA(At, 1, 1); PG8_STAGE(PG8_SB(1, 0), rB2, b3, voffB); PG8_STAGE(PG8_SB(1, 1), rB2, b3 + hstep, voffB); PG8_STAGE(PG8_SA(1, 0), rA2, a3, voffA);
;             PG8_WAIT_V(8); PG8_WAIT_L(0); PG8_BAR; PG8_MMA(1, 0, At, B0); PG8_MMA(1, 1, At, B1); PG8_BAR; PG8_SCHED;
	s_mov_b32 m0, s33
	s_mov_b32 s14, s38
	s_mov_b32 s15, s39
	s_nop 1
	buffer_load_dwordx4 v223, s[12:15], s55 offen lds
	s_mov_b32 m0, s34
	ds_read_b128 v[64:67], v161 offset:16384
	s_add_i32 s67, s55, s30
	buffer_load_dwordx4 v157, s[12:15], s55 offen lds
	s_mov_b32 m0, s35
	ds_read_b128 v[68:71], v161 offset:17408
	buffer_load_dwordx4 v223, s[12:15], s67 offen lds
	s_mov_b32 m0, s31
	ds_read_b128 v[72:75], v161 offset:18432
	buffer_load_dwordx4 v222, s[36:39], s66 offen lds
	s_mov_b32 m0, s42
	ds_read_b128 v[76:79], v161 offset:19456
	buffer_load_dwordx4 v156, s[36:39], s66 offen lds
	ds_read_b128 v[80:83], v161 offset:20480
	ds_read_b128 v[84:87], v161 offset:21504
	ds_read_b128 v[88:91], v161 offset:22528
	ds_read_b128 v[92:95], v161 offset:23552
	s_waitcnt vmcnt(7)
	s_waitcnt lgkmcnt(0)
	s_barrier
	s_setprio 1
	v_mfma_f32_16x16x128_f8f6f4 v[60:63], v[132:139], v[64:71], v[60:63]
	v_mfma_f32_16x16x128_f8f6f4 v[56:59], v[140:147], v[64:71], v[56:59]
	v_mfma_f32_16x16x128_f8f6f4 v[202:205], v[132:139], v[72:79], v[44:47]
	v_mfma_f32_16x16x128_f8f6f4 v[206:209], v[140:147], v[72:79], v[40:43]
	v_mfma_f32_16x16x128_f8f6f4 v[210:213], v[132:139], v[80:87], v[28:31]
	v_mfma_f32_16x16x128_f8f6f4 v[214:217], v[140:147], v[80:87], v[24:27]
	v_mfma_f32_16x16x128_f8f6f4 v[230:233], v[132:139], v[88:95], v[12:15]
	v_mfma_f32_16x16x128_f8f6f4 v[234:237], v[140:147], v[88:95], v[8:11]
	v_mfma_f32_16x16x128_f8f6f4 v[52:55], v[162:169], v[64:71], v[52:55]
	v_mfma_f32_16x16x128_f8f6f4 v[48:51], v[170:177], v[64:71], v[48:51]
	v_mfma_f32_16x16x128_f8f6f4 v[238:241], v[162:169], v[72:79], v[36:39]
	v_mfma_f32_16x16x128_f8f6f4 v[242:245], v[170:177], v[72:79], v[32:35]
	v_mfma_f32_16x16x128_f8f6f4 v[246:249], v[162:169], v[80:87], v[20:23]
	v_mfma_f32_16x16x128_f8f6f4 v[250:253], v[170:177], v[80:87], v[16:19]
	v_mfma_f32_16x16x128_f8f6f4 v[190:193], v[162:169], v[88:95], v[4:7]
	v_mfma_f32_16x16x128_f8f6f4 v[152:155], v[170:177], v[88:95], v[0:3]
	s_setprio 0
	s_barrier
	s_mov_b32 m0, s41
	s_nop 0
	buffer_load_dwordx4 v157, s[12:15], s67 offen lds
	v_add_u32_e32 v8, 0x18000, v160
	s_nop 3
	ds_read_b128 v[0:3], v8
	ds_read_b128 v[4:7], v8 offset:1024
	ds_read_b128 v[16:19], v8 offset:2048
	ds_read_b128 v[20:23], v8 offset:3072
	v_add_u32_e32 v8, 0x1c000, v160
	ds_read_b128 v[132:135], v8
	ds_read_b128 v[136:139], v8 offset:1024
	ds_read_b128 v[140:143], v8 offset:2048
	ds_read_b128 v[144:147], v8 offset:3072
	s_add_i32 s66, s66, s30
	s_mov_b32 m0, s43
	ds_read_b128 v[8:11], v161 offset:32768
	ds_read_b128 v[12:15], v161 offset:33792
	ds_read_b128 v[24:27], v161 offset:34816
	ds_read_b128 v[28:31], v161 offset:35840
	ds_read_b128 v[32:35], v161 offset:36864
	ds_read_b128 v[36:39], v161 offset:37888
	ds_read_b128 v[40:43], v161 offset:38912
	ds_read_b128 v[44:47], v161 offset:39936
	buffer_load_dwordx4 v222, s[36:39], s66 offen lds
	s_mov_b32 m0, s44
	s_nop 0
	buffer_load_dwordx4 v156, s[36:39], s66 offen lds
	s_waitcnt vmcnt(8)
	s_waitcnt lgkmcnt(0)
	s_barrier
	s_setprio 1
	v_mfma_f32_16x16x128_f8f6f4 v[128:131], v[0:7], v[8:15], v[120:123]
	v_mfma_f32_16x16x128_f8f6f4 v[124:127], v[16:23], v[8:15], v[124:127]
	v_mfma_f32_16x16x128_f8f6f4 v[108:111], v[0:7], v[24:31], v[108:111]
	v_mfma_f32_16x16x128_f8f6f4 v[104:107], v[16:23], v[24:31], v[104:107]
	v_mfma_f32_16x16x128_f8f6f4 v[92:95], v[0:7], v[32:39], v[148:151]
	v_mfma_f32_16x16x128_f8f6f4 v[88:91], v[16:23], v[32:39], v[186:189]
	v_mfma_f32_16x16x128_f8f6f4 v[76:79], v[0:7], v[40:47], v[218:221]
	v_mfma_f32_16x16x128_f8f6f4 v[72:75], v[16:23], v[40:47], v[226:229]
	v_mfma_f32_16x16x128_f8f6f4 v[116:119], v[132:139], v[8:15], v[116:119]
	v_mfma_f32_16x16x128_f8f6f4 v[112:115], v[140:147], v[8:15], v[112:115]
	v_mfma_f32_16x16x128_f8f6f4 v[100:103], v[132:139], v[24:31], v[100:103]
	v_mfma_f32_16x16x128_f8f6f4 v[96:99], v[140:147], v[24:31], v[96:99]
	v_mfma_f32_16x16x128_f8f6f4 v[84:87], v[132:139], v[32:39], v[178:181]
	v_mfma_f32_16x16x128_f8f6f4 v[80:83], v[140:147], v[32:39], v[182:185]
	v_mfma_f32_16x16x128_f8f6f4 v[68:71], v[132:139], v[40:47], v[194:197]
	v_mfma_f32_16x16x128_f8f6f4 v[64:67], v[140:147], v[40:47], v[198:201]
	s_setprio 0
	s_barrier
	s_mov_b32 m0, s45
	s_bitset1_b32 s55, 7
	buffer_load_dwordx4 v223, s[12:15], s55 offen lds
	s_mov_b32 m0, s46
	ds_read_b128 v[32:35], v161 offset:49152
	buffer_load_dwordx4 v157, s[12:15], s55 offen lds
	s_add_i32 s55, s55, s30
	s_mov_b32 m0, s52
	ds_read_b128 v[36:39], v161 offset:50176
	buffer_load_dwordx4 v223, s[12:15], s55 offen lds
	s_mov_b32 m0, s53
	ds_read_b128 v[162:165], v161 offset:51200
	buffer_load_dwordx4 v157, s[12:15], s55 offen lds
	s_mov_b32 m0, s47
	ds_read_b128 v[166:169], v161 offset:52224
	buffer_load_dwordx4 v222, s[36:39], s54 offen lds
	s_mov_b32 m0, s48
	ds_read_b128 v[170:173], v161 offset:53248
	buffer_load_dwordx4 v156, s[36:39], s54 offen lds
	ds_read_b128 v[174:177], v161 offset:54272
	ds_read_b128 v[178:181], v161 offset:55296
	ds_read_b128 v[182:185], v161 offset:56320
	s_waitcnt vmcnt(8)
	s_waitcnt lgkmcnt(0)
	s_barrier
	s_setprio 1
	v_mfma_f32_16x16x128_f8f6f4 v[60:63], v[0:7], v[32:39], v[60:63]
	v_mfma_f32_16x16x128_f8f6f4 v[56:59], v[16:23], v[32:39], v[56:59]
	v_mfma_f32_16x16x128_f8f6f4 v[44:47], v[0:7], v[162:169], v[202:205]
	v_mfma_f32_16x16x128_f8f6f4 v[40:43], v[16:23], v[162:169], v[206:209]
	v_mfma_f32_16x16x128_f8f6f4 v[28:31], v[0:7], v[170:177], v[210:213]
	v_mfma_f32_16x16x128_f8f6f4 v[24:27], v[16:23], v[170:177], v[214:217]
	v_mfma_f32_16x16x128_f8f6f4 v[12:15], v[0:7], v[178:185], v[230:233]
	v_mfma_f32_16x16x128_f8f6f4 v[8:11], v[16:23], v[178:185], v[234:237]
	v_mfma_f32_16x16x128_f8f6f4 v[52:55], v[132:139], v[32:39], v[52:55]
	v_mfma_f32_16x16x128_f8f6f4 v[48:51], v[140:147], v[32:39], v[48:51]
	v_mfma_f32_16x16x128_f8f6f4 v[36:39], v[132:139], v[162:169], v[238:241]
	v_mfma_f32_16x16x128_f8f6f4 v[32:35], v[140:147], v[162:169], v[242:245]
	v_mfma_f32_16x16x128_f8f6f4 v[20:23], v[132:139], v[170:177], v[246:249]
	v_mfma_f32_16x16x128_f8f6f4 v[16:19], v[140:147], v[170:177], v[250:253]
	v_mfma_f32_16x16x128_f8f6f4 v[4:7], v[132:139], v[178:185], v[190:193]
	v_mfma_f32_16x16x128_f8f6f4 v[0:3], v[140:147], v[178:185], v[152:155]
	s_setprio 0
	s_barrier
	s_add_i32 s11, s11, 2
	s_addk_i32 s4, 0x100
	s_addk_i32 s5, 0x100
	s_cmp_ge_i32 s11, s58
	s_cbranch_scc0 .LBB0_926

; #define PG8_STAGE(bufoff, rs_, soff_, voff) do { _Pragma("unroll") for (int _i = 0; _i < 2; ++_i) \
;         __builtin_amdgcn_raw_ptr_buffer_load_lds(rs_, (LAS void*)(lds + (bufoff) + ldsw + _i * 8192), 16, (int)(voff)[_i], (int)(soff_), 0, 0); } while (0)
; #define PG8_LDA(dst, b, h) do { _Pragma("unroll") for (int m = 0; m < 4; ++m) dst[m] = PG8_LD2(lds + PG8_SA(b, h) + aoff + m * 2048); } while (0)
; #define PG8_LDB(dst, b, h) do { _Pragma("unroll") for (int n = 0; n < 2; ++n) dst[n] = PG8_LD2(lds + PG8_SB(b, h) + boff + n * 2048); } while (0)
; #define PG8_WAIT_V(n) asm volatile("s_waitcnt vmcnt(" #n ")" ::: "memory")
; #define PG8_WAIT_L(n) asm volatile("s_waitcnt lgkmcnt(" #n ")" ::: "memory")
; #define PG8_BAR __builtin_amdgcn_s_barrier()
; #define PG8_SCHED __builtin_amdgcn_sched_barrier(0)
; template <class Epi, class Sched, bool ALIGN_EPI = false, bool SP2 = false, bool FP8 = false>
; __device__ __forceinline__ void gemm_phase(LAS unsigned char* lds, const Gemm g, const Sched& S, const Epi& E, int wbase) {
;     ...
;         for (int t = 0; t < nt; t += 2) {
;             const bool last = (t == nt - 2);
;             const unsigned a1 = cA + (unsigned)(t + 1) * kstep;
;             const unsigned a2 = last ? nA : cA + (unsigned)(t + 2) * kstep, b2 = last ? nB : cB + (unsigned)(t + 2) * kstep; const rsrc_t rA2 = (Sched::TWO && last) ? rAn : rAc, rB2 = (Sched::TWO && last) ? rBn : rBc;
;             const unsigned a3 = a2 + kstep, b3 = b2 + kstep;
;             if (last && has_next) S.a_ready(nxt);
;             if constexpr (SP2) {
;             PG8_LDB(B0, 0, 0); PG8_LDB(B1, 0, 1); PG8_SCHED; PG8_LDA(At, 0, 0); PG8_STAGE(PG8_SA(1, 1), rAc, a1 + hstep, voffA);
;             PG8_WAIT_V(8); PG8_WAIT_L(0); PG8_BAR; PG8_MMA(0, 0, At, B0); PG8_MMA(0, 1, At, B1); PG8_BAR; PG8_SCHED;
;             PG8_LDA(At, 0, 1); PG8_STAGE(PG8_SB(0, 0), rB2, b2, voffB); PG8_STAGE(PG8_SB(0, 1), rB2, b2 + hstep, voffB); PG8_STAGE(PG8_SA(0, 0), rA2, a2, voffA);
;             PG8_WAIT_V(8); PG8_WAIT_L(0); PG8_BAR; PG8_MMA(1, 0, At, B0); PG8_MMA(1, 1, At, B1); PG8_BAR; PG8_SCHED;
.LBB0_1002:
	s_lshl_b32 s81, s80, 19
	s_andn2_b64 vcc, exec, s[24:25]
	s_lshl_b32 s82, s79, 19
	s_cbranch_vccnz .LBB0_1058
	s_and_b64 s[2:3], s[28:29], exec
	s_waitcnt vmcnt(37)
	s_waitcnt vmcnt(36)
	s_waitcnt vmcnt(35)
	s_waitcnt vmcnt(32)
	s_waitcnt vmcnt(31)
	s_waitcnt vmcnt(27)
	s_waitcnt vmcnt(26)
	s_waitcnt vmcnt(24)
	s_waitcnt vmcnt(23)
	s_cselect_b32 s2, s81, s4
	s_cselect_b32 s3, s82, s5
	s_addk_i32 s4, 0x80
	s_addk_i32 s5, 0x100
	s_mov_b32 s11, 0
	s_waitcnt vmcnt(0)
	v_add_u32_e32 v132, 0x10000, v180
	v_add_u32_e32 v156, 0x14000, v180
	ds_read_b128 v[96:99], v132
	ds_read_b128 v[108:111], v132 offset:1024
	ds_read_b128 v[120:123], v132 offset:2048
	ds_read_b128 v[132:135], v132 offset:3072
	ds_read_b128 v[136:139], v156
	ds_read_b128 v[144:147], v156 offset:1024
	ds_read_b128 v[152:155], v156 offset:2048
	ds_read_b128 v[156:159], v156 offset:3072
	s_add_i32 s14, s4, 0x80
	s_cmp_eq_u32 s62, s11
	s_cselect_b32 s66, s2, s14
	s_cselect_b32 s55, s3, s5
	s_or_b32 s54, s66, 0x80
	s_add_i32 s14, s33, s4
	s_mov_b32 m0, s63
	ds_read_b128 v[160:163], v181
	ds_read_b128 v[164:167], v181 offset:1024
	ds_read_b128 v[168:171], v181 offset:2048
	ds_read_b128 v[182:185], v181 offset:3072
	ds_read_b128 v[186:189], v181 offset:4096
	ds_read_b128 v[190:193], v181 offset:5120
	ds_read_b128 v[194:197], v181 offset:6144
	ds_read_b128 v[198:201], v181 offset:7168
	buffer_load_dwordx4 v174, s[36:39], s14 offen lds
	s_mov_b32 m0, s65
	s_nop 0
	buffer_load_dwordx4 v176, s[36:39], s14 offen lds
	s_waitcnt vmcnt(8)
	s_waitcnt lgkmcnt(0)
	s_barrier
	s_setprio 1
	v_mfma_f32_16x16x32_bf16 v[148:151], v[96:99], v[160:163], 0
	v_mfma_f32_16x16x32_bf16 v[140:143], v[120:123], v[160:163], 0
	v_mfma_f32_16x16x32_bf16 v[116:119], v[96:99], v[168:171], 0
	v_mfma_f32_16x16x32_bf16 v[112:115], v[120:123], v[168:171], 0
	v_mfma_f32_16x16x32_bf16 v[92:95], v[96:99], v[186:189], 0
	v_mfma_f32_16x16x32_bf16 v[88:91], v[120:123], v[186:189], 0
	v_mfma_f32_16x16x32_bf16 v[76:79], v[96:99], v[194:197], 0
	v_mfma_f32_16x16x32_bf16 v[72:75], v[120:123], v[194:197], 0
	v_mfma_f32_16x16x32_bf16 v[148:151], v[108:111], v[164:167], v[148:151]
	v_mfma_f32_16x16x32_bf16 v[140:143], v[132:135], v[164:167], v[140:143]
	v_mfma_f32_16x16x32_bf16 v[116:119], v[108:111], v[182:185], v[116:119]
	v_mfma_f32_16x16x32_bf16 v[112:115], v[132:135], v[182:185], v[112:115]
	v_mfma_f32_16x16x32_bf16 v[92:95], v[108:111], v[190:193], v[92:95]
	v_mfma_f32_16x16x32_bf16 v[88:91], v[132:135], v[190:193], v[88:91]
	v_mfma_f32_16x16x32_bf16 v[76:79], v[108:111], v[198:201], v[76:79]
	v_mfma_f32_16x16x32_bf16 v[72:75], v[132:135], v[198:201], v[72:75]
	v_mfma_f32_16x16x32_bf16 v[128:131], v[136:139], v[160:163], 0
	v_mfma_f32_16x16x32_bf16 v[124:127], v[152:155], v[160:163], 0
	v_mfma_f32_16x16x32_bf16 v[104:107], v[136:139], v[168:171], 0
	v_mfma_f32_16x16x32_bf16 v[100:103], v[152:155], v[168:171], 0
	v_mfma_f32_16x16x32_bf16 v[84:87], v[136:139], v[186:189], 0
	v_mfma_f32_16x16x32_bf16 v[80:83], v[152:155], v[186:189], 0
	v_mfma_f32_16x16x32_bf16 v[68:71], v[136:139], v[194:197], 0
	v_mfma_f32_16x16x32_bf16 v[64:67], v[152:155], v[194:197], 0
	v_mfma_f32_16x16x32_bf16 v[128:131], v[144:147], v[164:167], v[128:131]
	v_mfma_f32_16x16x32_bf16 v[124:127], v[156:159], v[164:167], v[124:127]
	v_mfma_f32_16x16x32_bf16 v[104:107], v[144:147], v[182:185], v[104:107]
	v_mfma_f32_16x16x32_bf16 v[100:103], v[156:159], v[182:185], v[100:103]
	v_mfma_f32_16x16x32_bf16 v[84:87], v[144:147], v[190:193], v[84:87]
	v_mfma_f32_16x16x32_bf16 v[80:83], v[156:159], v[190:193], v[80:83]
	v_mfma_f32_16x16x32_bf16 v[68:71], v[144:147], v[198:201], v[68:71]
	v_mfma_f32_16x16x32_bf16 v[64:67], v[156:159], v[198:201], v[64:67]
	s_setprio 0
	s_barrier
	s_mov_b32 m0, s35
	s_mov_b32 s14, s38
	s_mov_b32 s15, s39
	buffer_load_dwordx4 v175, s[12:15], s55 offen lds
	s_mov_b32 m0, s41
	ds_read_b128 v[160:163], v181 offset:16384
	s_add_i32 s67, s55, s33
	buffer_load_dwordx4 v177, s[12:15], s55 offen lds
	s_mov_b32 m0, s42
	ds_read_b128 v[164:167], v181 offset:17408
	buffer_load_dwordx4 v175, s[12:15], s67 offen lds
	s_mov_b32 m0, s34
	ds_read_b128 v[168:171], v181 offset:18432
	buffer_load_dwordx4 v174, s[36:39], s66 offen lds
	s_mov_b32 m0, s44
	ds_read_b128 v[182:185], v181 offset:19456
	buffer_load_dwordx4 v176, s[36:39], s66 offen lds
	ds_read_b128 v[186:189], v181 offset:20480
	ds_read_b128 v[190:193], v181 offset:21504
	ds_read_b128 v[194:197], v181 offset:22528
	ds_read_b128 v[198:201], v181 offset:23552
	s_waitcnt vmcnt(7)
	s_waitcnt lgkmcnt(0)
	s_barrier
	s_setprio 1
	v_mfma_f32_16x16x32_bf16 v[60:63], v[96:99], v[160:163], 0
	v_mfma_f32_16x16x32_bf16 v[56:59], v[120:123], v[160:163], 0
	v_mfma_f32_16x16x32_bf16 v[44:47], v[96:99], v[168:171], 0
	v_mfma_f32_16x16x32_bf16 v[40:43], v[120:123], v[168:171], 0
	v_mfma_f32_16x16x32_bf16 v[28:31], v[96:99], v[186:189], 0
	v_mfma_f32_16x16x32_bf16 v[24:27], v[120:123], v[186:189], 0
	v_mfma_f32_16x16x32_bf16 v[12:15], v[96:99], v[194:197], 0
	v_mfma_f32_16x16x32_bf16 v[8:11], v[120:123], v[194:197], 0
	v_mfma_f32_16x16x32_bf16 v[60:63], v[108:111], v[164:167], v[60:63]
	v_mfma_f32_16x16x32_bf16 v[56:59], v[132:135], v[164:167], v[56:59]
	v_mfma_f32_16x16x32_bf16 v[44:47], v[108:111], v[182:185], v[44:47]
	v_mfma_f32_16x16x32_bf16 v[40:43], v[132:135], v[182:185], v[40:43]
	v_mfma_f32_16x16x32_bf16 v[28:31], v[108:111], v[190:193], v[28:31]
	v_mfma_f32_16x16x32_bf16 v[24:27], v[132:135], v[190:193], v[24:27]
	v_mfma_f32_16x16x32_bf16 v[12:15], v[108:111], v[198:201], v[12:15]
	v_mfma_f32_16x16x32_bf16 v[8:11], v[132:135], v[198:201], v[8:11]
	v_mfma_f32_16x16x32_bf16 v[52:55], v[136:139], v[160:163], 0
	v_mfma_f32_16x16x32_bf16 v[48:51], v[152:155], v[160:163], 0
	v_mfma_f32_16x16x32_bf16 v[36:39], v[136:139], v[168:171], 0
	v_mfma_f32_16x16x32_bf16 v[32:35], v[152:155], v[168:171], 0
	v_mfma_f32_16x16x32_bf16 v[20:23], v[136:139], v[186:189], 0
	v_mfma_f32_16x16x32_bf16 v[16:19], v[152:155], v[186:189], 0
	v_mfma_f32_16x16x32_bf16 v[4:7], v[136:139], v[194:197], 0
	v_mfma_f32_16x16x32_bf16 v[0:3], v[152:155], v[194:197], 0
	v_mfma_f32_16x16x32_bf16 v[52:55], v[144:147], v[164:167], v[52:55]
	v_mfma_f32_16x16x32_bf16 v[48:51], v[156:159], v[164:167], v[48:51]
	v_mfma_f32_16x16x32_bf16 v[36:39], v[144:147], v[182:185], v[36:39]
	v_mfma_f32_16x16x32_bf16 v[32:35], v[156:159], v[182:185], v[32:35]
	v_mfma_f32_16x16x32_bf16 v[20:23], v[144:147], v[190:193], v[20:23]
	v_mfma_f32_16x16x32_bf16 v[16:19], v[156:159], v[190:193], v[16:19]
	v_mfma_f32_16x16x32_bf16 v[4:7], v[144:147], v[198:201], v[4:7]
	v_mfma_f32_16x16x32_bf16 v[0:3], v[156:159], v[198:201], v[0:3]
	s_setprio 0
	s_barrier
; #define PG8_STAGE(bufoff, rs_, soff_, voff) do { _Pragma("unroll") for (int _i = 0; _i < 2; ++_i) \
;         __builtin_amdgcn_raw_ptr_buffer_load_lds(rs_, (LAS void*)(lds + (bufoff) + ldsw + _i * 8192), 16, (int)(voff)[_i], (int)(soff_), 0, 0); } while (0)
; #define PG8_LDA(dst, b, h) do { _Pragma("unroll") for (int m = 0; m < 4; ++m) dst[m] = PG8_LD2(lds + PG8_SA(b, h) + aoff + m * 2048); } while (0)
; #define PG8_LDB(dst, b, h) do { _Pragma("unroll") for (int n = 0; n < 2; ++n) dst[n] = PG8_LD2(lds + PG8_SB(b, h) + boff + n * 2048); } while (0)
; #define PG8_WAIT_V(n) asm volatile("s_waitcnt vmcnt(" #n ")" ::: "memory")
; #define PG8_WAIT_L(n) asm volatile("s_waitcnt lgkmcnt(" #n ")" ::: "memory")
; #define PG8_BAR __builtin_amdgcn_s_barrier()
; #define PG8_SCHED __builtin_amdgcn_sched_barrier(0)
; template <class Epi, class Sched, bool ALIGN_EPI = false, bool SP2 = false, bool FP8 = false>
; __device__ __forceinline__ void gemm_phase(LAS unsigned char* lds, const Gemm g, const Sched& S, const Epi& E, int wbase) {
;     ...
;             PG8_LDB(B0, 1, 0); PG8_LDB(B1, 1, 1); PG8_SCHED; PG8_LDA(At, 1, 0); PG8_STAGE(PG8_SA(0, 1), rA2, a2 + hstep, voffA);
;             PG8_WAIT_V(8); PG8_WAIT_L(0); PG8_BAR; PG8_MMA(0, 0, At, B0); PG8_MMA(0, 1, At, B1); PG8_BAR; PG8_SCHED;
;             PG8_LDA(At, 1, 1); PG8_STAGE(PG8_SB(1, 0), rB2, b3, voffB); PG8_STAGE(PG8_SB(1, 1), rB2, b3 + hstep, voffB); PG8_STAGE(PG8_SA(1, 0), rA2, a3, voffA);
;             PG8_WAIT_V(8); PG8_WAIT_L(0); PG8_BAR; PG8_MMA(1, 0, At, B0); PG8_MMA(1, 1, At, B1); PG8_BAR; PG8_SCHED;
	s_mov_b32 m0, s43
	s_nop 0
	buffer_load_dwordx4 v177, s[12:15], s67 offen lds
	v_add_u32_e32 v132, 0x18000, v180
	v_add_u32_e32 v156, 0x1c000, v180
	ds_read_b128 v[96:99], v132
	ds_read_b128 v[108:111], v132 offset:1024
	ds_read_b128 v[120:123], v132 offset:2048
	ds_read_b128 v[132:135], v132 offset:3072
	ds_read_b128 v[136:139], v156
	ds_read_b128 v[144:147], v156 offset:1024
	ds_read_b128 v[152:155], v156 offset:2048
	ds_read_b128 v[156:159], v156 offset:3072
	s_add_i32 s66, s66, s33
	s_mov_b32 m0, s45
	ds_read_b128 v[160:163], v181 offset:32768
	ds_read_b128 v[164:167], v181 offset:33792
	ds_read_b128 v[168:171], v181 offset:34816
	ds_read_b128 v[182:185], v181 offset:35840
	ds_read_b128 v[186:189], v181 offset:36864
	ds_read_b128 v[190:193], v181 offset:37888
	ds_read_b128 v[194:197], v181 offset:38912
	ds_read_b128 v[198:201], v181 offset:39936
	buffer_load_dwordx4 v174, s[36:39], s66 offen lds
	s_mov_b32 m0, s46
	s_nop 0
	buffer_load_dwordx4 v176, s[36:39], s66 offen lds
	s_waitcnt vmcnt(8)
	s_waitcnt lgkmcnt(0)
	s_barrier
	s_setprio 1
	v_mfma_f32_16x16x32_bf16 v[148:151], v[96:99], v[160:163], v[148:151]
	v_mfma_f32_16x16x32_bf16 v[140:143], v[120:123], v[160:163], v[140:143]
	v_mfma_f32_16x16x32_bf16 v[116:119], v[96:99], v[168:171], v[116:119]
	v_mfma_f32_16x16x32_bf16 v[112:115], v[120:123], v[168:171], v[112:115]
	v_mfma_f32_16x16x32_bf16 v[92:95], v[96:99], v[186:189], v[92:95]
	v_mfma_f32_16x16x32_bf16 v[88:91], v[120:123], v[186:189], v[88:91]
	v_mfma_f32_16x16x32_bf16 v[76:79], v[96:99], v[194:197], v[76:79]
	v_mfma_f32_16x16x32_bf16 v[72:75], v[120:123], v[194:197], v[72:75]
	v_mfma_f32_16x16x32_bf16 v[148:151], v[108:111], v[164:167], v[148:151]
	v_mfma_f32_16x16x32_bf16 v[140:143], v[132:135], v[164:167], v[140:143]
	v_mfma_f32_16x16x32_bf16 v[116:119], v[108:111], v[182:185], v[116:119]
	v_mfma_f32_16x16x32_bf16 v[112:115], v[132:135], v[182:185], v[112:115]
	v_mfma_f32_16x16x32_bf16 v[92:95], v[108:111], v[190:193], v[92:95]
	v_mfma_f32_16x16x32_bf16 v[88:91], v[132:135], v[190:193], v[88:91]
	v_mfma_f32_16x16x32_bf16 v[76:79], v[108:111], v[198:201], v[76:79]
	v_mfma_f32_16x16x32_bf16 v[72:75], v[132:135], v[198:201], v[72:75]
	v_mfma_f32_16x16x32_bf16 v[128:131], v[136:139], v[160:163], v[128:131]
	v_mfma_f32_16x16x32_bf16 v[124:127], v[152:155], v[160:163], v[124:127]
	v_mfma_f32_16x16x32_bf16 v[104:107], v[136:139], v[168:171], v[104:107]
	v_mfma_f32_16x16x32_bf16 v[100:103], v[152:155], v[168:171], v[100:103]
	v_mfma_f32_16x16x32_bf16 v[84:87], v[136:139], v[186:189], v[84:87]
	v_mfma_f32_16x16x32_bf16 v[80:83], v[152:155], v[186:189], v[80:83]
	v_mfma_f32_16x16x32_bf16 v[68:71], v[136:139], v[194:197], v[68:71]
	v_mfma_f32_16x16x32_bf16 v[64:67], v[152:155], v[194:197], v[64:67]
	v_mfma_f32_16x16x32_bf16 v[128:131], v[144:147], v[164:167], v[128:131]
	v_mfma_f32_16x16x32_bf16 v[124:127], v[156:159], v[164:167], v[124:127]
	v_mfma_f32_16x16x32_bf16 v[104:107], v[144:147], v[182:185], v[104:107]
	v_mfma_f32_16x16x32_bf16 v[100:103], v[156:159], v[182:185], v[100:103]
	v_mfma_f32_16x16x32_bf16 v[84:87], v[144:147], v[190:193], v[84:87]
	v_mfma_f32_16x16x32_bf16 v[80:83], v[156:159], v[190:193], v[80:83]
	v_mfma_f32_16x16x32_bf16 v[68:71], v[144:147], v[198:201], v[68:71]
	v_mfma_f32_16x16x32_bf16 v[64:67], v[156:159], v[198:201], v[64:67]
	s_setprio 0
	s_barrier
	s_mov_b32 m0, s47
	s_bitset1_b32 s55, 7
	buffer_load_dwordx4 v175, s[12:15], s55 offen lds
	s_mov_b32 m0, s48
	ds_read_b128 v[160:163], v181 offset:49152
	buffer_load_dwordx4 v177, s[12:15], s55 offen lds
	s_add_i32 s55, s55, s33
	s_mov_b32 m0, s56
	ds_read_b128 v[164:167], v181 offset:50176
	buffer_load_dwordx4 v175, s[12:15], s55 offen lds
	s_mov_b32 m0, s57
	ds_read_b128 v[168:171], v181 offset:51200
	buffer_load_dwordx4 v177, s[12:15], s55 offen lds
	s_mov_b32 m0, s52
	ds_read_b128 v[182:185], v181 offset:52224
	buffer_load_dwordx4 v174, s[36:39], s54 offen lds
	s_mov_b32 m0, s53
	ds_read_b128 v[186:189], v181 offset:53248
	buffer_load_dwordx4 v176, s[36:39], s54 offen lds
	ds_read_b128 v[190:193], v181 offset:54272
	ds_read_b128 v[194:197], v181 offset:55296
	ds_read_b128 v[198:201], v181 offset:56320
	s_waitcnt vmcnt(8)
	s_waitcnt lgkmcnt(0)
	s_barrier
	s_setprio 1
	v_mfma_f32_16x16x32_bf16 v[60:63], v[96:99], v[160:163], v[60:63]
	v_mfma_f32_16x16x32_bf16 v[56:59], v[120:123], v[160:163], v[56:59]
	v_mfma_f32_16x16x32_bf16 v[44:47], v[96:99], v[168:171], v[44:47]
	v_mfma_f32_16x16x32_bf16 v[40:43], v[120:123], v[168:171], v[40:43]
	v_mfma_f32_16x16x32_bf16 v[28:31], v[96:99], v[186:189], v[28:31]
	v_mfma_f32_16x16x32_bf16 v[24:27], v[120:123], v[186:189], v[24:27]
	v_mfma_f32_16x16x32_bf16 v[12:15], v[96:99], v[194:197], v[12:15]
	v_mfma_f32_16x16x32_bf16 v[8:11], v[120:123], v[194:197], v[8:11]
	v_mfma_f32_16x16x32_bf16 v[60:63], v[108:111], v[164:167], v[60:63]
	v_mfma_f32_16x16x32_bf16 v[56:59], v[132:135], v[164:167], v[56:59]
	v_mfma_f32_16x16x32_bf16 v[44:47], v[108:111], v[182:185], v[44:47]
	v_mfma_f32_16x16x32_bf16 v[40:43], v[132:135], v[182:185], v[40:43]
	v_mfma_f32_16x16x32_bf16 v[28:31], v[108:111], v[190:193], v[28:31]
	v_mfma_f32_16x16x32_bf16 v[24:27], v[132:135], v[190:193], v[24:27]
	v_mfma_f32_16x16x32_bf16 v[12:15], v[108:111], v[198:201], v[12:15]
	v_mfma_f32_16x16x32_bf16 v[8:11], v[132:135], v[198:201], v[8:11]
	v_mfma_f32_16x16x32_bf16 v[52:55], v[136:139], v[160:163], v[52:55]
	v_mfma_f32_16x16x32_bf16 v[48:51], v[152:155], v[160:163], v[48:51]
	v_mfma_f32_16x16x32_bf16 v[36:39], v[136:139], v[168:171], v[36:39]
	v_mfma_f32_16x16x32_bf16 v[32:35], v[152:155], v[168:171], v[32:35]
	v_mfma_f32_16x16x32_bf16 v[20:23], v[136:139], v[186:189], v[20:23]
	v_mfma_f32_16x16x32_bf16 v[16:19], v[152:155], v[186:189], v[16:19]
	v_mfma_f32_16x16x32_bf16 v[4:7], v[136:139], v[194:197], v[4:7]
	v_mfma_f32_16x16x32_bf16 v[0:3], v[152:155], v[194:197], v[0:3]
	v_mfma_f32_16x16x32_bf16 v[52:55], v[144:147], v[164:167], v[52:55]
	v_mfma_f32_16x16x32_bf16 v[48:51], v[156:159], v[164:167], v[48:51]
	v_mfma_f32_16x16x32_bf16 v[36:39], v[144:147], v[182:185], v[36:39]
	v_mfma_f32_16x16x32_bf16 v[32:35], v[156:159], v[182:185], v[32:35]
	v_mfma_f32_16x16x32_bf16 v[20:23], v[144:147], v[190:193], v[20:23]
	v_mfma_f32_16x16x32_bf16 v[16:19], v[156:159], v[190:193], v[16:19]
	v_mfma_f32_16x16x32_bf16 v[4:7], v[144:147], v[198:201], v[4:7]
	v_mfma_f32_16x16x32_bf16 v[0:3], v[156:159], v[198:201], v[0:3]
	s_setprio 0
	s_barrier
	s_add_i32 s11, s11, 2
	s_addk_i32 s4, 0x100
	s_addk_i32 s5, 0x100
	s_cmp_ge_i32 s11, s60
	s_cbranch_scc0 .LBB0_1004
	s_branch .Lzp_after_1004
; #define PG8_STAGE(bufoff, rs_, soff_, voff) do { _Pragma("unroll") for (int _i = 0; _i < 2; ++_i) \
;         __builtin_amdgcn_raw_ptr_buffer_load_lds(rs_, (LAS void*)(lds + (bufoff) + ldsw + _i * 8192), 16, (int)(voff)[_i], (int)(soff_), 0, 0); } while (0)
; #define PG8_LDA(dst, b, h) do { _Pragma("unroll") for (int m = 0; m < 4; ++m) dst[m] = PG8_LD2(lds + PG8_SA(b, h) + aoff + m * 2048); } while (0)
; #define PG8_LDB(dst, b, h) do { _Pragma("unroll") for (int n = 0; n < 2; ++n) dst[n] = PG8_LD2(lds + PG8_SB(b, h) + boff + n * 2048); } while (0)
; #define PG8_WAIT_V(n) asm volatile("s_waitcnt vmcnt(" #n ")" ::: "memory")
; #define PG8_WAIT_L(n) asm volatile("s_waitcnt lgkmcnt(" #n ")" ::: "memory")
; #define PG8_BAR __builtin_amdgcn_s_barrier()
; #define PG8_SCHED __builtin_amdgcn_sched_barrier(0)
; template <class Epi, class Sched, bool ALIGN_EPI = false, bool SP2 = false, bool FP8 = false>
; __device__ __forceinline__ void gemm_phase(LAS unsigned char* lds, const Gemm g, const Sched& S, const Epi& E, int wbase) {
;     ...
;             PG8_LDB(B0, 0, 0); PG8_LDB(B1, 0, 1); PG8_SCHED; PG8_LDA(At, 0, 0); PG8_STAGE(PG8_SA(1, 1), rAc, a1 + hstep, voffA);
;             PG8_WAIT_V(8); PG8_WAIT_L(0); PG8_BAR; PG8_MMA(0, 0, At, B0); PG8_MMA(0, 1, At, B1); PG8_BAR; PG8_SCHED;
;             PG8_LDA(At, 0, 1); PG8_STAGE(PG8_SB(0, 0), rB2, b2, voffB); PG8_STAGE(PG8_SB(0, 1), rB2, b2 + hstep, voffB); PG8_STAGE(PG8_SA(0, 0), rA2, a2, voffA);
;             PG8_WAIT_V(8); PG8_WAIT_L(0); PG8_BAR; PG8_MMA(1, 0, At, B0); PG8_MMA(1, 1, At, B1); PG8_BAR; PG8_SCHED;
.LBB0_1004:
	v_add_u32_e32 v132, 0x10000, v180
	v_add_u32_e32 v156, 0x14000, v180
	ds_read_b128 v[96:99], v132
	ds_read_b128 v[108:111], v132 offset:1024
	ds_read_b128 v[120:123], v132 offset:2048
	ds_read_b128 v[132:135], v132 offset:3072
	ds_read_b128 v[136:139], v156
	ds_read_b128 v[144:147], v156 offset:1024
	ds_read_b128 v[152:155], v156 offset:2048
	ds_read_b128 v[156:159], v156 offset:3072
	s_add_i32 s14, s4, 0x80
	s_cmp_eq_u32 s62, s11
	s_cselect_b32 s66, s2, s14
	s_cselect_b32 s55, s3, s5
	s_or_b32 s54, s66, 0x80
	s_add_i32 s14, s33, s4
	s_mov_b32 m0, s63
	ds_read_b128 v[160:163], v181
	ds_read_b128 v[164:167], v181 offset:1024
	ds_read_b128 v[168:171], v181 offset:2048
	ds_read_b128 v[182:185], v181 offset:3072
	ds_read_b128 v[186:189], v181 offset:4096
	ds_read_b128 v[190:193], v181 offset:5120
	ds_read_b128 v[194:197], v181 offset:6144
	ds_read_b128 v[198:201], v181 offset:7168
	buffer_load_dwordx4 v174, s[36:39], s14 offen lds
	s_mov_b32 m0, s65
	s_nop 0
	buffer_load_dwordx4 v176, s[36:39], s14 offen lds
	s_waitcnt vmcnt(8)
	s_waitcnt lgkmcnt(0)
	s_barrier
	s_setprio 1
	v_mfma_f32_16x16x32_bf16 v[148:151], v[96:99], v[160:163], v[148:151]
	v_mfma_f32_16x16x32_bf16 v[140:143], v[120:123], v[160:163], v[140:143]
	v_mfma_f32_16x16x32_bf16 v[116:119], v[96:99], v[168:171], v[116:119]
	v_mfma_f32_16x16x32_bf16 v[112:115], v[120:123], v[168:171], v[112:115]
	v_mfma_f32_16x16x32_bf16 v[92:95], v[96:99], v[186:189], v[92:95]
	v_mfma_f32_16x16x32_bf16 v[88:91], v[120:123], v[186:189], v[88:91]
	v_mfma_f32_16x16x32_bf16 v[76:79], v[96:99], v[194:197], v[76:79]
	v_mfma_f32_16x16x32_bf16 v[72:75], v[120:123], v[194:197], v[72:75]
	v_mfma_f32_16x16x32_bf16 v[148:151], v[108:111], v[164:167], v[148:151]
	v_mfma_f32_16x16x32_bf16 v[140:143], v[132:135], v[164:167], v[140:143]
	v_mfma_f32_16x16x32_bf16 v[116:119], v[108:111], v[182:185], v[116:119]
	v_mfma_f32_16x16x32_bf16 v[112:115], v[132:135], v[182:185], v[112:115]
	v_mfma_f32_16x16x32_bf16 v[92:95], v[108:111], v[190:193], v[92:95]
	v_mfma_f32_16x16x32_bf16 v[88:91], v[132:135], v[190:193], v[88:91]
	v_mfma_f32_16x16x32_bf16 v[76:79], v[108:111], v[198:201], v[76:79]
	v_mfma_f32_16x16x32_bf16 v[72:75], v[132:135], v[198:201], v[72:75]
	v_mfma_f32_16x16x32_bf16 v[128:131], v[136:139], v[160:163], v[128:131]
	v_mfma_f32_16x16x32_bf16 v[124:127], v[152:155], v[160:163], v[124:127]
	v_mfma_f32_16x16x32_bf16 v[104:107], v[136:139], v[168:171], v[104:107]
	v_mfma_f32_16x16x32_bf16 v[100:103], v[152:155], v[168:171], v[100:103]
	v_mfma_f32_16x16x32_bf16 v[84:87], v[136:139], v[186:189], v[84:87]
	v_mfma_f32_16x16x32_bf16 v[80:83], v[152:155], v[186:189], v[80:83]
	v_mfma_f32_16x16x32_bf16 v[68:71], v[136:139], v[194:197], v[68:71]
	v_mfma_f32_16x16x32_bf16 v[64:67], v[152:155], v[194:197], v[64:67]
	v_mfma_f32_16x16x32_bf16 v[128:131], v[144:147], v[164:167], v[128:131]
	v_mfma_f32_16x16x32_bf16 v[124:127], v[156:159], v[164:167], v[124:127]
	v_mfma_f32_16x16x32_bf16 v[104:107], v[144:147], v[182:185], v[104:107]
	v_mfma_f32_16x16x32_bf16 v[100:103], v[156:159], v[182:185], v[100:103]
	v_mfma_f32_16x16x32_bf16 v[84:87], v[144:147], v[190:193], v[84:87]
	v_mfma_f32_16x16x32_bf16 v[80:83], v[156:159], v[190:193], v[80:83]
	v_mfma_f32_16x16x32_bf16 v[68:71], v[144:147], v[198:201], v[68:71]
	v_mfma_f32_16x16x32_bf16 v[64:67], v[156:159], v[198:201], v[64:67]
	s_setprio 0
	s_barrier
	s_mov_b32 m0, s35
	s_mov_b32 s14, s38
	s_mov_b32 s15, s39
	buffer_load_dwordx4 v175, s[12:15], s55 offen lds
	s_mov_b32 m0, s41
	ds_read_b128 v[160:163], v181 offset:16384
	s_add_i32 s67, s55, s33
	buffer_load_dwordx4 v177, s[12:15], s55 offen lds
	s_mov_b32 m0, s42
	ds_read_b128 v[164:167], v181 offset:17408
	buffer_load_dwordx4 v175, s[12:15], s67 offen lds
	s_mov_b32 m0, s34
	ds_read_b128 v[168:171], v181 offset:18432
	buffer_load_dwordx4 v174, s[36:39], s66 offen lds
	s_mov_b32 m0, s44
	ds_read_b128 v[182:185], v181 offset:19456
	buffer_load_dwordx4 v176, s[36:39], s66 offen lds
	ds_read_b128 v[186:189], v181 offset:20480
	ds_read_b128 v[190:193], v181 offset:21504
	ds_read_b128 v[194:197], v181 offset:22528
	ds_read_b128 v[198:201], v181 offset:23552
	s_waitcnt vmcnt(7)
	s_waitcnt lgkmcnt(0)
	s_barrier
	s_setprio 1
	v_mfma_f32_16x16x32_bf16 v[60:63], v[96:99], v[160:163], v[60:63]
	v_mfma_f32_16x16x32_bf16 v[56:59], v[120:123], v[160:163], v[56:59]
	v_mfma_f32_16x16x32_bf16 v[44:47], v[96:99], v[168:171], v[44:47]
	v_mfma_f32_16x16x32_bf16 v[40:43], v[120:123], v[168:171], v[40:43]
	v_mfma_f32_16x16x32_bf16 v[28:31], v[96:99], v[186:189], v[28:31]
	v_mfma_f32_16x16x32_bf16 v[24:27], v[120:123], v[186:189], v[24:27]
	v_mfma_f32_16x16x32_bf16 v[12:15], v[96:99], v[194:197], v[12:15]
	v_mfma_f32_16x16x32_bf16 v[8:11], v[120:123], v[194:197], v[8:11]
	v_mfma_f32_16x16x32_bf16 v[60:63], v[108:111], v[164:167], v[60:63]
	v_mfma_f32_16x16x32_bf16 v[56:59], v[132:135], v[164:167], v[56:59]
	v_mfma_f32_16x16x32_bf16 v[44:47], v[108:111], v[182:185], v[44:47]
	v_mfma_f32_16x16x32_bf16 v[40:43], v[132:135], v[182:185], v[40:43]
	v_mfma_f32_16x16x32_bf16 v[28:31], v[108:111], v[190:193], v[28:31]
	v_mfma_f32_16x16x32_bf16 v[24:27], v[132:135], v[190:193], v[24:27]
	v_mfma_f32_16x16x32_bf16 v[12:15], v[108:111], v[198:201], v[12:15]
	v_mfma_f32_16x16x32_bf16 v[8:11], v[132:135], v[198:201], v[8:11]
	v_mfma_f32_16x16x32_bf16 v[52:55], v[136:139], v[160:163], v[52:55]
	v_mfma_f32_16x16x32_bf16 v[48:51], v[152:155], v[160:163], v[48:51]
	v_mfma_f32_16x16x32_bf16 v[36:39], v[136:139], v[168:171], v[36:39]
	v_mfma_f32_16x16x32_bf16 v[32:35], v[152:155], v[168:171], v[32:35]
	v_mfma_f32_16x16x32_bf16 v[20:23], v[136:139], v[186:189], v[20:23]
	v_mfma_f32_16x16x32_bf16 v[16:19], v[152:155], v[186:189], v[16:19]
	v_mfma_f32_16x16x32_bf16 v[4:7], v[136:139], v[194:197], v[4:7]
	v_mfma_f32_16x16x32_bf16 v[0:3], v[152:155], v[194:197], v[0:3]
	v_mfma_f32_16x16x32_bf16 v[52:55], v[144:147], v[164:167], v[52:55]
	v_mfma_f32_16x16x32_bf16 v[48:51], v[156:159], v[164:167], v[48:51]
	v_mfma_f32_16x16x32_bf16 v[36:39], v[144:147], v[182:185], v[36:39]
	v_mfma_f32_16x16x32_bf16 v[32:35], v[156:159], v[182:185], v[32:35]
	v_mfma_f32_16x16x32_bf16 v[20:23], v[144:147], v[190:193], v[20:23]
	v_mfma_f32_16x16x32_bf16 v[16:19], v[156:159], v[190:193], v[16:19]
	v_mfma_f32_16x16x32_bf16 v[4:7], v[144:147], v[198:201], v[4:7]
	v_mfma_f32_16x16x32_bf16 v[0:3], v[156:159], v[198:201], v[0:3]
	s_setprio 0
	s_barrier
; #define PG8_STAGE(bufoff, rs_, soff_, voff) do { _Pragma("unroll") for (int _i = 0; _i < 2; ++_i) \
;         __builtin_amdgcn_raw_ptr_buffer_load_lds(rs_, (LAS void*)(lds + (bufoff) + ldsw + _i * 8192), 16, (int)(voff)[_i], (int)(soff_), 0, 0); } while (0)
; #define PG8_LDA(dst, b, h) do { _Pragma("unroll") for (int m = 0; m < 4; ++m) dst[m] = PG8_LD2(lds + PG8_SA(b, h) + aoff + m * 2048); } while (0)
; #define PG8_LDB(dst, b, h) do { _Pragma("unroll") for (int n = 0; n < 2; ++n) dst[n] = PG8_LD2(lds + PG8_SB(b, h) + boff + n * 2048); } while (0)
; #define PG8_WAIT_V(n) asm volatile("s_waitcnt vmcnt(" #n ")" ::: "memory")
; #define PG8_WAIT_L(n) asm volatile("s_waitcnt lgkmcnt(" #n ")" ::: "memory")
; #define PG8_BAR __builtin_amdgcn_s_barrier()
; #define PG8_SCHED __builtin_amdgcn_sched_barrier(0)
; template <class Epi, class Sched, bool ALIGN_EPI = false, bool SP2 = false, bool FP8 = false>
; __device__ __forceinline__ void gemm_phase(LAS unsigned char* lds, const Gemm g, const Sched& S, const Epi& E, int wbase) {
;     ...
;             PG8_LDB(B0, 1, 0); PG8_LDB(B1, 1, 1); PG8_SCHED; PG8_LDA(At, 1, 0); PG8_STAGE(PG8_SA(0, 1), rA2, a2 + hstep, voffA);
;             PG8_WAIT_V(8); PG8_WAIT_L(0); PG8_BAR; PG8_MMA(0, 0, At, B0); PG8_MMA(0, 1, At, B1); PG8_BAR; PG8_SCHED;
;             PG8_LDA(At, 1, 1); PG8_STAGE(PG8_SB(1, 0), rB2, b3, voffB); PG8_STAGE(PG8_SB(1, 1), rB2, b3 + hstep, voffB); PG8_STAGE(PG8_SA(1, 0), rA2, a3, voffA);
;             PG8_WAIT_V(8); PG8_WAIT_L(0); PG8_BAR; PG8_MMA(1, 0, At, B0); PG8_MMA(1, 1, At, B1); PG8_BAR; PG8_SCHED;
	s_mov_b32 m0, s43
	s_nop 0
	buffer_load_dwordx4 v177, s[12:15], s67 offen lds
	v_add_u32_e32 v132, 0x18000, v180
	v_add_u32_e32 v156, 0x1c000, v180
	ds_read_b128 v[96:99], v132
	ds_read_b128 v[108:111], v132 offset:1024
	ds_read_b128 v[120:123], v132 offset:2048
	ds_read_b128 v[132:135], v132 offset:3072
	ds_read_b128 v[136:139], v156
	ds_read_b128 v[144:147], v156 offset:1024
	ds_read_b128 v[152:155], v156 offset:2048
	ds_read_b128 v[156:159], v156 offset:3072
	s_add_i32 s66, s66, s33
	s_mov_b32 m0, s45
	ds_read_b128 v[160:163], v181 offset:32768
	ds_read_b128 v[164:167], v181 offset:33792
	ds_read_b128 v[168:171], v181 offset:34816
	ds_read_b128 v[182:185], v181 offset:35840
	ds_read_b128 v[186:189], v181 offset:36864
	ds_read_b128 v[190:193], v181 offset:37888
	ds_read_b128 v[194:197], v181 offset:38912
	ds_read_b128 v[198:201], v181 offset:39936
	buffer_load_dwordx4 v174, s[36:39], s66 offen lds
	s_mov_b32 m0, s46
	s_nop 0
	buffer_load_dwordx4 v176, s[36:39], s66 offen lds
	s_waitcnt vmcnt(8)
	s_waitcnt lgkmcnt(0)
	s_barrier
	s_setprio 1
	v_mfma_f32_16x16x32_bf16 v[148:151], v[96:99], v[160:163], v[148:151]
	v_mfma_f32_16x16x32_bf16 v[140:143], v[120:123], v[160:163], v[140:143]
	v_mfma_f32_16x16x32_bf16 v[116:119], v[96:99], v[168:171], v[116:119]
	v_mfma_f32_16x16x32_bf16 v[112:115], v[120:123], v[168:171], v[112:115]
	v_mfma_f32_16x16x32_bf16 v[92:95], v[96:99], v[186:189], v[92:95]
	v_mfma_f32_16x16x32_bf16 v[88:91], v[120:123], v[186:189], v[88:91]
	v_mfma_f32_16x16x32_bf16 v[76:79], v[96:99], v[194:197], v[76:79]
	v_mfma_f32_16x16x32_bf16 v[72:75], v[120:123], v[194:197], v[72:75]
	v_mfma_f32_16x16x32_bf16 v[148:151], v[108:111], v[164:167], v[148:151]
	v_mfma_f32_16x16x32_bf16 v[140:143], v[132:135], v[164:167], v[140:143]
	v_mfma_f32_16x16x32_bf16 v[116:119], v[108:111], v[182:185], v[116:119]
	v_mfma_f32_16x16x32_bf16 v[112:115], v[132:135], v[182:185], v[112:115]
	v_mfma_f32_16x16x32_bf16 v[92:95], v[108:111], v[190:193], v[92:95]
	v_mfma_f32_16x16x32_bf16 v[88:91], v[132:135], v[190:193], v[88:91]
	v_mfma_f32_16x16x32_bf16 v[76:79], v[108:111], v[198:201], v[76:79]
	v_mfma_f32_16x16x32_bf16 v[72:75], v[132:135], v[198:201], v[72:75]
	v_mfma_f32_16x16x32_bf16 v[128:131], v[136:139], v[160:163], v[128:131]
	v_mfma_f32_16x16x32_bf16 v[124:127], v[152:155], v[160:163], v[124:127]
	v_mfma_f32_16x16x32_bf16 v[104:107], v[136:139], v[168:171], v[104:107]
	v_mfma_f32_16x16x32_bf16 v[100:103], v[152:155], v[168:171], v[100:103]
	v_mfma_f32_16x16x32_bf16 v[84:87], v[136:139], v[186:189], v[84:87]
	v_mfma_f32_16x16x32_bf16 v[80:83], v[152:155], v[186:189], v[80:83]
	v_mfma_f32_16x16x32_bf16 v[68:71], v[136:139], v[194:197], v[68:71]
	v_mfma_f32_16x16x32_bf16 v[64:67], v[152:155], v[194:197], v[64:67]
	v_mfma_f32_16x16x32_bf16 v[128:131], v[144:147], v[164:167], v[128:131]
	v_mfma_f32_16x16x32_bf16 v[124:127], v[156:159], v[164:167], v[124:127]
	v_mfma_f32_16x16x32_bf16 v[104:107], v[144:147], v[182:185], v[104:107]
	v_mfma_f32_16x16x32_bf16 v[100:103], v[156:159], v[182:185], v[100:103]
	v_mfma_f32_16x16x32_bf16 v[84:87], v[144:147], v[190:193], v[84:87]
	v_mfma_f32_16x16x32_bf16 v[80:83], v[156:159], v[190:193], v[80:83]
	v_mfma_f32_16x16x32_bf16 v[68:71], v[144:147], v[198:201], v[68:71]
	v_mfma_f32_16x16x32_bf16 v[64:67], v[156:159], v[198:201], v[64:67]
	s_setprio 0
	s_barrier
	s_mov_b32 m0, s47
	s_bitset1_b32 s55, 7
	buffer_load_dwordx4 v175, s[12:15], s55 offen lds
	s_mov_b32 m0, s48
	ds_read_b128 v[160:163], v181 offset:49152
	buffer_load_dwordx4 v177, s[12:15], s55 offen lds
	s_add_i32 s55, s55, s33
	s_mov_b32 m0, s56
	ds_read_b128 v[164:167], v181 offset:50176
	buffer_load_dwordx4 v175, s[12:15], s55 offen lds
	s_mov_b32 m0, s57
	ds_read_b128 v[168:171], v181 offset:51200
	buffer_load_dwordx4 v177, s[12:15], s55 offen lds
	s_mov_b32 m0, s52
	ds_read_b128 v[182:185], v181 offset:52224
	buffer_load_dwordx4 v174, s[36:39], s54 offen lds
	s_mov_b32 m0, s53
	ds_read_b128 v[186:189], v181 offset:53248
	buffer_load_dwordx4 v176, s[36:39], s54 offen lds
	ds_read_b128 v[190:193], v181 offset:54272
	ds_read_b128 v[194:197], v181 offset:55296
	ds_read_b128 v[198:201], v181 offset:56320
	s_waitcnt vmcnt(8)
	s_waitcnt lgkmcnt(0)
	s_barrier
	s_setprio 1
	v_mfma_f32_16x16x32_bf16 v[60:63], v[96:99], v[160:163], v[60:63]
	v_mfma_f32_16x16x32_bf16 v[56:59], v[120:123], v[160:163], v[56:59]
	v_mfma_f32_16x16x32_bf16 v[44:47], v[96:99], v[168:171], v[44:47]
	v_mfma_f32_16x16x32_bf16 v[40:43], v[120:123], v[168:171], v[40:43]
	v_mfma_f32_16x16x32_bf16 v[28:31], v[96:99], v[186:189], v[28:31]
	v_mfma_f32_16x16x32_bf16 v[24:27], v[120:123], v[186:189], v[24:27]
	v_mfma_f32_16x16x32_bf16 v[12:15], v[96:99], v[194:197], v[12:15]
	v_mfma_f32_16x16x32_bf16 v[8:11], v[120:123], v[194:197], v[8:11]
	v_mfma_f32_16x16x32_bf16 v[60:63], v[108:111], v[164:167], v[60:63]
	v_mfma_f32_16x16x32_bf16 v[56:59], v[132:135], v[164:167], v[56:59]
	v_mfma_f32_16x16x32_bf16 v[44:47], v[108:111], v[182:185], v[44:47]
	v_mfma_f32_16x16x32_bf16 v[40:43], v[132:135], v[182:185], v[40:43]
	v_mfma_f32_16x16x32_bf16 v[28:31], v[108:111], v[190:193], v[28:31]
	v_mfma_f32_16x16x32_bf16 v[24:27], v[132:135], v[190:193], v[24:27]
	v_mfma_f32_16x16x32_bf16 v[12:15], v[108:111], v[198:201], v[12:15]
	v_mfma_f32_16x16x32_bf16 v[8:11], v[132:135], v[198:201], v[8:11]
	v_mfma_f32_16x16x32_bf16 v[52:55], v[136:139], v[160:163], v[52:55]
	v_mfma_f32_16x16x32_bf16 v[48:51], v[152:155], v[160:163], v[48:51]
	v_mfma_f32_16x16x32_bf16 v[36:39], v[136:139], v[168:171], v[36:39]
	v_mfma_f32_16x16x32_bf16 v[32:35], v[152:155], v[168:171], v[32:35]
	v_mfma_f32_16x16x32_bf16 v[20:23], v[136:139], v[186:189], v[20:23]
	v_mfma_f32_16x16x32_bf16 v[16:19], v[152:155], v[186:189], v[16:19]
	v_mfma_f32_16x16x32_bf16 v[4:7], v[136:139], v[194:197], v[4:7]
	v_mfma_f32_16x16x32_bf16 v[0:3], v[152:155], v[194:197], v[0:3]
	v_mfma_f32_16x16x32_bf16 v[52:55], v[144:147], v[164:167], v[52:55]
	v_mfma_f32_16x16x32_bf16 v[48:51], v[156:159], v[164:167], v[48:51]
	v_mfma_f32_16x16x32_bf16 v[36:39], v[144:147], v[182:185], v[36:39]
	v_mfma_f32_16x16x32_bf16 v[32:35], v[156:159], v[182:185], v[32:35]
	v_mfma_f32_16x16x32_bf16 v[20:23], v[144:147], v[190:193], v[20:23]
	v_mfma_f32_16x16x32_bf16 v[16:19], v[156:159], v[190:193], v[16:19]
	v_mfma_f32_16x16x32_bf16 v[4:7], v[144:147], v[198:201], v[4:7]
	v_mfma_f32_16x16x32_bf16 v[0:3], v[156:159], v[198:201], v[0:3]
	s_setprio 0
	s_barrier
	s_add_i32 s11, s11, 2
	s_addk_i32 s4, 0x100
	s_addk_i32 s5, 0x100
	s_cmp_ge_i32 s11, s60
	s_cbranch_scc0 .LBB0_1004

; #define PG8_STAGE(bufoff, rs_, soff_, voff) do { _Pragma("unroll") for (int _i = 0; _i < 2; ++_i) \
;         __builtin_amdgcn_raw_ptr_buffer_load_lds(rs_, (LAS void*)(lds + (bufoff) + ldsw + _i * 8192), 16, (int)(voff)[_i], (int)(soff_), 0, 0); } while (0)
; #define PG8_LDA(dst, b, h) do { _Pragma("unroll") for (int m = 0; m < 4; ++m) dst[m] = PG8_LD2(lds + PG8_SA(b, h) + aoff + m * 2048); } while (0)
; #define PG8_LDB(dst, b, h) do { _Pragma("unroll") for (int n = 0; n < 2; ++n) dst[n] = PG8_LD2(lds + PG8_SB(b, h) + boff + n * 2048); } while (0)
; #define PG8_WAIT_V(n) asm volatile("s_waitcnt vmcnt(" #n ")" ::: "memory")
; #define PG8_WAIT_L(n) asm volatile("s_waitcnt lgkmcnt(" #n ")" ::: "memory")
; #define PG8_BAR __builtin_amdgcn_s_barrier()
; #define PG8_SCHED __builtin_amdgcn_sched_barrier(0)
; template <class Epi, class Sched, bool ALIGN_EPI = false, bool SP2 = false, bool FP8 = false>
; __device__ __forceinline__ void gemm_phase(LAS unsigned char* lds, const Gemm g, const Sched& S, const Epi& E, int wbase) {
;     ...
;             PG8_LDB(B0, 0, 0); PG8_LDB(B1, 0, 1); PG8_SCHED; PG8_LDA(At, 0, 0); PG8_STAGE(PG8_SA(1, 1), rAc, a1 + hstep, voffA);
;             PG8_WAIT_V(8); PG8_WAIT_L(0); PG8_BAR; PG8_MMA(0, 0, At, B0); PG8_MMA(0, 1, At, B1); PG8_BAR; PG8_SCHED;
;             PG8_LDA(At, 0, 1); PG8_STAGE(PG8_SB(0, 0), rB2, b2, voffB); PG8_STAGE(PG8_SB(0, 1), rB2, b2 + hstep, voffB); PG8_STAGE(PG8_SA(0, 0), rA2, a2, voffA);
;             PG8_WAIT_V(8); PG8_WAIT_L(0); PG8_BAR; PG8_MMA(1, 0, At, B0); PG8_MMA(1, 1, At, B1); PG8_BAR; PG8_SCHED;
.LBB0_1348:
	v_add_u32_e32 v12, 0x10000, v199
	v_add_u32_e32 v28, 0x14000, v199
	ds_read_b128 v[0:3], v12
	ds_read_b128 v[4:7], v12 offset:1024
	ds_read_b128 v[8:11], v12 offset:2048
	ds_read_b128 v[12:15], v12 offset:3072
	ds_read_b128 v[16:19], v28
	ds_read_b128 v[20:23], v28 offset:1024
	ds_read_b128 v[24:27], v28 offset:2048
	ds_read_b128 v[28:31], v28 offset:3072
	s_add_i32 s6, s67, 0x80
	s_cmp_eq_u32 s65, s85
	s_cselect_b32 s54, s66, s6
	s_cselect_b64 vcc, -1, 0
	v_cndmask_b32_e32 v211, v210, v201, vcc
	s_or_b32 s78, s54, 0x80
	s_add_i32 s6, s41, s67
	s_mov_b32 m0, s76
	ds_read_b128 v[32:35], v200
	ds_read_b128 v[36:39], v200 offset:1024
	ds_read_b128 v[40:43], v200 offset:2048
	ds_read_b128 v[44:47], v200 offset:3072
	ds_read_b128 v[48:51], v200 offset:4096
	ds_read_b128 v[52:55], v200 offset:5120
	ds_read_b128 v[56:59], v200 offset:6144
	ds_read_b128 v[60:63], v200 offset:7168
	v_readfirstlane_b32 s55, v211
	s_add_i32 s20, s55, s41
	buffer_load_dwordx4 v192, s[36:39], s6 offen lds
	s_mov_b32 m0, s77
	s_nop 0
	buffer_load_dwordx4 v195, s[36:39], s6 offen lds
	s_waitcnt vmcnt(8)
	s_waitcnt lgkmcnt(0)
	s_barrier
	s_setprio 1
	v_mfma_f32_16x16x128_f8f6f4 v[184:187], v[0:7], v[32:39], v[184:187]
	v_mfma_f32_16x16x128_f8f6f4 v[188:191], v[8:15], v[32:39], v[188:191]
	v_mfma_f32_16x16x128_f8f6f4 v[168:171], v[0:7], v[40:47], v[168:171]
	v_mfma_f32_16x16x128_f8f6f4 v[172:175], v[8:15], v[40:47], v[172:175]
	v_mfma_f32_16x16x128_f8f6f4 v[152:155], v[0:7], v[48:55], v[152:155]
	v_mfma_f32_16x16x128_f8f6f4 v[156:159], v[8:15], v[48:55], v[156:159]
	v_mfma_f32_16x16x128_f8f6f4 v[136:139], v[0:7], v[56:63], v[136:139]
	v_mfma_f32_16x16x128_f8f6f4 v[140:143], v[8:15], v[56:63], v[140:143]
	v_mfma_f32_16x16x128_f8f6f4 v[176:179], v[16:23], v[32:39], v[176:179]
	v_mfma_f32_16x16x128_f8f6f4 v[180:183], v[24:31], v[32:39], v[180:183]
	v_mfma_f32_16x16x128_f8f6f4 v[160:163], v[16:23], v[40:47], v[160:163]
	v_mfma_f32_16x16x128_f8f6f4 v[164:167], v[24:31], v[40:47], v[164:167]
	v_mfma_f32_16x16x128_f8f6f4 v[144:147], v[16:23], v[48:55], v[144:147]
	v_mfma_f32_16x16x128_f8f6f4 v[148:151], v[24:31], v[48:55], v[148:151]
	v_mfma_f32_16x16x128_f8f6f4 v[128:131], v[16:23], v[56:63], v[128:131]
	v_mfma_f32_16x16x128_f8f6f4 v[132:135], v[24:31], v[56:63], v[132:135]
	s_setprio 0
	s_barrier
	s_mov_b32 s6, s38
	s_mov_b32 s7, s39
	s_mov_b32 m0, s43
	ds_read_b128 v[32:35], v200 offset:16384
	buffer_load_dwordx4 v194, s[4:7], s55 offen lds
	s_mov_b32 m0, s44
	ds_read_b128 v[36:39], v200 offset:17408
	buffer_load_dwordx4 v196, s[4:7], s55 offen lds
	s_mov_b32 m0, s45
	ds_read_b128 v[40:43], v200 offset:18432
	buffer_load_dwordx4 v194, s[4:7], s20 offen lds
	s_mov_b32 m0, s42
	ds_read_b128 v[44:47], v200 offset:19456
	buffer_load_dwordx4 v192, s[36:39], s54 offen lds
	s_mov_b32 m0, s47
	ds_read_b128 v[48:51], v200 offset:20480
	buffer_load_dwordx4 v195, s[36:39], s54 offen lds
	ds_read_b128 v[52:55], v200 offset:21504
	ds_read_b128 v[56:59], v200 offset:22528
	ds_read_b128 v[60:63], v200 offset:23552
	s_waitcnt vmcnt(7)
	s_waitcnt lgkmcnt(0)
	s_barrier
	s_setprio 1
	v_mfma_f32_16x16x128_f8f6f4 v[120:123], v[0:7], v[32:39], v[120:123]
	v_mfma_f32_16x16x128_f8f6f4 v[124:127], v[8:15], v[32:39], v[124:127]
	v_mfma_f32_16x16x128_f8f6f4 v[104:107], v[0:7], v[40:47], v[104:107]
	v_mfma_f32_16x16x128_f8f6f4 v[108:111], v[8:15], v[40:47], v[108:111]
	v_mfma_f32_16x16x128_f8f6f4 v[88:91], v[0:7], v[48:55], v[88:91]
	v_mfma_f32_16x16x128_f8f6f4 v[92:95], v[8:15], v[48:55], v[92:95]
	v_mfma_f32_16x16x128_f8f6f4 v[72:75], v[0:7], v[56:63], v[72:75]
	v_mfma_f32_16x16x128_f8f6f4 v[76:79], v[8:15], v[56:63], v[76:79]
	v_mfma_f32_16x16x128_f8f6f4 v[112:115], v[16:23], v[32:39], v[112:115]
	v_mfma_f32_16x16x128_f8f6f4 v[116:119], v[24:31], v[32:39], v[116:119]
	v_mfma_f32_16x16x128_f8f6f4 v[96:99], v[16:23], v[40:47], v[96:99]
	v_mfma_f32_16x16x128_f8f6f4 v[100:103], v[24:31], v[40:47], v[100:103]
	v_mfma_f32_16x16x128_f8f6f4 v[80:83], v[16:23], v[48:55], v[80:83]
	v_mfma_f32_16x16x128_f8f6f4 v[84:87], v[24:31], v[48:55], v[84:87]
	v_mfma_f32_16x16x128_f8f6f4 v[68:71], v[16:23], v[56:63], v[68:71]
	v_mfma_f32_16x16x128_f8f6f4 v[64:67], v[24:31], v[56:63], v[64:67]
	s_setprio 0
	s_barrier
; #define PG8_STAGE(bufoff, rs_, soff_, voff) do { _Pragma("unroll") for (int _i = 0; _i < 2; ++_i) \
;         __builtin_amdgcn_raw_ptr_buffer_load_lds(rs_, (LAS void*)(lds + (bufoff) + ldsw + _i * 8192), 16, (int)(voff)[_i], (int)(soff_), 0, 0); } while (0)
; #define PG8_LDA(dst, b, h) do { _Pragma("unroll") for (int m = 0; m < 4; ++m) dst[m] = PG8_LD2(lds + PG8_SA(b, h) + aoff + m * 2048); } while (0)
; #define PG8_LDB(dst, b, h) do { _Pragma("unroll") for (int n = 0; n < 2; ++n) dst[n] = PG8_LD2(lds + PG8_SB(b, h) + boff + n * 2048); } while (0)
; #define PG8_WAIT_V(n) asm volatile("s_waitcnt vmcnt(" #n ")" ::: "memory")
; #define PG8_WAIT_L(n) asm volatile("s_waitcnt lgkmcnt(" #n ")" ::: "memory")
; #define PG8_BAR __builtin_amdgcn_s_barrier()
; #define PG8_SCHED __builtin_amdgcn_sched_barrier(0)
; template <class Epi, class Sched, bool ALIGN_EPI = false, bool SP2 = false, bool FP8 = false>
; __device__ __forceinline__ void gemm_phase(LAS unsigned char* lds, const Gemm g, const Sched& S, const Epi& E, int wbase) {
;     ...
;             PG8_LDB(B0, 1, 0); PG8_LDB(B1, 1, 1); PG8_SCHED; PG8_LDA(At, 1, 0); PG8_STAGE(PG8_SA(0, 1), rA2, a2 + hstep, voffA);
;             PG8_WAIT_V(8); PG8_WAIT_L(0); PG8_BAR; PG8_MMA(0, 0, At, B0); PG8_MMA(0, 1, At, B1); PG8_BAR; PG8_SCHED;
;             PG8_LDA(At, 1, 1); PG8_STAGE(PG8_SB(1, 0), rB2, b3, voffB); PG8_STAGE(PG8_SB(1, 1), rB2, b3 + hstep, voffB); PG8_STAGE(PG8_SA(1, 0), rA2, a3, voffA);
;             PG8_WAIT_V(8); PG8_WAIT_L(0); PG8_BAR; PG8_MMA(1, 0, At, B0); PG8_MMA(1, 1, At, B1); PG8_BAR; PG8_SCHED;
	s_mov_b32 m0, s46
	s_nop 0
	buffer_load_dwordx4 v196, s[4:7], s20 offen lds
	v_add_u32_e32 v12, 0x18000, v199
	v_add_u32_e32 v28, 0x1c000, v199
	ds_read_b128 v[0:3], v12
	ds_read_b128 v[4:7], v12 offset:1024
	ds_read_b128 v[8:11], v12 offset:2048
	ds_read_b128 v[12:15], v12 offset:3072
	ds_read_b128 v[16:19], v28
	ds_read_b128 v[20:23], v28 offset:1024
	ds_read_b128 v[24:27], v28 offset:2048
	ds_read_b128 v[28:31], v28 offset:3072
	s_add_i32 s54, s54, s41
	s_mov_b32 m0, s48
	ds_read_b128 v[32:35], v200 offset:32768
	ds_read_b128 v[36:39], v200 offset:33792
	ds_read_b128 v[40:43], v200 offset:34816
	ds_read_b128 v[44:47], v200 offset:35840
	ds_read_b128 v[48:51], v200 offset:36864
	ds_read_b128 v[52:55], v200 offset:37888
	ds_read_b128 v[56:59], v200 offset:38912
	ds_read_b128 v[60:63], v200 offset:39936
	buffer_load_dwordx4 v192, s[36:39], s54 offen lds
	s_mov_b32 m0, s52
	s_nop 0
	buffer_load_dwordx4 v195, s[36:39], s54 offen lds
	s_waitcnt vmcnt(8)
	s_waitcnt lgkmcnt(0)
	s_barrier
	s_setprio 1
	v_mfma_f32_16x16x128_f8f6f4 v[184:187], v[0:7], v[32:39], v[184:187]
	v_mfma_f32_16x16x128_f8f6f4 v[188:191], v[8:15], v[32:39], v[188:191]
	v_mfma_f32_16x16x128_f8f6f4 v[168:171], v[0:7], v[40:47], v[168:171]
	v_mfma_f32_16x16x128_f8f6f4 v[172:175], v[8:15], v[40:47], v[172:175]
	v_mfma_f32_16x16x128_f8f6f4 v[152:155], v[0:7], v[48:55], v[152:155]
	v_mfma_f32_16x16x128_f8f6f4 v[156:159], v[8:15], v[48:55], v[156:159]
	v_mfma_f32_16x16x128_f8f6f4 v[136:139], v[0:7], v[56:63], v[136:139]
	v_mfma_f32_16x16x128_f8f6f4 v[140:143], v[8:15], v[56:63], v[140:143]
	v_mfma_f32_16x16x128_f8f6f4 v[176:179], v[16:23], v[32:39], v[176:179]
	v_mfma_f32_16x16x128_f8f6f4 v[180:183], v[24:31], v[32:39], v[180:183]
	v_mfma_f32_16x16x128_f8f6f4 v[160:163], v[16:23], v[40:47], v[160:163]
	v_mfma_f32_16x16x128_f8f6f4 v[164:167], v[24:31], v[40:47], v[164:167]
	v_mfma_f32_16x16x128_f8f6f4 v[144:147], v[16:23], v[48:55], v[144:147]
	v_mfma_f32_16x16x128_f8f6f4 v[148:151], v[24:31], v[48:55], v[148:151]
	v_mfma_f32_16x16x128_f8f6f4 v[128:131], v[16:23], v[56:63], v[128:131]
	v_mfma_f32_16x16x128_f8f6f4 v[132:135], v[24:31], v[56:63], v[132:135]
	s_setprio 0
	s_barrier
	s_addk_i32 s55, 0x80
	s_addk_i32 s20, 0x80
	s_mov_b32 m0, s57
	ds_read_b128 v[32:35], v200 offset:49152
	buffer_load_dwordx4 v194, s[4:7], s55 offen lds
	s_mov_b32 m0, s58
	ds_read_b128 v[36:39], v200 offset:50176
	buffer_load_dwordx4 v196, s[4:7], s55 offen lds
	s_mov_b32 m0, s61
	ds_read_b128 v[40:43], v200 offset:51200
	buffer_load_dwordx4 v194, s[4:7], s20 offen lds
	s_mov_b32 m0, s62
	ds_read_b128 v[44:47], v200 offset:52224
	buffer_load_dwordx4 v196, s[4:7], s20 offen lds
	s_mov_b32 m0, s59
	ds_read_b128 v[48:51], v200 offset:53248
	buffer_load_dwordx4 v192, s[36:39], s78 offen lds
	s_mov_b32 m0, s60
	ds_read_b128 v[52:55], v200 offset:54272
	buffer_load_dwordx4 v195, s[36:39], s78 offen lds
	ds_read_b128 v[56:59], v200 offset:55296
	ds_read_b128 v[60:63], v200 offset:56320
	s_waitcnt vmcnt(8)
	s_waitcnt lgkmcnt(0)
	s_barrier
	s_setprio 1
	v_mfma_f32_16x16x128_f8f6f4 v[120:123], v[0:7], v[32:39], v[120:123]
	v_mfma_f32_16x16x128_f8f6f4 v[124:127], v[8:15], v[32:39], v[124:127]
	v_mfma_f32_16x16x128_f8f6f4 v[104:107], v[0:7], v[40:47], v[104:107]
	v_mfma_f32_16x16x128_f8f6f4 v[108:111], v[8:15], v[40:47], v[108:111]
	v_mfma_f32_16x16x128_f8f6f4 v[88:91], v[0:7], v[48:55], v[88:91]
	v_mfma_f32_16x16x128_f8f6f4 v[92:95], v[8:15], v[48:55], v[92:95]
	v_mfma_f32_16x16x128_f8f6f4 v[72:75], v[0:7], v[56:63], v[72:75]
	v_mfma_f32_16x16x128_f8f6f4 v[76:79], v[8:15], v[56:63], v[76:79]
	v_mfma_f32_16x16x128_f8f6f4 v[112:115], v[16:23], v[32:39], v[112:115]
	v_mfma_f32_16x16x128_f8f6f4 v[116:119], v[24:31], v[32:39], v[116:119]
	v_mfma_f32_16x16x128_f8f6f4 v[96:99], v[16:23], v[40:47], v[96:99]
	v_mfma_f32_16x16x128_f8f6f4 v[100:103], v[24:31], v[40:47], v[100:103]
	v_mfma_f32_16x16x128_f8f6f4 v[80:83], v[16:23], v[48:55], v[80:83]
	v_mfma_f32_16x16x128_f8f6f4 v[84:87], v[24:31], v[48:55], v[84:87]
	v_mfma_f32_16x16x128_f8f6f4 v[68:71], v[16:23], v[56:63], v[68:71]
	v_mfma_f32_16x16x128_f8f6f4 v[64:67], v[24:31], v[56:63], v[64:67]
	s_setprio 0
	s_barrier
	s_add_i32 s85, s85, 2
	s_addk_i32 s67, 0x100
	s_cmp_ge_i32 s85, s53
	v_add_u32_e32 v210, 0x100, v210
	s_cbranch_scc0 .LBB0_1348
	v_readlane_b32 s54, v255, 25
	v_readlane_b32 s55, v255, 26
	s_and_b64 vcc, exec, s[18:19]
	s_cbranch_vccnz .LBB0_1367
	s_branch .LBB0_1368

; #define KWS (kargs()->ws)
; __device__ __forceinline__ void combine_rows2(bf16* hA, float* ssqA, const bf16* a1, const bf16* a2, bf16* hB, float* ssqB, const bf16* b1, const bf16* b2, int lane, unsigned char* h8A = nullptr, unsigned char* h8B = nullptr) {
;     u32x2 ra[3][4], rb[3][4];
; #pragma unroll
;     for (int j = 0; j < 4; ++j) { ra[0][j] = *((const u32x2*)hA + lane + 64 * j); ra[1][j] = *((const u32x2*)a1 + lane + 64 * j); ra[2][j] = *((const u32x2*)a2 + lane + 64 * j);
;                                   rb[0][j] = *((const u32x2*)hB + lane + 64 * j); rb[1][j] = *((const u32x2*)b1 + lane + 64 * j); rb[2][j] = *((const u32x2*)b2 + lane + 64 * j); }
;     float sa[4], sb[4];
; #pragma unroll
;     for (int j = 0; j < 4; ++j) { const f32x4 v = unpack_lo(ra[0][j]) + unpack_lo(ra[1][j]) + unpack_lo(ra[2][j]), w = unpack_lo(rb[0][j]) + unpack_lo(rb[1][j]) + unpack_lo(rb[2][j]);
;         sa[j] = (v.x * v.x + v.y * v.y) + (v.z * v.z + v.w * v.w); sb[j] = (w.x * w.x + w.y * w.y) + (w.z * w.z + w.w * w.w);
;         u32x2 o; o.x = cvt_pk_bf16(v.x, v.y); o.y = cvt_pk_bf16(v.z, v.w); *((u32x2*)hA + lane + 64 * j) = o; o.x = cvt_pk_bf16(w.x, w.y); o.y = cvt_pk_bf16(w.z, w.w); *((u32x2*)hB + lane + 64 * j) = o;
; __global__ void __launch_bounds__(512, 2) mega(Ptrs Pdummy) {
;     ...
;             { WAVE_IDS(); unsigned char* ws = KWS; const int* TSLOT = (const int*)(ws + WS_SEL + 512 * 1024); const bf16* XG = (const bf16*)(ws + WS_R + R_XG);
;               for (int m = gw; m < M; m += 2 * ngw) { const int m2 = m + ngw;
;                   if (m2 >= M) { rowstats_row<true>(nullptr, HBUF(hc) + (size_t)m * DM, SBUF(sc ^ 1) + 16 * (size_t)m, XG + (size_t)TSLOT[2 * m] * DM, XG + (size_t)TSLOT[2 * m + 1] * DM, lane); break; }
;                   const int s1 = TSLOT[2 * m], s2 = TSLOT[2 * m + 1], s3 = TSLOT[2 * m2], s4 = TSLOT[2 * m2 + 1];
;                   const bool p8 = (PLE_FP8_MASK >> l) & 1;
;                   combine_rows2(HBUF(hc) + (size_t)m * DM, SBUF(sc ^ 1) + 16 * (size_t)m, XG + (size_t)s1 * DM, XG + (size_t)s2 * DM,
;                                 HBUF(hc) + (size_t)m2 * DM, SBUF(sc ^ 1) + 16 * (size_t)m2, XG + (size_t)s3 * DM, XG + (size_t)s4 * DM, lane,
;                                 p8 ? ws + WS_HB8 + (size_t)m * DM : nullptr, p8 ? ws + WS_HB8 + (size_t)m2 * DM : nullptr); } }
.LBB0_1540:
	s_and_b64 vcc, exec, s[8:9]
	s_cbranch_vccz .LBB0_1525
	s_ashr_i32 s13, s12, 31
	s_lshl_b64 s[8:9], s[12:13], 2
	s_add_u32 s18, s1, s8
	s_addc_u32 s19, s22, s9
	global_load_dwordx2 v[8:9], v233, s[18:19]
	v_readlane_b32 s8, v255, 2
	s_add_i32 s8, s8, s12
	s_ashr_i32 s9, s8, 31
	s_lshl_b64 s[8:9], s[8:9], 2
	s_add_u32 s20, s1, s8
	s_addc_u32 s21, s22, s9
	global_load_dwordx2 v[20:21], v233, s[20:21]
	s_ashr_i32 s11, s10, 31
	s_ashr_i32 s17, s16, 31
	s_lshl_b64 s[8:9], s[10:11], 10
	s_lshl_b64 s[18:19], s[16:17], 10
	s_add_u32 s13, s23, s8
	v_readlane_b32 s26, v255, 36
	v_readlane_b32 s27, v255, 37
	s_waitcnt vmcnt(1)
	v_ashrrev_i32_e32 v11, 31, v8
	v_mov_b32_e32 v10, v8
	v_ashrrev_i32_e32 v13, 31, v9
	v_mov_b32_e32 v12, v9
	s_nop 0
	s_addc_u32 s20, s24, s9
	s_and_b64 s[8:9], s[26:27], exec
	s_cselect_b32 s9, s20, 0
	s_cselect_b32 s8, s13, 0
	s_add_u32 s13, s23, s18
	s_addc_u32 s20, s24, s19
	s_and_b64 s[18:19], s[26:27], exec
	v_lshlrev_b64 v[10:11], 11, v[10:11]
	s_cselect_b32 s21, s20, 0
	s_cselect_b32 s20, s13, 0
	s_lshl_b64 s[18:19], s[10:11], 11
	v_lshlrev_b64 v[12:13], 11, v[12:13]
	v_lshl_add_u64 v[18:19], v[4:5], 0, v[10:11]
	v_lshl_add_u64 v[12:13], v[4:5], 0, v[12:13]
	v_lshl_add_u64 v[26:27], s[8:9], 0, v[232:233]
	s_waitcnt vmcnt(0)
	v_ashrrev_i32_e32 v15, 31, v20
	v_mov_b32_e32 v14, v20
	v_ashrrev_i32_e32 v17, 31, v21
	v_mov_b32_e32 v16, v21
	v_lshlrev_b64 v[16:17], 11, v[16:17]
	v_lshlrev_b64 v[14:15], 11, v[14:15]
	v_lshl_add_u64 v[8:9], v[2:3], 0, s[18:19]
	s_lshl_b64 s[18:19], s[16:17], 11
	v_lshl_add_u64 v[10:11], v[2:3], 0, s[18:19]
	v_lshl_add_u64 v[14:15], v[4:5], 0, v[14:15]
	v_lshl_add_u64 v[22:23], v[4:5], 0, v[16:17]
	global_load_dwordx2 v[62:63], v[8:9], off
	global_load_dwordx2 v[64:65], v[18:19], off
	global_load_dwordx2 v[66:67], v[12:13], off
	global_load_dwordx2 v[60:61], v[10:11], off
	global_load_dwordx2 v[30:31], v[14:15], off
	global_load_dwordx2 v[28:29], v[22:23], off
	global_load_dwordx2 v[58:59], v[8:9], off offset:512
	global_load_dwordx2 v[56:57], v[18:19], off offset:512
	global_load_dwordx2 v[54:55], v[12:13], off offset:512
	global_load_dwordx2 v[52:53], v[10:11], off offset:512
	global_load_dwordx2 v[50:51], v[14:15], off offset:512
	global_load_dwordx2 v[48:49], v[22:23], off offset:512
	global_load_dwordx2 v[46:47], v[8:9], off offset:1024
	global_load_dwordx2 v[44:45], v[18:19], off offset:1024
	global_load_dwordx2 v[42:43], v[12:13], off offset:1024
	global_load_dwordx2 v[40:41], v[10:11], off offset:1024
	global_load_dwordx2 v[38:39], v[14:15], off offset:1024
	global_load_dwordx2 v[36:37], v[22:23], off offset:1024
	global_load_dwordx2 v[24:25], v[8:9], off offset:1536
	global_load_dwordx2 v[20:21], v[18:19], off offset:1536
	global_load_dwordx2 v[16:17], v[12:13], off offset:1536
	s_nop 0
	global_load_dwordx2 v[18:19], v[10:11], off offset:1536
	global_load_dwordx2 v[34:35], v[14:15], off offset:1536
	global_load_dwordx2 v[32:33], v[22:23], off offset:1536
	s_cmp_lg_u64 s[8:9], 0
	s_cselect_b64 s[18:19], -1, 0
	s_cmp_eq_u64 s[8:9], 0
	v_lshl_add_u64 v[22:23], s[20:21], 0, v[232:233]
	s_waitcnt vmcnt(23)
	v_lshlrev_b32_e32 v12, 16, v62
	v_and_b32_e32 v13, 0xffff0000, v62
	v_lshlrev_b32_e32 v14, 16, v63
	v_and_b32_e32 v15, 0xffff0000, v63
	s_waitcnt vmcnt(22)
	v_lshlrev_b32_e32 v62, 16, v64
	v_and_b32_e32 v63, 0xffff0000, v64
	v_lshlrev_b32_e32 v64, 16, v65
	v_and_b32_e32 v65, 0xffff0000, v65
	v_pk_add_f32 v[62:63], v[12:13], v[62:63]
	v_pk_add_f32 v[12:13], v[14:15], v[64:65]
	s_waitcnt vmcnt(21)
	v_lshlrev_b32_e32 v14, 16, v66
	v_and_b32_e32 v15, 0xffff0000, v66
	v_lshlrev_b32_e32 v64, 16, v67
	v_and_b32_e32 v65, 0xffff0000, v67
	v_pk_add_f32 v[12:13], v[12:13], v[64:65]
	v_pk_add_f32 v[14:15], v[62:63], v[14:15]
	s_waitcnt vmcnt(20)
	v_lshlrev_b32_e32 v62, 16, v60
	v_and_b32_e32 v63, 0xffff0000, v60
	v_lshlrev_b32_e32 v60, 16, v61
	v_and_b32_e32 v61, 0xffff0000, v61
	s_waitcnt vmcnt(19)
	v_lshlrev_b32_e32 v64, 16, v30
	v_and_b32_e32 v65, 0xffff0000, v30
	v_lshlrev_b32_e32 v30, 16, v31
	v_and_b32_e32 v31, 0xffff0000, v31
	v_pk_add_f32 v[62:63], v[62:63], v[64:65]
	v_pk_add_f32 v[30:31], v[60:61], v[30:31]
	s_waitcnt vmcnt(18)
	v_lshlrev_b32_e32 v60, 16, v28
	v_and_b32_e32 v61, 0xffff0000, v28
	v_lshlrev_b32_e32 v28, 16, v29
	v_and_b32_e32 v29, 0xffff0000, v29
	v_pk_add_f32 v[28:29], v[30:31], v[28:29]
	v_pk_add_f32 v[30:31], v[62:63], v[60:61]
	v_cvt_pk_bf16_f32 v60, v14, v15
	v_cvt_pk_bf16_f32 v61, v12, v13
	global_store_dwordx2 v[8:9], v[60:61], off
	v_cvt_pk_bf16_f32 v60, v30, v31
	v_cvt_pk_bf16_f32 v61, v28, v29
	global_store_dwordx2 v[10:11], v[60:61], off
	s_cbranch_scc1 .LBB0_1543
	v_med3_f32 v1, v14, s49, v254
	v_med3_f32 v60, v15, s49, v254
	v_cvt_pk_fp8_f32 v1, v1, v60
	v_med3_f32 v61, v12, s49, v254
	v_med3_f32 v62, v13, s49, v254
	v_med3_f32 v60, v31, s49, v254
	v_cvt_pk_fp8_f32 v1, v61, v62 op_sel:[0,0,1]
	v_med3_f32 v61, v28, s49, v254
	v_med3_f32 v62, v29, s49, v254
	global_store_dword v[26:27], v1, off
	v_med3_f32 v1, v30, s49, v254
	v_cvt_pk_fp8_f32 v1, v1, v60
	v_cvt_pk_fp8_f32 v1, v61, v62 op_sel:[0,0,1]
	global_store_dword v[22:23], v1, off

; #define PG8_STAGE(bufoff, rs_, soff_, voff) do { _Pragma("unroll") for (int _i = 0; _i < 2; ++_i) \
;         __builtin_amdgcn_raw_ptr_buffer_load_lds(rs_, (LAS void*)(lds + (bufoff) + ldsw + _i * 8192), 16, (int)(voff)[_i], (int)(soff_), 0, 0); } while (0)
; #define PG8_LDA(dst, b, h) do { _Pragma("unroll") for (int m = 0; m < 4; ++m) dst[m] = PG8_LD2(lds + PG8_SA(b, h) + aoff + m * 2048); } while (0)
; #define PG8_LDB(dst, b, h) do { _Pragma("unroll") for (int n = 0; n < 2; ++n) dst[n] = PG8_LD2(lds + PG8_SB(b, h) + boff + n * 2048); } while (0)
; #define PG8_WAIT_V(n) asm volatile("s_waitcnt vmcnt(" #n ")" ::: "memory")
; #define PG8_WAIT_L(n) asm volatile("s_waitcnt lgkmcnt(" #n ")" ::: "memory")
; #define PG8_BAR __builtin_amdgcn_s_barrier()
; #define PG8_SCHED __builtin_amdgcn_sched_barrier(0)
; template <class Epi, class Sched, bool ALIGN_EPI = false, bool SP2 = false, bool FP8 = false>
; __device__ __forceinline__ void gemm_phase(LAS unsigned char* lds, const Gemm g, const Sched& S, const Epi& E, int wbase) {
;     ...
;         for (int t = 0; t < nt; t += 2) {
;             const bool last = (t == nt - 2);
;             const unsigned a1 = cA + (unsigned)(t + 1) * kstep;
;             const unsigned a2 = last ? nA : cA + (unsigned)(t + 2) * kstep, b2 = last ? nB : cB + (unsigned)(t + 2) * kstep; const rsrc_t rA2 = (Sched::TWO && last) ? rAn : rAc, rB2 = (Sched::TWO && last) ? rBn : rBc;
;             const unsigned a3 = a2 + kstep, b3 = b2 + kstep;
;             if (last && has_next) S.a_ready(nxt);
;             if constexpr (SP2) {
;             PG8_LDB(B0, 0, 0); PG8_LDB(B1, 0, 1); PG8_SCHED; PG8_LDA(At, 0, 0); PG8_STAGE(PG8_SA(1, 1), rAc, a1 + hstep, voffA);
;             PG8_WAIT_V(8); PG8_WAIT_L(0); PG8_BAR; PG8_MMA(0, 0, At, B0); PG8_MMA(0, 1, At, B1); PG8_BAR; PG8_SCHED;
;             PG8_LDA(At, 0, 1); PG8_STAGE(PG8_SB(0, 0), rB2, b2, voffB); PG8_STAGE(PG8_SB(0, 1), rB2, b2 + hstep, voffB); PG8_STAGE(PG8_SA(0, 0), rA2, a2, voffA);
;             PG8_WAIT_V(8); PG8_WAIT_L(0); PG8_BAR; PG8_MMA(1, 0, At, B0); PG8_MMA(1, 1, At, B1); PG8_BAR; PG8_SCHED;
.LBB0_1626:
	s_lshl_b32 s56, s53, 19
	s_andn2_b64 vcc, exec, s[12:13]
	s_lshl_b32 s57, s52, 19
	s_cbranch_vccnz .LBB0_1634
	s_and_b64 s[6:7], s[18:19], exec
	s_waitcnt vmcnt(37)
	s_waitcnt vmcnt(35)
	s_waitcnt vmcnt(31)
	s_waitcnt vmcnt(27)
	s_waitcnt vmcnt(23)
	s_waitcnt vmcnt(22)
	s_cselect_b32 s59, s56, s55
	s_cselect_b32 s60, s57, s54
	s_add_i32 s61, s55, 0x80
	s_add_i32 s62, s54, 0x100
	s_mov_b32 s63, 0
	v_add_u32_e32 v136, 0x10000, v161
	ds_read_b128 v[128:131], v136
	ds_read_b128 v[132:135], v136 offset:1024
	ds_read_b128 v[164:167], v136 offset:2048
	ds_read_b128 v[168:171], v136 offset:3072
	v_add_u32_e32 v136, 0x14000, v161
	ds_read_b128 v[172:175], v136
	ds_read_b128 v[176:179], v136 offset:1024
	ds_read_b128 v[180:183], v136 offset:2048
	ds_read_b128 v[184:187], v136 offset:3072
	s_add_i32 s6, s61, 0x80
	s_cmp_eq_u32 s46, s63
	s_cselect_b32 s65, s59, s6
	s_cselect_b32 s55, s60, s62
	s_or_b32 s54, s65, 0x80
	s_add_i32 s6, s22, s61
	s_mov_b32 m0, s47
	ds_read_b128 v[188:191], v162
	ds_read_b128 v[192:195], v162 offset:1024
	ds_read_b128 v[196:199], v162 offset:2048
	ds_read_b128 v[200:203], v162 offset:3072
	ds_read_b128 v[204:207], v162 offset:4096
	ds_read_b128 v[208:211], v162 offset:5120
	ds_read_b128 v[212:215], v162 offset:6144
	ds_read_b128 v[216:219], v162 offset:7168
	buffer_load_dwordx4 v137, s[36:39], s6 offen lds
	s_mov_b32 m0, s48
	s_nop 0
	buffer_load_dwordx4 v145, s[36:39], s6 offen lds
	s_waitcnt vmcnt(8)
	s_waitcnt lgkmcnt(0)
	s_barrier
	s_setprio 1
	v_mfma_f32_16x16x32_bf16 v[120:123], v[128:131], v[188:191], 0
	v_mfma_f32_16x16x32_bf16 v[124:127], v[164:167], v[188:191], 0
	v_mfma_f32_16x16x32_bf16 v[104:107], v[128:131], v[196:199], 0
	v_mfma_f32_16x16x32_bf16 v[108:111], v[164:167], v[196:199], 0
	v_mfma_f32_16x16x32_bf16 v[88:91], v[128:131], v[204:207], 0
	v_mfma_f32_16x16x32_bf16 v[92:95], v[164:167], v[204:207], 0
	v_mfma_f32_16x16x32_bf16 v[72:75], v[128:131], v[212:215], 0
	v_mfma_f32_16x16x32_bf16 v[76:79], v[164:167], v[212:215], 0
	v_mfma_f32_16x16x32_bf16 v[120:123], v[132:135], v[192:195], v[120:123]
	v_mfma_f32_16x16x32_bf16 v[124:127], v[168:171], v[192:195], v[124:127]
	v_mfma_f32_16x16x32_bf16 v[104:107], v[132:135], v[200:203], v[104:107]
	v_mfma_f32_16x16x32_bf16 v[108:111], v[168:171], v[200:203], v[108:111]
	v_mfma_f32_16x16x32_bf16 v[88:91], v[132:135], v[208:211], v[88:91]
	v_mfma_f32_16x16x32_bf16 v[92:95], v[168:171], v[208:211], v[92:95]
	v_mfma_f32_16x16x32_bf16 v[72:75], v[132:135], v[216:219], v[72:75]
	v_mfma_f32_16x16x32_bf16 v[76:79], v[168:171], v[216:219], v[76:79]
	v_mfma_f32_16x16x32_bf16 v[112:115], v[172:175], v[188:191], 0
	v_mfma_f32_16x16x32_bf16 v[116:119], v[180:183], v[188:191], 0
	v_mfma_f32_16x16x32_bf16 v[96:99], v[172:175], v[196:199], 0
	v_mfma_f32_16x16x32_bf16 v[100:103], v[180:183], v[196:199], 0
	v_mfma_f32_16x16x32_bf16 v[80:83], v[172:175], v[204:207], 0
	v_mfma_f32_16x16x32_bf16 v[84:87], v[180:183], v[204:207], 0
	v_mfma_f32_16x16x32_bf16 v[64:67], v[172:175], v[212:215], 0
	v_mfma_f32_16x16x32_bf16 v[68:71], v[180:183], v[212:215], 0
	v_mfma_f32_16x16x32_bf16 v[112:115], v[176:179], v[192:195], v[112:115]
	v_mfma_f32_16x16x32_bf16 v[116:119], v[184:187], v[192:195], v[116:119]
	v_mfma_f32_16x16x32_bf16 v[96:99], v[176:179], v[200:203], v[96:99]
	v_mfma_f32_16x16x32_bf16 v[100:103], v[184:187], v[200:203], v[100:103]
	v_mfma_f32_16x16x32_bf16 v[80:83], v[176:179], v[208:211], v[80:83]
	v_mfma_f32_16x16x32_bf16 v[84:87], v[184:187], v[208:211], v[84:87]
	v_mfma_f32_16x16x32_bf16 v[64:67], v[176:179], v[216:219], v[64:67]
	v_mfma_f32_16x16x32_bf16 v[68:71], v[184:187], v[216:219], v[68:71]
	s_setprio 0
	s_barrier
	s_mov_b32 m0, s24
	s_mov_b32 s6, s38
	s_mov_b32 s7, s39
	buffer_load_dwordx4 v141, s[4:7], s55 offen lds
	s_mov_b32 m0, s25
	ds_read_b128 v[188:191], v162 offset:16384
	s_add_i32 s66, s55, s22
	buffer_load_dwordx4 v149, s[4:7], s55 offen lds
	s_mov_b32 m0, s26
	ds_read_b128 v[192:195], v162 offset:17408
	buffer_load_dwordx4 v141, s[4:7], s66 offen lds
	s_mov_b32 m0, s23
	ds_read_b128 v[196:199], v162 offset:18432
	buffer_load_dwordx4 v137, s[36:39], s65 offen lds
	s_mov_b32 m0, s28
	ds_read_b128 v[200:203], v162 offset:19456
	buffer_load_dwordx4 v145, s[36:39], s65 offen lds
	ds_read_b128 v[204:207], v162 offset:20480
	ds_read_b128 v[208:211], v162 offset:21504
	ds_read_b128 v[212:215], v162 offset:22528
	ds_read_b128 v[216:219], v162 offset:23552
	s_waitcnt vmcnt(7)
	s_waitcnt lgkmcnt(0)
	s_barrier
	s_setprio 1
	v_mfma_f32_16x16x32_bf16 v[56:59], v[128:131], v[188:191], 0
	v_mfma_f32_16x16x32_bf16 v[60:63], v[164:167], v[188:191], 0
	v_mfma_f32_16x16x32_bf16 v[40:43], v[128:131], v[196:199], 0
	v_mfma_f32_16x16x32_bf16 v[44:47], v[164:167], v[196:199], 0
	v_mfma_f32_16x16x32_bf16 v[24:27], v[128:131], v[204:207], 0
	v_mfma_f32_16x16x32_bf16 v[28:31], v[164:167], v[204:207], 0
	v_mfma_f32_16x16x32_bf16 v[8:11], v[128:131], v[212:215], 0
	v_mfma_f32_16x16x32_bf16 v[12:15], v[164:167], v[212:215], 0
	v_mfma_f32_16x16x32_bf16 v[56:59], v[132:135], v[192:195], v[56:59]
	v_mfma_f32_16x16x32_bf16 v[60:63], v[168:171], v[192:195], v[60:63]
	v_mfma_f32_16x16x32_bf16 v[40:43], v[132:135], v[200:203], v[40:43]
	v_mfma_f32_16x16x32_bf16 v[44:47], v[168:171], v[200:203], v[44:47]
	v_mfma_f32_16x16x32_bf16 v[24:27], v[132:135], v[208:211], v[24:27]
	v_mfma_f32_16x16x32_bf16 v[28:31], v[168:171], v[208:211], v[28:31]
	v_mfma_f32_16x16x32_bf16 v[8:11], v[132:135], v[216:219], v[8:11]
	v_mfma_f32_16x16x32_bf16 v[12:15], v[168:171], v[216:219], v[12:15]
	v_mfma_f32_16x16x32_bf16 v[48:51], v[172:175], v[188:191], 0
	v_mfma_f32_16x16x32_bf16 v[52:55], v[180:183], v[188:191], 0
	v_mfma_f32_16x16x32_bf16 v[32:35], v[172:175], v[196:199], 0
	v_mfma_f32_16x16x32_bf16 v[36:39], v[180:183], v[196:199], 0
	v_mfma_f32_16x16x32_bf16 v[16:19], v[172:175], v[204:207], 0
	v_mfma_f32_16x16x32_bf16 v[20:23], v[180:183], v[204:207], 0
	v_mfma_f32_16x16x32_bf16 v[4:7], v[172:175], v[212:215], 0
	v_mfma_f32_16x16x32_bf16 v[0:3], v[180:183], v[212:215], 0
	v_mfma_f32_16x16x32_bf16 v[48:51], v[176:179], v[192:195], v[48:51]
	v_mfma_f32_16x16x32_bf16 v[52:55], v[184:187], v[192:195], v[52:55]
	v_mfma_f32_16x16x32_bf16 v[32:35], v[176:179], v[200:203], v[32:35]
	v_mfma_f32_16x16x32_bf16 v[36:39], v[184:187], v[200:203], v[36:39]
	v_mfma_f32_16x16x32_bf16 v[16:19], v[176:179], v[208:211], v[16:19]
	v_mfma_f32_16x16x32_bf16 v[20:23], v[184:187], v[208:211], v[20:23]
	v_mfma_f32_16x16x32_bf16 v[4:7], v[176:179], v[216:219], v[4:7]
	v_mfma_f32_16x16x32_bf16 v[0:3], v[184:187], v[216:219], v[0:3]
	s_setprio 0
	s_barrier
; #define PG8_STAGE(bufoff, rs_, soff_, voff) do { _Pragma("unroll") for (int _i = 0; _i < 2; ++_i) \
;         __builtin_amdgcn_raw_ptr_buffer_load_lds(rs_, (LAS void*)(lds + (bufoff) + ldsw + _i * 8192), 16, (int)(voff)[_i], (int)(soff_), 0, 0); } while (0)
; #define PG8_LDA(dst, b, h) do { _Pragma("unroll") for (int m = 0; m < 4; ++m) dst[m] = PG8_LD2(lds + PG8_SA(b, h) + aoff + m * 2048); } while (0)
; #define PG8_LDB(dst, b, h) do { _Pragma("unroll") for (int n = 0; n < 2; ++n) dst[n] = PG8_LD2(lds + PG8_SB(b, h) + boff + n * 2048); } while (0)
; #define PG8_WAIT_V(n) asm volatile("s_waitcnt vmcnt(" #n ")" ::: "memory")
; #define PG8_WAIT_L(n) asm volatile("s_waitcnt lgkmcnt(" #n ")" ::: "memory")
; #define PG8_BAR __builtin_amdgcn_s_barrier()
; #define PG8_SCHED __builtin_amdgcn_sched_barrier(0)
; template <class Epi, class Sched, bool ALIGN_EPI = false, bool SP2 = false, bool FP8 = false>
; __device__ __forceinline__ void gemm_phase(LAS unsigned char* lds, const Gemm g, const Sched& S, const Epi& E, int wbase) {
;     ...
;             PG8_LDB(B0, 1, 0); PG8_LDB(B1, 1, 1); PG8_SCHED; PG8_LDA(At, 1, 0); PG8_STAGE(PG8_SA(0, 1), rA2, a2 + hstep, voffA);
;             PG8_WAIT_V(8); PG8_WAIT_L(0); PG8_BAR; PG8_MMA(0, 0, At, B0); PG8_MMA(0, 1, At, B1); PG8_BAR; PG8_SCHED;
;             PG8_LDA(At, 1, 1); PG8_STAGE(PG8_SB(1, 0), rB2, b3, voffB); PG8_STAGE(PG8_SB(1, 1), rB2, b3 + hstep, voffB); PG8_STAGE(PG8_SA(1, 0), rA2, a3, voffA);
;             PG8_WAIT_V(8); PG8_WAIT_L(0); PG8_BAR; PG8_MMA(1, 0, At, B0); PG8_MMA(1, 1, At, B1); PG8_BAR; PG8_SCHED;
	s_mov_b32 m0, s27
	s_nop 0
	buffer_load_dwordx4 v149, s[4:7], s66 offen lds
	v_add_u32_e32 v136, 0x18000, v161
	ds_read_b128 v[128:131], v136
	ds_read_b128 v[132:135], v136 offset:1024
	ds_read_b128 v[164:167], v136 offset:2048
	ds_read_b128 v[168:171], v136 offset:3072
	v_add_u32_e32 v136, 0x1c000, v161
	ds_read_b128 v[172:175], v136
	ds_read_b128 v[176:179], v136 offset:1024
	ds_read_b128 v[180:183], v136 offset:2048
	ds_read_b128 v[184:187], v136 offset:3072
	s_add_i32 s65, s65, s22
	s_mov_b32 m0, s29
	ds_read_b128 v[188:191], v162 offset:32768
	ds_read_b128 v[192:195], v162 offset:33792
	ds_read_b128 v[196:199], v162 offset:34816
	ds_read_b128 v[200:203], v162 offset:35840
	ds_read_b128 v[204:207], v162 offset:36864
	ds_read_b128 v[208:211], v162 offset:37888
	ds_read_b128 v[212:215], v162 offset:38912
	ds_read_b128 v[216:219], v162 offset:39936
	buffer_load_dwordx4 v137, s[36:39], s65 offen lds
	s_mov_b32 m0, s30
	s_nop 0
	buffer_load_dwordx4 v145, s[36:39], s65 offen lds
	s_waitcnt vmcnt(8)
	s_waitcnt lgkmcnt(0)
	s_barrier
	s_setprio 1
	v_mfma_f32_16x16x32_bf16 v[120:123], v[128:131], v[188:191], v[120:123]
	v_mfma_f32_16x16x32_bf16 v[124:127], v[164:167], v[188:191], v[124:127]
	v_mfma_f32_16x16x32_bf16 v[104:107], v[128:131], v[196:199], v[104:107]
	v_mfma_f32_16x16x32_bf16 v[108:111], v[164:167], v[196:199], v[108:111]
	v_mfma_f32_16x16x32_bf16 v[88:91], v[128:131], v[204:207], v[88:91]
	v_mfma_f32_16x16x32_bf16 v[92:95], v[164:167], v[204:207], v[92:95]
	v_mfma_f32_16x16x32_bf16 v[72:75], v[128:131], v[212:215], v[72:75]
	v_mfma_f32_16x16x32_bf16 v[76:79], v[164:167], v[212:215], v[76:79]
	v_mfma_f32_16x16x32_bf16 v[120:123], v[132:135], v[192:195], v[120:123]
	v_mfma_f32_16x16x32_bf16 v[124:127], v[168:171], v[192:195], v[124:127]
	v_mfma_f32_16x16x32_bf16 v[104:107], v[132:135], v[200:203], v[104:107]
	v_mfma_f32_16x16x32_bf16 v[108:111], v[168:171], v[200:203], v[108:111]
	v_mfma_f32_16x16x32_bf16 v[88:91], v[132:135], v[208:211], v[88:91]
	v_mfma_f32_16x16x32_bf16 v[92:95], v[168:171], v[208:211], v[92:95]
	v_mfma_f32_16x16x32_bf16 v[72:75], v[132:135], v[216:219], v[72:75]
	v_mfma_f32_16x16x32_bf16 v[76:79], v[168:171], v[216:219], v[76:79]
	v_mfma_f32_16x16x32_bf16 v[112:115], v[172:175], v[188:191], v[112:115]
	v_mfma_f32_16x16x32_bf16 v[116:119], v[180:183], v[188:191], v[116:119]
	v_mfma_f32_16x16x32_bf16 v[96:99], v[172:175], v[196:199], v[96:99]
	v_mfma_f32_16x16x32_bf16 v[100:103], v[180:183], v[196:199], v[100:103]
	v_mfma_f32_16x16x32_bf16 v[80:83], v[172:175], v[204:207], v[80:83]
	v_mfma_f32_16x16x32_bf16 v[84:87], v[180:183], v[204:207], v[84:87]
	v_mfma_f32_16x16x32_bf16 v[64:67], v[172:175], v[212:215], v[64:67]
	v_mfma_f32_16x16x32_bf16 v[68:71], v[180:183], v[212:215], v[68:71]
	v_mfma_f32_16x16x32_bf16 v[112:115], v[176:179], v[192:195], v[112:115]
	v_mfma_f32_16x16x32_bf16 v[116:119], v[184:187], v[192:195], v[116:119]
	v_mfma_f32_16x16x32_bf16 v[96:99], v[176:179], v[200:203], v[96:99]
	v_mfma_f32_16x16x32_bf16 v[100:103], v[184:187], v[200:203], v[100:103]
	v_mfma_f32_16x16x32_bf16 v[80:83], v[176:179], v[208:211], v[80:83]
	v_mfma_f32_16x16x32_bf16 v[84:87], v[184:187], v[208:211], v[84:87]
	v_mfma_f32_16x16x32_bf16 v[64:67], v[176:179], v[216:219], v[64:67]
	v_mfma_f32_16x16x32_bf16 v[68:71], v[184:187], v[216:219], v[68:71]
	s_setprio 0
	s_barrier
	s_mov_b32 m0, s31
	s_bitset1_b32 s55, 7
	buffer_load_dwordx4 v141, s[4:7], s55 offen lds
	s_mov_b32 m0, s33
	ds_read_b128 v[188:191], v162 offset:49152
	buffer_load_dwordx4 v149, s[4:7], s55 offen lds
	s_add_i32 s55, s55, s22
	s_mov_b32 m0, s41
	ds_read_b128 v[192:195], v162 offset:50176
	buffer_load_dwordx4 v141, s[4:7], s55 offen lds
	s_mov_b32 m0, s42
	ds_read_b128 v[196:199], v162 offset:51200
	buffer_load_dwordx4 v149, s[4:7], s55 offen lds
	s_mov_b32 m0, s34
	ds_read_b128 v[200:203], v162 offset:52224
	buffer_load_dwordx4 v137, s[36:39], s54 offen lds
	s_mov_b32 m0, s35
	ds_read_b128 v[204:207], v162 offset:53248
	buffer_load_dwordx4 v145, s[36:39], s54 offen lds
	ds_read_b128 v[208:211], v162 offset:54272
	ds_read_b128 v[212:215], v162 offset:55296
	ds_read_b128 v[216:219], v162 offset:56320
	s_waitcnt vmcnt(8)
	s_waitcnt lgkmcnt(0)
	s_barrier
	s_setprio 1
	v_mfma_f32_16x16x32_bf16 v[56:59], v[128:131], v[188:191], v[56:59]
	v_mfma_f32_16x16x32_bf16 v[60:63], v[164:167], v[188:191], v[60:63]
	v_mfma_f32_16x16x32_bf16 v[40:43], v[128:131], v[196:199], v[40:43]
	v_mfma_f32_16x16x32_bf16 v[44:47], v[164:167], v[196:199], v[44:47]
	v_mfma_f32_16x16x32_bf16 v[24:27], v[128:131], v[204:207], v[24:27]
	v_mfma_f32_16x16x32_bf16 v[28:31], v[164:167], v[204:207], v[28:31]
	v_mfma_f32_16x16x32_bf16 v[8:11], v[128:131], v[212:215], v[8:11]
	v_mfma_f32_16x16x32_bf16 v[12:15], v[164:167], v[212:215], v[12:15]
	v_mfma_f32_16x16x32_bf16 v[56:59], v[132:135], v[192:195], v[56:59]
	v_mfma_f32_16x16x32_bf16 v[60:63], v[168:171], v[192:195], v[60:63]
	v_mfma_f32_16x16x32_bf16 v[40:43], v[132:135], v[200:203], v[40:43]
	v_mfma_f32_16x16x32_bf16 v[44:47], v[168:171], v[200:203], v[44:47]
	v_mfma_f32_16x16x32_bf16 v[24:27], v[132:135], v[208:211], v[24:27]
	v_mfma_f32_16x16x32_bf16 v[28:31], v[168:171], v[208:211], v[28:31]
	v_mfma_f32_16x16x32_bf16 v[8:11], v[132:135], v[216:219], v[8:11]
	v_mfma_f32_16x16x32_bf16 v[12:15], v[168:171], v[216:219], v[12:15]
	v_mfma_f32_16x16x32_bf16 v[48:51], v[172:175], v[188:191], v[48:51]
	v_mfma_f32_16x16x32_bf16 v[52:55], v[180:183], v[188:191], v[52:55]
	v_mfma_f32_16x16x32_bf16 v[32:35], v[172:175], v[196:199], v[32:35]
	v_mfma_f32_16x16x32_bf16 v[36:39], v[180:183], v[196:199], v[36:39]
	v_mfma_f32_16x16x32_bf16 v[16:19], v[172:175], v[204:207], v[16:19]
	v_mfma_f32_16x16x32_bf16 v[20:23], v[180:183], v[204:207], v[20:23]
	v_mfma_f32_16x16x32_bf16 v[4:7], v[172:175], v[212:215], v[4:7]
	v_mfma_f32_16x16x32_bf16 v[0:3], v[180:183], v[212:215], v[0:3]
	v_mfma_f32_16x16x32_bf16 v[48:51], v[176:179], v[192:195], v[48:51]
	v_mfma_f32_16x16x32_bf16 v[52:55], v[184:187], v[192:195], v[52:55]
	v_mfma_f32_16x16x32_bf16 v[32:35], v[176:179], v[200:203], v[32:35]
	v_mfma_f32_16x16x32_bf16 v[36:39], v[184:187], v[200:203], v[36:39]
	v_mfma_f32_16x16x32_bf16 v[16:19], v[176:179], v[208:211], v[16:19]
	v_mfma_f32_16x16x32_bf16 v[20:23], v[184:187], v[208:211], v[20:23]
	v_mfma_f32_16x16x32_bf16 v[4:7], v[176:179], v[216:219], v[4:7]
	v_mfma_f32_16x16x32_bf16 v[0:3], v[184:187], v[216:219], v[0:3]
	s_setprio 0
	s_barrier
	s_add_i32 s63, s63, 2
	s_addk_i32 s61, 0x100
	s_addk_i32 s62, 0x100
	s_cmp_ge_i32 s63, s44
	s_cbranch_scc0 .LBB0_1628
	s_branch .Lzp_after_1628
; #define PG8_STAGE(bufoff, rs_, soff_, voff) do { _Pragma("unroll") for (int _i = 0; _i < 2; ++_i) \
;         __builtin_amdgcn_raw_ptr_buffer_load_lds(rs_, (LAS void*)(lds + (bufoff) + ldsw + _i * 8192), 16, (int)(voff)[_i], (int)(soff_), 0, 0); } while (0)
; #define PG8_LDA(dst, b, h) do { _Pragma("unroll") for (int m = 0; m < 4; ++m) dst[m] = PG8_LD2(lds + PG8_SA(b, h) + aoff + m * 2048); } while (0)
; #define PG8_LDB(dst, b, h) do { _Pragma("unroll") for (int n = 0; n < 2; ++n) dst[n] = PG8_LD2(lds + PG8_SB(b, h) + boff + n * 2048); } while (0)
; #define PG8_WAIT_V(n) asm volatile("s_waitcnt vmcnt(" #n ")" ::: "memory")
; #define PG8_WAIT_L(n) asm volatile("s_waitcnt lgkmcnt(" #n ")" ::: "memory")
; #define PG8_BAR __builtin_amdgcn_s_barrier()
; #define PG8_SCHED __builtin_amdgcn_sched_barrier(0)
; template <class Epi, class Sched, bool ALIGN_EPI = false, bool SP2 = false, bool FP8 = false>
; __device__ __forceinline__ void gemm_phase(LAS unsigned char* lds, const Gemm g, const Sched& S, const Epi& E, int wbase) {
;     ...
;             PG8_LDB(B0, 0, 0); PG8_LDB(B1, 0, 1); PG8_SCHED; PG8_LDA(At, 0, 0); PG8_STAGE(PG8_SA(1, 1), rAc, a1 + hstep, voffA);
;             PG8_WAIT_V(8); PG8_WAIT_L(0); PG8_BAR; PG8_MMA(0, 0, At, B0); PG8_MMA(0, 1, At, B1); PG8_BAR; PG8_SCHED;
;             PG8_LDA(At, 0, 1); PG8_STAGE(PG8_SB(0, 0), rB2, b2, voffB); PG8_STAGE(PG8_SB(0, 1), rB2, b2 + hstep, voffB); PG8_STAGE(PG8_SA(0, 0), rA2, a2, voffA);
;             PG8_WAIT_V(8); PG8_WAIT_L(0); PG8_BAR; PG8_MMA(1, 0, At, B0); PG8_MMA(1, 1, At, B1); PG8_BAR; PG8_SCHED;
.LBB0_1628:
	v_add_u32_e32 v136, 0x10000, v161
	ds_read_b128 v[128:131], v136
	ds_read_b128 v[132:135], v136 offset:1024
	ds_read_b128 v[164:167], v136 offset:2048
	ds_read_b128 v[168:171], v136 offset:3072
	v_add_u32_e32 v136, 0x14000, v161
	ds_read_b128 v[172:175], v136
	ds_read_b128 v[176:179], v136 offset:1024
	ds_read_b128 v[180:183], v136 offset:2048
	ds_read_b128 v[184:187], v136 offset:3072
	s_add_i32 s6, s61, 0x80
	s_cmp_eq_u32 s46, s63
	s_cselect_b32 s65, s59, s6
	s_cselect_b32 s55, s60, s62
	s_or_b32 s54, s65, 0x80
	s_add_i32 s6, s22, s61
	s_mov_b32 m0, s47
	ds_read_b128 v[188:191], v162
	ds_read_b128 v[192:195], v162 offset:1024
	ds_read_b128 v[196:199], v162 offset:2048
	ds_read_b128 v[200:203], v162 offset:3072
	ds_read_b128 v[204:207], v162 offset:4096
	ds_read_b128 v[208:211], v162 offset:5120
	ds_read_b128 v[212:215], v162 offset:6144
	ds_read_b128 v[216:219], v162 offset:7168
	buffer_load_dwordx4 v137, s[36:39], s6 offen lds
	s_mov_b32 m0, s48
	s_nop 0
	buffer_load_dwordx4 v145, s[36:39], s6 offen lds
	s_waitcnt vmcnt(8)
	s_waitcnt lgkmcnt(0)
	s_barrier
	s_setprio 1
	v_mfma_f32_16x16x32_bf16 v[120:123], v[128:131], v[188:191], v[120:123]
	v_mfma_f32_16x16x32_bf16 v[124:127], v[164:167], v[188:191], v[124:127]
	v_mfma_f32_16x16x32_bf16 v[104:107], v[128:131], v[196:199], v[104:107]
	v_mfma_f32_16x16x32_bf16 v[108:111], v[164:167], v[196:199], v[108:111]
	v_mfma_f32_16x16x32_bf16 v[88:91], v[128:131], v[204:207], v[88:91]
	v_mfma_f32_16x16x32_bf16 v[92:95], v[164:167], v[204:207], v[92:95]
	v_mfma_f32_16x16x32_bf16 v[72:75], v[128:131], v[212:215], v[72:75]
	v_mfma_f32_16x16x32_bf16 v[76:79], v[164:167], v[212:215], v[76:79]
	v_mfma_f32_16x16x32_bf16 v[120:123], v[132:135], v[192:195], v[120:123]
	v_mfma_f32_16x16x32_bf16 v[124:127], v[168:171], v[192:195], v[124:127]
	v_mfma_f32_16x16x32_bf16 v[104:107], v[132:135], v[200:203], v[104:107]
	v_mfma_f32_16x16x32_bf16 v[108:111], v[168:171], v[200:203], v[108:111]
	v_mfma_f32_16x16x32_bf16 v[88:91], v[132:135], v[208:211], v[88:91]
	v_mfma_f32_16x16x32_bf16 v[92:95], v[168:171], v[208:211], v[92:95]
	v_mfma_f32_16x16x32_bf16 v[72:75], v[132:135], v[216:219], v[72:75]
	v_mfma_f32_16x16x32_bf16 v[76:79], v[168:171], v[216:219], v[76:79]
	v_mfma_f32_16x16x32_bf16 v[112:115], v[172:175], v[188:191], v[112:115]
	v_mfma_f32_16x16x32_bf16 v[116:119], v[180:183], v[188:191], v[116:119]
	v_mfma_f32_16x16x32_bf16 v[96:99], v[172:175], v[196:199], v[96:99]
	v_mfma_f32_16x16x32_bf16 v[100:103], v[180:183], v[196:199], v[100:103]
	v_mfma_f32_16x16x32_bf16 v[80:83], v[172:175], v[204:207], v[80:83]
	v_mfma_f32_16x16x32_bf16 v[84:87], v[180:183], v[204:207], v[84:87]
	v_mfma_f32_16x16x32_bf16 v[64:67], v[172:175], v[212:215], v[64:67]
	v_mfma_f32_16x16x32_bf16 v[68:71], v[180:183], v[212:215], v[68:71]
	v_mfma_f32_16x16x32_bf16 v[112:115], v[176:179], v[192:195], v[112:115]
	v_mfma_f32_16x16x32_bf16 v[116:119], v[184:187], v[192:195], v[116:119]
	v_mfma_f32_16x16x32_bf16 v[96:99], v[176:179], v[200:203], v[96:99]
	v_mfma_f32_16x16x32_bf16 v[100:103], v[184:187], v[200:203], v[100:103]
	v_mfma_f32_16x16x32_bf16 v[80:83], v[176:179], v[208:211], v[80:83]
	v_mfma_f32_16x16x32_bf16 v[84:87], v[184:187], v[208:211], v[84:87]
	v_mfma_f32_16x16x32_bf16 v[64:67], v[176:179], v[216:219], v[64:67]
	v_mfma_f32_16x16x32_bf16 v[68:71], v[184:187], v[216:219], v[68:71]
	s_setprio 0
	s_barrier
	s_mov_b32 m0, s24
	s_mov_b32 s6, s38
	s_mov_b32 s7, s39
	buffer_load_dwordx4 v141, s[4:7], s55 offen lds
	s_mov_b32 m0, s25
	ds_read_b128 v[188:191], v162 offset:16384
	s_add_i32 s66, s55, s22
	buffer_load_dwordx4 v149, s[4:7], s55 offen lds
	s_mov_b32 m0, s26
	ds_read_b128 v[192:195], v162 offset:17408
	buffer_load_dwordx4 v141, s[4:7], s66 offen lds
	s_mov_b32 m0, s23
	ds_read_b128 v[196:199], v162 offset:18432
	buffer_load_dwordx4 v137, s[36:39], s65 offen lds
	s_mov_b32 m0, s28
	ds_read_b128 v[200:203], v162 offset:19456
	buffer_load_dwordx4 v145, s[36:39], s65 offen lds
	ds_read_b128 v[204:207], v162 offset:20480
	ds_read_b128 v[208:211], v162 offset:21504
	ds_read_b128 v[212:215], v162 offset:22528
	ds_read_b128 v[216:219], v162 offset:23552
	s_waitcnt vmcnt(7)
	s_waitcnt lgkmcnt(0)
	s_barrier
	s_setprio 1
	v_mfma_f32_16x16x32_bf16 v[56:59], v[128:131], v[188:191], v[56:59]
	v_mfma_f32_16x16x32_bf16 v[60:63], v[164:167], v[188:191], v[60:63]
	v_mfma_f32_16x16x32_bf16 v[40:43], v[128:131], v[196:199], v[40:43]
	v_mfma_f32_16x16x32_bf16 v[44:47], v[164:167], v[196:199], v[44:47]
	v_mfma_f32_16x16x32_bf16 v[24:27], v[128:131], v[204:207], v[24:27]
	v_mfma_f32_16x16x32_bf16 v[28:31], v[164:167], v[204:207], v[28:31]
	v_mfma_f32_16x16x32_bf16 v[8:11], v[128:131], v[212:215], v[8:11]
	v_mfma_f32_16x16x32_bf16 v[12:15], v[164:167], v[212:215], v[12:15]
	v_mfma_f32_16x16x32_bf16 v[56:59], v[132:135], v[192:195], v[56:59]
	v_mfma_f32_16x16x32_bf16 v[60:63], v[168:171], v[192:195], v[60:63]
	v_mfma_f32_16x16x32_bf16 v[40:43], v[132:135], v[200:203], v[40:43]
	v_mfma_f32_16x16x32_bf16 v[44:47], v[168:171], v[200:203], v[44:47]
	v_mfma_f32_16x16x32_bf16 v[24:27], v[132:135], v[208:211], v[24:27]
	v_mfma_f32_16x16x32_bf16 v[28:31], v[168:171], v[208:211], v[28:31]
	v_mfma_f32_16x16x32_bf16 v[8:11], v[132:135], v[216:219], v[8:11]
	v_mfma_f32_16x16x32_bf16 v[12:15], v[168:171], v[216:219], v[12:15]
	v_mfma_f32_16x16x32_bf16 v[48:51], v[172:175], v[188:191], v[48:51]
	v_mfma_f32_16x16x32_bf16 v[52:55], v[180:183], v[188:191], v[52:55]
	v_mfma_f32_16x16x32_bf16 v[32:35], v[172:175], v[196:199], v[32:35]
	v_mfma_f32_16x16x32_bf16 v[36:39], v[180:183], v[196:199], v[36:39]
	v_mfma_f32_16x16x32_bf16 v[16:19], v[172:175], v[204:207], v[16:19]
	v_mfma_f32_16x16x32_bf16 v[20:23], v[180:183], v[204:207], v[20:23]
	v_mfma_f32_16x16x32_bf16 v[4:7], v[172:175], v[212:215], v[4:7]
	v_mfma_f32_16x16x32_bf16 v[0:3], v[180:183], v[212:215], v[0:3]
	v_mfma_f32_16x16x32_bf16 v[48:51], v[176:179], v[192:195], v[48:51]
	v_mfma_f32_16x16x32_bf16 v[52:55], v[184:187], v[192:195], v[52:55]
	v_mfma_f32_16x16x32_bf16 v[32:35], v[176:179], v[200:203], v[32:35]
	v_mfma_f32_16x16x32_bf16 v[36:39], v[184:187], v[200:203], v[36:39]
	v_mfma_f32_16x16x32_bf16 v[16:19], v[176:179], v[208:211], v[16:19]
	v_mfma_f32_16x16x32_bf16 v[20:23], v[184:187], v[208:211], v[20:23]
	v_mfma_f32_16x16x32_bf16 v[4:7], v[176:179], v[216:219], v[4:7]
	v_mfma_f32_16x16x32_bf16 v[0:3], v[184:187], v[216:219], v[0:3]
	s_setprio 0
	s_barrier
; #define PG8_STAGE(bufoff, rs_, soff_, voff) do { _Pragma("unroll") for (int _i = 0; _i < 2; ++_i) \
;         __builtin_amdgcn_raw_ptr_buffer_load_lds(rs_, (LAS void*)(lds + (bufoff) + ldsw + _i * 8192), 16, (int)(voff)[_i], (int)(soff_), 0, 0); } while (0)
; #define PG8_LDA(dst, b, h) do { _Pragma("unroll") for (int m = 0; m < 4; ++m) dst[m] = PG8_LD2(lds + PG8_SA(b, h) + aoff + m * 2048); } while (0)
; #define PG8_LDB(dst, b, h) do { _Pragma("unroll") for (int n = 0; n < 2; ++n) dst[n] = PG8_LD2(lds + PG8_SB(b, h) + boff + n * 2048); } while (0)
; #define PG8_WAIT_V(n) asm volatile("s_waitcnt vmcnt(" #n ")" ::: "memory")
; #define PG8_WAIT_L(n) asm volatile("s_waitcnt lgkmcnt(" #n ")" ::: "memory")
; #define PG8_BAR __builtin_amdgcn_s_barrier()
; #define PG8_SCHED __builtin_amdgcn_sched_barrier(0)
; template <class Epi, class Sched, bool ALIGN_EPI = false, bool SP2 = false, bool FP8 = false>
; __device__ __forceinline__ void gemm_phase(LAS unsigned char* lds, const Gemm g, const Sched& S, const Epi& E, int wbase) {
;     ...
;             PG8_LDB(B0, 1, 0); PG8_LDB(B1, 1, 1); PG8_SCHED; PG8_LDA(At, 1, 0); PG8_STAGE(PG8_SA(0, 1), rA2, a2 + hstep, voffA);
;             PG8_WAIT_V(8); PG8_WAIT_L(0); PG8_BAR; PG8_MMA(0, 0, At, B0); PG8_MMA(0, 1, At, B1); PG8_BAR; PG8_SCHED;
;             PG8_LDA(At, 1, 1); PG8_STAGE(PG8_SB(1, 0), rB2, b3, voffB); PG8_STAGE(PG8_SB(1, 1), rB2, b3 + hstep, voffB); PG8_STAGE(PG8_SA(1, 0), rA2, a3, voffA);
;             PG8_WAIT_V(8); PG8_WAIT_L(0); PG8_BAR; PG8_MMA(1, 0, At, B0); PG8_MMA(1, 1, At, B1); PG8_BAR; PG8_SCHED;
	s_mov_b32 m0, s27
	s_nop 0
	buffer_load_dwordx4 v149, s[4:7], s66 offen lds
	v_add_u32_e32 v136, 0x18000, v161
	ds_read_b128 v[128:131], v136
	ds_read_b128 v[132:135], v136 offset:1024
	ds_read_b128 v[164:167], v136 offset:2048
	ds_read_b128 v[168:171], v136 offset:3072
	v_add_u32_e32 v136, 0x1c000, v161
	ds_read_b128 v[172:175], v136
	ds_read_b128 v[176:179], v136 offset:1024
	ds_read_b128 v[180:183], v136 offset:2048
	ds_read_b128 v[184:187], v136 offset:3072
	s_add_i32 s65, s65, s22
	s_mov_b32 m0, s29
	ds_read_b128 v[188:191], v162 offset:32768
	ds_read_b128 v[192:195], v162 offset:33792
	ds_read_b128 v[196:199], v162 offset:34816
	ds_read_b128 v[200:203], v162 offset:35840
	ds_read_b128 v[204:207], v162 offset:36864
	ds_read_b128 v[208:211], v162 offset:37888
	ds_read_b128 v[212:215], v162 offset:38912
	ds_read_b128 v[216:219], v162 offset:39936
	buffer_load_dwordx4 v137, s[36:39], s65 offen lds
	s_mov_b32 m0, s30
	s_nop 0
	buffer_load_dwordx4 v145, s[36:39], s65 offen lds
	s_waitcnt vmcnt(8)
	s_waitcnt lgkmcnt(0)
	s_barrier
	s_setprio 1
	v_mfma_f32_16x16x32_bf16 v[120:123], v[128:131], v[188:191], v[120:123]
	v_mfma_f32_16x16x32_bf16 v[124:127], v[164:167], v[188:191], v[124:127]
	v_mfma_f32_16x16x32_bf16 v[104:107], v[128:131], v[196:199], v[104:107]
	v_mfma_f32_16x16x32_bf16 v[108:111], v[164:167], v[196:199], v[108:111]
	v_mfma_f32_16x16x32_bf16 v[88:91], v[128:131], v[204:207], v[88:91]
	v_mfma_f32_16x16x32_bf16 v[92:95], v[164:167], v[204:207], v[92:95]
	v_mfma_f32_16x16x32_bf16 v[72:75], v[128:131], v[212:215], v[72:75]
	v_mfma_f32_16x16x32_bf16 v[76:79], v[164:167], v[212:215], v[76:79]
	v_mfma_f32_16x16x32_bf16 v[120:123], v[132:135], v[192:195], v[120:123]
	v_mfma_f32_16x16x32_bf16 v[124:127], v[168:171], v[192:195], v[124:127]
	v_mfma_f32_16x16x32_bf16 v[104:107], v[132:135], v[200:203], v[104:107]
	v_mfma_f32_16x16x32_bf16 v[108:111], v[168:171], v[200:203], v[108:111]
	v_mfma_f32_16x16x32_bf16 v[88:91], v[132:135], v[208:211], v[88:91]
	v_mfma_f32_16x16x32_bf16 v[92:95], v[168:171], v[208:211], v[92:95]
	v_mfma_f32_16x16x32_bf16 v[72:75], v[132:135], v[216:219], v[72:75]
	v_mfma_f32_16x16x32_bf16 v[76:79], v[168:171], v[216:219], v[76:79]
	v_mfma_f32_16x16x32_bf16 v[112:115], v[172:175], v[188:191], v[112:115]
	v_mfma_f32_16x16x32_bf16 v[116:119], v[180:183], v[188:191], v[116:119]
	v_mfma_f32_16x16x32_bf16 v[96:99], v[172:175], v[196:199], v[96:99]
	v_mfma_f32_16x16x32_bf16 v[100:103], v[180:183], v[196:199], v[100:103]
	v_mfma_f32_16x16x32_bf16 v[80:83], v[172:175], v[204:207], v[80:83]
	v_mfma_f32_16x16x32_bf16 v[84:87], v[180:183], v[204:207], v[84:87]
	v_mfma_f32_16x16x32_bf16 v[64:67], v[172:175], v[212:215], v[64:67]
	v_mfma_f32_16x16x32_bf16 v[68:71], v[180:183], v[212:215], v[68:71]
	v_mfma_f32_16x16x32_bf16 v[112:115], v[176:179], v[192:195], v[112:115]
	v_mfma_f32_16x16x32_bf16 v[116:119], v[184:187], v[192:195], v[116:119]
	v_mfma_f32_16x16x32_bf16 v[96:99], v[176:179], v[200:203], v[96:99]
	v_mfma_f32_16x16x32_bf16 v[100:103], v[184:187], v[200:203], v[100:103]
	v_mfma_f32_16x16x32_bf16 v[80:83], v[176:179], v[208:211], v[80:83]
	v_mfma_f32_16x16x32_bf16 v[84:87], v[184:187], v[208:211], v[84:87]
	v_mfma_f32_16x16x32_bf16 v[64:67], v[176:179], v[216:219], v[64:67]
	v_mfma_f32_16x16x32_bf16 v[68:71], v[184:187], v[216:219], v[68:71]
	s_setprio 0
	s_barrier
	s_mov_b32 m0, s31
	s_bitset1_b32 s55, 7
	buffer_load_dwordx4 v141, s[4:7], s55 offen lds
	s_mov_b32 m0, s33
	ds_read_b128 v[188:191], v162 offset:49152
	buffer_load_dwordx4 v149, s[4:7], s55 offen lds
	s_add_i32 s55, s55, s22
	s_mov_b32 m0, s41
	ds_read_b128 v[192:195], v162 offset:50176
	buffer_load_dwordx4 v141, s[4:7], s55 offen lds
	s_mov_b32 m0, s42
	ds_read_b128 v[196:199], v162 offset:51200
	buffer_load_dwordx4 v149, s[4:7], s55 offen lds
	s_mov_b32 m0, s34
	ds_read_b128 v[200:203], v162 offset:52224
	buffer_load_dwordx4 v137, s[36:39], s54 offen lds
	s_mov_b32 m0, s35
	ds_read_b128 v[204:207], v162 offset:53248
	buffer_load_dwordx4 v145, s[36:39], s54 offen lds
	ds_read_b128 v[208:211], v162 offset:54272
	ds_read_b128 v[212:215], v162 offset:55296
	ds_read_b128 v[216:219], v162 offset:56320
	s_waitcnt vmcnt(8)
	s_waitcnt lgkmcnt(0)
	s_barrier
	s_setprio 1
	v_mfma_f32_16x16x32_bf16 v[56:59], v[128:131], v[188:191], v[56:59]
	v_mfma_f32_16x16x32_bf16 v[60:63], v[164:167], v[188:191], v[60:63]
	v_mfma_f32_16x16x32_bf16 v[40:43], v[128:131], v[196:199], v[40:43]
	v_mfma_f32_16x16x32_bf16 v[44:47], v[164:167], v[196:199], v[44:47]
	v_mfma_f32_16x16x32_bf16 v[24:27], v[128:131], v[204:207], v[24:27]
	v_mfma_f32_16x16x32_bf16 v[28:31], v[164:167], v[204:207], v[28:31]
	v_mfma_f32_16x16x32_bf16 v[8:11], v[128:131], v[212:215], v[8:11]
	v_mfma_f32_16x16x32_bf16 v[12:15], v[164:167], v[212:215], v[12:15]
	v_mfma_f32_16x16x32_bf16 v[56:59], v[132:135], v[192:195], v[56:59]
	v_mfma_f32_16x16x32_bf16 v[60:63], v[168:171], v[192:195], v[60:63]
	v_mfma_f32_16x16x32_bf16 v[40:43], v[132:135], v[200:203], v[40:43]
	v_mfma_f32_16x16x32_bf16 v[44:47], v[168:171], v[200:203], v[44:47]
	v_mfma_f32_16x16x32_bf16 v[24:27], v[132:135], v[208:211], v[24:27]
	v_mfma_f32_16x16x32_bf16 v[28:31], v[168:171], v[208:211], v[28:31]
	v_mfma_f32_16x16x32_bf16 v[8:11], v[132:135], v[216:219], v[8:11]
	v_mfma_f32_16x16x32_bf16 v[12:15], v[168:171], v[216:219], v[12:15]
	v_mfma_f32_16x16x32_bf16 v[48:51], v[172:175], v[188:191], v[48:51]
	v_mfma_f32_16x16x32_bf16 v[52:55], v[180:183], v[188:191], v[52:55]
	v_mfma_f32_16x16x32_bf16 v[32:35], v[172:175], v[196:199], v[32:35]
	v_mfma_f32_16x16x32_bf16 v[36:39], v[180:183], v[196:199], v[36:39]
	v_mfma_f32_16x16x32_bf16 v[16:19], v[172:175], v[204:207], v[16:19]
	v_mfma_f32_16x16x32_bf16 v[20:23], v[180:183], v[204:207], v[20:23]
	v_mfma_f32_16x16x32_bf16 v[4:7], v[172:175], v[212:215], v[4:7]
	v_mfma_f32_16x16x32_bf16 v[0:3], v[180:183], v[212:215], v[0:3]
	v_mfma_f32_16x16x32_bf16 v[48:51], v[176:179], v[192:195], v[48:51]
	v_mfma_f32_16x16x32_bf16 v[52:55], v[184:187], v[192:195], v[52:55]
	v_mfma_f32_16x16x32_bf16 v[32:35], v[176:179], v[200:203], v[32:35]
	v_mfma_f32_16x16x32_bf16 v[36:39], v[184:187], v[200:203], v[36:39]
	v_mfma_f32_16x16x32_bf16 v[16:19], v[176:179], v[208:211], v[16:19]
	v_mfma_f32_16x16x32_bf16 v[20:23], v[184:187], v[208:211], v[20:23]
	v_mfma_f32_16x16x32_bf16 v[4:7], v[176:179], v[216:219], v[4:7]
	v_mfma_f32_16x16x32_bf16 v[0:3], v[184:187], v[216:219], v[0:3]
	s_setprio 0
	s_barrier
	s_add_i32 s63, s63, 2
	s_addk_i32 s61, 0x100
	s_addk_i32 s62, 0x100
	s_cmp_ge_i32 s63, s44
	s_cbranch_scc0 .LBB0_1628

; #define PG8_STAGE(bufoff, rs_, soff_, voff) do { _Pragma("unroll") for (int _i = 0; _i < 2; ++_i) \
;         __builtin_amdgcn_raw_ptr_buffer_load_lds(rs_, (LAS void*)(lds + (bufoff) + ldsw + _i * 8192), 16, (int)(voff)[_i], (int)(soff_), 0, 0); } while (0)
; #define PG8_LDA(dst, b, h) do { _Pragma("unroll") for (int m = 0; m < 4; ++m) dst[m] = PG8_LD2(lds + PG8_SA(b, h) + aoff + m * 2048); } while (0)
; #define PG8_LDB(dst, b, h) do { _Pragma("unroll") for (int n = 0; n < 2; ++n) dst[n] = PG8_LD2(lds + PG8_SB(b, h) + boff + n * 2048); } while (0)
; #define PG8_WAIT_V(n) asm volatile("s_waitcnt vmcnt(" #n ")" ::: "memory")
; #define PG8_WAIT_L(n) asm volatile("s_waitcnt lgkmcnt(" #n ")" ::: "memory")
; #define PG8_BAR __builtin_amdgcn_s_barrier()
; #define PG8_SCHED __builtin_amdgcn_sched_barrier(0)
; template <class Epi, class Sched, bool ALIGN_EPI = false, bool SP2 = false, bool FP8 = false>
; __device__ __forceinline__ void gemm_phase(LAS unsigned char* lds, const Gemm g, const Sched& S, const Epi& E, int wbase) {
;     ...
;         for (int t = 0; t < nt; t += 2) {
;             const bool last = (t == nt - 2);
;             const unsigned a1 = cA + (unsigned)(t + 1) * kstep;
;             const unsigned a2 = last ? nA : cA + (unsigned)(t + 2) * kstep, b2 = last ? nB : cB + (unsigned)(t + 2) * kstep; const rsrc_t rA2 = (Sched::TWO && last) ? rAn : rAc, rB2 = (Sched::TWO && last) ? rBn : rBc;
;             const unsigned a3 = a2 + kstep, b3 = b2 + kstep;
;             if (last && has_next) S.a_ready(nxt);
;             if constexpr (SP2) {
;             PG8_LDB(B0, 0, 0); PG8_LDB(B1, 0, 1); PG8_SCHED; PG8_LDA(At, 0, 0); PG8_STAGE(PG8_SA(1, 1), rAc, a1 + hstep, voffA);
;             PG8_WAIT_V(8); PG8_WAIT_L(0); PG8_BAR; PG8_MMA(0, 0, At, B0); PG8_MMA(0, 1, At, B1); PG8_BAR; PG8_SCHED;
;             PG8_LDA(At, 0, 1); PG8_STAGE(PG8_SB(0, 0), rB2, b2, voffB); PG8_STAGE(PG8_SB(0, 1), rB2, b2 + hstep, voffB); PG8_STAGE(PG8_SA(0, 0), rA2, a2, voffA);
;             PG8_WAIT_V(8); PG8_WAIT_L(0); PG8_BAR; PG8_MMA(1, 0, At, B0); PG8_MMA(1, 1, At, B1); PG8_BAR; PG8_SCHED;
.LBB0_1699:
	s_mul_i32 s61, s60, 0x1c0000
	s_andn2_b64 vcc, exec, s[14:15]
	s_mul_i32 s62, s59, 0x1c0000
	s_cbranch_vccnz .LBB0_1703
	s_and_b64 s[6:7], s[18:19], exec
	s_waitcnt vmcnt(37)
	s_waitcnt vmcnt(36)
	s_waitcnt vmcnt(35)
	s_waitcnt vmcnt(32)
	s_waitcnt vmcnt(31)
	s_waitcnt vmcnt(28)
	s_waitcnt vmcnt(27)
	s_waitcnt vmcnt(23)
	s_waitcnt vmcnt(22)
	s_cselect_b32 s21, s61, s55
	s_cselect_b32 s63, s62, s54
	s_add_i32 s65, s55, 0x80
	s_add_i32 s66, s54, 0x100
	s_mov_b32 s67, 0
	v_add_u32_e32 v140, 0x10000, v176
	v_add_u32_e32 v156, 0x14000, v176
	ds_read_b128 v[112:115], v140
	ds_read_b128 v[124:127], v140 offset:1024
	ds_read_b128 v[136:139], v140 offset:2048
	ds_read_b128 v[140:143], v140 offset:3072
	ds_read_b128 v[144:147], v156
	ds_read_b128 v[148:151], v156 offset:1024
	ds_read_b128 v[152:155], v156 offset:2048
	ds_read_b128 v[156:159], v156 offset:3072
	s_add_i32 s6, s65, 0x80
	s_cmp_eq_u32 s52, s67
	s_cselect_b32 s68, s21, s6
	s_cselect_b32 s55, s63, s66
	s_or_b32 s54, s68, 0x80
	s_add_i32 s6, s25, s65
	s_mov_b32 m0, s53
	ds_read_b128 v[160:163], v177
	ds_read_b128 v[164:167], v177 offset:1024
	ds_read_b128 v[178:181], v177 offset:2048
	ds_read_b128 v[182:185], v177 offset:3072
	ds_read_b128 v[186:189], v177 offset:4096
	ds_read_b128 v[190:193], v177 offset:5120
	ds_read_b128 v[194:197], v177 offset:6144
	ds_read_b128 v[198:201], v177 offset:7168
	buffer_load_dwordx4 v170, s[36:39], s6 offen lds
	s_mov_b32 m0, s56
	s_nop 0
	buffer_load_dwordx4 v172, s[36:39], s6 offen lds
	s_waitcnt vmcnt(8)
	s_waitcnt lgkmcnt(0)
	s_barrier
	s_setprio 1
	v_mfma_f32_16x16x32_bf16 v[132:135], v[112:115], v[160:163], 0
	v_mfma_f32_16x16x32_bf16 v[128:131], v[136:139], v[160:163], 0
	v_mfma_f32_16x16x32_bf16 v[108:111], v[112:115], v[178:181], 0
	v_mfma_f32_16x16x32_bf16 v[104:107], v[136:139], v[178:181], 0
	v_mfma_f32_16x16x32_bf16 v[92:95], v[112:115], v[186:189], 0
	v_mfma_f32_16x16x32_bf16 v[88:91], v[136:139], v[186:189], 0
	v_mfma_f32_16x16x32_bf16 v[76:79], v[112:115], v[194:197], 0
	v_mfma_f32_16x16x32_bf16 v[72:75], v[136:139], v[194:197], 0
	v_mfma_f32_16x16x32_bf16 v[132:135], v[124:127], v[164:167], v[132:135]
	v_mfma_f32_16x16x32_bf16 v[128:131], v[140:143], v[164:167], v[128:131]
	v_mfma_f32_16x16x32_bf16 v[108:111], v[124:127], v[182:185], v[108:111]
	v_mfma_f32_16x16x32_bf16 v[104:107], v[140:143], v[182:185], v[104:107]
	v_mfma_f32_16x16x32_bf16 v[92:95], v[124:127], v[190:193], v[92:95]
	v_mfma_f32_16x16x32_bf16 v[88:91], v[140:143], v[190:193], v[88:91]
	v_mfma_f32_16x16x32_bf16 v[76:79], v[124:127], v[198:201], v[76:79]
	v_mfma_f32_16x16x32_bf16 v[72:75], v[140:143], v[198:201], v[72:75]
	v_mfma_f32_16x16x32_bf16 v[120:123], v[144:147], v[160:163], 0
	v_mfma_f32_16x16x32_bf16 v[116:119], v[152:155], v[160:163], 0
	v_mfma_f32_16x16x32_bf16 v[100:103], v[144:147], v[178:181], 0
	v_mfma_f32_16x16x32_bf16 v[96:99], v[152:155], v[178:181], 0
	v_mfma_f32_16x16x32_bf16 v[84:87], v[144:147], v[186:189], 0
	v_mfma_f32_16x16x32_bf16 v[80:83], v[152:155], v[186:189], 0
	v_mfma_f32_16x16x32_bf16 v[68:71], v[144:147], v[194:197], 0
	v_mfma_f32_16x16x32_bf16 v[64:67], v[152:155], v[194:197], 0
	v_mfma_f32_16x16x32_bf16 v[120:123], v[148:151], v[164:167], v[120:123]
	v_mfma_f32_16x16x32_bf16 v[116:119], v[156:159], v[164:167], v[116:119]
	v_mfma_f32_16x16x32_bf16 v[100:103], v[148:151], v[182:185], v[100:103]
	v_mfma_f32_16x16x32_bf16 v[96:99], v[156:159], v[182:185], v[96:99]
	v_mfma_f32_16x16x32_bf16 v[84:87], v[148:151], v[190:193], v[84:87]
	v_mfma_f32_16x16x32_bf16 v[80:83], v[156:159], v[190:193], v[80:83]
	v_mfma_f32_16x16x32_bf16 v[68:71], v[148:151], v[198:201], v[68:71]
	v_mfma_f32_16x16x32_bf16 v[64:67], v[156:159], v[198:201], v[64:67]
	s_setprio 0
	s_barrier
	s_mov_b32 m0, s27
	s_mov_b32 s6, s38
	s_mov_b32 s7, s39
	buffer_load_dwordx4 v171, s[4:7], s55 offen lds
	s_mov_b32 m0, s28
	ds_read_b128 v[160:163], v177 offset:16384
	s_add_i32 s69, s55, s25
	buffer_load_dwordx4 v173, s[4:7], s55 offen lds
	s_mov_b32 m0, s29
	ds_read_b128 v[164:167], v177 offset:17408
	buffer_load_dwordx4 v171, s[4:7], s69 offen lds
	s_mov_b32 m0, s26
	ds_read_b128 v[178:181], v177 offset:18432
	buffer_load_dwordx4 v170, s[36:39], s68 offen lds
	s_mov_b32 m0, s31
	ds_read_b128 v[182:185], v177 offset:19456
	buffer_load_dwordx4 v172, s[36:39], s68 offen lds
	ds_read_b128 v[186:189], v177 offset:20480
	ds_read_b128 v[190:193], v177 offset:21504
	ds_read_b128 v[194:197], v177 offset:22528
	ds_read_b128 v[198:201], v177 offset:23552
	s_waitcnt vmcnt(7)
	s_waitcnt lgkmcnt(0)
	s_barrier
	s_setprio 1
	v_mfma_f32_16x16x32_bf16 v[60:63], v[112:115], v[160:163], 0
	v_mfma_f32_16x16x32_bf16 v[56:59], v[136:139], v[160:163], 0
	v_mfma_f32_16x16x32_bf16 v[44:47], v[112:115], v[178:181], 0
	v_mfma_f32_16x16x32_bf16 v[40:43], v[136:139], v[178:181], 0
	v_mfma_f32_16x16x32_bf16 v[28:31], v[112:115], v[186:189], 0
	v_mfma_f32_16x16x32_bf16 v[24:27], v[136:139], v[186:189], 0
	v_mfma_f32_16x16x32_bf16 v[12:15], v[112:115], v[194:197], 0
	v_mfma_f32_16x16x32_bf16 v[8:11], v[136:139], v[194:197], 0
	v_mfma_f32_16x16x32_bf16 v[60:63], v[124:127], v[164:167], v[60:63]
	v_mfma_f32_16x16x32_bf16 v[56:59], v[140:143], v[164:167], v[56:59]
	v_mfma_f32_16x16x32_bf16 v[44:47], v[124:127], v[182:185], v[44:47]
	v_mfma_f32_16x16x32_bf16 v[40:43], v[140:143], v[182:185], v[40:43]
	v_mfma_f32_16x16x32_bf16 v[28:31], v[124:127], v[190:193], v[28:31]
	v_mfma_f32_16x16x32_bf16 v[24:27], v[140:143], v[190:193], v[24:27]
	v_mfma_f32_16x16x32_bf16 v[12:15], v[124:127], v[198:201], v[12:15]
	v_mfma_f32_16x16x32_bf16 v[8:11], v[140:143], v[198:201], v[8:11]
	v_mfma_f32_16x16x32_bf16 v[52:55], v[144:147], v[160:163], 0
	v_mfma_f32_16x16x32_bf16 v[48:51], v[152:155], v[160:163], 0
	v_mfma_f32_16x16x32_bf16 v[36:39], v[144:147], v[178:181], 0
	v_mfma_f32_16x16x32_bf16 v[32:35], v[152:155], v[178:181], 0
	v_mfma_f32_16x16x32_bf16 v[20:23], v[144:147], v[186:189], 0
	v_mfma_f32_16x16x32_bf16 v[16:19], v[152:155], v[186:189], 0
	v_mfma_f32_16x16x32_bf16 v[4:7], v[144:147], v[194:197], 0
	v_mfma_f32_16x16x32_bf16 v[0:3], v[152:155], v[194:197], 0
	v_mfma_f32_16x16x32_bf16 v[52:55], v[148:151], v[164:167], v[52:55]
	v_mfma_f32_16x16x32_bf16 v[48:51], v[156:159], v[164:167], v[48:51]
	v_mfma_f32_16x16x32_bf16 v[36:39], v[148:151], v[182:185], v[36:39]
	v_mfma_f32_16x16x32_bf16 v[32:35], v[156:159], v[182:185], v[32:35]
	v_mfma_f32_16x16x32_bf16 v[20:23], v[148:151], v[190:193], v[20:23]
	v_mfma_f32_16x16x32_bf16 v[16:19], v[156:159], v[190:193], v[16:19]
	v_mfma_f32_16x16x32_bf16 v[4:7], v[148:151], v[198:201], v[4:7]
	v_mfma_f32_16x16x32_bf16 v[0:3], v[156:159], v[198:201], v[0:3]
	s_setprio 0
	s_barrier
; #define PG8_STAGE(bufoff, rs_, soff_, voff) do { _Pragma("unroll") for (int _i = 0; _i < 2; ++_i) \
;         __builtin_amdgcn_raw_ptr_buffer_load_lds(rs_, (LAS void*)(lds + (bufoff) + ldsw + _i * 8192), 16, (int)(voff)[_i], (int)(soff_), 0, 0); } while (0)
; #define PG8_LDA(dst, b, h) do { _Pragma("unroll") for (int m = 0; m < 4; ++m) dst[m] = PG8_LD2(lds + PG8_SA(b, h) + aoff + m * 2048); } while (0)
; #define PG8_LDB(dst, b, h) do { _Pragma("unroll") for (int n = 0; n < 2; ++n) dst[n] = PG8_LD2(lds + PG8_SB(b, h) + boff + n * 2048); } while (0)
; #define PG8_WAIT_V(n) asm volatile("s_waitcnt vmcnt(" #n ")" ::: "memory")
; #define PG8_WAIT_L(n) asm volatile("s_waitcnt lgkmcnt(" #n ")" ::: "memory")
; #define PG8_BAR __builtin_amdgcn_s_barrier()
; #define PG8_SCHED __builtin_amdgcn_sched_barrier(0)
; template <class Epi, class Sched, bool ALIGN_EPI = false, bool SP2 = false, bool FP8 = false>
; __device__ __forceinline__ void gemm_phase(LAS unsigned char* lds, const Gemm g, const Sched& S, const Epi& E, int wbase) {
;     ...
;             PG8_LDB(B0, 1, 0); PG8_LDB(B1, 1, 1); PG8_SCHED; PG8_LDA(At, 1, 0); PG8_STAGE(PG8_SA(0, 1), rA2, a2 + hstep, voffA);
;             PG8_WAIT_V(8); PG8_WAIT_L(0); PG8_BAR; PG8_MMA(0, 0, At, B0); PG8_MMA(0, 1, At, B1); PG8_BAR; PG8_SCHED;
;             PG8_LDA(At, 1, 1); PG8_STAGE(PG8_SB(1, 0), rB2, b3, voffB); PG8_STAGE(PG8_SB(1, 1), rB2, b3 + hstep, voffB); PG8_STAGE(PG8_SA(1, 0), rA2, a3, voffA);
;             PG8_WAIT_V(8); PG8_WAIT_L(0); PG8_BAR; PG8_MMA(1, 0, At, B0); PG8_MMA(1, 1, At, B1); PG8_BAR; PG8_SCHED;
	s_mov_b32 m0, s30
	s_nop 0
	buffer_load_dwordx4 v173, s[4:7], s69 offen lds
	v_add_u32_e32 v140, 0x18000, v176
	v_add_u32_e32 v156, 0x1c000, v176
	ds_read_b128 v[112:115], v140
	ds_read_b128 v[124:127], v140 offset:1024
	ds_read_b128 v[136:139], v140 offset:2048
	ds_read_b128 v[140:143], v140 offset:3072
	ds_read_b128 v[144:147], v156
	ds_read_b128 v[148:151], v156 offset:1024
	ds_read_b128 v[152:155], v156 offset:2048
	ds_read_b128 v[156:159], v156 offset:3072
	s_add_i32 s68, s68, s25
	s_mov_b32 m0, s33
	ds_read_b128 v[160:163], v177 offset:32768
	ds_read_b128 v[164:167], v177 offset:33792
	ds_read_b128 v[178:181], v177 offset:34816
	ds_read_b128 v[182:185], v177 offset:35840
	ds_read_b128 v[186:189], v177 offset:36864
	ds_read_b128 v[190:193], v177 offset:37888
	ds_read_b128 v[194:197], v177 offset:38912
	ds_read_b128 v[198:201], v177 offset:39936
	buffer_load_dwordx4 v170, s[36:39], s68 offen lds
	s_mov_b32 m0, s34
	s_nop 0
	buffer_load_dwordx4 v172, s[36:39], s68 offen lds
	s_waitcnt vmcnt(8)
	s_waitcnt lgkmcnt(0)
	s_barrier
	s_setprio 1
	v_mfma_f32_16x16x32_bf16 v[132:135], v[112:115], v[160:163], v[132:135]
	v_mfma_f32_16x16x32_bf16 v[128:131], v[136:139], v[160:163], v[128:131]
	v_mfma_f32_16x16x32_bf16 v[108:111], v[112:115], v[178:181], v[108:111]
	v_mfma_f32_16x16x32_bf16 v[104:107], v[136:139], v[178:181], v[104:107]
	v_mfma_f32_16x16x32_bf16 v[92:95], v[112:115], v[186:189], v[92:95]
	v_mfma_f32_16x16x32_bf16 v[88:91], v[136:139], v[186:189], v[88:91]
	v_mfma_f32_16x16x32_bf16 v[76:79], v[112:115], v[194:197], v[76:79]
	v_mfma_f32_16x16x32_bf16 v[72:75], v[136:139], v[194:197], v[72:75]
	v_mfma_f32_16x16x32_bf16 v[132:135], v[124:127], v[164:167], v[132:135]
	v_mfma_f32_16x16x32_bf16 v[128:131], v[140:143], v[164:167], v[128:131]
	v_mfma_f32_16x16x32_bf16 v[108:111], v[124:127], v[182:185], v[108:111]
	v_mfma_f32_16x16x32_bf16 v[104:107], v[140:143], v[182:185], v[104:107]
	v_mfma_f32_16x16x32_bf16 v[92:95], v[124:127], v[190:193], v[92:95]
	v_mfma_f32_16x16x32_bf16 v[88:91], v[140:143], v[190:193], v[88:91]
	v_mfma_f32_16x16x32_bf16 v[76:79], v[124:127], v[198:201], v[76:79]
	v_mfma_f32_16x16x32_bf16 v[72:75], v[140:143], v[198:201], v[72:75]
	v_mfma_f32_16x16x32_bf16 v[120:123], v[144:147], v[160:163], v[120:123]
	v_mfma_f32_16x16x32_bf16 v[116:119], v[152:155], v[160:163], v[116:119]
	v_mfma_f32_16x16x32_bf16 v[100:103], v[144:147], v[178:181], v[100:103]
	v_mfma_f32_16x16x32_bf16 v[96:99], v[152:155], v[178:181], v[96:99]
	v_mfma_f32_16x16x32_bf16 v[84:87], v[144:147], v[186:189], v[84:87]
	v_mfma_f32_16x16x32_bf16 v[80:83], v[152:155], v[186:189], v[80:83]
	v_mfma_f32_16x16x32_bf16 v[68:71], v[144:147], v[194:197], v[68:71]
	v_mfma_f32_16x16x32_bf16 v[64:67], v[152:155], v[194:197], v[64:67]
	v_mfma_f32_16x16x32_bf16 v[120:123], v[148:151], v[164:167], v[120:123]
	v_mfma_f32_16x16x32_bf16 v[116:119], v[156:159], v[164:167], v[116:119]
	v_mfma_f32_16x16x32_bf16 v[100:103], v[148:151], v[182:185], v[100:103]
	v_mfma_f32_16x16x32_bf16 v[96:99], v[156:159], v[182:185], v[96:99]
	v_mfma_f32_16x16x32_bf16 v[84:87], v[148:151], v[190:193], v[84:87]
	v_mfma_f32_16x16x32_bf16 v[80:83], v[156:159], v[190:193], v[80:83]
	v_mfma_f32_16x16x32_bf16 v[68:71], v[148:151], v[198:201], v[68:71]
	v_mfma_f32_16x16x32_bf16 v[64:67], v[156:159], v[198:201], v[64:67]
	s_setprio 0
	s_barrier
	s_mov_b32 m0, s1
	s_bitset1_b32 s55, 7
	buffer_load_dwordx4 v171, s[4:7], s55 offen lds
	s_mov_b32 m0, s35
	ds_read_b128 v[160:163], v177 offset:49152
	buffer_load_dwordx4 v173, s[4:7], s55 offen lds
	s_add_i32 s55, s55, s25
	s_mov_b32 m0, s43
	ds_read_b128 v[164:167], v177 offset:50176
	buffer_load_dwordx4 v171, s[4:7], s55 offen lds
	s_mov_b32 m0, s44
	ds_read_b128 v[178:181], v177 offset:51200
	buffer_load_dwordx4 v173, s[4:7], s55 offen lds
	s_mov_b32 m0, s41
	ds_read_b128 v[182:185], v177 offset:52224
	buffer_load_dwordx4 v170, s[36:39], s54 offen lds
	s_mov_b32 m0, s42
	ds_read_b128 v[186:189], v177 offset:53248
	buffer_load_dwordx4 v172, s[36:39], s54 offen lds
	ds_read_b128 v[190:193], v177 offset:54272
	ds_read_b128 v[194:197], v177 offset:55296
	ds_read_b128 v[198:201], v177 offset:56320
	s_waitcnt vmcnt(8)
	s_waitcnt lgkmcnt(0)
	s_barrier
	s_setprio 1
	v_mfma_f32_16x16x32_bf16 v[60:63], v[112:115], v[160:163], v[60:63]
	v_mfma_f32_16x16x32_bf16 v[56:59], v[136:139], v[160:163], v[56:59]
	v_mfma_f32_16x16x32_bf16 v[44:47], v[112:115], v[178:181], v[44:47]
	v_mfma_f32_16x16x32_bf16 v[40:43], v[136:139], v[178:181], v[40:43]
	v_mfma_f32_16x16x32_bf16 v[28:31], v[112:115], v[186:189], v[28:31]
	v_mfma_f32_16x16x32_bf16 v[24:27], v[136:139], v[186:189], v[24:27]
	v_mfma_f32_16x16x32_bf16 v[12:15], v[112:115], v[194:197], v[12:15]
	v_mfma_f32_16x16x32_bf16 v[8:11], v[136:139], v[194:197], v[8:11]
	v_mfma_f32_16x16x32_bf16 v[60:63], v[124:127], v[164:167], v[60:63]
	v_mfma_f32_16x16x32_bf16 v[56:59], v[140:143], v[164:167], v[56:59]
	v_mfma_f32_16x16x32_bf16 v[44:47], v[124:127], v[182:185], v[44:47]
	v_mfma_f32_16x16x32_bf16 v[40:43], v[140:143], v[182:185], v[40:43]
	v_mfma_f32_16x16x32_bf16 v[28:31], v[124:127], v[190:193], v[28:31]
	v_mfma_f32_16x16x32_bf16 v[24:27], v[140:143], v[190:193], v[24:27]
	v_mfma_f32_16x16x32_bf16 v[12:15], v[124:127], v[198:201], v[12:15]
	v_mfma_f32_16x16x32_bf16 v[8:11], v[140:143], v[198:201], v[8:11]
	v_mfma_f32_16x16x32_bf16 v[52:55], v[144:147], v[160:163], v[52:55]
	v_mfma_f32_16x16x32_bf16 v[48:51], v[152:155], v[160:163], v[48:51]
	v_mfma_f32_16x16x32_bf16 v[36:39], v[144:147], v[178:181], v[36:39]
	v_mfma_f32_16x16x32_bf16 v[32:35], v[152:155], v[178:181], v[32:35]
	v_mfma_f32_16x16x32_bf16 v[20:23], v[144:147], v[186:189], v[20:23]
	v_mfma_f32_16x16x32_bf16 v[16:19], v[152:155], v[186:189], v[16:19]
	v_mfma_f32_16x16x32_bf16 v[4:7], v[144:147], v[194:197], v[4:7]
	v_mfma_f32_16x16x32_bf16 v[0:3], v[152:155], v[194:197], v[0:3]
	v_mfma_f32_16x16x32_bf16 v[52:55], v[148:151], v[164:167], v[52:55]
	v_mfma_f32_16x16x32_bf16 v[48:51], v[156:159], v[164:167], v[48:51]
	v_mfma_f32_16x16x32_bf16 v[36:39], v[148:151], v[182:185], v[36:39]
	v_mfma_f32_16x16x32_bf16 v[32:35], v[156:159], v[182:185], v[32:35]
	v_mfma_f32_16x16x32_bf16 v[20:23], v[148:151], v[190:193], v[20:23]
	v_mfma_f32_16x16x32_bf16 v[16:19], v[156:159], v[190:193], v[16:19]
	v_mfma_f32_16x16x32_bf16 v[4:7], v[148:151], v[198:201], v[4:7]
	v_mfma_f32_16x16x32_bf16 v[0:3], v[156:159], v[198:201], v[0:3]
	s_setprio 0
	s_barrier
	s_add_i32 s67, s67, 2
	s_addk_i32 s65, 0x100
	s_addk_i32 s66, 0x100
	s_cmp_ge_i32 s67, s47
	s_cbranch_scc0 .LBB0_1701
	s_branch .Lzp_after_1701
; #define PG8_STAGE(bufoff, rs_, soff_, voff) do { _Pragma("unroll") for (int _i = 0; _i < 2; ++_i) \
;         __builtin_amdgcn_raw_ptr_buffer_load_lds(rs_, (LAS void*)(lds + (bufoff) + ldsw + _i * 8192), 16, (int)(voff)[_i], (int)(soff_), 0, 0); } while (0)
; #define PG8_LDA(dst, b, h) do { _Pragma("unroll") for (int m = 0; m < 4; ++m) dst[m] = PG8_LD2(lds + PG8_SA(b, h) + aoff + m * 2048); } while (0)
; #define PG8_LDB(dst, b, h) do { _Pragma("unroll") for (int n = 0; n < 2; ++n) dst[n] = PG8_LD2(lds + PG8_SB(b, h) + boff + n * 2048); } while (0)
; #define PG8_WAIT_V(n) asm volatile("s_waitcnt vmcnt(" #n ")" ::: "memory")
; #define PG8_WAIT_L(n) asm volatile("s_waitcnt lgkmcnt(" #n ")" ::: "memory")
; #define PG8_BAR __builtin_amdgcn_s_barrier()
; #define PG8_SCHED __builtin_amdgcn_sched_barrier(0)
; template <class Epi, class Sched, bool ALIGN_EPI = false, bool SP2 = false, bool FP8 = false>
; __device__ __forceinline__ void gemm_phase(LAS unsigned char* lds, const Gemm g, const Sched& S, const Epi& E, int wbase) {
;     ...
;         for (int t = 0; t < nt; t += 2) {
;             const bool last = (t == nt - 2);
;             const unsigned a1 = cA + (unsigned)(t + 1) * kstep;
;             const unsigned a2 = last ? nA : cA + (unsigned)(t + 2) * kstep, b2 = last ? nB : cB + (unsigned)(t + 2) * kstep; const rsrc_t rA2 = (Sched::TWO && last) ? rAn : rAc, rB2 = (Sched::TWO && last) ? rBn : rBc;
;             const unsigned a3 = a2 + kstep, b3 = b2 + kstep;
;             if (last && has_next) S.a_ready(nxt);
;             if constexpr (SP2) {
;             PG8_LDB(B0, 0, 0); PG8_LDB(B1, 0, 1); PG8_SCHED; PG8_LDA(At, 0, 0); PG8_STAGE(PG8_SA(1, 1), rAc, a1 + hstep, voffA);
;             PG8_WAIT_V(8); PG8_WAIT_L(0); PG8_BAR; PG8_MMA(0, 0, At, B0); PG8_MMA(0, 1, At, B1); PG8_BAR; PG8_SCHED;
;             PG8_LDA(At, 0, 1); PG8_STAGE(PG8_SB(0, 0), rB2, b2, voffB); PG8_STAGE(PG8_SB(0, 1), rB2, b2 + hstep, voffB); PG8_STAGE(PG8_SA(0, 0), rA2, a2, voffA);
;             PG8_WAIT_V(8); PG8_WAIT_L(0); PG8_BAR; PG8_MMA(1, 0, At, B0); PG8_MMA(1, 1, At, B1); PG8_BAR; PG8_SCHED;
.LBB0_1701:
	v_add_u32_e32 v140, 0x10000, v176
	v_add_u32_e32 v156, 0x14000, v176
	ds_read_b128 v[112:115], v140
	ds_read_b128 v[124:127], v140 offset:1024
	ds_read_b128 v[136:139], v140 offset:2048
	ds_read_b128 v[140:143], v140 offset:3072
	ds_read_b128 v[144:147], v156
	ds_read_b128 v[148:151], v156 offset:1024
	ds_read_b128 v[152:155], v156 offset:2048
	ds_read_b128 v[156:159], v156 offset:3072
	s_add_i32 s6, s65, 0x80
	s_cmp_eq_u32 s52, s67
	s_cselect_b32 s68, s21, s6
	s_cselect_b32 s55, s63, s66
	s_or_b32 s54, s68, 0x80
	s_add_i32 s6, s25, s65
	s_mov_b32 m0, s53
	ds_read_b128 v[160:163], v177
	ds_read_b128 v[164:167], v177 offset:1024
	ds_read_b128 v[178:181], v177 offset:2048
	ds_read_b128 v[182:185], v177 offset:3072
	ds_read_b128 v[186:189], v177 offset:4096
	ds_read_b128 v[190:193], v177 offset:5120
	ds_read_b128 v[194:197], v177 offset:6144
	ds_read_b128 v[198:201], v177 offset:7168
	buffer_load_dwordx4 v170, s[36:39], s6 offen lds
	s_mov_b32 m0, s56
	s_nop 0
	buffer_load_dwordx4 v172, s[36:39], s6 offen lds
	s_waitcnt vmcnt(8)
	s_waitcnt lgkmcnt(0)
	s_barrier
	s_setprio 1
	v_mfma_f32_16x16x32_bf16 v[132:135], v[112:115], v[160:163], v[132:135]
	v_mfma_f32_16x16x32_bf16 v[128:131], v[136:139], v[160:163], v[128:131]
	v_mfma_f32_16x16x32_bf16 v[108:111], v[112:115], v[178:181], v[108:111]
	v_mfma_f32_16x16x32_bf16 v[104:107], v[136:139], v[178:181], v[104:107]
	v_mfma_f32_16x16x32_bf16 v[92:95], v[112:115], v[186:189], v[92:95]
	v_mfma_f32_16x16x32_bf16 v[88:91], v[136:139], v[186:189], v[88:91]
	v_mfma_f32_16x16x32_bf16 v[76:79], v[112:115], v[194:197], v[76:79]
	v_mfma_f32_16x16x32_bf16 v[72:75], v[136:139], v[194:197], v[72:75]
	v_mfma_f32_16x16x32_bf16 v[132:135], v[124:127], v[164:167], v[132:135]
	v_mfma_f32_16x16x32_bf16 v[128:131], v[140:143], v[164:167], v[128:131]
	v_mfma_f32_16x16x32_bf16 v[108:111], v[124:127], v[182:185], v[108:111]
	v_mfma_f32_16x16x32_bf16 v[104:107], v[140:143], v[182:185], v[104:107]
	v_mfma_f32_16x16x32_bf16 v[92:95], v[124:127], v[190:193], v[92:95]
	v_mfma_f32_16x16x32_bf16 v[88:91], v[140:143], v[190:193], v[88:91]
	v_mfma_f32_16x16x32_bf16 v[76:79], v[124:127], v[198:201], v[76:79]
	v_mfma_f32_16x16x32_bf16 v[72:75], v[140:143], v[198:201], v[72:75]
	v_mfma_f32_16x16x32_bf16 v[120:123], v[144:147], v[160:163], v[120:123]
	v_mfma_f32_16x16x32_bf16 v[116:119], v[152:155], v[160:163], v[116:119]
	v_mfma_f32_16x16x32_bf16 v[100:103], v[144:147], v[178:181], v[100:103]
	v_mfma_f32_16x16x32_bf16 v[96:99], v[152:155], v[178:181], v[96:99]
	v_mfma_f32_16x16x32_bf16 v[84:87], v[144:147], v[186:189], v[84:87]
	v_mfma_f32_16x16x32_bf16 v[80:83], v[152:155], v[186:189], v[80:83]
	v_mfma_f32_16x16x32_bf16 v[68:71], v[144:147], v[194:197], v[68:71]
	v_mfma_f32_16x16x32_bf16 v[64:67], v[152:155], v[194:197], v[64:67]
	v_mfma_f32_16x16x32_bf16 v[120:123], v[148:151], v[164:167], v[120:123]
	v_mfma_f32_16x16x32_bf16 v[116:119], v[156:159], v[164:167], v[116:119]
	v_mfma_f32_16x16x32_bf16 v[100:103], v[148:151], v[182:185], v[100:103]
	v_mfma_f32_16x16x32_bf16 v[96:99], v[156:159], v[182:185], v[96:99]
	v_mfma_f32_16x16x32_bf16 v[84:87], v[148:151], v[190:193], v[84:87]
	v_mfma_f32_16x16x32_bf16 v[80:83], v[156:159], v[190:193], v[80:83]
	v_mfma_f32_16x16x32_bf16 v[68:71], v[148:151], v[198:201], v[68:71]
	v_mfma_f32_16x16x32_bf16 v[64:67], v[156:159], v[198:201], v[64:67]
	s_setprio 0
	s_barrier
	s_mov_b32 m0, s27
	s_mov_b32 s6, s38
	s_mov_b32 s7, s39
	buffer_load_dwordx4 v171, s[4:7], s55 offen lds
	s_mov_b32 m0, s28
	ds_read_b128 v[160:163], v177 offset:16384
	s_add_i32 s69, s55, s25
	buffer_load_dwordx4 v173, s[4:7], s55 offen lds
	s_mov_b32 m0, s29
	ds_read_b128 v[164:167], v177 offset:17408
	buffer_load_dwordx4 v171, s[4:7], s69 offen lds
	s_mov_b32 m0, s26
	ds_read_b128 v[178:181], v177 offset:18432
	buffer_load_dwordx4 v170, s[36:39], s68 offen lds
	s_mov_b32 m0, s31
	ds_read_b128 v[182:185], v177 offset:19456
	buffer_load_dwordx4 v172, s[36:39], s68 offen lds
	ds_read_b128 v[186:189], v177 offset:20480
	ds_read_b128 v[190:193], v177 offset:21504
	ds_read_b128 v[194:197], v177 offset:22528
	ds_read_b128 v[198:201], v177 offset:23552
	s_waitcnt vmcnt(7)
	s_waitcnt lgkmcnt(0)
	s_barrier
	s_setprio 1
	v_mfma_f32_16x16x32_bf16 v[60:63], v[112:115], v[160:163], v[60:63]
	v_mfma_f32_16x16x32_bf16 v[56:59], v[136:139], v[160:163], v[56:59]
	v_mfma_f32_16x16x32_bf16 v[44:47], v[112:115], v[178:181], v[44:47]
	v_mfma_f32_16x16x32_bf16 v[40:43], v[136:139], v[178:181], v[40:43]
	v_mfma_f32_16x16x32_bf16 v[28:31], v[112:115], v[186:189], v[28:31]
	v_mfma_f32_16x16x32_bf16 v[24:27], v[136:139], v[186:189], v[24:27]
	v_mfma_f32_16x16x32_bf16 v[12:15], v[112:115], v[194:197], v[12:15]
	v_mfma_f32_16x16x32_bf16 v[8:11], v[136:139], v[194:197], v[8:11]
	v_mfma_f32_16x16x32_bf16 v[60:63], v[124:127], v[164:167], v[60:63]
	v_mfma_f32_16x16x32_bf16 v[56:59], v[140:143], v[164:167], v[56:59]
	v_mfma_f32_16x16x32_bf16 v[44:47], v[124:127], v[182:185], v[44:47]
	v_mfma_f32_16x16x32_bf16 v[40:43], v[140:143], v[182:185], v[40:43]
	v_mfma_f32_16x16x32_bf16 v[28:31], v[124:127], v[190:193], v[28:31]
	v_mfma_f32_16x16x32_bf16 v[24:27], v[140:143], v[190:193], v[24:27]
	v_mfma_f32_16x16x32_bf16 v[12:15], v[124:127], v[198:201], v[12:15]
	v_mfma_f32_16x16x32_bf16 v[8:11], v[140:143], v[198:201], v[8:11]
	v_mfma_f32_16x16x32_bf16 v[52:55], v[144:147], v[160:163], v[52:55]
	v_mfma_f32_16x16x32_bf16 v[48:51], v[152:155], v[160:163], v[48:51]
	v_mfma_f32_16x16x32_bf16 v[36:39], v[144:147], v[178:181], v[36:39]
	v_mfma_f32_16x16x32_bf16 v[32:35], v[152:155], v[178:181], v[32:35]
	v_mfma_f32_16x16x32_bf16 v[20:23], v[144:147], v[186:189], v[20:23]
	v_mfma_f32_16x16x32_bf16 v[16:19], v[152:155], v[186:189], v[16:19]
	v_mfma_f32_16x16x32_bf16 v[4:7], v[144:147], v[194:197], v[4:7]
	v_mfma_f32_16x16x32_bf16 v[0:3], v[152:155], v[194:197], v[0:3]
	v_mfma_f32_16x16x32_bf16 v[52:55], v[148:151], v[164:167], v[52:55]
	v_mfma_f32_16x16x32_bf16 v[48:51], v[156:159], v[164:167], v[48:51]
	v_mfma_f32_16x16x32_bf16 v[36:39], v[148:151], v[182:185], v[36:39]
	v_mfma_f32_16x16x32_bf16 v[32:35], v[156:159], v[182:185], v[32:35]
	v_mfma_f32_16x16x32_bf16 v[20:23], v[148:151], v[190:193], v[20:23]
	v_mfma_f32_16x16x32_bf16 v[16:19], v[156:159], v[190:193], v[16:19]
	v_mfma_f32_16x16x32_bf16 v[4:7], v[148:151], v[198:201], v[4:7]
	v_mfma_f32_16x16x32_bf16 v[0:3], v[156:159], v[198:201], v[0:3]
	s_setprio 0
	s_barrier
; #define PG8_STAGE(bufoff, rs_, soff_, voff) do { _Pragma("unroll") for (int _i = 0; _i < 2; ++_i) \
;         __builtin_amdgcn_raw_ptr_buffer_load_lds(rs_, (LAS void*)(lds + (bufoff) + ldsw + _i * 8192), 16, (int)(voff)[_i], (int)(soff_), 0, 0); } while (0)
; #define PG8_LDA(dst, b, h) do { _Pragma("unroll") for (int m = 0; m < 4; ++m) dst[m] = PG8_LD2(lds + PG8_SA(b, h) + aoff + m * 2048); } while (0)
; #define PG8_LDB(dst, b, h) do { _Pragma("unroll") for (int n = 0; n < 2; ++n) dst[n] = PG8_LD2(lds + PG8_SB(b, h) + boff + n * 2048); } while (0)
; #define PG8_WAIT_V(n) asm volatile("s_waitcnt vmcnt(" #n ")" ::: "memory")
; #define PG8_WAIT_L(n) asm volatile("s_waitcnt lgkmcnt(" #n ")" ::: "memory")
; #define PG8_BAR __builtin_amdgcn_s_barrier()
; #define PG8_SCHED __builtin_amdgcn_sched_barrier(0)
; template <class Epi, class Sched, bool ALIGN_EPI = false, bool SP2 = false, bool FP8 = false>
; __device__ __forceinline__ void gemm_phase(LAS unsigned char* lds, const Gemm g, const Sched& S, const Epi& E, int wbase) {
;     ...
;             PG8_LDB(B0, 1, 0); PG8_LDB(B1, 1, 1); PG8_SCHED; PG8_LDA(At, 1, 0); PG8_STAGE(PG8_SA(0, 1), rA2, a2 + hstep, voffA);
;             PG8_WAIT_V(8); PG8_WAIT_L(0); PG8_BAR; PG8_MMA(0, 0, At, B0); PG8_MMA(0, 1, At, B1); PG8_BAR; PG8_SCHED;
;             PG8_LDA(At, 1, 1); PG8_STAGE(PG8_SB(1, 0), rB2, b3, voffB); PG8_STAGE(PG8_SB(1, 1), rB2, b3 + hstep, voffB); PG8_STAGE(PG8_SA(1, 0), rA2, a3, voffA);
;             PG8_WAIT_V(8); PG8_WAIT_L(0); PG8_BAR; PG8_MMA(1, 0, At, B0); PG8_MMA(1, 1, At, B1); PG8_BAR; PG8_SCHED;
	s_mov_b32 m0, s30
	s_nop 0
	buffer_load_dwordx4 v173, s[4:7], s69 offen lds
	v_add_u32_e32 v140, 0x18000, v176
	v_add_u32_e32 v156, 0x1c000, v176
	ds_read_b128 v[112:115], v140
	ds_read_b128 v[124:127], v140 offset:1024
	ds_read_b128 v[136:139], v140 offset:2048
	ds_read_b128 v[140:143], v140 offset:3072
	ds_read_b128 v[144:147], v156
	ds_read_b128 v[148:151], v156 offset:1024
	ds_read_b128 v[152:155], v156 offset:2048
	ds_read_b128 v[156:159], v156 offset:3072
	s_add_i32 s68, s68, s25
	s_mov_b32 m0, s33
	ds_read_b128 v[160:163], v177 offset:32768
	ds_read_b128 v[164:167], v177 offset:33792
	ds_read_b128 v[178:181], v177 offset:34816
	ds_read_b128 v[182:185], v177 offset:35840
	ds_read_b128 v[186:189], v177 offset:36864
	ds_read_b128 v[190:193], v177 offset:37888
	ds_read_b128 v[194:197], v177 offset:38912
	ds_read_b128 v[198:201], v177 offset:39936
	buffer_load_dwordx4 v170, s[36:39], s68 offen lds
	s_mov_b32 m0, s34
	s_nop 0
	buffer_load_dwordx4 v172, s[36:39], s68 offen lds
	s_waitcnt vmcnt(8)
	s_waitcnt lgkmcnt(0)
	s_barrier
	s_setprio 1
	v_mfma_f32_16x16x32_bf16 v[132:135], v[112:115], v[160:163], v[132:135]
	v_mfma_f32_16x16x32_bf16 v[128:131], v[136:139], v[160:163], v[128:131]
	v_mfma_f32_16x16x32_bf16 v[108:111], v[112:115], v[178:181], v[108:111]
	v_mfma_f32_16x16x32_bf16 v[104:107], v[136:139], v[178:181], v[104:107]
	v_mfma_f32_16x16x32_bf16 v[92:95], v[112:115], v[186:189], v[92:95]
	v_mfma_f32_16x16x32_bf16 v[88:91], v[136:139], v[186:189], v[88:91]
	v_mfma_f32_16x16x32_bf16 v[76:79], v[112:115], v[194:197], v[76:79]
	v_mfma_f32_16x16x32_bf16 v[72:75], v[136:139], v[194:197], v[72:75]
	v_mfma_f32_16x16x32_bf16 v[132:135], v[124:127], v[164:167], v[132:135]
	v_mfma_f32_16x16x32_bf16 v[128:131], v[140:143], v[164:167], v[128:131]
	v_mfma_f32_16x16x32_bf16 v[108:111], v[124:127], v[182:185], v[108:111]
	v_mfma_f32_16x16x32_bf16 v[104:107], v[140:143], v[182:185], v[104:107]
	v_mfma_f32_16x16x32_bf16 v[92:95], v[124:127], v[190:193], v[92:95]
	v_mfma_f32_16x16x32_bf16 v[88:91], v[140:143], v[190:193], v[88:91]
	v_mfma_f32_16x16x32_bf16 v[76:79], v[124:127], v[198:201], v[76:79]
	v_mfma_f32_16x16x32_bf16 v[72:75], v[140:143], v[198:201], v[72:75]
	v_mfma_f32_16x16x32_bf16 v[120:123], v[144:147], v[160:163], v[120:123]
	v_mfma_f32_16x16x32_bf16 v[116:119], v[152:155], v[160:163], v[116:119]
	v_mfma_f32_16x16x32_bf16 v[100:103], v[144:147], v[178:181], v[100:103]
	v_mfma_f32_16x16x32_bf16 v[96:99], v[152:155], v[178:181], v[96:99]
	v_mfma_f32_16x16x32_bf16 v[84:87], v[144:147], v[186:189], v[84:87]
	v_mfma_f32_16x16x32_bf16 v[80:83], v[152:155], v[186:189], v[80:83]
	v_mfma_f32_16x16x32_bf16 v[68:71], v[144:147], v[194:197], v[68:71]
	v_mfma_f32_16x16x32_bf16 v[64:67], v[152:155], v[194:197], v[64:67]
	v_mfma_f32_16x16x32_bf16 v[120:123], v[148:151], v[164:167], v[120:123]
	v_mfma_f32_16x16x32_bf16 v[116:119], v[156:159], v[164:167], v[116:119]
	v_mfma_f32_16x16x32_bf16 v[100:103], v[148:151], v[182:185], v[100:103]
	v_mfma_f32_16x16x32_bf16 v[96:99], v[156:159], v[182:185], v[96:99]
	v_mfma_f32_16x16x32_bf16 v[84:87], v[148:151], v[190:193], v[84:87]
	v_mfma_f32_16x16x32_bf16 v[80:83], v[156:159], v[190:193], v[80:83]
	v_mfma_f32_16x16x32_bf16 v[68:71], v[148:151], v[198:201], v[68:71]
	v_mfma_f32_16x16x32_bf16 v[64:67], v[156:159], v[198:201], v[64:67]
	s_setprio 0
	s_barrier
	s_mov_b32 m0, s1
	s_bitset1_b32 s55, 7
	buffer_load_dwordx4 v171, s[4:7], s55 offen lds
	s_mov_b32 m0, s35
	ds_read_b128 v[160:163], v177 offset:49152
	buffer_load_dwordx4 v173, s[4:7], s55 offen lds
	s_add_i32 s55, s55, s25
	s_mov_b32 m0, s43
	ds_read_b128 v[164:167], v177 offset:50176
	buffer_load_dwordx4 v171, s[4:7], s55 offen lds
	s_mov_b32 m0, s44
	ds_read_b128 v[178:181], v177 offset:51200
	buffer_load_dwordx4 v173, s[4:7], s55 offen lds
	s_mov_b32 m0, s41
	ds_read_b128 v[182:185], v177 offset:52224
	buffer_load_dwordx4 v170, s[36:39], s54 offen lds
	s_mov_b32 m0, s42
	ds_read_b128 v[186:189], v177 offset:53248
	buffer_load_dwordx4 v172, s[36:39], s54 offen lds
	ds_read_b128 v[190:193], v177 offset:54272
	ds_read_b128 v[194:197], v177 offset:55296
	ds_read_b128 v[198:201], v177 offset:56320
	s_waitcnt vmcnt(8)
	s_waitcnt lgkmcnt(0)
	s_barrier
	s_setprio 1
	v_mfma_f32_16x16x32_bf16 v[60:63], v[112:115], v[160:163], v[60:63]
	v_mfma_f32_16x16x32_bf16 v[56:59], v[136:139], v[160:163], v[56:59]
	v_mfma_f32_16x16x32_bf16 v[44:47], v[112:115], v[178:181], v[44:47]
	v_mfma_f32_16x16x32_bf16 v[40:43], v[136:139], v[178:181], v[40:43]
	v_mfma_f32_16x16x32_bf16 v[28:31], v[112:115], v[186:189], v[28:31]
	v_mfma_f32_16x16x32_bf16 v[24:27], v[136:139], v[186:189], v[24:27]
	v_mfma_f32_16x16x32_bf16 v[12:15], v[112:115], v[194:197], v[12:15]
	v_mfma_f32_16x16x32_bf16 v[8:11], v[136:139], v[194:197], v[8:11]
	v_mfma_f32_16x16x32_bf16 v[60:63], v[124:127], v[164:167], v[60:63]
	v_mfma_f32_16x16x32_bf16 v[56:59], v[140:143], v[164:167], v[56:59]
	v_mfma_f32_16x16x32_bf16 v[44:47], v[124:127], v[182:185], v[44:47]
	v_mfma_f32_16x16x32_bf16 v[40:43], v[140:143], v[182:185], v[40:43]
	v_mfma_f32_16x16x32_bf16 v[28:31], v[124:127], v[190:193], v[28:31]
	v_mfma_f32_16x16x32_bf16 v[24:27], v[140:143], v[190:193], v[24:27]
	v_mfma_f32_16x16x32_bf16 v[12:15], v[124:127], v[198:201], v[12:15]
	v_mfma_f32_16x16x32_bf16 v[8:11], v[140:143], v[198:201], v[8:11]
	v_mfma_f32_16x16x32_bf16 v[52:55], v[144:147], v[160:163], v[52:55]
	v_mfma_f32_16x16x32_bf16 v[48:51], v[152:155], v[160:163], v[48:51]
	v_mfma_f32_16x16x32_bf16 v[36:39], v[144:147], v[178:181], v[36:39]
	v_mfma_f32_16x16x32_bf16 v[32:35], v[152:155], v[178:181], v[32:35]
	v_mfma_f32_16x16x32_bf16 v[20:23], v[144:147], v[186:189], v[20:23]
	v_mfma_f32_16x16x32_bf16 v[16:19], v[152:155], v[186:189], v[16:19]
	v_mfma_f32_16x16x32_bf16 v[4:7], v[144:147], v[194:197], v[4:7]
	v_mfma_f32_16x16x32_bf16 v[0:3], v[152:155], v[194:197], v[0:3]
	v_mfma_f32_16x16x32_bf16 v[52:55], v[148:151], v[164:167], v[52:55]
	v_mfma_f32_16x16x32_bf16 v[48:51], v[156:159], v[164:167], v[48:51]
	v_mfma_f32_16x16x32_bf16 v[36:39], v[148:151], v[182:185], v[36:39]
	v_mfma_f32_16x16x32_bf16 v[32:35], v[156:159], v[182:185], v[32:35]
	v_mfma_f32_16x16x32_bf16 v[20:23], v[148:151], v[190:193], v[20:23]
	v_mfma_f32_16x16x32_bf16 v[16:19], v[156:159], v[190:193], v[16:19]
	v_mfma_f32_16x16x32_bf16 v[4:7], v[148:151], v[198:201], v[4:7]
	v_mfma_f32_16x16x32_bf16 v[0:3], v[156:159], v[198:201], v[0:3]
	s_setprio 0
	s_barrier
	s_add_i32 s67, s67, 2
	s_addk_i32 s65, 0x100
	s_addk_i32 s66, 0x100
	s_cmp_ge_i32 s67, s47
	s_cbranch_scc0 .LBB0_1701

;     __device__ __forceinline__ unsigned a_off(const Unit& u, const Gemm& g) const { return (unsigned)u.pm * (unsigned)(BM * 2) * (unsigned)g.K; }
;     __device__ __forceinline__ unsigned b_off(const Unit& u, const Gemm& g) const { return (unsigned)u.pn * (unsigned)(BM * 2) * (unsigned)g.K; }
;     __device__ __forceinline__ bool next(int i, Unit& u) const { return so.next(i, u); }
;     __device__ __forceinline__ unsigned a_off(const Unit& u, const Gemm& g) const { return (unsigned)u.pm * (unsigned)(BM * 2) * (unsigned)g.K; }
; template <class Epi, class Sched, bool ALIGN_EPI = false, bool SP2 = false, bool FP8 = false>
; __device__ __forceinline__ void gemm_phase(LAS unsigned char* lds, const Gemm g, const Sched& S, const Epi& E, int wbase) {
;     ...
;         const bool has_next = S.next(ui + 1, nxt);
;         const unsigned nA = has_next ? S.a_off(nxt, g) : cA, nB = has_next ? S.b_off(nxt, g) : cB;
;         const rsrc_t rAn = (Sched::TWO && has_next) ? (nxt.part ? rA1 : rA0) : rAc, rBn = (Sched::TWO && has_next) ? (nxt.part ? rB1 : rB0) : rBc;
;         float pre_[8] = {0.f, 0.f, 0.f, 0.f, 0.f, 0.f, 0.f, 0.f};
;         if constexpr (Epi::HAS_PRE) E.pre_load(pre_, cur, wr);
;         for (int t = 0; t < nt; t += 2) {
;             const bool last = (t == nt - 2);
;             const unsigned a1 = cA + (unsigned)(t + 1) * kstep;
;             const unsigned a2 = last ? nA : cA + (unsigned)(t + 2) * kstep, b2 = last ? nB : cB + (unsigned)(t + 2) * kstep; const rsrc_t rA2 = (Sched::TWO && last) ? rAn : rAc, rB2 = (Sched::TWO && last) ? rBn : rBc;
;             const unsigned a3 = a2 + kstep, b3 = b2 + kstep;
;             if (last && has_next) S.a_ready(nxt);
;             if constexpr (SP2) {
;             PG8_LDB(B0, 0, 0); PG8_LDB(B1, 0, 1); PG8_SCHED; PG8_LDA(At, 0, 0); PG8_STAGE(PG8_SA(1, 1), rAc, a1 + hstep, voffA);
;             PG8_WAIT_V(8); PG8_WAIT_L(0); PG8_BAR; PG8_MMA(0, 0, At, B0); PG8_MMA(0, 1, At, B1); PG8_BAR; PG8_SCHED;
;             PG8_LDA(At, 0, 1); PG8_STAGE(PG8_SB(0, 0), rB2, b2, voffB); PG8_STAGE(PG8_SB(0, 1), rB2, b2 + hstep, voffB); PG8_STAGE(PG8_SA(0, 0), rA2, a2, voffA);
;             PG8_WAIT_V(8); PG8_WAIT_L(0); PG8_BAR; PG8_MMA(1, 0, At, B0); PG8_MMA(1, 1, At, B1); PG8_BAR; PG8_SCHED;
;             PG8_LDB(B0, 1, 0); PG8_LDB(B1, 1, 1); PG8_SCHED; PG8_LDA(At, 1, 0); PG8_STAGE(PG8_SA(0, 1), rA2, a2 + hstep, voffA);
.LBB0_1779:
	s_lshl_b32 s53, s52, 18
	s_andn2_b64 vcc, exec, s[14:15]
	s_lshl_b32 s56, s48, 18
	s_cbranch_vccnz .LBB0_1783
	s_and_b64 s[6:7], s[18:19], exec
	s_waitcnt vmcnt(37)
	s_waitcnt vmcnt(35)
	s_waitcnt vmcnt(31)
	s_waitcnt vmcnt(27)
	s_waitcnt vmcnt(23)
	s_waitcnt vmcnt(22)
	v_mov_b32_e32 v225, 1
	v_mov_b32_e32 v223, v233
	v_mov_b32_e32 v222, 0x358637bd
	s_cselect_b32 s59, s53, s55
	s_cselect_b32 s60, s56, s54
	s_add_i32 s61, s55, 0x80
	s_add_i32 s62, s54, 0x100
	s_mov_b32 s63, 0
	v_add_u32_e32 v140, 0x10000, v154
	v_add_u32_e32 v144, 0x14000, v154
	ds_read_b128 v[128:131], v140
	ds_read_b128 v[132:135], v140 offset:1024
	ds_read_b128 v[136:139], v140 offset:2048
	ds_read_b128 v[140:143], v140 offset:3072
	ds_read_b128 v[156:159], v144
	ds_read_b128 v[160:163], v144 offset:1024
	ds_read_b128 v[164:167], v144 offset:2048
	ds_read_b128 v[168:171], v144 offset:3072
	s_add_i32 s6, s61, 0x80
	s_cmp_eq_u32 s45, s63
	s_cselect_b32 s65, s59, s6
	s_cselect_b32 s55, s60, s62
	s_or_b32 s54, s65, 0x80
	s_add_i32 s6, s21, s61
	s_mov_b32 m0, s46
	ds_read_b128 v[172:175], v155
	ds_read_b128 v[176:179], v155 offset:1024
	ds_read_b128 v[180:183], v155 offset:2048
	ds_read_b128 v[184:187], v155 offset:3072
	ds_read_b128 v[194:197], v155 offset:4096
	ds_read_b128 v[198:201], v155 offset:5120
	ds_read_b128 v[202:205], v155 offset:6144
	ds_read_b128 v[206:209], v155 offset:7168
	buffer_load_dwordx4 v148, s[36:39], s6 offen lds
	s_mov_b32 m0, s47
	s_nop 0
	buffer_load_dwordx4 v150, s[36:39], s6 offen lds
	s_waitcnt vmcnt(8)
	s_waitcnt lgkmcnt(0)
	s_barrier
	s_setprio 1
	v_mfma_f32_16x16x128_f8f6f4 v[120:123], v[128:135], v[172:179], 0
	v_mfma_f32_16x16x128_f8f6f4 v[124:127], v[136:143], v[172:179], 0
	v_mfma_f32_16x16x128_f8f6f4 v[104:107], v[128:135], v[180:187], 0
	v_mfma_f32_16x16x128_f8f6f4 v[108:111], v[136:143], v[180:187], 0
	v_mfma_f32_16x16x128_f8f6f4 v[144:147], v[128:135], v[194:201], 0
	v_mfma_f32_16x16x128_f8f6f4 v[188:191], v[136:143], v[194:201], 0
	v_mfma_f32_16x16x128_f8f6f4 v[210:213], v[128:135], v[202:209], 0
	v_mfma_f32_16x16x128_f8f6f4 v[214:217], v[136:143], v[202:209], 0
	v_mfma_f32_16x16x128_f8f6f4 v[112:115], v[156:163], v[172:179], 0
	v_mfma_f32_16x16x128_f8f6f4 v[116:119], v[164:171], v[172:179], 0
	v_mfma_f32_16x16x128_f8f6f4 v[96:99], v[156:163], v[180:187], 0
	v_mfma_f32_16x16x128_f8f6f4 v[100:103], v[164:171], v[180:187], 0
	v_mfma_f32_16x16x128_f8f6f4 v[172:175], v[156:163], v[194:201], 0
	v_mfma_f32_16x16x128_f8f6f4 v[176:179], v[164:171], v[194:201], 0
	v_mfma_f32_16x16x128_f8f6f4 v[180:183], v[156:163], v[202:209], 0
	v_mfma_f32_16x16x128_f8f6f4 v[184:187], v[164:171], v[202:209], 0
	s_setprio 0
	s_barrier
	s_mov_b32 m0, s23
	s_mov_b32 s6, s38
	s_mov_b32 s7, s39
	s_nop 0
	buffer_load_dwordx4 v149, s[4:7], s55 offen lds
	s_mov_b32 m0, s24
	ds_read_b128 v[64:67], v155 offset:16384
	s_add_i32 s66, s55, s21
	buffer_load_dwordx4 v151, s[4:7], s55 offen lds
	s_mov_b32 m0, s25
	ds_read_b128 v[68:71], v155 offset:17408
	buffer_load_dwordx4 v149, s[4:7], s66 offen lds
	s_mov_b32 m0, s22
	ds_read_b128 v[72:75], v155 offset:18432
	buffer_load_dwordx4 v148, s[36:39], s65 offen lds
	s_mov_b32 m0, s27
	ds_read_b128 v[76:79], v155 offset:19456
	buffer_load_dwordx4 v150, s[36:39], s65 offen lds
	ds_read_b128 v[80:83], v155 offset:20480
	ds_read_b128 v[84:87], v155 offset:21504
	ds_read_b128 v[88:91], v155 offset:22528
	ds_read_b128 v[92:95], v155 offset:23552
	s_waitcnt vmcnt(7)
	s_waitcnt lgkmcnt(0)
	s_barrier
	s_setprio 1
	v_mfma_f32_16x16x128_f8f6f4 v[56:59], v[128:135], v[64:71], 0
	v_mfma_f32_16x16x128_f8f6f4 v[60:63], v[136:143], v[64:71], 0
	v_mfma_f32_16x16x128_f8f6f4 v[8:11], v[128:135], v[88:95], 0
	v_mfma_f32_16x16x128_f8f6f4 v[192:195], v[128:135], v[72:79], 0
	v_mfma_f32_16x16x128_f8f6f4 v[196:199], v[136:143], v[72:79], 0
	v_mfma_f32_16x16x128_f8f6f4 v[200:203], v[128:135], v[80:87], 0
	v_mfma_f32_16x16x128_f8f6f4 v[204:207], v[136:143], v[80:87], 0
	v_mfma_f32_16x16x128_f8f6f4 v[218:221], v[136:143], v[88:95], 0
	v_mfma_f32_16x16x128_f8f6f4 v[52:55], v[164:171], v[64:71], 0
	v_mfma_f32_16x16x128_f8f6f4 v[226:229], v[156:163], v[64:71], 0
	v_mfma_f32_16x16x128_f8f6f4 v[230:233], v[156:163], v[72:79], 0
	v_mfma_f32_16x16x128_f8f6f4 v[234:237], v[164:171], v[72:79], 0
	v_mfma_f32_16x16x128_f8f6f4 v[238:241], v[156:163], v[80:87], 0
	v_mfma_f32_16x16x128_f8f6f4 v[242:245], v[164:171], v[80:87], 0
	v_mfma_f32_16x16x128_f8f6f4 v[246:249], v[156:163], v[88:95], 0
	v_mfma_f32_16x16x128_f8f6f4 v[250:253], v[164:171], v[88:95], 0
	s_setprio 0
	s_barrier
	s_mov_b32 m0, s26
	s_nop 0
	buffer_load_dwordx4 v151, s[4:7], s66 offen lds
	s_nop 1
	v_add_u32_e32 v16, 0x18000, v154
	v_add_u32_e32 v20, 0x1c000, v154
	s_nop 0
	ds_read_b128 v[0:3], v16
	ds_read_b128 v[4:7], v16 offset:1024
	ds_read_b128 v[12:15], v16 offset:2048
	ds_read_b128 v[16:19], v16 offset:3072
	ds_read_b128 v[128:131], v20
	ds_read_b128 v[132:135], v20 offset:1024
	ds_read_b128 v[136:139], v20 offset:2048
	ds_read_b128 v[140:143], v20 offset:3072
	s_add_i32 s65, s65, s21
	s_mov_b32 m0, s28
	ds_read_b128 v[20:23], v155 offset:32768
	ds_read_b128 v[24:27], v155 offset:33792
	ds_read_b128 v[28:31], v155 offset:34816
	ds_read_b128 v[32:35], v155 offset:35840
	ds_read_b128 v[36:39], v155 offset:36864
	ds_read_b128 v[40:43], v155 offset:37888
	ds_read_b128 v[44:47], v155 offset:38912
	ds_read_b128 v[48:51], v155 offset:39936
	buffer_load_dwordx4 v148, s[36:39], s65 offen lds
	s_mov_b32 m0, s29
	s_nop 0
	buffer_load_dwordx4 v150, s[36:39], s65 offen lds
	s_waitcnt vmcnt(8)
	s_waitcnt lgkmcnt(0)
	s_barrier
; #define PG8_STAGE(bufoff, rs_, soff_, voff) do { _Pragma("unroll") for (int _i = 0; _i < 2; ++_i) \
;         __builtin_amdgcn_raw_ptr_buffer_load_lds(rs_, (LAS void*)(lds + (bufoff) + ldsw + _i * 8192), 16, (int)(voff)[_i], (int)(soff_), 0, 0); } while (0)
; #define PG8_LDA(dst, b, h) do { _Pragma("unroll") for (int m = 0; m < 4; ++m) dst[m] = PG8_LD2(lds + PG8_SA(b, h) + aoff + m * 2048); } while (0)
; #define PG8_LDB(dst, b, h) do { _Pragma("unroll") for (int n = 0; n < 2; ++n) dst[n] = PG8_LD2(lds + PG8_SB(b, h) + boff + n * 2048); } while (0)
; #define PG8_WAIT_V(n) asm volatile("s_waitcnt vmcnt(" #n ")" ::: "memory")
; #define PG8_WAIT_L(n) asm volatile("s_waitcnt lgkmcnt(" #n ")" ::: "memory")
; #define PG8_BAR __builtin_amdgcn_s_barrier()
; #define PG8_SCHED __builtin_amdgcn_sched_barrier(0)
; template <class Epi, class Sched, bool ALIGN_EPI = false, bool SP2 = false, bool FP8 = false>
; __device__ __forceinline__ void gemm_phase(LAS unsigned char* lds, const Gemm g, const Sched& S, const Epi& E, int wbase) {
;     ...
;             PG8_LDB(B0, 0, 0); PG8_LDB(B1, 0, 1); PG8_SCHED; PG8_LDA(At, 0, 0); PG8_STAGE(PG8_SA(1, 1), rAc, a1 + hstep, voffA);
;             PG8_WAIT_V(8); PG8_WAIT_L(0); PG8_BAR; PG8_MMA(0, 0, At, B0); PG8_MMA(0, 1, At, B1); PG8_BAR; PG8_SCHED;
;             PG8_LDA(At, 0, 1); PG8_STAGE(PG8_SB(0, 0), rB2, b2, voffB); PG8_STAGE(PG8_SB(0, 1), rB2, b2 + hstep, voffB); PG8_STAGE(PG8_SA(0, 0), rA2, a2, voffA);
;             PG8_WAIT_V(8); PG8_WAIT_L(0); PG8_BAR; PG8_MMA(1, 0, At, B0); PG8_MMA(1, 1, At, B1); PG8_BAR; PG8_SCHED;
;             PG8_LDB(B0, 1, 0); PG8_LDB(B1, 1, 1); PG8_SCHED; PG8_LDA(At, 1, 0); PG8_STAGE(PG8_SA(0, 1), rA2, a2 + hstep, voffA);
;             PG8_WAIT_V(8); PG8_WAIT_L(0); PG8_BAR; PG8_MMA(0, 0, At, B0); PG8_MMA(0, 1, At, B1); PG8_BAR; PG8_SCHED;
;             PG8_LDA(At, 1, 1); PG8_STAGE(PG8_SB(1, 0), rB2, b3, voffB); PG8_STAGE(PG8_SB(1, 1), rB2, b3 + hstep, voffB); PG8_STAGE(PG8_SA(1, 0), rA2, a3, voffA);
;             PG8_WAIT_V(8); PG8_WAIT_L(0); PG8_BAR; PG8_MMA(1, 0, At, B0); PG8_MMA(1, 1, At, B1); PG8_BAR; PG8_SCHED;
	s_setprio 1
	v_mfma_f32_16x16x128_f8f6f4 v[120:123], v[0:7], v[20:27], v[120:123]
	v_mfma_f32_16x16x128_f8f6f4 v[124:127], v[12:19], v[20:27], v[124:127]
	v_mfma_f32_16x16x128_f8f6f4 v[104:107], v[0:7], v[28:35], v[104:107]
	v_mfma_f32_16x16x128_f8f6f4 v[108:111], v[12:19], v[28:35], v[108:111]
	v_mfma_f32_16x16x128_f8f6f4 v[88:91], v[0:7], v[36:43], v[144:147]
	v_mfma_f32_16x16x128_f8f6f4 v[92:95], v[12:19], v[36:43], v[188:191]
	v_mfma_f32_16x16x128_f8f6f4 v[72:75], v[0:7], v[44:51], v[210:213]
	v_mfma_f32_16x16x128_f8f6f4 v[76:79], v[12:19], v[44:51], v[214:217]
	v_mfma_f32_16x16x128_f8f6f4 v[112:115], v[128:135], v[20:27], v[112:115]
	v_mfma_f32_16x16x128_f8f6f4 v[116:119], v[136:143], v[20:27], v[116:119]
	v_mfma_f32_16x16x128_f8f6f4 v[96:99], v[128:135], v[28:35], v[96:99]
	v_mfma_f32_16x16x128_f8f6f4 v[100:103], v[136:143], v[28:35], v[100:103]
	v_mfma_f32_16x16x128_f8f6f4 v[80:83], v[128:135], v[36:43], v[172:175]
	v_mfma_f32_16x16x128_f8f6f4 v[84:87], v[136:143], v[36:43], v[176:179]
	v_mfma_f32_16x16x128_f8f6f4 v[64:67], v[128:135], v[44:51], v[180:183]
	v_mfma_f32_16x16x128_f8f6f4 v[68:71], v[136:143], v[44:51], v[184:187]
	s_setprio 0
	s_barrier
	s_mov_b32 m0, s30
	s_bitset1_b32 s55, 7
	buffer_load_dwordx4 v149, s[4:7], s55 offen lds
	s_mov_b32 m0, s31
	ds_read_b128 v[32:35], v155 offset:49152
	buffer_load_dwordx4 v151, s[4:7], s55 offen lds
	s_add_i32 s55, s55, s21
	s_mov_b32 m0, s35
	ds_read_b128 v[36:39], v155 offset:50176
	buffer_load_dwordx4 v149, s[4:7], s55 offen lds
	s_mov_b32 m0, s41
	ds_read_b128 v[156:159], v155 offset:51200
	buffer_load_dwordx4 v151, s[4:7], s55 offen lds
	s_mov_b32 m0, s33
	ds_read_b128 v[160:163], v155 offset:52224
	buffer_load_dwordx4 v148, s[36:39], s54 offen lds
	s_mov_b32 m0, s34
	ds_read_b128 v[164:167], v155 offset:53248
	buffer_load_dwordx4 v150, s[36:39], s54 offen lds
	ds_read_b128 v[168:171], v155 offset:54272
	ds_read_b128 v[172:175], v155 offset:55296
	ds_read_b128 v[176:179], v155 offset:56320
	s_waitcnt vmcnt(8)
	s_waitcnt lgkmcnt(0)
	s_barrier
	s_setprio 1
	v_mfma_f32_16x16x128_f8f6f4 v[56:59], v[0:7], v[32:39], v[56:59]
	v_mfma_f32_16x16x128_f8f6f4 v[60:63], v[12:19], v[32:39], v[60:63]
	v_mfma_f32_16x16x128_f8f6f4 v[40:43], v[0:7], v[156:163], v[192:195]
	v_mfma_f32_16x16x128_f8f6f4 v[44:47], v[12:19], v[156:163], v[196:199]
	v_mfma_f32_16x16x128_f8f6f4 v[24:27], v[0:7], v[164:171], v[200:203]
	v_mfma_f32_16x16x128_f8f6f4 v[28:31], v[12:19], v[164:171], v[204:207]
	v_mfma_f32_16x16x128_f8f6f4 v[8:11], v[0:7], v[172:179], v[8:11]
	v_mfma_f32_16x16x128_f8f6f4 v[12:15], v[12:19], v[172:179], v[218:221]
	v_mfma_f32_16x16x128_f8f6f4 v[48:51], v[128:135], v[32:39], v[226:229]
	v_mfma_f32_16x16x128_f8f6f4 v[52:55], v[136:143], v[32:39], v[52:55]
	v_mfma_f32_16x16x128_f8f6f4 v[32:35], v[128:135], v[156:163], v[230:233]
	v_mfma_f32_16x16x128_f8f6f4 v[36:39], v[136:143], v[156:163], v[234:237]
	v_mfma_f32_16x16x128_f8f6f4 v[16:19], v[128:135], v[164:171], v[238:241]
	v_mfma_f32_16x16x128_f8f6f4 v[20:23], v[136:143], v[164:171], v[242:245]
	v_mfma_f32_16x16x128_f8f6f4 v[4:7], v[128:135], v[172:179], v[246:249]
	v_mfma_f32_16x16x128_f8f6f4 v[0:3], v[136:143], v[172:179], v[250:253]
	s_setprio 0
	s_barrier
	s_add_i32 s63, s63, 2
	s_addk_i32 s61, 0x100
	s_addk_i32 s62, 0x100
	s_cmp_ge_i32 s63, s43
	s_cbranch_scc0 .LBB0_1781
	s_branch .Lzp_after_1781
.LBB0_1781:
	v_add_u32_e32 v140, 0x10000, v154
	v_add_u32_e32 v144, 0x14000, v154
	ds_read_b128 v[128:131], v140
	ds_read_b128 v[132:135], v140 offset:1024
	ds_read_b128 v[136:139], v140 offset:2048
	ds_read_b128 v[140:143], v140 offset:3072
	ds_read_b128 v[156:159], v144
	ds_read_b128 v[160:163], v144 offset:1024
	ds_read_b128 v[164:167], v144 offset:2048
	ds_read_b128 v[168:171], v144 offset:3072
	s_add_i32 s6, s61, 0x80
	s_cmp_eq_u32 s45, s63
	s_cselect_b32 s65, s59, s6
	s_cselect_b32 s55, s60, s62
	s_or_b32 s54, s65, 0x80
	s_add_i32 s6, s21, s61
	s_mov_b32 m0, s46
	ds_read_b128 v[172:175], v155
	ds_read_b128 v[176:179], v155 offset:1024
	ds_read_b128 v[180:183], v155 offset:2048
	ds_read_b128 v[184:187], v155 offset:3072
	ds_read_b128 v[194:197], v155 offset:4096
	ds_read_b128 v[198:201], v155 offset:5120
	ds_read_b128 v[202:205], v155 offset:6144
	ds_read_b128 v[206:209], v155 offset:7168
	buffer_load_dwordx4 v148, s[36:39], s6 offen lds
	s_mov_b32 m0, s47
	s_nop 0
	buffer_load_dwordx4 v150, s[36:39], s6 offen lds
	s_waitcnt vmcnt(8)
	s_waitcnt lgkmcnt(0)
	s_barrier
	s_setprio 1
	v_mfma_f32_16x16x128_f8f6f4 v[120:123], v[128:135], v[172:179], v[120:123]
	v_mfma_f32_16x16x128_f8f6f4 v[124:127], v[136:143], v[172:179], v[124:127]
	v_mfma_f32_16x16x128_f8f6f4 v[104:107], v[128:135], v[180:187], v[104:107]
	v_mfma_f32_16x16x128_f8f6f4 v[108:111], v[136:143], v[180:187], v[108:111]
	v_mfma_f32_16x16x128_f8f6f4 v[144:147], v[128:135], v[194:201], v[88:91]
	v_mfma_f32_16x16x128_f8f6f4 v[188:191], v[136:143], v[194:201], v[92:95]
	v_mfma_f32_16x16x128_f8f6f4 v[210:213], v[128:135], v[202:209], v[72:75]
	v_mfma_f32_16x16x128_f8f6f4 v[214:217], v[136:143], v[202:209], v[76:79]
	v_mfma_f32_16x16x128_f8f6f4 v[112:115], v[156:163], v[172:179], v[112:115]
	v_mfma_f32_16x16x128_f8f6f4 v[116:119], v[164:171], v[172:179], v[116:119]
	v_mfma_f32_16x16x128_f8f6f4 v[96:99], v[156:163], v[180:187], v[96:99]
	v_mfma_f32_16x16x128_f8f6f4 v[100:103], v[164:171], v[180:187], v[100:103]
	v_mfma_f32_16x16x128_f8f6f4 v[172:175], v[156:163], v[194:201], v[80:83]
	v_mfma_f32_16x16x128_f8f6f4 v[176:179], v[164:171], v[194:201], v[84:87]
	v_mfma_f32_16x16x128_f8f6f4 v[180:183], v[156:163], v[202:209], v[64:67]
	v_mfma_f32_16x16x128_f8f6f4 v[184:187], v[164:171], v[202:209], v[68:71]
	s_setprio 0
	s_barrier
; #define PG8_STAGE(bufoff, rs_, soff_, voff) do { _Pragma("unroll") for (int _i = 0; _i < 2; ++_i) \
;         __builtin_amdgcn_raw_ptr_buffer_load_lds(rs_, (LAS void*)(lds + (bufoff) + ldsw + _i * 8192), 16, (int)(voff)[_i], (int)(soff_), 0, 0); } while (0)
; #define PG8_LDA(dst, b, h) do { _Pragma("unroll") for (int m = 0; m < 4; ++m) dst[m] = PG8_LD2(lds + PG8_SA(b, h) + aoff + m * 2048); } while (0)
; #define PG8_LDB(dst, b, h) do { _Pragma("unroll") for (int n = 0; n < 2; ++n) dst[n] = PG8_LD2(lds + PG8_SB(b, h) + boff + n * 2048); } while (0)
; #define PG8_WAIT_V(n) asm volatile("s_waitcnt vmcnt(" #n ")" ::: "memory")
; #define PG8_WAIT_L(n) asm volatile("s_waitcnt lgkmcnt(" #n ")" ::: "memory")
; #define PG8_BAR __builtin_amdgcn_s_barrier()
; #define PG8_SCHED __builtin_amdgcn_sched_barrier(0)
; template <class Epi, class Sched, bool ALIGN_EPI = false, bool SP2 = false, bool FP8 = false>
; __device__ __forceinline__ void gemm_phase(LAS unsigned char* lds, const Gemm g, const Sched& S, const Epi& E, int wbase) {
;     ...
;             PG8_LDA(At, 0, 1); PG8_STAGE(PG8_SB(0, 0), rB2, b2, voffB); PG8_STAGE(PG8_SB(0, 1), rB2, b2 + hstep, voffB); PG8_STAGE(PG8_SA(0, 0), rA2, a2, voffA);
;             PG8_WAIT_V(8); PG8_WAIT_L(0); PG8_BAR; PG8_MMA(1, 0, At, B0); PG8_MMA(1, 1, At, B1); PG8_BAR; PG8_SCHED;
;             PG8_LDB(B0, 1, 0); PG8_LDB(B1, 1, 1); PG8_SCHED; PG8_LDA(At, 1, 0); PG8_STAGE(PG8_SA(0, 1), rA2, a2 + hstep, voffA);
;             PG8_WAIT_V(8); PG8_WAIT_L(0); PG8_BAR; PG8_MMA(0, 0, At, B0); PG8_MMA(0, 1, At, B1); PG8_BAR; PG8_SCHED;
;             PG8_LDA(At, 1, 1); PG8_STAGE(PG8_SB(1, 0), rB2, b3, voffB); PG8_STAGE(PG8_SB(1, 1), rB2, b3 + hstep, voffB); PG8_STAGE(PG8_SA(1, 0), rA2, a3, voffA);
;             PG8_WAIT_V(8); PG8_WAIT_L(0); PG8_BAR; PG8_MMA(1, 0, At, B0); PG8_MMA(1, 1, At, B1); PG8_BAR; PG8_SCHED;
	s_mov_b32 m0, s23
	s_mov_b32 s6, s38
	s_mov_b32 s7, s39
	s_nop 0
	buffer_load_dwordx4 v149, s[4:7], s55 offen lds
	s_mov_b32 m0, s24
	ds_read_b128 v[64:67], v155 offset:16384
	s_add_i32 s66, s55, s21
	buffer_load_dwordx4 v151, s[4:7], s55 offen lds
	s_mov_b32 m0, s25
	ds_read_b128 v[68:71], v155 offset:17408
	buffer_load_dwordx4 v149, s[4:7], s66 offen lds
	s_mov_b32 m0, s22
	ds_read_b128 v[72:75], v155 offset:18432
	buffer_load_dwordx4 v148, s[36:39], s65 offen lds
	s_mov_b32 m0, s27
	ds_read_b128 v[76:79], v155 offset:19456
	buffer_load_dwordx4 v150, s[36:39], s65 offen lds
	ds_read_b128 v[80:83], v155 offset:20480
	ds_read_b128 v[84:87], v155 offset:21504
	ds_read_b128 v[88:91], v155 offset:22528
	ds_read_b128 v[92:95], v155 offset:23552
	s_waitcnt vmcnt(7)
	s_waitcnt lgkmcnt(0)
	s_barrier
	s_setprio 1
	v_mfma_f32_16x16x128_f8f6f4 v[56:59], v[128:135], v[64:71], v[56:59]
	v_mfma_f32_16x16x128_f8f6f4 v[60:63], v[136:143], v[64:71], v[60:63]
	v_mfma_f32_16x16x128_f8f6f4 v[8:11], v[128:135], v[88:95], v[8:11]
	v_mfma_f32_16x16x128_f8f6f4 v[192:195], v[128:135], v[72:79], v[40:43]
	v_mfma_f32_16x16x128_f8f6f4 v[196:199], v[136:143], v[72:79], v[44:47]
	v_mfma_f32_16x16x128_f8f6f4 v[200:203], v[128:135], v[80:87], v[24:27]
	v_mfma_f32_16x16x128_f8f6f4 v[204:207], v[136:143], v[80:87], v[28:31]
	v_mfma_f32_16x16x128_f8f6f4 v[218:221], v[136:143], v[88:95], v[12:15]
	v_mfma_f32_16x16x128_f8f6f4 v[52:55], v[164:171], v[64:71], v[52:55]
	v_mfma_f32_16x16x128_f8f6f4 v[226:229], v[156:163], v[64:71], v[48:51]
	v_mfma_f32_16x16x128_f8f6f4 v[230:233], v[156:163], v[72:79], v[32:35]
	v_mfma_f32_16x16x128_f8f6f4 v[234:237], v[164:171], v[72:79], v[36:39]
	v_mfma_f32_16x16x128_f8f6f4 v[238:241], v[156:163], v[80:87], v[16:19]
	v_mfma_f32_16x16x128_f8f6f4 v[242:245], v[164:171], v[80:87], v[20:23]
	v_mfma_f32_16x16x128_f8f6f4 v[246:249], v[156:163], v[88:95], v[4:7]
	v_mfma_f32_16x16x128_f8f6f4 v[250:253], v[164:171], v[88:95], v[0:3]
	s_setprio 0
	s_barrier
	s_mov_b32 m0, s26
	s_nop 0
	buffer_load_dwordx4 v151, s[4:7], s66 offen lds
	s_nop 1
	v_add_u32_e32 v16, 0x18000, v154
	v_add_u32_e32 v20, 0x1c000, v154
	s_nop 0
	ds_read_b128 v[0:3], v16
	ds_read_b128 v[4:7], v16 offset:1024
	ds_read_b128 v[12:15], v16 offset:2048
	ds_read_b128 v[16:19], v16 offset:3072
	ds_read_b128 v[128:131], v20
	ds_read_b128 v[132:135], v20 offset:1024
	ds_read_b128 v[136:139], v20 offset:2048
	ds_read_b128 v[140:143], v20 offset:3072
	s_add_i32 s65, s65, s21
	s_mov_b32 m0, s28
	ds_read_b128 v[20:23], v155 offset:32768
	ds_read_b128 v[24:27], v155 offset:33792
	ds_read_b128 v[28:31], v155 offset:34816
	ds_read_b128 v[32:35], v155 offset:35840
	ds_read_b128 v[36:39], v155 offset:36864
	ds_read_b128 v[40:43], v155 offset:37888
	ds_read_b128 v[44:47], v155 offset:38912
	ds_read_b128 v[48:51], v155 offset:39936
	buffer_load_dwordx4 v148, s[36:39], s65 offen lds
	s_mov_b32 m0, s29
	s_nop 0
	buffer_load_dwordx4 v150, s[36:39], s65 offen lds
	s_waitcnt vmcnt(8)
	s_waitcnt lgkmcnt(0)
	s_barrier
	s_setprio 1
	v_mfma_f32_16x16x128_f8f6f4 v[120:123], v[0:7], v[20:27], v[120:123]
	v_mfma_f32_16x16x128_f8f6f4 v[124:127], v[12:19], v[20:27], v[124:127]
	v_mfma_f32_16x16x128_f8f6f4 v[104:107], v[0:7], v[28:35], v[104:107]
	v_mfma_f32_16x16x128_f8f6f4 v[108:111], v[12:19], v[28:35], v[108:111]
	v_mfma_f32_16x16x128_f8f6f4 v[88:91], v[0:7], v[36:43], v[144:147]
	v_mfma_f32_16x16x128_f8f6f4 v[92:95], v[12:19], v[36:43], v[188:191]
	v_mfma_f32_16x16x128_f8f6f4 v[72:75], v[0:7], v[44:51], v[210:213]
	v_mfma_f32_16x16x128_f8f6f4 v[76:79], v[12:19], v[44:51], v[214:217]
	v_mfma_f32_16x16x128_f8f6f4 v[112:115], v[128:135], v[20:27], v[112:115]
	v_mfma_f32_16x16x128_f8f6f4 v[116:119], v[136:143], v[20:27], v[116:119]
	v_mfma_f32_16x16x128_f8f6f4 v[96:99], v[128:135], v[28:35], v[96:99]
	v_mfma_f32_16x16x128_f8f6f4 v[100:103], v[136:143], v[28:35], v[100:103]
	v_mfma_f32_16x16x128_f8f6f4 v[80:83], v[128:135], v[36:43], v[172:175]
	v_mfma_f32_16x16x128_f8f6f4 v[84:87], v[136:143], v[36:43], v[176:179]
	v_mfma_f32_16x16x128_f8f6f4 v[64:67], v[128:135], v[44:51], v[180:183]
	v_mfma_f32_16x16x128_f8f6f4 v[68:71], v[136:143], v[44:51], v[184:187]
	s_setprio 0
	s_barrier
	s_mov_b32 m0, s30
	s_bitset1_b32 s55, 7
	buffer_load_dwordx4 v149, s[4:7], s55 offen lds
	s_mov_b32 m0, s31
	ds_read_b128 v[32:35], v155 offset:49152
	buffer_load_dwordx4 v151, s[4:7], s55 offen lds
	s_add_i32 s55, s55, s21
	s_mov_b32 m0, s35
	ds_read_b128 v[36:39], v155 offset:50176
	buffer_load_dwordx4 v149, s[4:7], s55 offen lds
	s_mov_b32 m0, s41
	ds_read_b128 v[156:159], v155 offset:51200
	buffer_load_dwordx4 v151, s[4:7], s55 offen lds
	s_mov_b32 m0, s33
	ds_read_b128 v[160:163], v155 offset:52224
	buffer_load_dwordx4 v148, s[36:39], s54 offen lds
	s_mov_b32 m0, s34
	ds_read_b128 v[164:167], v155 offset:53248
	buffer_load_dwordx4 v150, s[36:39], s54 offen lds
	ds_read_b128 v[168:171], v155 offset:54272
	ds_read_b128 v[172:175], v155 offset:55296
	ds_read_b128 v[176:179], v155 offset:56320
	s_waitcnt vmcnt(8)
	s_waitcnt lgkmcnt(0)
	s_barrier
	s_setprio 1
	v_mfma_f32_16x16x128_f8f6f4 v[56:59], v[0:7], v[32:39], v[56:59]
	v_mfma_f32_16x16x128_f8f6f4 v[60:63], v[12:19], v[32:39], v[60:63]
	v_mfma_f32_16x16x128_f8f6f4 v[40:43], v[0:7], v[156:163], v[192:195]
	v_mfma_f32_16x16x128_f8f6f4 v[44:47], v[12:19], v[156:163], v[196:199]
	v_mfma_f32_16x16x128_f8f6f4 v[24:27], v[0:7], v[164:171], v[200:203]
	v_mfma_f32_16x16x128_f8f6f4 v[28:31], v[12:19], v[164:171], v[204:207]
	v_mfma_f32_16x16x128_f8f6f4 v[8:11], v[0:7], v[172:179], v[8:11]
	v_mfma_f32_16x16x128_f8f6f4 v[12:15], v[12:19], v[172:179], v[218:221]
	v_mfma_f32_16x16x128_f8f6f4 v[48:51], v[128:135], v[32:39], v[226:229]
	v_mfma_f32_16x16x128_f8f6f4 v[52:55], v[136:143], v[32:39], v[52:55]
	v_mfma_f32_16x16x128_f8f6f4 v[32:35], v[128:135], v[156:163], v[230:233]
	v_mfma_f32_16x16x128_f8f6f4 v[36:39], v[136:143], v[156:163], v[234:237]
	v_mfma_f32_16x16x128_f8f6f4 v[16:19], v[128:135], v[164:171], v[238:241]
	v_mfma_f32_16x16x128_f8f6f4 v[20:23], v[136:143], v[164:171], v[242:245]
	v_mfma_f32_16x16x128_f8f6f4 v[4:7], v[128:135], v[172:179], v[246:249]
	v_mfma_f32_16x16x128_f8f6f4 v[0:3], v[136:143], v[172:179], v[250:253]
	s_setprio 0
	s_barrier
	s_add_i32 s63, s63, 2
	s_addk_i32 s61, 0x100
	s_addk_i32 s62, 0x100
	s_cmp_ge_i32 s63, s43
	s_cbranch_scc0 .LBB0_1781

;     __device__ __forceinline__ unsigned a_off(const Unit& u, const Gemm& g) const { return (unsigned)u.pm * (unsigned)(BM * 2) * (unsigned)g.K; }
;     __device__ __forceinline__ unsigned b_off(const Unit& u, const Gemm& g) const { return (unsigned)u.pn * (unsigned)(BM * 2) * (unsigned)g.K; }
;     __device__ __forceinline__ bool next(int i, Unit& u) const { return so.next(i, u); }
;     __device__ __forceinline__ unsigned a_off(const Unit& u, const Gemm& g) const { return (unsigned)u.pm * (unsigned)(BM * 2) * (unsigned)g.K; }
; template <class Epi, class Sched, bool ALIGN_EPI = false, bool SP2 = false, bool FP8 = false>
; __device__ __forceinline__ void gemm_phase(LAS unsigned char* lds, const Gemm g, const Sched& S, const Epi& E, int wbase) {
;     ...
;         const bool has_next = S.next(ui + 1, nxt);
;         const unsigned nA = has_next ? S.a_off(nxt, g) : cA, nB = has_next ? S.b_off(nxt, g) : cB;
;         const rsrc_t rAn = (Sched::TWO && has_next) ? (nxt.part ? rA1 : rA0) : rAc, rBn = (Sched::TWO && has_next) ? (nxt.part ? rB1 : rB0) : rBc;
;         float pre_[8] = {0.f, 0.f, 0.f, 0.f, 0.f, 0.f, 0.f, 0.f};
;         if constexpr (Epi::HAS_PRE) E.pre_load(pre_, cur, wr);
;         for (int t = 0; t < nt; t += 2) {
;             const bool last = (t == nt - 2);
;             const unsigned a1 = cA + (unsigned)(t + 1) * kstep;
;             const unsigned a2 = last ? nA : cA + (unsigned)(t + 2) * kstep, b2 = last ? nB : cB + (unsigned)(t + 2) * kstep; const rsrc_t rA2 = (Sched::TWO && last) ? rAn : rAc, rB2 = (Sched::TWO && last) ? rBn : rBc;
;             const unsigned a3 = a2 + kstep, b3 = b2 + kstep;
;             if (last && has_next) S.a_ready(nxt);
;             if constexpr (SP2) {
;             PG8_LDB(B0, 0, 0); PG8_LDB(B1, 0, 1); PG8_SCHED; PG8_LDA(At, 0, 0); PG8_STAGE(PG8_SA(1, 1), rAc, a1 + hstep, voffA);
;             PG8_WAIT_V(8); PG8_WAIT_L(0); PG8_BAR; PG8_MMA(0, 0, At, B0); PG8_MMA(0, 1, At, B1); PG8_BAR; PG8_SCHED;
;             PG8_LDA(At, 0, 1); PG8_STAGE(PG8_SB(0, 0), rB2, b2, voffB); PG8_STAGE(PG8_SB(0, 1), rB2, b2 + hstep, voffB); PG8_STAGE(PG8_SA(0, 0), rA2, a2, voffA);
;             PG8_WAIT_V(8); PG8_WAIT_L(0); PG8_BAR; PG8_MMA(1, 0, At, B0); PG8_MMA(1, 1, At, B1); PG8_BAR; PG8_SCHED;
;             PG8_LDB(B0, 1, 0); PG8_LDB(B1, 1, 1); PG8_SCHED; PG8_LDA(At, 1, 0); PG8_STAGE(PG8_SA(0, 1), rA2, a2 + hstep, voffA);
.LBB0_1852:
	s_mul_i32 s61, s60, 0xe0000
	s_andn2_b64 vcc, exec, s[14:15]
	s_mul_i32 s62, s59, 0xe0000
	s_cbranch_vccnz .LBB0_1856
	s_and_b64 s[6:7], s[18:19], exec
	s_waitcnt vmcnt(37)
	s_waitcnt vmcnt(36)
	s_waitcnt vmcnt(35)
	s_waitcnt vmcnt(32)
	s_waitcnt vmcnt(31)
	s_waitcnt vmcnt(28)
	s_waitcnt vmcnt(27)
	s_waitcnt vmcnt(24)
	s_waitcnt vmcnt(23)
	s_waitcnt vmcnt(22)
	v_mov_b32_e32 v223, 0xff61b1e6
	v_mov_b32_e32 v222, 1
	v_mov_b32_e32 v169, v233
	v_mov_b32_e32 v168, 0x358637bd
	s_cselect_b32 s21, s61, s55
	s_cselect_b32 s63, s62, s54
	s_add_i32 s65, s55, 0x80
	s_add_i32 s66, s54, 0x100
	s_mov_b32 s67, 0
	v_add_u32_e32 v140, 0x10000, v176
	v_add_u32_e32 v156, 0x14000, v176
	ds_read_b128 v[128:131], v140
	ds_read_b128 v[132:135], v140 offset:1024
	ds_read_b128 v[136:139], v140 offset:2048
	ds_read_b128 v[140:143], v140 offset:3072
	ds_read_b128 v[144:147], v156
	ds_read_b128 v[148:151], v156 offset:1024
	ds_read_b128 v[152:155], v156 offset:2048
	ds_read_b128 v[156:159], v156 offset:3072
	s_add_i32 s6, s65, 0x80
	s_cmp_eq_u32 s52, s67
	s_cselect_b32 s68, s21, s6
	s_cselect_b32 s55, s63, s66
	s_or_b32 s54, s68, 0x80
	s_add_i32 s6, s24, s65
	s_mov_b32 m0, s53
	ds_read_b128 v[160:163], v177
	ds_read_b128 v[164:167], v177 offset:1024
	ds_read_b128 v[178:181], v177 offset:2048
	ds_read_b128 v[182:185], v177 offset:3072
	ds_read_b128 v[194:197], v177 offset:4096
	ds_read_b128 v[198:201], v177 offset:5120
	ds_read_b128 v[202:205], v177 offset:6144
	ds_read_b128 v[206:209], v177 offset:7168
	buffer_load_dwordx4 v170, s[36:39], s6 offen lds
	s_mov_b32 m0, s56
	s_nop 0
	buffer_load_dwordx4 v172, s[36:39], s6 offen lds
	s_waitcnt vmcnt(8)
	s_waitcnt lgkmcnt(0)
	s_barrier
	s_setprio 1
	v_mfma_f32_16x16x128_f8f6f4 v[124:127], v[128:135], v[160:167], 0
	v_mfma_f32_16x16x128_f8f6f4 v[120:123], v[136:143], v[160:167], 0
	v_mfma_f32_16x16x128_f8f6f4 v[108:111], v[128:135], v[178:185], 0
	v_mfma_f32_16x16x128_f8f6f4 v[104:107], v[136:143], v[178:185], 0
	v_mfma_f32_16x16x128_f8f6f4 v[186:189], v[128:135], v[194:201], 0
	v_mfma_f32_16x16x128_f8f6f4 v[190:193], v[136:143], v[194:201], 0
	v_mfma_f32_16x16x128_f8f6f4 v[210:213], v[128:135], v[202:209], 0
	v_mfma_f32_16x16x128_f8f6f4 v[214:217], v[136:143], v[202:209], 0
	v_mfma_f32_16x16x128_f8f6f4 v[116:119], v[144:151], v[160:167], 0
	v_mfma_f32_16x16x128_f8f6f4 v[112:115], v[152:159], v[160:167], 0
	v_mfma_f32_16x16x128_f8f6f4 v[100:103], v[144:151], v[178:185], 0
	v_mfma_f32_16x16x128_f8f6f4 v[96:99], v[152:159], v[178:185], 0
	v_mfma_f32_16x16x128_f8f6f4 v[160:163], v[144:151], v[194:201], 0
	v_mfma_f32_16x16x128_f8f6f4 v[164:167], v[152:159], v[194:201], 0
	v_mfma_f32_16x16x128_f8f6f4 v[178:181], v[144:151], v[202:209], 0
	v_mfma_f32_16x16x128_f8f6f4 v[182:185], v[152:159], v[202:209], 0
	s_setprio 0
	s_barrier
	s_mov_b32 m0, s26
	s_mov_b32 s6, s38
	s_mov_b32 s7, s39
	s_nop 1
	buffer_load_dwordx4 v171, s[4:7], s55 offen lds
	s_mov_b32 m0, s27
	ds_read_b128 v[64:67], v177 offset:16384
	s_add_i32 s69, s55, s24
	buffer_load_dwordx4 v173, s[4:7], s55 offen lds
	s_mov_b32 m0, s28
	ds_read_b128 v[68:71], v177 offset:17408
	buffer_load_dwordx4 v171, s[4:7], s69 offen lds
	s_mov_b32 m0, s25
	ds_read_b128 v[72:75], v177 offset:18432
	buffer_load_dwordx4 v170, s[36:39], s68 offen lds
	s_mov_b32 m0, s30
	ds_read_b128 v[76:79], v177 offset:19456
	buffer_load_dwordx4 v172, s[36:39], s68 offen lds
	ds_read_b128 v[80:83], v177 offset:20480
	ds_read_b128 v[84:87], v177 offset:21504
	ds_read_b128 v[88:91], v177 offset:22528
	ds_read_b128 v[92:95], v177 offset:23552
	s_waitcnt vmcnt(7)
	s_waitcnt lgkmcnt(0)
	s_barrier
	s_setprio 1
	v_mfma_f32_16x16x128_f8f6f4 v[60:63], v[128:135], v[64:71], 0
	v_mfma_f32_16x16x128_f8f6f4 v[56:59], v[136:143], v[64:71], 0
	v_mfma_f32_16x16x128_f8f6f4 v[194:197], v[128:135], v[72:79], 0
	v_mfma_f32_16x16x128_f8f6f4 v[198:201], v[136:143], v[72:79], 0
	v_mfma_f32_16x16x128_f8f6f4 v[202:205], v[128:135], v[80:87], 0
	v_mfma_f32_16x16x128_f8f6f4 v[206:209], v[136:143], v[80:87], 0
	v_mfma_f32_16x16x128_f8f6f4 v[218:221], v[128:135], v[88:95], 0
	v_mfma_f32_16x16x128_f8f6f4 v[226:229], v[136:143], v[88:95], 0
	v_mfma_f32_16x16x128_f8f6f4 v[52:55], v[144:151], v[64:71], 0
	v_mfma_f32_16x16x128_f8f6f4 v[48:51], v[152:159], v[64:71], 0
	v_mfma_f32_16x16x128_f8f6f4 v[230:233], v[144:151], v[72:79], 0
	v_mfma_f32_16x16x128_f8f6f4 v[234:237], v[152:159], v[72:79], 0
	v_mfma_f32_16x16x128_f8f6f4 v[238:241], v[144:151], v[80:87], 0
	v_mfma_f32_16x16x128_f8f6f4 v[242:245], v[152:159], v[80:87], 0
	v_mfma_f32_16x16x128_f8f6f4 v[246:249], v[144:151], v[88:95], 0
	v_mfma_f32_16x16x128_f8f6f4 v[250:253], v[152:159], v[88:95], 0
	s_setprio 0
	s_barrier
	s_mov_b32 m0, s29
	s_nop 0
	buffer_load_dwordx4 v173, s[4:7], s69 offen lds
	v_add_u32_e32 v8, 0x18000, v176
	s_nop 3
	ds_read_b128 v[0:3], v8
	ds_read_b128 v[4:7], v8 offset:1024
	ds_read_b128 v[16:19], v8 offset:2048
	ds_read_b128 v[20:23], v8 offset:3072
	v_add_u32_e32 v8, 0x1c000, v176
	ds_read_b128 v[128:131], v8
	ds_read_b128 v[132:135], v8 offset:1024
	ds_read_b128 v[136:139], v8 offset:2048
	ds_read_b128 v[140:143], v8 offset:3072
	s_add_i32 s68, s68, s24
	s_mov_b32 m0, s31
	ds_read_b128 v[8:11], v177 offset:32768
	ds_read_b128 v[12:15], v177 offset:33792
	ds_read_b128 v[24:27], v177 offset:34816
	ds_read_b128 v[28:31], v177 offset:35840
	ds_read_b128 v[32:35], v177 offset:36864
	ds_read_b128 v[36:39], v177 offset:37888
	ds_read_b128 v[40:43], v177 offset:38912
	ds_read_b128 v[44:47], v177 offset:39936
	buffer_load_dwordx4 v170, s[36:39], s68 offen lds
	s_mov_b32 m0, s33
	s_nop 0
	buffer_load_dwordx4 v172, s[36:39], s68 offen lds
	s_waitcnt vmcnt(8)
	s_waitcnt lgkmcnt(0)
	s_barrier
; #define PG8_STAGE(bufoff, rs_, soff_, voff) do { _Pragma("unroll") for (int _i = 0; _i < 2; ++_i) \
;         __builtin_amdgcn_raw_ptr_buffer_load_lds(rs_, (LAS void*)(lds + (bufoff) + ldsw + _i * 8192), 16, (int)(voff)[_i], (int)(soff_), 0, 0); } while (0)
; #define PG8_LDA(dst, b, h) do { _Pragma("unroll") for (int m = 0; m < 4; ++m) dst[m] = PG8_LD2(lds + PG8_SA(b, h) + aoff + m * 2048); } while (0)
; #define PG8_LDB(dst, b, h) do { _Pragma("unroll") for (int n = 0; n < 2; ++n) dst[n] = PG8_LD2(lds + PG8_SB(b, h) + boff + n * 2048); } while (0)
; #define PG8_WAIT_V(n) asm volatile("s_waitcnt vmcnt(" #n ")" ::: "memory")
; #define PG8_WAIT_L(n) asm volatile("s_waitcnt lgkmcnt(" #n ")" ::: "memory")
; #define PG8_BAR __builtin_amdgcn_s_barrier()
; #define PG8_SCHED __builtin_amdgcn_sched_barrier(0)
; template <class Epi, class Sched, bool ALIGN_EPI = false, bool SP2 = false, bool FP8 = false>
; __device__ __forceinline__ void gemm_phase(LAS unsigned char* lds, const Gemm g, const Sched& S, const Epi& E, int wbase) {
;     ...
;             PG8_LDB(B0, 0, 0); PG8_LDB(B1, 0, 1); PG8_SCHED; PG8_LDA(At, 0, 0); PG8_STAGE(PG8_SA(1, 1), rAc, a1 + hstep, voffA);
;             PG8_WAIT_V(8); PG8_WAIT_L(0); PG8_BAR; PG8_MMA(0, 0, At, B0); PG8_MMA(0, 1, At, B1); PG8_BAR; PG8_SCHED;
;             PG8_LDA(At, 0, 1); PG8_STAGE(PG8_SB(0, 0), rB2, b2, voffB); PG8_STAGE(PG8_SB(0, 1), rB2, b2 + hstep, voffB); PG8_STAGE(PG8_SA(0, 0), rA2, a2, voffA);
;             PG8_WAIT_V(8); PG8_WAIT_L(0); PG8_BAR; PG8_MMA(1, 0, At, B0); PG8_MMA(1, 1, At, B1); PG8_BAR; PG8_SCHED;
;             PG8_LDB(B0, 1, 0); PG8_LDB(B1, 1, 1); PG8_SCHED; PG8_LDA(At, 1, 0); PG8_STAGE(PG8_SA(0, 1), rA2, a2 + hstep, voffA);
;             PG8_WAIT_V(8); PG8_WAIT_L(0); PG8_BAR; PG8_MMA(0, 0, At, B0); PG8_MMA(0, 1, At, B1); PG8_BAR; PG8_SCHED;
;             PG8_LDA(At, 1, 1); PG8_STAGE(PG8_SB(1, 0), rB2, b3, voffB); PG8_STAGE(PG8_SB(1, 1), rB2, b3 + hstep, voffB); PG8_STAGE(PG8_SA(1, 0), rA2, a3, voffA);
;             PG8_WAIT_V(8); PG8_WAIT_L(0); PG8_BAR; PG8_MMA(1, 0, At, B0); PG8_MMA(1, 1, At, B1); PG8_BAR; PG8_SCHED;
	s_setprio 1
	v_mfma_f32_16x16x128_f8f6f4 v[124:127], v[0:7], v[8:15], v[124:127]
	v_mfma_f32_16x16x128_f8f6f4 v[120:123], v[16:23], v[8:15], v[120:123]
	v_mfma_f32_16x16x128_f8f6f4 v[108:111], v[0:7], v[24:31], v[108:111]
	v_mfma_f32_16x16x128_f8f6f4 v[104:107], v[16:23], v[24:31], v[104:107]
	v_mfma_f32_16x16x128_f8f6f4 v[92:95], v[0:7], v[32:39], v[186:189]
	v_mfma_f32_16x16x128_f8f6f4 v[88:91], v[16:23], v[32:39], v[190:193]
	v_mfma_f32_16x16x128_f8f6f4 v[76:79], v[0:7], v[40:47], v[210:213]
	v_mfma_f32_16x16x128_f8f6f4 v[72:75], v[16:23], v[40:47], v[214:217]
	v_mfma_f32_16x16x128_f8f6f4 v[116:119], v[128:135], v[8:15], v[116:119]
	v_mfma_f32_16x16x128_f8f6f4 v[112:115], v[136:143], v[8:15], v[112:115]
	v_mfma_f32_16x16x128_f8f6f4 v[100:103], v[128:135], v[24:31], v[100:103]
	v_mfma_f32_16x16x128_f8f6f4 v[96:99], v[136:143], v[24:31], v[96:99]
	v_mfma_f32_16x16x128_f8f6f4 v[84:87], v[128:135], v[32:39], v[160:163]
	v_mfma_f32_16x16x128_f8f6f4 v[80:83], v[136:143], v[32:39], v[164:167]
	v_mfma_f32_16x16x128_f8f6f4 v[68:71], v[128:135], v[40:47], v[178:181]
	v_mfma_f32_16x16x128_f8f6f4 v[64:67], v[136:143], v[40:47], v[182:185]
	s_setprio 0
	s_barrier
	s_mov_b32 m0, s34
	s_bitset1_b32 s55, 7
	buffer_load_dwordx4 v171, s[4:7], s55 offen lds
	s_mov_b32 m0, s35
	ds_read_b128 v[32:35], v177 offset:49152
	buffer_load_dwordx4 v173, s[4:7], s55 offen lds
	s_add_i32 s55, s55, s24
	s_mov_b32 m0, s43
	ds_read_b128 v[36:39], v177 offset:50176
	buffer_load_dwordx4 v171, s[4:7], s55 offen lds
	s_mov_b32 m0, s44
	ds_read_b128 v[144:147], v177 offset:51200
	buffer_load_dwordx4 v173, s[4:7], s55 offen lds
	s_mov_b32 m0, s41
	ds_read_b128 v[148:151], v177 offset:52224
	buffer_load_dwordx4 v170, s[36:39], s54 offen lds
	s_mov_b32 m0, s42
	ds_read_b128 v[152:155], v177 offset:53248
	buffer_load_dwordx4 v172, s[36:39], s54 offen lds
	ds_read_b128 v[156:159], v177 offset:54272
	ds_read_b128 v[160:163], v177 offset:55296
	ds_read_b128 v[164:167], v177 offset:56320
	s_waitcnt vmcnt(8)
	s_waitcnt lgkmcnt(0)
	s_barrier
	s_setprio 1
	v_mfma_f32_16x16x128_f8f6f4 v[60:63], v[0:7], v[32:39], v[60:63]
	v_mfma_f32_16x16x128_f8f6f4 v[56:59], v[16:23], v[32:39], v[56:59]
	v_mfma_f32_16x16x128_f8f6f4 v[44:47], v[0:7], v[144:151], v[194:197]
	v_mfma_f32_16x16x128_f8f6f4 v[40:43], v[16:23], v[144:151], v[198:201]
	v_mfma_f32_16x16x128_f8f6f4 v[28:31], v[0:7], v[152:159], v[202:205]
	v_mfma_f32_16x16x128_f8f6f4 v[24:27], v[16:23], v[152:159], v[206:209]
	v_mfma_f32_16x16x128_f8f6f4 v[12:15], v[0:7], v[160:167], v[218:221]
	v_mfma_f32_16x16x128_f8f6f4 v[8:11], v[16:23], v[160:167], v[226:229]
	v_mfma_f32_16x16x128_f8f6f4 v[52:55], v[128:135], v[32:39], v[52:55]
	v_mfma_f32_16x16x128_f8f6f4 v[48:51], v[136:143], v[32:39], v[48:51]
	v_mfma_f32_16x16x128_f8f6f4 v[36:39], v[128:135], v[144:151], v[230:233]
	v_mfma_f32_16x16x128_f8f6f4 v[32:35], v[136:143], v[144:151], v[234:237]
	v_mfma_f32_16x16x128_f8f6f4 v[20:23], v[128:135], v[152:159], v[238:241]
	v_mfma_f32_16x16x128_f8f6f4 v[16:19], v[136:143], v[152:159], v[242:245]
	v_mfma_f32_16x16x128_f8f6f4 v[4:7], v[128:135], v[160:167], v[246:249]
	v_mfma_f32_16x16x128_f8f6f4 v[0:3], v[136:143], v[160:167], v[250:253]
	s_setprio 0
	s_barrier
	s_add_i32 s67, s67, 2
	s_addk_i32 s65, 0x100
	s_addk_i32 s66, 0x100
	s_cmp_ge_i32 s67, s47
	s_cbranch_scc0 .LBB0_1854
	s_branch .Lzp_after_1854
.LBB0_1854:
	v_add_u32_e32 v140, 0x10000, v176
	v_add_u32_e32 v156, 0x14000, v176
	ds_read_b128 v[128:131], v140
	ds_read_b128 v[132:135], v140 offset:1024
	ds_read_b128 v[136:139], v140 offset:2048
	ds_read_b128 v[140:143], v140 offset:3072
	ds_read_b128 v[144:147], v156
	ds_read_b128 v[148:151], v156 offset:1024
	ds_read_b128 v[152:155], v156 offset:2048
	ds_read_b128 v[156:159], v156 offset:3072
	s_add_i32 s6, s65, 0x80
	s_cmp_eq_u32 s52, s67
	s_cselect_b32 s68, s21, s6
	s_cselect_b32 s55, s63, s66
	s_or_b32 s54, s68, 0x80
	s_add_i32 s6, s24, s65
	s_mov_b32 m0, s53
	ds_read_b128 v[160:163], v177
	ds_read_b128 v[164:167], v177 offset:1024
	ds_read_b128 v[178:181], v177 offset:2048
	ds_read_b128 v[182:185], v177 offset:3072
	ds_read_b128 v[194:197], v177 offset:4096
	ds_read_b128 v[198:201], v177 offset:5120
	ds_read_b128 v[202:205], v177 offset:6144
	ds_read_b128 v[206:209], v177 offset:7168
	buffer_load_dwordx4 v170, s[36:39], s6 offen lds
	s_mov_b32 m0, s56
	s_nop 0
	buffer_load_dwordx4 v172, s[36:39], s6 offen lds
	s_waitcnt vmcnt(8)
	s_waitcnt lgkmcnt(0)
	s_barrier
	s_setprio 1
	v_mfma_f32_16x16x128_f8f6f4 v[124:127], v[128:135], v[160:167], v[124:127]
	v_mfma_f32_16x16x128_f8f6f4 v[120:123], v[136:143], v[160:167], v[120:123]
	v_mfma_f32_16x16x128_f8f6f4 v[108:111], v[128:135], v[178:185], v[108:111]
	v_mfma_f32_16x16x128_f8f6f4 v[104:107], v[136:143], v[178:185], v[104:107]
	v_mfma_f32_16x16x128_f8f6f4 v[186:189], v[128:135], v[194:201], v[92:95]
	v_mfma_f32_16x16x128_f8f6f4 v[190:193], v[136:143], v[194:201], v[88:91]
	v_mfma_f32_16x16x128_f8f6f4 v[210:213], v[128:135], v[202:209], v[76:79]
	v_mfma_f32_16x16x128_f8f6f4 v[214:217], v[136:143], v[202:209], v[72:75]
	v_mfma_f32_16x16x128_f8f6f4 v[116:119], v[144:151], v[160:167], v[116:119]
	v_mfma_f32_16x16x128_f8f6f4 v[112:115], v[152:159], v[160:167], v[112:115]
	v_mfma_f32_16x16x128_f8f6f4 v[100:103], v[144:151], v[178:185], v[100:103]
	v_mfma_f32_16x16x128_f8f6f4 v[96:99], v[152:159], v[178:185], v[96:99]
	v_mfma_f32_16x16x128_f8f6f4 v[160:163], v[144:151], v[194:201], v[84:87]
	v_mfma_f32_16x16x128_f8f6f4 v[164:167], v[152:159], v[194:201], v[80:83]
	v_mfma_f32_16x16x128_f8f6f4 v[178:181], v[144:151], v[202:209], v[68:71]
	v_mfma_f32_16x16x128_f8f6f4 v[182:185], v[152:159], v[202:209], v[64:67]
	s_setprio 0
	s_barrier
; #define PG8_STAGE(bufoff, rs_, soff_, voff) do { _Pragma("unroll") for (int _i = 0; _i < 2; ++_i) \
;         __builtin_amdgcn_raw_ptr_buffer_load_lds(rs_, (LAS void*)(lds + (bufoff) + ldsw + _i * 8192), 16, (int)(voff)[_i], (int)(soff_), 0, 0); } while (0)
; #define PG8_LDA(dst, b, h) do { _Pragma("unroll") for (int m = 0; m < 4; ++m) dst[m] = PG8_LD2(lds + PG8_SA(b, h) + aoff + m * 2048); } while (0)
; #define PG8_LDB(dst, b, h) do { _Pragma("unroll") for (int n = 0; n < 2; ++n) dst[n] = PG8_LD2(lds + PG8_SB(b, h) + boff + n * 2048); } while (0)
; #define PG8_WAIT_V(n) asm volatile("s_waitcnt vmcnt(" #n ")" ::: "memory")
; #define PG8_WAIT_L(n) asm volatile("s_waitcnt lgkmcnt(" #n ")" ::: "memory")
; #define PG8_BAR __builtin_amdgcn_s_barrier()
; #define PG8_SCHED __builtin_amdgcn_sched_barrier(0)
; template <class Epi, class Sched, bool ALIGN_EPI = false, bool SP2 = false, bool FP8 = false>
; __device__ __forceinline__ void gemm_phase(LAS unsigned char* lds, const Gemm g, const Sched& S, const Epi& E, int wbase) {
;     ...
;             PG8_LDA(At, 0, 1); PG8_STAGE(PG8_SB(0, 0), rB2, b2, voffB); PG8_STAGE(PG8_SB(0, 1), rB2, b2 + hstep, voffB); PG8_STAGE(PG8_SA(0, 0), rA2, a2, voffA);
;             PG8_WAIT_V(8); PG8_WAIT_L(0); PG8_BAR; PG8_MMA(1, 0, At, B0); PG8_MMA(1, 1, At, B1); PG8_BAR; PG8_SCHED;
;             PG8_LDB(B0, 1, 0); PG8_LDB(B1, 1, 1); PG8_SCHED; PG8_LDA(At, 1, 0); PG8_STAGE(PG8_SA(0, 1), rA2, a2 + hstep, voffA);
;             PG8_WAIT_V(8); PG8_WAIT_L(0); PG8_BAR; PG8_MMA(0, 0, At, B0); PG8_MMA(0, 1, At, B1); PG8_BAR; PG8_SCHED;
;             PG8_LDA(At, 1, 1); PG8_STAGE(PG8_SB(1, 0), rB2, b3, voffB); PG8_STAGE(PG8_SB(1, 1), rB2, b3 + hstep, voffB); PG8_STAGE(PG8_SA(1, 0), rA2, a3, voffA);
;             PG8_WAIT_V(8); PG8_WAIT_L(0); PG8_BAR; PG8_MMA(1, 0, At, B0); PG8_MMA(1, 1, At, B1); PG8_BAR; PG8_SCHED;
	s_mov_b32 m0, s26
	s_mov_b32 s6, s38
	s_mov_b32 s7, s39
	s_nop 1
	buffer_load_dwordx4 v171, s[4:7], s55 offen lds
	s_mov_b32 m0, s27
	ds_read_b128 v[64:67], v177 offset:16384
	s_add_i32 s69, s55, s24
	buffer_load_dwordx4 v173, s[4:7], s55 offen lds
	s_mov_b32 m0, s28
	ds_read_b128 v[68:71], v177 offset:17408
	buffer_load_dwordx4 v171, s[4:7], s69 offen lds
	s_mov_b32 m0, s25
	ds_read_b128 v[72:75], v177 offset:18432
	buffer_load_dwordx4 v170, s[36:39], s68 offen lds
	s_mov_b32 m0, s30
	ds_read_b128 v[76:79], v177 offset:19456
	buffer_load_dwordx4 v172, s[36:39], s68 offen lds
	ds_read_b128 v[80:83], v177 offset:20480
	ds_read_b128 v[84:87], v177 offset:21504
	ds_read_b128 v[88:91], v177 offset:22528
	ds_read_b128 v[92:95], v177 offset:23552
	s_waitcnt vmcnt(7)
	s_waitcnt lgkmcnt(0)
	s_barrier
	s_setprio 1
	v_mfma_f32_16x16x128_f8f6f4 v[60:63], v[128:135], v[64:71], v[60:63]
	v_mfma_f32_16x16x128_f8f6f4 v[56:59], v[136:143], v[64:71], v[56:59]
	v_mfma_f32_16x16x128_f8f6f4 v[194:197], v[128:135], v[72:79], v[44:47]
	v_mfma_f32_16x16x128_f8f6f4 v[198:201], v[136:143], v[72:79], v[40:43]
	v_mfma_f32_16x16x128_f8f6f4 v[202:205], v[128:135], v[80:87], v[28:31]
	v_mfma_f32_16x16x128_f8f6f4 v[206:209], v[136:143], v[80:87], v[24:27]
	v_mfma_f32_16x16x128_f8f6f4 v[218:221], v[128:135], v[88:95], v[12:15]
	v_mfma_f32_16x16x128_f8f6f4 v[226:229], v[136:143], v[88:95], v[8:11]
	v_mfma_f32_16x16x128_f8f6f4 v[52:55], v[144:151], v[64:71], v[52:55]
	v_mfma_f32_16x16x128_f8f6f4 v[48:51], v[152:159], v[64:71], v[48:51]
	v_mfma_f32_16x16x128_f8f6f4 v[230:233], v[144:151], v[72:79], v[36:39]
	v_mfma_f32_16x16x128_f8f6f4 v[234:237], v[152:159], v[72:79], v[32:35]
	v_mfma_f32_16x16x128_f8f6f4 v[238:241], v[144:151], v[80:87], v[20:23]
	v_mfma_f32_16x16x128_f8f6f4 v[242:245], v[152:159], v[80:87], v[16:19]
	v_mfma_f32_16x16x128_f8f6f4 v[246:249], v[144:151], v[88:95], v[4:7]
	v_mfma_f32_16x16x128_f8f6f4 v[250:253], v[152:159], v[88:95], v[0:3]
	s_setprio 0
	s_barrier
	s_mov_b32 m0, s29
	s_nop 0
	buffer_load_dwordx4 v173, s[4:7], s69 offen lds
	v_add_u32_e32 v8, 0x18000, v176
	s_nop 3
	ds_read_b128 v[0:3], v8
	ds_read_b128 v[4:7], v8 offset:1024
	ds_read_b128 v[16:19], v8 offset:2048
	ds_read_b128 v[20:23], v8 offset:3072
	v_add_u32_e32 v8, 0x1c000, v176
	ds_read_b128 v[128:131], v8
	ds_read_b128 v[132:135], v8 offset:1024
	ds_read_b128 v[136:139], v8 offset:2048
	ds_read_b128 v[140:143], v8 offset:3072
	s_add_i32 s68, s68, s24
	s_mov_b32 m0, s31
	ds_read_b128 v[8:11], v177 offset:32768
	ds_read_b128 v[12:15], v177 offset:33792
	ds_read_b128 v[24:27], v177 offset:34816
	ds_read_b128 v[28:31], v177 offset:35840
	ds_read_b128 v[32:35], v177 offset:36864
	ds_read_b128 v[36:39], v177 offset:37888
	ds_read_b128 v[40:43], v177 offset:38912
	ds_read_b128 v[44:47], v177 offset:39936
	buffer_load_dwordx4 v170, s[36:39], s68 offen lds
	s_mov_b32 m0, s33
	s_nop 0
	buffer_load_dwordx4 v172, s[36:39], s68 offen lds
	s_waitcnt vmcnt(8)
	s_waitcnt lgkmcnt(0)
	s_barrier
	s_setprio 1
	v_mfma_f32_16x16x128_f8f6f4 v[124:127], v[0:7], v[8:15], v[124:127]
	v_mfma_f32_16x16x128_f8f6f4 v[120:123], v[16:23], v[8:15], v[120:123]
	v_mfma_f32_16x16x128_f8f6f4 v[108:111], v[0:7], v[24:31], v[108:111]
	v_mfma_f32_16x16x128_f8f6f4 v[104:107], v[16:23], v[24:31], v[104:107]
	v_mfma_f32_16x16x128_f8f6f4 v[92:95], v[0:7], v[32:39], v[186:189]
	v_mfma_f32_16x16x128_f8f6f4 v[88:91], v[16:23], v[32:39], v[190:193]
	v_mfma_f32_16x16x128_f8f6f4 v[76:79], v[0:7], v[40:47], v[210:213]
	v_mfma_f32_16x16x128_f8f6f4 v[72:75], v[16:23], v[40:47], v[214:217]
	v_mfma_f32_16x16x128_f8f6f4 v[116:119], v[128:135], v[8:15], v[116:119]
	v_mfma_f32_16x16x128_f8f6f4 v[112:115], v[136:143], v[8:15], v[112:115]
	v_mfma_f32_16x16x128_f8f6f4 v[100:103], v[128:135], v[24:31], v[100:103]
	v_mfma_f32_16x16x128_f8f6f4 v[96:99], v[136:143], v[24:31], v[96:99]
	v_mfma_f32_16x16x128_f8f6f4 v[84:87], v[128:135], v[32:39], v[160:163]
	v_mfma_f32_16x16x128_f8f6f4 v[80:83], v[136:143], v[32:39], v[164:167]
	v_mfma_f32_16x16x128_f8f6f4 v[68:71], v[128:135], v[40:47], v[178:181]
	v_mfma_f32_16x16x128_f8f6f4 v[64:67], v[136:143], v[40:47], v[182:185]
	s_setprio 0
	s_barrier
	s_mov_b32 m0, s34
	s_bitset1_b32 s55, 7
	buffer_load_dwordx4 v171, s[4:7], s55 offen lds
	s_mov_b32 m0, s35
	ds_read_b128 v[32:35], v177 offset:49152
	buffer_load_dwordx4 v173, s[4:7], s55 offen lds
	s_add_i32 s55, s55, s24
	s_mov_b32 m0, s43
	ds_read_b128 v[36:39], v177 offset:50176
	buffer_load_dwordx4 v171, s[4:7], s55 offen lds
	s_mov_b32 m0, s44
	ds_read_b128 v[144:147], v177 offset:51200
	buffer_load_dwordx4 v173, s[4:7], s55 offen lds
	s_mov_b32 m0, s41
	ds_read_b128 v[148:151], v177 offset:52224
	buffer_load_dwordx4 v170, s[36:39], s54 offen lds
	s_mov_b32 m0, s42
	ds_read_b128 v[152:155], v177 offset:53248
	buffer_load_dwordx4 v172, s[36:39], s54 offen lds
	ds_read_b128 v[156:159], v177 offset:54272
	ds_read_b128 v[160:163], v177 offset:55296
	ds_read_b128 v[164:167], v177 offset:56320
	s_waitcnt vmcnt(8)
	s_waitcnt lgkmcnt(0)
	s_barrier
	s_setprio 1
	v_mfma_f32_16x16x128_f8f6f4 v[60:63], v[0:7], v[32:39], v[60:63]
	v_mfma_f32_16x16x128_f8f6f4 v[56:59], v[16:23], v[32:39], v[56:59]
	v_mfma_f32_16x16x128_f8f6f4 v[44:47], v[0:7], v[144:151], v[194:197]
	v_mfma_f32_16x16x128_f8f6f4 v[40:43], v[16:23], v[144:151], v[198:201]
	v_mfma_f32_16x16x128_f8f6f4 v[28:31], v[0:7], v[152:159], v[202:205]
	v_mfma_f32_16x16x128_f8f6f4 v[24:27], v[16:23], v[152:159], v[206:209]
	v_mfma_f32_16x16x128_f8f6f4 v[12:15], v[0:7], v[160:167], v[218:221]
	v_mfma_f32_16x16x128_f8f6f4 v[8:11], v[16:23], v[160:167], v[226:229]
	v_mfma_f32_16x16x128_f8f6f4 v[52:55], v[128:135], v[32:39], v[52:55]
	v_mfma_f32_16x16x128_f8f6f4 v[48:51], v[136:143], v[32:39], v[48:51]
	v_mfma_f32_16x16x128_f8f6f4 v[36:39], v[128:135], v[144:151], v[230:233]
	v_mfma_f32_16x16x128_f8f6f4 v[32:35], v[136:143], v[144:151], v[234:237]
	v_mfma_f32_16x16x128_f8f6f4 v[20:23], v[128:135], v[152:159], v[238:241]
	v_mfma_f32_16x16x128_f8f6f4 v[16:19], v[136:143], v[152:159], v[242:245]
	v_mfma_f32_16x16x128_f8f6f4 v[4:7], v[128:135], v[160:167], v[246:249]
	v_mfma_f32_16x16x128_f8f6f4 v[0:3], v[136:143], v[160:167], v[250:253]
	s_setprio 0
	s_barrier
	s_add_i32 s67, s67, 2
	s_addk_i32 s65, 0x100
	s_addk_i32 s66, 0x100
	s_cmp_ge_i32 s67, s47
	s_cbranch_scc0 .LBB0_1854

;     __device__ __forceinline__ unsigned a_off(const Unit& u, const Gemm& g) const { return (unsigned)u.pm * (unsigned)(BM * 2) * (unsigned)g.K; }
;     __device__ __forceinline__ unsigned b_off(const Unit& u, const Gemm& g) const { return (unsigned)u.pn * (unsigned)(BM * 2) * (unsigned)g.K; }
;     __device__ __forceinline__ bool next(int i, Unit& u) const { return so.next(i, u); }
;     __device__ __forceinline__ unsigned a_off(const Unit& u, const Gemm& g) const { return (unsigned)u.pm * (unsigned)(BM * 2) * (unsigned)g.K; }
;     __device__ __forceinline__ bool next(int i, Unit& u) const { const bool ok = so.next(i >> 1, u); u.part = i & 1; return ok; }
; template <class Epi, class Sched, bool ALIGN_EPI = false, bool SP2 = false, bool FP8 = false>
; __device__ __forceinline__ void gemm_phase(LAS unsigned char* lds, const Gemm g, const Sched& S, const Epi& E, int wbase) {
;     ...
;         const bool has_next = S.next(ui + 1, nxt);
;         const unsigned nA = has_next ? S.a_off(nxt, g) : cA, nB = has_next ? S.b_off(nxt, g) : cB;
;         const rsrc_t rAn = (Sched::TWO && has_next) ? (nxt.part ? rA1 : rA0) : rAc, rBn = (Sched::TWO && has_next) ? (nxt.part ? rB1 : rB0) : rBc;
;         float pre_[8] = {0.f, 0.f, 0.f, 0.f, 0.f, 0.f, 0.f, 0.f};
;         if constexpr (Epi::HAS_PRE) E.pre_load(pre_, cur, wr);
;         for (int t = 0; t < nt; t += 2) {
;             const bool last = (t == nt - 2);
;             const unsigned a1 = cA + (unsigned)(t + 1) * kstep;
;             const unsigned a2 = last ? nA : cA + (unsigned)(t + 2) * kstep, b2 = last ? nB : cB + (unsigned)(t + 2) * kstep; const rsrc_t rA2 = (Sched::TWO && last) ? rAn : rAc, rB2 = (Sched::TWO && last) ? rBn : rBc;
;             const unsigned a3 = a2 + kstep, b3 = b2 + kstep;
;             if (last && has_next) S.a_ready(nxt);
;             if constexpr (SP2) {
;             PG8_LDB(B0, 0, 0); PG8_LDB(B1, 0, 1); PG8_SCHED; PG8_LDA(At, 0, 0); PG8_STAGE(PG8_SA(1, 1), rAc, a1 + hstep, voffA);
;             PG8_WAIT_V(8); PG8_WAIT_L(0); PG8_BAR; PG8_MMA(0, 0, At, B0); PG8_MMA(0, 1, At, B1); PG8_BAR; PG8_SCHED;
;             PG8_LDA(At, 0, 1); PG8_STAGE(PG8_SB(0, 0), rB2, b2, voffB); PG8_STAGE(PG8_SB(0, 1), rB2, b2 + hstep, voffB); PG8_STAGE(PG8_SA(0, 0), rA2, a2, voffA);
;             PG8_WAIT_V(8); PG8_WAIT_L(0); PG8_BAR; PG8_MMA(1, 0, At, B0); PG8_MMA(1, 1, At, B1); PG8_BAR; PG8_SCHED;
.LBB0_1942:
	s_mov_b32 s68, s94
	s_lshl_b32 s85, s84, 19
	s_andn2_b64 vcc, exec, s[22:23]
	s_lshl_b32 s94, s83, 19
	s_cbranch_vccnz .LBB0_1966
	s_and_b64 s[6:7], s[26:27], exec
	s_waitcnt vmcnt(37)
	s_waitcnt vmcnt(36)
	s_waitcnt vmcnt(35)
	s_waitcnt vmcnt(32)
	s_waitcnt vmcnt(31)
	s_waitcnt vmcnt(28)
	s_waitcnt vmcnt(27)
	s_waitcnt vmcnt(24)
	s_waitcnt vmcnt(23)
	s_cselect_b32 s29, s85, s55
	s_cselect_b32 s60, s94, s54
	s_add_i32 s61, s55, 0x80
	s_add_i32 s62, s54, 0x100
	s_mov_b32 s63, 0
	s_waitcnt vmcnt(0)
	v_add_u32_e32 v136, 0x10000, v174
	v_add_u32_e32 v156, 0x14000, v174
	ds_read_b128 v[120:123], v136
	ds_read_b128 v[124:127], v136 offset:1024
	ds_read_b128 v[132:135], v136 offset:2048
	ds_read_b128 v[136:139], v136 offset:3072
	ds_read_b128 v[144:147], v156
	ds_read_b128 v[148:151], v156 offset:1024
	ds_read_b128 v[152:155], v156 offset:2048
	ds_read_b128 v[156:159], v156 offset:3072
	s_add_i32 s6, s61, 0x80
	s_cmp_eq_u32 s77, s63
	s_cselect_b32 s66, s29, s6
	s_cselect_b32 s55, s60, s62
	s_or_b32 s54, s66, 0x80
	s_add_i32 s6, s33, s61
	s_mov_b32 m0, s79
	ds_read_b128 v[160:163], v175
	ds_read_b128 v[164:167], v175 offset:1024
	ds_read_b128 v[176:179], v175 offset:2048
	ds_read_b128 v[180:183], v175 offset:3072
	ds_read_b128 v[184:187], v175 offset:4096
	ds_read_b128 v[188:191], v175 offset:5120
	ds_read_b128 v[192:195], v175 offset:6144
	ds_read_b128 v[196:199], v175 offset:7168
	buffer_load_dwordx4 v168, s[36:39], s6 offen lds
	s_mov_b32 m0, s82
	s_nop 0
	buffer_load_dwordx4 v170, s[36:39], s6 offen lds
	s_waitcnt vmcnt(8)
	s_waitcnt lgkmcnt(0)
	s_barrier
	s_setprio 1
	v_mfma_f32_16x16x32_bf16 v[140:143], v[120:123], v[160:163], 0
	v_mfma_f32_16x16x32_bf16 v[128:131], v[132:135], v[160:163], 0
	v_mfma_f32_16x16x32_bf16 v[108:111], v[120:123], v[176:179], 0
	v_mfma_f32_16x16x32_bf16 v[104:107], v[132:135], v[176:179], 0
	v_mfma_f32_16x16x32_bf16 v[92:95], v[120:123], v[184:187], 0
	v_mfma_f32_16x16x32_bf16 v[88:91], v[132:135], v[184:187], 0
	v_mfma_f32_16x16x32_bf16 v[76:79], v[120:123], v[192:195], 0
	v_mfma_f32_16x16x32_bf16 v[72:75], v[132:135], v[192:195], 0
	v_mfma_f32_16x16x32_bf16 v[140:143], v[124:127], v[164:167], v[140:143]
	v_mfma_f32_16x16x32_bf16 v[128:131], v[136:139], v[164:167], v[128:131]
	v_mfma_f32_16x16x32_bf16 v[108:111], v[124:127], v[180:183], v[108:111]
	v_mfma_f32_16x16x32_bf16 v[104:107], v[136:139], v[180:183], v[104:107]
	v_mfma_f32_16x16x32_bf16 v[92:95], v[124:127], v[188:191], v[92:95]
	v_mfma_f32_16x16x32_bf16 v[88:91], v[136:139], v[188:191], v[88:91]
	v_mfma_f32_16x16x32_bf16 v[76:79], v[124:127], v[196:199], v[76:79]
	v_mfma_f32_16x16x32_bf16 v[72:75], v[136:139], v[196:199], v[72:75]
	v_mfma_f32_16x16x32_bf16 v[116:119], v[144:147], v[160:163], 0
	v_mfma_f32_16x16x32_bf16 v[112:115], v[152:155], v[160:163], 0
	v_mfma_f32_16x16x32_bf16 v[100:103], v[144:147], v[176:179], 0
	v_mfma_f32_16x16x32_bf16 v[96:99], v[152:155], v[176:179], 0
	v_mfma_f32_16x16x32_bf16 v[84:87], v[144:147], v[184:187], 0
	v_mfma_f32_16x16x32_bf16 v[80:83], v[152:155], v[184:187], 0
	v_mfma_f32_16x16x32_bf16 v[68:71], v[144:147], v[192:195], 0
	v_mfma_f32_16x16x32_bf16 v[64:67], v[152:155], v[192:195], 0
	v_mfma_f32_16x16x32_bf16 v[116:119], v[148:151], v[164:167], v[116:119]
	v_mfma_f32_16x16x32_bf16 v[112:115], v[156:159], v[164:167], v[112:115]
	v_mfma_f32_16x16x32_bf16 v[100:103], v[148:151], v[180:183], v[100:103]
	v_mfma_f32_16x16x32_bf16 v[96:99], v[156:159], v[180:183], v[96:99]
	v_mfma_f32_16x16x32_bf16 v[84:87], v[148:151], v[188:191], v[84:87]
	v_mfma_f32_16x16x32_bf16 v[80:83], v[156:159], v[188:191], v[80:83]
	v_mfma_f32_16x16x32_bf16 v[68:71], v[148:151], v[196:199], v[68:71]
	v_mfma_f32_16x16x32_bf16 v[64:67], v[156:159], v[196:199], v[64:67]
	s_setprio 0
	s_barrier
	s_mov_b32 m0, s35
	s_mov_b32 s6, s38
	s_mov_b32 s7, s39
	buffer_load_dwordx4 v169, s[4:7], s55 offen lds
	s_mov_b32 m0, s41
	ds_read_b128 v[160:163], v175 offset:16384
	s_add_i32 s67, s55, s33
	buffer_load_dwordx4 v171, s[4:7], s55 offen lds
	s_mov_b32 m0, s42
	ds_read_b128 v[164:167], v175 offset:17408
	buffer_load_dwordx4 v169, s[4:7], s67 offen lds
	s_mov_b32 m0, s34
	ds_read_b128 v[176:179], v175 offset:18432
	buffer_load_dwordx4 v168, s[36:39], s66 offen lds
	s_mov_b32 m0, s44
	ds_read_b128 v[180:183], v175 offset:19456
	buffer_load_dwordx4 v170, s[36:39], s66 offen lds
	ds_read_b128 v[184:187], v175 offset:20480
	ds_read_b128 v[188:191], v175 offset:21504
	ds_read_b128 v[192:195], v175 offset:22528
	ds_read_b128 v[196:199], v175 offset:23552
	s_waitcnt vmcnt(7)
	s_waitcnt lgkmcnt(0)
	s_barrier
	s_setprio 1
	v_mfma_f32_16x16x32_bf16 v[60:63], v[120:123], v[160:163], 0
	v_mfma_f32_16x16x32_bf16 v[56:59], v[132:135], v[160:163], 0
	v_mfma_f32_16x16x32_bf16 v[44:47], v[120:123], v[176:179], 0
	v_mfma_f32_16x16x32_bf16 v[40:43], v[132:135], v[176:179], 0
	v_mfma_f32_16x16x32_bf16 v[28:31], v[120:123], v[184:187], 0
	v_mfma_f32_16x16x32_bf16 v[24:27], v[132:135], v[184:187], 0
	v_mfma_f32_16x16x32_bf16 v[12:15], v[120:123], v[192:195], 0
	v_mfma_f32_16x16x32_bf16 v[8:11], v[132:135], v[192:195], 0
	v_mfma_f32_16x16x32_bf16 v[60:63], v[124:127], v[164:167], v[60:63]
	v_mfma_f32_16x16x32_bf16 v[56:59], v[136:139], v[164:167], v[56:59]
	v_mfma_f32_16x16x32_bf16 v[44:47], v[124:127], v[180:183], v[44:47]
	v_mfma_f32_16x16x32_bf16 v[40:43], v[136:139], v[180:183], v[40:43]
	v_mfma_f32_16x16x32_bf16 v[28:31], v[124:127], v[188:191], v[28:31]
	v_mfma_f32_16x16x32_bf16 v[24:27], v[136:139], v[188:191], v[24:27]
	v_mfma_f32_16x16x32_bf16 v[12:15], v[124:127], v[196:199], v[12:15]
	v_mfma_f32_16x16x32_bf16 v[8:11], v[136:139], v[196:199], v[8:11]
	v_mfma_f32_16x16x32_bf16 v[52:55], v[144:147], v[160:163], 0
	v_mfma_f32_16x16x32_bf16 v[48:51], v[152:155], v[160:163], 0
	v_mfma_f32_16x16x32_bf16 v[36:39], v[144:147], v[176:179], 0
	v_mfma_f32_16x16x32_bf16 v[32:35], v[152:155], v[176:179], 0
	v_mfma_f32_16x16x32_bf16 v[20:23], v[144:147], v[184:187], 0
	v_mfma_f32_16x16x32_bf16 v[16:19], v[152:155], v[184:187], 0
	v_mfma_f32_16x16x32_bf16 v[4:7], v[144:147], v[192:195], 0
	v_mfma_f32_16x16x32_bf16 v[0:3], v[152:155], v[192:195], 0
	v_mfma_f32_16x16x32_bf16 v[52:55], v[148:151], v[164:167], v[52:55]
	v_mfma_f32_16x16x32_bf16 v[48:51], v[156:159], v[164:167], v[48:51]
	v_mfma_f32_16x16x32_bf16 v[36:39], v[148:151], v[180:183], v[36:39]
	v_mfma_f32_16x16x32_bf16 v[32:35], v[156:159], v[180:183], v[32:35]
	v_mfma_f32_16x16x32_bf16 v[20:23], v[148:151], v[188:191], v[20:23]
	v_mfma_f32_16x16x32_bf16 v[16:19], v[156:159], v[188:191], v[16:19]
	v_mfma_f32_16x16x32_bf16 v[4:7], v[148:151], v[196:199], v[4:7]
	v_mfma_f32_16x16x32_bf16 v[0:3], v[156:159], v[196:199], v[0:3]
	s_setprio 0
	s_barrier
; #define PG8_STAGE(bufoff, rs_, soff_, voff) do { _Pragma("unroll") for (int _i = 0; _i < 2; ++_i) \
;         __builtin_amdgcn_raw_ptr_buffer_load_lds(rs_, (LAS void*)(lds + (bufoff) + ldsw + _i * 8192), 16, (int)(voff)[_i], (int)(soff_), 0, 0); } while (0)
; #define PG8_LDA(dst, b, h) do { _Pragma("unroll") for (int m = 0; m < 4; ++m) dst[m] = PG8_LD2(lds + PG8_SA(b, h) + aoff + m * 2048); } while (0)
; #define PG8_LDB(dst, b, h) do { _Pragma("unroll") for (int n = 0; n < 2; ++n) dst[n] = PG8_LD2(lds + PG8_SB(b, h) + boff + n * 2048); } while (0)
; #define PG8_WAIT_V(n) asm volatile("s_waitcnt vmcnt(" #n ")" ::: "memory")
; #define PG8_WAIT_L(n) asm volatile("s_waitcnt lgkmcnt(" #n ")" ::: "memory")
; #define PG8_BAR __builtin_amdgcn_s_barrier()
; #define PG8_SCHED __builtin_amdgcn_sched_barrier(0)
; template <class Epi, class Sched, bool ALIGN_EPI = false, bool SP2 = false, bool FP8 = false>
; __device__ __forceinline__ void gemm_phase(LAS unsigned char* lds, const Gemm g, const Sched& S, const Epi& E, int wbase) {
;     ...
;             PG8_LDB(B0, 1, 0); PG8_LDB(B1, 1, 1); PG8_SCHED; PG8_LDA(At, 1, 0); PG8_STAGE(PG8_SA(0, 1), rA2, a2 + hstep, voffA);
;             PG8_WAIT_V(8); PG8_WAIT_L(0); PG8_BAR; PG8_MMA(0, 0, At, B0); PG8_MMA(0, 1, At, B1); PG8_BAR; PG8_SCHED;
;             PG8_LDA(At, 1, 1); PG8_STAGE(PG8_SB(1, 0), rB2, b3, voffB); PG8_STAGE(PG8_SB(1, 1), rB2, b3 + hstep, voffB); PG8_STAGE(PG8_SA(1, 0), rA2, a3, voffA);
;             PG8_WAIT_V(8); PG8_WAIT_L(0); PG8_BAR; PG8_MMA(1, 0, At, B0); PG8_MMA(1, 1, At, B1); PG8_BAR; PG8_SCHED;
	s_mov_b32 m0, s43
	s_nop 0
	buffer_load_dwordx4 v171, s[4:7], s67 offen lds
	v_add_u32_e32 v136, 0x18000, v174
	v_add_u32_e32 v156, 0x1c000, v174
	ds_read_b128 v[120:123], v136
	ds_read_b128 v[124:127], v136 offset:1024
	ds_read_b128 v[132:135], v136 offset:2048
	ds_read_b128 v[136:139], v136 offset:3072
	ds_read_b128 v[144:147], v156
	ds_read_b128 v[148:151], v156 offset:1024
	ds_read_b128 v[152:155], v156 offset:2048
	ds_read_b128 v[156:159], v156 offset:3072
	s_add_i32 s66, s66, s33
	s_mov_b32 m0, s45
	ds_read_b128 v[160:163], v175 offset:32768
	ds_read_b128 v[164:167], v175 offset:33792
	ds_read_b128 v[176:179], v175 offset:34816
	ds_read_b128 v[180:183], v175 offset:35840
	ds_read_b128 v[184:187], v175 offset:36864
	ds_read_b128 v[188:191], v175 offset:37888
	ds_read_b128 v[192:195], v175 offset:38912
	ds_read_b128 v[196:199], v175 offset:39936
	buffer_load_dwordx4 v168, s[36:39], s66 offen lds
	s_mov_b32 m0, s46
	s_nop 0
	buffer_load_dwordx4 v170, s[36:39], s66 offen lds
	s_waitcnt vmcnt(8)
	s_waitcnt lgkmcnt(0)
	s_barrier
	s_setprio 1
	v_mfma_f32_16x16x32_bf16 v[140:143], v[120:123], v[160:163], v[140:143]
	v_mfma_f32_16x16x32_bf16 v[128:131], v[132:135], v[160:163], v[128:131]
	v_mfma_f32_16x16x32_bf16 v[108:111], v[120:123], v[176:179], v[108:111]
	v_mfma_f32_16x16x32_bf16 v[104:107], v[132:135], v[176:179], v[104:107]
	v_mfma_f32_16x16x32_bf16 v[92:95], v[120:123], v[184:187], v[92:95]
	v_mfma_f32_16x16x32_bf16 v[88:91], v[132:135], v[184:187], v[88:91]
	v_mfma_f32_16x16x32_bf16 v[76:79], v[120:123], v[192:195], v[76:79]
	v_mfma_f32_16x16x32_bf16 v[72:75], v[132:135], v[192:195], v[72:75]
	v_mfma_f32_16x16x32_bf16 v[140:143], v[124:127], v[164:167], v[140:143]
	v_mfma_f32_16x16x32_bf16 v[128:131], v[136:139], v[164:167], v[128:131]
	v_mfma_f32_16x16x32_bf16 v[108:111], v[124:127], v[180:183], v[108:111]
	v_mfma_f32_16x16x32_bf16 v[104:107], v[136:139], v[180:183], v[104:107]
	v_mfma_f32_16x16x32_bf16 v[92:95], v[124:127], v[188:191], v[92:95]
	v_mfma_f32_16x16x32_bf16 v[88:91], v[136:139], v[188:191], v[88:91]
	v_mfma_f32_16x16x32_bf16 v[76:79], v[124:127], v[196:199], v[76:79]
	v_mfma_f32_16x16x32_bf16 v[72:75], v[136:139], v[196:199], v[72:75]
	v_mfma_f32_16x16x32_bf16 v[116:119], v[144:147], v[160:163], v[116:119]
	v_mfma_f32_16x16x32_bf16 v[112:115], v[152:155], v[160:163], v[112:115]
	v_mfma_f32_16x16x32_bf16 v[100:103], v[144:147], v[176:179], v[100:103]
	v_mfma_f32_16x16x32_bf16 v[96:99], v[152:155], v[176:179], v[96:99]
	v_mfma_f32_16x16x32_bf16 v[84:87], v[144:147], v[184:187], v[84:87]
	v_mfma_f32_16x16x32_bf16 v[80:83], v[152:155], v[184:187], v[80:83]
	v_mfma_f32_16x16x32_bf16 v[68:71], v[144:147], v[192:195], v[68:71]
	v_mfma_f32_16x16x32_bf16 v[64:67], v[152:155], v[192:195], v[64:67]
	v_mfma_f32_16x16x32_bf16 v[116:119], v[148:151], v[164:167], v[116:119]
	v_mfma_f32_16x16x32_bf16 v[112:115], v[156:159], v[164:167], v[112:115]
	v_mfma_f32_16x16x32_bf16 v[100:103], v[148:151], v[180:183], v[100:103]
	v_mfma_f32_16x16x32_bf16 v[96:99], v[156:159], v[180:183], v[96:99]
	v_mfma_f32_16x16x32_bf16 v[84:87], v[148:151], v[188:191], v[84:87]
	v_mfma_f32_16x16x32_bf16 v[80:83], v[156:159], v[188:191], v[80:83]
	v_mfma_f32_16x16x32_bf16 v[68:71], v[148:151], v[196:199], v[68:71]
	v_mfma_f32_16x16x32_bf16 v[64:67], v[156:159], v[196:199], v[64:67]
	s_setprio 0
	s_barrier
	s_mov_b32 m0, s47
	s_bitset1_b32 s55, 7
	buffer_load_dwordx4 v169, s[4:7], s55 offen lds
	s_mov_b32 m0, s48
	ds_read_b128 v[160:163], v175 offset:49152
	buffer_load_dwordx4 v171, s[4:7], s55 offen lds
	s_add_i32 s55, s55, s33
	s_mov_b32 m0, s56
	ds_read_b128 v[164:167], v175 offset:50176
	buffer_load_dwordx4 v169, s[4:7], s55 offen lds
	s_mov_b32 m0, s57
	ds_read_b128 v[176:179], v175 offset:51200
	buffer_load_dwordx4 v171, s[4:7], s55 offen lds
	s_mov_b32 m0, s52
	ds_read_b128 v[180:183], v175 offset:52224
	buffer_load_dwordx4 v168, s[36:39], s54 offen lds
	s_mov_b32 m0, s53
	ds_read_b128 v[184:187], v175 offset:53248
	buffer_load_dwordx4 v170, s[36:39], s54 offen lds
	ds_read_b128 v[188:191], v175 offset:54272
	ds_read_b128 v[192:195], v175 offset:55296
	ds_read_b128 v[196:199], v175 offset:56320
	s_waitcnt vmcnt(8)
	s_waitcnt lgkmcnt(0)
	s_barrier
	s_setprio 1
	v_mfma_f32_16x16x32_bf16 v[60:63], v[120:123], v[160:163], v[60:63]
	v_mfma_f32_16x16x32_bf16 v[56:59], v[132:135], v[160:163], v[56:59]
	v_mfma_f32_16x16x32_bf16 v[44:47], v[120:123], v[176:179], v[44:47]
	v_mfma_f32_16x16x32_bf16 v[40:43], v[132:135], v[176:179], v[40:43]
	v_mfma_f32_16x16x32_bf16 v[28:31], v[120:123], v[184:187], v[28:31]
	v_mfma_f32_16x16x32_bf16 v[24:27], v[132:135], v[184:187], v[24:27]
	v_mfma_f32_16x16x32_bf16 v[12:15], v[120:123], v[192:195], v[12:15]
	v_mfma_f32_16x16x32_bf16 v[8:11], v[132:135], v[192:195], v[8:11]
	v_mfma_f32_16x16x32_bf16 v[60:63], v[124:127], v[164:167], v[60:63]
	v_mfma_f32_16x16x32_bf16 v[56:59], v[136:139], v[164:167], v[56:59]
	v_mfma_f32_16x16x32_bf16 v[44:47], v[124:127], v[180:183], v[44:47]
	v_mfma_f32_16x16x32_bf16 v[40:43], v[136:139], v[180:183], v[40:43]
	v_mfma_f32_16x16x32_bf16 v[28:31], v[124:127], v[188:191], v[28:31]
	v_mfma_f32_16x16x32_bf16 v[24:27], v[136:139], v[188:191], v[24:27]
	v_mfma_f32_16x16x32_bf16 v[12:15], v[124:127], v[196:199], v[12:15]
	v_mfma_f32_16x16x32_bf16 v[8:11], v[136:139], v[196:199], v[8:11]
	v_mfma_f32_16x16x32_bf16 v[52:55], v[144:147], v[160:163], v[52:55]
	v_mfma_f32_16x16x32_bf16 v[48:51], v[152:155], v[160:163], v[48:51]
	v_mfma_f32_16x16x32_bf16 v[36:39], v[144:147], v[176:179], v[36:39]
	v_mfma_f32_16x16x32_bf16 v[32:35], v[152:155], v[176:179], v[32:35]
	v_mfma_f32_16x16x32_bf16 v[20:23], v[144:147], v[184:187], v[20:23]
	v_mfma_f32_16x16x32_bf16 v[16:19], v[152:155], v[184:187], v[16:19]
	v_mfma_f32_16x16x32_bf16 v[4:7], v[144:147], v[192:195], v[4:7]
	v_mfma_f32_16x16x32_bf16 v[0:3], v[152:155], v[192:195], v[0:3]
	v_mfma_f32_16x16x32_bf16 v[52:55], v[148:151], v[164:167], v[52:55]
	v_mfma_f32_16x16x32_bf16 v[48:51], v[156:159], v[164:167], v[48:51]
	v_mfma_f32_16x16x32_bf16 v[36:39], v[148:151], v[180:183], v[36:39]
	v_mfma_f32_16x16x32_bf16 v[32:35], v[156:159], v[180:183], v[32:35]
	v_mfma_f32_16x16x32_bf16 v[20:23], v[148:151], v[188:191], v[20:23]
	v_mfma_f32_16x16x32_bf16 v[16:19], v[156:159], v[188:191], v[16:19]
	v_mfma_f32_16x16x32_bf16 v[4:7], v[148:151], v[196:199], v[4:7]
	v_mfma_f32_16x16x32_bf16 v[0:3], v[156:159], v[196:199], v[0:3]
	s_setprio 0
	s_barrier
	s_add_i32 s63, s63, 2
	s_addk_i32 s61, 0x100
	s_addk_i32 s62, 0x100
	s_cmp_ge_i32 s63, s65
	s_cbranch_scc0 .LBB0_1944
	s_branch .Lzp_after_1944
; #define PG8_STAGE(bufoff, rs_, soff_, voff) do { _Pragma("unroll") for (int _i = 0; _i < 2; ++_i) \
;         __builtin_amdgcn_raw_ptr_buffer_load_lds(rs_, (LAS void*)(lds + (bufoff) + ldsw + _i * 8192), 16, (int)(voff)[_i], (int)(soff_), 0, 0); } while (0)
; #define PG8_LDA(dst, b, h) do { _Pragma("unroll") for (int m = 0; m < 4; ++m) dst[m] = PG8_LD2(lds + PG8_SA(b, h) + aoff + m * 2048); } while (0)
; #define PG8_LDB(dst, b, h) do { _Pragma("unroll") for (int n = 0; n < 2; ++n) dst[n] = PG8_LD2(lds + PG8_SB(b, h) + boff + n * 2048); } while (0)
; #define PG8_WAIT_V(n) asm volatile("s_waitcnt vmcnt(" #n ")" ::: "memory")
; #define PG8_WAIT_L(n) asm volatile("s_waitcnt lgkmcnt(" #n ")" ::: "memory")
; #define PG8_BAR __builtin_amdgcn_s_barrier()
; #define PG8_SCHED __builtin_amdgcn_sched_barrier(0)
; template <class Epi, class Sched, bool ALIGN_EPI = false, bool SP2 = false, bool FP8 = false>
; __device__ __forceinline__ void gemm_phase(LAS unsigned char* lds, const Gemm g, const Sched& S, const Epi& E, int wbase) {
;     ...
;         for (int t = 0; t < nt; t += 2) {
;             const bool last = (t == nt - 2);
;             const unsigned a1 = cA + (unsigned)(t + 1) * kstep;
;             const unsigned a2 = last ? nA : cA + (unsigned)(t + 2) * kstep, b2 = last ? nB : cB + (unsigned)(t + 2) * kstep; const rsrc_t rA2 = (Sched::TWO && last) ? rAn : rAc, rB2 = (Sched::TWO && last) ? rBn : rBc;
;             const unsigned a3 = a2 + kstep, b3 = b2 + kstep;
;             if (last && has_next) S.a_ready(nxt);
;             if constexpr (SP2) {
;             PG8_LDB(B0, 0, 0); PG8_LDB(B1, 0, 1); PG8_SCHED; PG8_LDA(At, 0, 0); PG8_STAGE(PG8_SA(1, 1), rAc, a1 + hstep, voffA);
;             PG8_WAIT_V(8); PG8_WAIT_L(0); PG8_BAR; PG8_MMA(0, 0, At, B0); PG8_MMA(0, 1, At, B1); PG8_BAR; PG8_SCHED;
;             PG8_LDA(At, 0, 1); PG8_STAGE(PG8_SB(0, 0), rB2, b2, voffB); PG8_STAGE(PG8_SB(0, 1), rB2, b2 + hstep, voffB); PG8_STAGE(PG8_SA(0, 0), rA2, a2, voffA);
;             PG8_WAIT_V(8); PG8_WAIT_L(0); PG8_BAR; PG8_MMA(1, 0, At, B0); PG8_MMA(1, 1, At, B1); PG8_BAR; PG8_SCHED;
.LBB0_1944:
	v_add_u32_e32 v136, 0x10000, v174
	v_add_u32_e32 v156, 0x14000, v174
	ds_read_b128 v[120:123], v136
	ds_read_b128 v[124:127], v136 offset:1024
	ds_read_b128 v[132:135], v136 offset:2048
	ds_read_b128 v[136:139], v136 offset:3072
	ds_read_b128 v[144:147], v156
	ds_read_b128 v[148:151], v156 offset:1024
	ds_read_b128 v[152:155], v156 offset:2048
	ds_read_b128 v[156:159], v156 offset:3072
	s_add_i32 s6, s61, 0x80
	s_cmp_eq_u32 s77, s63
	s_cselect_b32 s66, s29, s6
	s_cselect_b32 s55, s60, s62
	s_or_b32 s54, s66, 0x80
	s_add_i32 s6, s33, s61
	s_mov_b32 m0, s79
	ds_read_b128 v[160:163], v175
	ds_read_b128 v[164:167], v175 offset:1024
	ds_read_b128 v[176:179], v175 offset:2048
	ds_read_b128 v[180:183], v175 offset:3072
	ds_read_b128 v[184:187], v175 offset:4096
	ds_read_b128 v[188:191], v175 offset:5120
	ds_read_b128 v[192:195], v175 offset:6144
	ds_read_b128 v[196:199], v175 offset:7168
	buffer_load_dwordx4 v168, s[36:39], s6 offen lds
	s_mov_b32 m0, s82
	s_nop 0
	buffer_load_dwordx4 v170, s[36:39], s6 offen lds
	s_waitcnt vmcnt(8)
	s_waitcnt lgkmcnt(0)
	s_barrier
	s_setprio 1
	v_mfma_f32_16x16x32_bf16 v[140:143], v[120:123], v[160:163], v[140:143]
	v_mfma_f32_16x16x32_bf16 v[128:131], v[132:135], v[160:163], v[128:131]
	v_mfma_f32_16x16x32_bf16 v[108:111], v[120:123], v[176:179], v[108:111]
	v_mfma_f32_16x16x32_bf16 v[104:107], v[132:135], v[176:179], v[104:107]
	v_mfma_f32_16x16x32_bf16 v[92:95], v[120:123], v[184:187], v[92:95]
	v_mfma_f32_16x16x32_bf16 v[88:91], v[132:135], v[184:187], v[88:91]
	v_mfma_f32_16x16x32_bf16 v[76:79], v[120:123], v[192:195], v[76:79]
	v_mfma_f32_16x16x32_bf16 v[72:75], v[132:135], v[192:195], v[72:75]
	v_mfma_f32_16x16x32_bf16 v[140:143], v[124:127], v[164:167], v[140:143]
	v_mfma_f32_16x16x32_bf16 v[128:131], v[136:139], v[164:167], v[128:131]
	v_mfma_f32_16x16x32_bf16 v[108:111], v[124:127], v[180:183], v[108:111]
	v_mfma_f32_16x16x32_bf16 v[104:107], v[136:139], v[180:183], v[104:107]
	v_mfma_f32_16x16x32_bf16 v[92:95], v[124:127], v[188:191], v[92:95]
	v_mfma_f32_16x16x32_bf16 v[88:91], v[136:139], v[188:191], v[88:91]
	v_mfma_f32_16x16x32_bf16 v[76:79], v[124:127], v[196:199], v[76:79]
	v_mfma_f32_16x16x32_bf16 v[72:75], v[136:139], v[196:199], v[72:75]
	v_mfma_f32_16x16x32_bf16 v[116:119], v[144:147], v[160:163], v[116:119]
	v_mfma_f32_16x16x32_bf16 v[112:115], v[152:155], v[160:163], v[112:115]
	v_mfma_f32_16x16x32_bf16 v[100:103], v[144:147], v[176:179], v[100:103]
	v_mfma_f32_16x16x32_bf16 v[96:99], v[152:155], v[176:179], v[96:99]
	v_mfma_f32_16x16x32_bf16 v[84:87], v[144:147], v[184:187], v[84:87]
	v_mfma_f32_16x16x32_bf16 v[80:83], v[152:155], v[184:187], v[80:83]
	v_mfma_f32_16x16x32_bf16 v[68:71], v[144:147], v[192:195], v[68:71]
	v_mfma_f32_16x16x32_bf16 v[64:67], v[152:155], v[192:195], v[64:67]
	v_mfma_f32_16x16x32_bf16 v[116:119], v[148:151], v[164:167], v[116:119]
	v_mfma_f32_16x16x32_bf16 v[112:115], v[156:159], v[164:167], v[112:115]
	v_mfma_f32_16x16x32_bf16 v[100:103], v[148:151], v[180:183], v[100:103]
	v_mfma_f32_16x16x32_bf16 v[96:99], v[156:159], v[180:183], v[96:99]
	v_mfma_f32_16x16x32_bf16 v[84:87], v[148:151], v[188:191], v[84:87]
	v_mfma_f32_16x16x32_bf16 v[80:83], v[156:159], v[188:191], v[80:83]
	v_mfma_f32_16x16x32_bf16 v[68:71], v[148:151], v[196:199], v[68:71]
	v_mfma_f32_16x16x32_bf16 v[64:67], v[156:159], v[196:199], v[64:67]
	s_setprio 0
	s_barrier
	s_mov_b32 m0, s35
	s_mov_b32 s6, s38
	s_mov_b32 s7, s39
	buffer_load_dwordx4 v169, s[4:7], s55 offen lds
	s_mov_b32 m0, s41
	ds_read_b128 v[160:163], v175 offset:16384
	s_add_i32 s67, s55, s33
	buffer_load_dwordx4 v171, s[4:7], s55 offen lds
	s_mov_b32 m0, s42
	ds_read_b128 v[164:167], v175 offset:17408
	buffer_load_dwordx4 v169, s[4:7], s67 offen lds
	s_mov_b32 m0, s34
	ds_read_b128 v[176:179], v175 offset:18432
	buffer_load_dwordx4 v168, s[36:39], s66 offen lds
	s_mov_b32 m0, s44
	ds_read_b128 v[180:183], v175 offset:19456
	buffer_load_dwordx4 v170, s[36:39], s66 offen lds
	ds_read_b128 v[184:187], v175 offset:20480
	ds_read_b128 v[188:191], v175 offset:21504
	ds_read_b128 v[192:195], v175 offset:22528
	ds_read_b128 v[196:199], v175 offset:23552
	s_waitcnt vmcnt(7)
	s_waitcnt lgkmcnt(0)
	s_barrier
	s_setprio 1
	v_mfma_f32_16x16x32_bf16 v[60:63], v[120:123], v[160:163], v[60:63]
	v_mfma_f32_16x16x32_bf16 v[56:59], v[132:135], v[160:163], v[56:59]
	v_mfma_f32_16x16x32_bf16 v[44:47], v[120:123], v[176:179], v[44:47]
	v_mfma_f32_16x16x32_bf16 v[40:43], v[132:135], v[176:179], v[40:43]
	v_mfma_f32_16x16x32_bf16 v[28:31], v[120:123], v[184:187], v[28:31]
	v_mfma_f32_16x16x32_bf16 v[24:27], v[132:135], v[184:187], v[24:27]
	v_mfma_f32_16x16x32_bf16 v[12:15], v[120:123], v[192:195], v[12:15]
	v_mfma_f32_16x16x32_bf16 v[8:11], v[132:135], v[192:195], v[8:11]
	v_mfma_f32_16x16x32_bf16 v[60:63], v[124:127], v[164:167], v[60:63]
	v_mfma_f32_16x16x32_bf16 v[56:59], v[136:139], v[164:167], v[56:59]
	v_mfma_f32_16x16x32_bf16 v[44:47], v[124:127], v[180:183], v[44:47]
	v_mfma_f32_16x16x32_bf16 v[40:43], v[136:139], v[180:183], v[40:43]
	v_mfma_f32_16x16x32_bf16 v[28:31], v[124:127], v[188:191], v[28:31]
	v_mfma_f32_16x16x32_bf16 v[24:27], v[136:139], v[188:191], v[24:27]
	v_mfma_f32_16x16x32_bf16 v[12:15], v[124:127], v[196:199], v[12:15]
	v_mfma_f32_16x16x32_bf16 v[8:11], v[136:139], v[196:199], v[8:11]
	v_mfma_f32_16x16x32_bf16 v[52:55], v[144:147], v[160:163], v[52:55]
	v_mfma_f32_16x16x32_bf16 v[48:51], v[152:155], v[160:163], v[48:51]
	v_mfma_f32_16x16x32_bf16 v[36:39], v[144:147], v[176:179], v[36:39]
	v_mfma_f32_16x16x32_bf16 v[32:35], v[152:155], v[176:179], v[32:35]
	v_mfma_f32_16x16x32_bf16 v[20:23], v[144:147], v[184:187], v[20:23]
	v_mfma_f32_16x16x32_bf16 v[16:19], v[152:155], v[184:187], v[16:19]
	v_mfma_f32_16x16x32_bf16 v[4:7], v[144:147], v[192:195], v[4:7]
	v_mfma_f32_16x16x32_bf16 v[0:3], v[152:155], v[192:195], v[0:3]
	v_mfma_f32_16x16x32_bf16 v[52:55], v[148:151], v[164:167], v[52:55]
	v_mfma_f32_16x16x32_bf16 v[48:51], v[156:159], v[164:167], v[48:51]
	v_mfma_f32_16x16x32_bf16 v[36:39], v[148:151], v[180:183], v[36:39]
	v_mfma_f32_16x16x32_bf16 v[32:35], v[156:159], v[180:183], v[32:35]
	v_mfma_f32_16x16x32_bf16 v[20:23], v[148:151], v[188:191], v[20:23]
	v_mfma_f32_16x16x32_bf16 v[16:19], v[156:159], v[188:191], v[16:19]
	v_mfma_f32_16x16x32_bf16 v[4:7], v[148:151], v[196:199], v[4:7]
	v_mfma_f32_16x16x32_bf16 v[0:3], v[156:159], v[196:199], v[0:3]
	s_setprio 0
	s_barrier
; #define PG8_STAGE(bufoff, rs_, soff_, voff) do { _Pragma("unroll") for (int _i = 0; _i < 2; ++_i) \
;         __builtin_amdgcn_raw_ptr_buffer_load_lds(rs_, (LAS void*)(lds + (bufoff) + ldsw + _i * 8192), 16, (int)(voff)[_i], (int)(soff_), 0, 0); } while (0)
; #define PG8_LDA(dst, b, h) do { _Pragma("unroll") for (int m = 0; m < 4; ++m) dst[m] = PG8_LD2(lds + PG8_SA(b, h) + aoff + m * 2048); } while (0)
; #define PG8_LDB(dst, b, h) do { _Pragma("unroll") for (int n = 0; n < 2; ++n) dst[n] = PG8_LD2(lds + PG8_SB(b, h) + boff + n * 2048); } while (0)
; #define PG8_WAIT_V(n) asm volatile("s_waitcnt vmcnt(" #n ")" ::: "memory")
; #define PG8_WAIT_L(n) asm volatile("s_waitcnt lgkmcnt(" #n ")" ::: "memory")
; #define PG8_BAR __builtin_amdgcn_s_barrier()
; #define PG8_SCHED __builtin_amdgcn_sched_barrier(0)
; template <class Epi, class Sched, bool ALIGN_EPI = false, bool SP2 = false, bool FP8 = false>
; __device__ __forceinline__ void gemm_phase(LAS unsigned char* lds, const Gemm g, const Sched& S, const Epi& E, int wbase) {
;     ...
;             PG8_LDB(B0, 1, 0); PG8_LDB(B1, 1, 1); PG8_SCHED; PG8_LDA(At, 1, 0); PG8_STAGE(PG8_SA(0, 1), rA2, a2 + hstep, voffA);
;             PG8_WAIT_V(8); PG8_WAIT_L(0); PG8_BAR; PG8_MMA(0, 0, At, B0); PG8_MMA(0, 1, At, B1); PG8_BAR; PG8_SCHED;
;             PG8_LDA(At, 1, 1); PG8_STAGE(PG8_SB(1, 0), rB2, b3, voffB); PG8_STAGE(PG8_SB(1, 1), rB2, b3 + hstep, voffB); PG8_STAGE(PG8_SA(1, 0), rA2, a3, voffA);
;             PG8_WAIT_V(8); PG8_WAIT_L(0); PG8_BAR; PG8_MMA(1, 0, At, B0); PG8_MMA(1, 1, At, B1); PG8_BAR; PG8_SCHED;
	s_mov_b32 m0, s43
	s_nop 0
	buffer_load_dwordx4 v171, s[4:7], s67 offen lds
	v_add_u32_e32 v136, 0x18000, v174
	v_add_u32_e32 v156, 0x1c000, v174
	ds_read_b128 v[120:123], v136
	ds_read_b128 v[124:127], v136 offset:1024
	ds_read_b128 v[132:135], v136 offset:2048
	ds_read_b128 v[136:139], v136 offset:3072
	ds_read_b128 v[144:147], v156
	ds_read_b128 v[148:151], v156 offset:1024
	ds_read_b128 v[152:155], v156 offset:2048
	ds_read_b128 v[156:159], v156 offset:3072
	s_add_i32 s66, s66, s33
	s_mov_b32 m0, s45
	ds_read_b128 v[160:163], v175 offset:32768
	ds_read_b128 v[164:167], v175 offset:33792
	ds_read_b128 v[176:179], v175 offset:34816
	ds_read_b128 v[180:183], v175 offset:35840
	ds_read_b128 v[184:187], v175 offset:36864
	ds_read_b128 v[188:191], v175 offset:37888
	ds_read_b128 v[192:195], v175 offset:38912
	ds_read_b128 v[196:199], v175 offset:39936
	buffer_load_dwordx4 v168, s[36:39], s66 offen lds
	s_mov_b32 m0, s46
	s_nop 0
	buffer_load_dwordx4 v170, s[36:39], s66 offen lds
	s_waitcnt vmcnt(8)
	s_waitcnt lgkmcnt(0)
	s_barrier
	s_setprio 1
	v_mfma_f32_16x16x32_bf16 v[140:143], v[120:123], v[160:163], v[140:143]
	v_mfma_f32_16x16x32_bf16 v[128:131], v[132:135], v[160:163], v[128:131]
	v_mfma_f32_16x16x32_bf16 v[108:111], v[120:123], v[176:179], v[108:111]
	v_mfma_f32_16x16x32_bf16 v[104:107], v[132:135], v[176:179], v[104:107]
	v_mfma_f32_16x16x32_bf16 v[92:95], v[120:123], v[184:187], v[92:95]
	v_mfma_f32_16x16x32_bf16 v[88:91], v[132:135], v[184:187], v[88:91]
	v_mfma_f32_16x16x32_bf16 v[76:79], v[120:123], v[192:195], v[76:79]
	v_mfma_f32_16x16x32_bf16 v[72:75], v[132:135], v[192:195], v[72:75]
	v_mfma_f32_16x16x32_bf16 v[140:143], v[124:127], v[164:167], v[140:143]
	v_mfma_f32_16x16x32_bf16 v[128:131], v[136:139], v[164:167], v[128:131]
	v_mfma_f32_16x16x32_bf16 v[108:111], v[124:127], v[180:183], v[108:111]
	v_mfma_f32_16x16x32_bf16 v[104:107], v[136:139], v[180:183], v[104:107]
	v_mfma_f32_16x16x32_bf16 v[92:95], v[124:127], v[188:191], v[92:95]
	v_mfma_f32_16x16x32_bf16 v[88:91], v[136:139], v[188:191], v[88:91]
	v_mfma_f32_16x16x32_bf16 v[76:79], v[124:127], v[196:199], v[76:79]
	v_mfma_f32_16x16x32_bf16 v[72:75], v[136:139], v[196:199], v[72:75]
	v_mfma_f32_16x16x32_bf16 v[116:119], v[144:147], v[160:163], v[116:119]
	v_mfma_f32_16x16x32_bf16 v[112:115], v[152:155], v[160:163], v[112:115]
	v_mfma_f32_16x16x32_bf16 v[100:103], v[144:147], v[176:179], v[100:103]
	v_mfma_f32_16x16x32_bf16 v[96:99], v[152:155], v[176:179], v[96:99]
	v_mfma_f32_16x16x32_bf16 v[84:87], v[144:147], v[184:187], v[84:87]
	v_mfma_f32_16x16x32_bf16 v[80:83], v[152:155], v[184:187], v[80:83]
	v_mfma_f32_16x16x32_bf16 v[68:71], v[144:147], v[192:195], v[68:71]
	v_mfma_f32_16x16x32_bf16 v[64:67], v[152:155], v[192:195], v[64:67]
	v_mfma_f32_16x16x32_bf16 v[116:119], v[148:151], v[164:167], v[116:119]
	v_mfma_f32_16x16x32_bf16 v[112:115], v[156:159], v[164:167], v[112:115]
	v_mfma_f32_16x16x32_bf16 v[100:103], v[148:151], v[180:183], v[100:103]
	v_mfma_f32_16x16x32_bf16 v[96:99], v[156:159], v[180:183], v[96:99]
	v_mfma_f32_16x16x32_bf16 v[84:87], v[148:151], v[188:191], v[84:87]
	v_mfma_f32_16x16x32_bf16 v[80:83], v[156:159], v[188:191], v[80:83]
	v_mfma_f32_16x16x32_bf16 v[68:71], v[148:151], v[196:199], v[68:71]
	v_mfma_f32_16x16x32_bf16 v[64:67], v[156:159], v[196:199], v[64:67]
	s_setprio 0
	s_barrier
	s_mov_b32 m0, s47
	s_bitset1_b32 s55, 7
	buffer_load_dwordx4 v169, s[4:7], s55 offen lds
	s_mov_b32 m0, s48
	ds_read_b128 v[160:163], v175 offset:49152
	buffer_load_dwordx4 v171, s[4:7], s55 offen lds
	s_add_i32 s55, s55, s33
	s_mov_b32 m0, s56
	ds_read_b128 v[164:167], v175 offset:50176
	buffer_load_dwordx4 v169, s[4:7], s55 offen lds
	s_mov_b32 m0, s57
	ds_read_b128 v[176:179], v175 offset:51200
	buffer_load_dwordx4 v171, s[4:7], s55 offen lds
	s_mov_b32 m0, s52
	ds_read_b128 v[180:183], v175 offset:52224
	buffer_load_dwordx4 v168, s[36:39], s54 offen lds
	s_mov_b32 m0, s53
	ds_read_b128 v[184:187], v175 offset:53248
	buffer_load_dwordx4 v170, s[36:39], s54 offen lds
	ds_read_b128 v[188:191], v175 offset:54272
	ds_read_b128 v[192:195], v175 offset:55296
	ds_read_b128 v[196:199], v175 offset:56320
	s_waitcnt vmcnt(8)
	s_waitcnt lgkmcnt(0)
	s_barrier
	s_setprio 1
	v_mfma_f32_16x16x32_bf16 v[60:63], v[120:123], v[160:163], v[60:63]
	v_mfma_f32_16x16x32_bf16 v[56:59], v[132:135], v[160:163], v[56:59]
	v_mfma_f32_16x16x32_bf16 v[44:47], v[120:123], v[176:179], v[44:47]
	v_mfma_f32_16x16x32_bf16 v[40:43], v[132:135], v[176:179], v[40:43]
	v_mfma_f32_16x16x32_bf16 v[28:31], v[120:123], v[184:187], v[28:31]
	v_mfma_f32_16x16x32_bf16 v[24:27], v[132:135], v[184:187], v[24:27]
	v_mfma_f32_16x16x32_bf16 v[12:15], v[120:123], v[192:195], v[12:15]
	v_mfma_f32_16x16x32_bf16 v[8:11], v[132:135], v[192:195], v[8:11]
	v_mfma_f32_16x16x32_bf16 v[60:63], v[124:127], v[164:167], v[60:63]
	v_mfma_f32_16x16x32_bf16 v[56:59], v[136:139], v[164:167], v[56:59]
	v_mfma_f32_16x16x32_bf16 v[44:47], v[124:127], v[180:183], v[44:47]
	v_mfma_f32_16x16x32_bf16 v[40:43], v[136:139], v[180:183], v[40:43]
	v_mfma_f32_16x16x32_bf16 v[28:31], v[124:127], v[188:191], v[28:31]
	v_mfma_f32_16x16x32_bf16 v[24:27], v[136:139], v[188:191], v[24:27]
	v_mfma_f32_16x16x32_bf16 v[12:15], v[124:127], v[196:199], v[12:15]
	v_mfma_f32_16x16x32_bf16 v[8:11], v[136:139], v[196:199], v[8:11]
	v_mfma_f32_16x16x32_bf16 v[52:55], v[144:147], v[160:163], v[52:55]
	v_mfma_f32_16x16x32_bf16 v[48:51], v[152:155], v[160:163], v[48:51]
	v_mfma_f32_16x16x32_bf16 v[36:39], v[144:147], v[176:179], v[36:39]
	v_mfma_f32_16x16x32_bf16 v[32:35], v[152:155], v[176:179], v[32:35]
	v_mfma_f32_16x16x32_bf16 v[20:23], v[144:147], v[184:187], v[20:23]
	v_mfma_f32_16x16x32_bf16 v[16:19], v[152:155], v[184:187], v[16:19]
	v_mfma_f32_16x16x32_bf16 v[4:7], v[144:147], v[192:195], v[4:7]
	v_mfma_f32_16x16x32_bf16 v[0:3], v[152:155], v[192:195], v[0:3]
	v_mfma_f32_16x16x32_bf16 v[52:55], v[148:151], v[164:167], v[52:55]
	v_mfma_f32_16x16x32_bf16 v[48:51], v[156:159], v[164:167], v[48:51]
	v_mfma_f32_16x16x32_bf16 v[36:39], v[148:151], v[180:183], v[36:39]
	v_mfma_f32_16x16x32_bf16 v[32:35], v[156:159], v[180:183], v[32:35]
	v_mfma_f32_16x16x32_bf16 v[20:23], v[148:151], v[188:191], v[20:23]
	v_mfma_f32_16x16x32_bf16 v[16:19], v[156:159], v[188:191], v[16:19]
	v_mfma_f32_16x16x32_bf16 v[4:7], v[148:151], v[196:199], v[4:7]
	v_mfma_f32_16x16x32_bf16 v[0:3], v[156:159], v[196:199], v[0:3]
	s_setprio 0
	s_barrier
	s_add_i32 s63, s63, 2
	s_addk_i32 s61, 0x100
	s_addk_i32 s62, 0x100
	s_cmp_ge_i32 s63, s65
	s_cbranch_scc0 .LBB0_1944

;     __device__ __forceinline__ unsigned a_off(const Unit& u, const Gemm& g) const { return (unsigned)u.pm * (unsigned)(BM * 2) * (unsigned)g.K; }
;     __device__ __forceinline__ unsigned b_off(const Unit& u, const Gemm& g) const { return (unsigned)u.pn * (unsigned)(BM * 2) * (unsigned)g.K; }
;     __device__ __forceinline__ bool next(int i, Unit& u) const { return so.next(i, u); }
;     __device__ __forceinline__ unsigned a_off(const Unit& u, const Gemm& g) const { return (unsigned)u.pm * (unsigned)(BM * 2) * (unsigned)g.K; }
; template <class Epi, class Sched, bool ALIGN_EPI = false, bool SP2 = false, bool FP8 = false>
; __device__ __forceinline__ void gemm_phase(LAS unsigned char* lds, const Gemm g, const Sched& S, const Epi& E, int wbase) {
;     ...
;         const bool has_next = S.next(ui + 1, nxt);
;         const unsigned nA = has_next ? S.a_off(nxt, g) : cA, nB = has_next ? S.b_off(nxt, g) : cB;
;         const rsrc_t rAn = (Sched::TWO && has_next) ? (nxt.part ? rA1 : rA0) : rAc, rBn = (Sched::TWO && has_next) ? (nxt.part ? rB1 : rB0) : rBc;
;         float pre_[8] = {0.f, 0.f, 0.f, 0.f, 0.f, 0.f, 0.f, 0.f};
;         if constexpr (Epi::HAS_PRE) E.pre_load(pre_, cur, wr);
;         for (int t = 0; t < nt; t += 2) {
;             const bool last = (t == nt - 2);
;             const unsigned a1 = cA + (unsigned)(t + 1) * kstep;
;             const unsigned a2 = last ? nA : cA + (unsigned)(t + 2) * kstep, b2 = last ? nB : cB + (unsigned)(t + 2) * kstep; const rsrc_t rA2 = (Sched::TWO && last) ? rAn : rAc, rB2 = (Sched::TWO && last) ? rBn : rBc;
;             const unsigned a3 = a2 + kstep, b3 = b2 + kstep;
;             if (last && has_next) S.a_ready(nxt);
;             if constexpr (SP2) {
;             PG8_LDB(B0, 0, 0); PG8_LDB(B1, 0, 1); PG8_SCHED; PG8_LDA(At, 0, 0); PG8_STAGE(PG8_SA(1, 1), rAc, a1 + hstep, voffA);
;             PG8_WAIT_V(8); PG8_WAIT_L(0); PG8_BAR; PG8_MMA(0, 0, At, B0); PG8_MMA(0, 1, At, B1); PG8_BAR; PG8_SCHED;
;             PG8_LDA(At, 0, 1); PG8_STAGE(PG8_SB(0, 0), rB2, b2, voffB); PG8_STAGE(PG8_SB(0, 1), rB2, b2 + hstep, voffB); PG8_STAGE(PG8_SA(0, 0), rA2, a2, voffA);
;             PG8_WAIT_V(8); PG8_WAIT_L(0); PG8_BAR; PG8_MMA(1, 0, At, B0); PG8_MMA(1, 1, At, B1); PG8_BAR; PG8_SCHED;
;             PG8_LDB(B0, 1, 0); PG8_LDB(B1, 1, 1); PG8_SCHED; PG8_LDA(At, 1, 0); PG8_STAGE(PG8_SA(0, 1), rA2, a2 + hstep, voffA);
.LBB0_1988:
	s_lshl_b32 s95, s94, 18
	s_andn2_b64 vcc, exec, s[26:27]
	s_lshl_b32 s96, s9, 18
	s_cbranch_vccnz .LBB0_1992
	s_and_b64 s[2:3], s[34:35], exec
	s_waitcnt vmcnt(37)
	s_waitcnt vmcnt(36)
	s_waitcnt vmcnt(35)
	s_waitcnt vmcnt(32)
	s_waitcnt vmcnt(31)
	s_waitcnt vmcnt(28)
	s_waitcnt vmcnt(27)
	s_waitcnt vmcnt(24)
	s_waitcnt vmcnt(23)
	v_mov_b32_e32 v223, 0xff61b1e6
	v_mov_b32_e32 v222, 1
	v_mov_b32_e32 v173, v233
	v_mov_b32_e32 v172, 0x358637bd
	s_cselect_b32 s2, s95, s4
	s_cselect_b32 s3, s96, s5
	s_addk_i32 s4, 0x80
	s_addk_i32 s5, 0x100
	s_mov_b32 s61, 0
	s_waitcnt vmcnt(0)
	v_add_u32_e32 v136, 0x10000, v180
	v_add_u32_e32 v156, 0x14000, v180
	ds_read_b128 v[120:123], v136
	ds_read_b128 v[124:127], v136 offset:1024
	ds_read_b128 v[132:135], v136 offset:2048
	ds_read_b128 v[136:139], v136 offset:3072
	ds_read_b128 v[144:147], v156
	ds_read_b128 v[148:151], v156 offset:1024
	ds_read_b128 v[152:155], v156 offset:2048
	ds_read_b128 v[156:159], v156 offset:3072
	s_add_i32 s14, s4, 0x80
	s_cmp_eq_u32 s84, s61
	s_cselect_b32 s62, s2, s14
	s_cselect_b32 s55, s3, s5
	s_or_b32 s54, s62, 0x80
	s_add_i32 s14, s42, s4
	s_mov_b32 m0, s85
	ds_read_b128 v[160:163], v181
	ds_read_b128 v[164:167], v181 offset:1024
	ds_read_b128 v[182:185], v181 offset:2048
	ds_read_b128 v[186:189], v181 offset:3072
	ds_read_b128 v[194:197], v181 offset:4096
	ds_read_b128 v[198:201], v181 offset:5120
	ds_read_b128 v[202:205], v181 offset:6144
	ds_read_b128 v[206:209], v181 offset:7168
	buffer_load_dwordx4 v174, s[36:39], s14 offen lds
	s_mov_b32 m0, s8
	s_nop 0
	buffer_load_dwordx4 v176, s[36:39], s14 offen lds
	s_waitcnt vmcnt(8)
	s_waitcnt lgkmcnt(0)
	s_barrier
	s_setprio 1
	v_mfma_f32_16x16x128_f8f6f4 v[140:143], v[120:127], v[160:167], 0
	v_mfma_f32_16x16x128_f8f6f4 v[128:131], v[132:139], v[160:167], 0
	v_mfma_f32_16x16x128_f8f6f4 v[108:111], v[120:127], v[182:189], 0
	v_mfma_f32_16x16x128_f8f6f4 v[104:107], v[132:139], v[182:189], 0
	v_mfma_f32_16x16x128_f8f6f4 v[168:171], v[120:127], v[194:201], 0
	v_mfma_f32_16x16x128_f8f6f4 v[190:193], v[132:139], v[194:201], 0
	v_mfma_f32_16x16x128_f8f6f4 v[210:213], v[120:127], v[202:209], 0
	v_mfma_f32_16x16x128_f8f6f4 v[214:217], v[132:139], v[202:209], 0
	v_mfma_f32_16x16x128_f8f6f4 v[116:119], v[144:151], v[160:167], 0
	v_mfma_f32_16x16x128_f8f6f4 v[112:115], v[152:159], v[160:167], 0
	v_mfma_f32_16x16x128_f8f6f4 v[100:103], v[144:151], v[182:189], 0
	v_mfma_f32_16x16x128_f8f6f4 v[96:99], v[152:159], v[182:189], 0
	v_mfma_f32_16x16x128_f8f6f4 v[160:163], v[144:151], v[194:201], 0
	v_mfma_f32_16x16x128_f8f6f4 v[164:167], v[152:159], v[194:201], 0
	v_mfma_f32_16x16x128_f8f6f4 v[182:185], v[144:151], v[202:209], 0
	v_mfma_f32_16x16x128_f8f6f4 v[186:189], v[152:159], v[202:209], 0
	s_setprio 0
	s_barrier
	s_mov_b32 m0, s44
	s_mov_b32 s14, s38
	s_mov_b32 s15, s39
	s_nop 1
	buffer_load_dwordx4 v175, s[12:15], s55 offen lds
	s_mov_b32 m0, s45
	ds_read_b128 v[64:67], v181 offset:16384
	s_add_i32 s63, s55, s42
	buffer_load_dwordx4 v177, s[12:15], s55 offen lds
	s_mov_b32 m0, s46
	ds_read_b128 v[68:71], v181 offset:17408
	buffer_load_dwordx4 v175, s[12:15], s63 offen lds
	s_mov_b32 m0, s43
	ds_read_b128 v[72:75], v181 offset:18432
	buffer_load_dwordx4 v174, s[36:39], s62 offen lds
	s_mov_b32 m0, s48
	ds_read_b128 v[76:79], v181 offset:19456
	buffer_load_dwordx4 v176, s[36:39], s62 offen lds
	ds_read_b128 v[80:83], v181 offset:20480
	ds_read_b128 v[84:87], v181 offset:21504
	ds_read_b128 v[88:91], v181 offset:22528
	ds_read_b128 v[92:95], v181 offset:23552
	s_waitcnt vmcnt(7)
	s_waitcnt lgkmcnt(0)
	s_barrier
	s_setprio 1
	v_mfma_f32_16x16x128_f8f6f4 v[60:63], v[120:127], v[64:71], 0
	v_mfma_f32_16x16x128_f8f6f4 v[56:59], v[132:139], v[64:71], 0
	v_mfma_f32_16x16x128_f8f6f4 v[194:197], v[120:127], v[72:79], 0
	v_mfma_f32_16x16x128_f8f6f4 v[198:201], v[132:139], v[72:79], 0
	v_mfma_f32_16x16x128_f8f6f4 v[202:205], v[120:127], v[80:87], 0
	v_mfma_f32_16x16x128_f8f6f4 v[206:209], v[132:139], v[80:87], 0
	v_mfma_f32_16x16x128_f8f6f4 v[218:221], v[120:127], v[88:95], 0
	v_mfma_f32_16x16x128_f8f6f4 v[226:229], v[132:139], v[88:95], 0
	v_mfma_f32_16x16x128_f8f6f4 v[52:55], v[144:151], v[64:71], 0
	v_mfma_f32_16x16x128_f8f6f4 v[48:51], v[152:159], v[64:71], 0
	v_mfma_f32_16x16x128_f8f6f4 v[230:233], v[144:151], v[72:79], 0
	v_mfma_f32_16x16x128_f8f6f4 v[234:237], v[152:159], v[72:79], 0
	v_mfma_f32_16x16x128_f8f6f4 v[238:241], v[144:151], v[80:87], 0
	v_mfma_f32_16x16x128_f8f6f4 v[242:245], v[152:159], v[80:87], 0
	v_mfma_f32_16x16x128_f8f6f4 v[246:249], v[144:151], v[88:95], 0
	v_mfma_f32_16x16x128_f8f6f4 v[250:253], v[152:159], v[88:95], 0
	s_setprio 0
	s_barrier
	s_mov_b32 m0, s47
	s_nop 0
	buffer_load_dwordx4 v177, s[12:15], s63 offen lds
	v_add_u32_e32 v8, 0x18000, v180
	s_nop 3
	ds_read_b128 v[0:3], v8
	ds_read_b128 v[4:7], v8 offset:1024
	ds_read_b128 v[16:19], v8 offset:2048
	ds_read_b128 v[20:23], v8 offset:3072
	v_add_u32_e32 v8, 0x1c000, v180
	ds_read_b128 v[120:123], v8
	ds_read_b128 v[124:127], v8 offset:1024
	ds_read_b128 v[132:135], v8 offset:2048
	ds_read_b128 v[136:139], v8 offset:3072
	s_add_i32 s62, s62, s42
	s_mov_b32 m0, s52
	ds_read_b128 v[8:11], v181 offset:32768
	ds_read_b128 v[12:15], v181 offset:33792
	ds_read_b128 v[24:27], v181 offset:34816
	ds_read_b128 v[28:31], v181 offset:35840
	ds_read_b128 v[32:35], v181 offset:36864
	ds_read_b128 v[36:39], v181 offset:37888
	ds_read_b128 v[40:43], v181 offset:38912
	ds_read_b128 v[44:47], v181 offset:39936
	buffer_load_dwordx4 v174, s[36:39], s62 offen lds
	s_mov_b32 m0, s53
	s_nop 0
	buffer_load_dwordx4 v176, s[36:39], s62 offen lds
	s_waitcnt vmcnt(8)
	s_waitcnt lgkmcnt(0)
	s_barrier
; #define PG8_STAGE(bufoff, rs_, soff_, voff) do { _Pragma("unroll") for (int _i = 0; _i < 2; ++_i) \
;         __builtin_amdgcn_raw_ptr_buffer_load_lds(rs_, (LAS void*)(lds + (bufoff) + ldsw + _i * 8192), 16, (int)(voff)[_i], (int)(soff_), 0, 0); } while (0)
; #define PG8_LDA(dst, b, h) do { _Pragma("unroll") for (int m = 0; m < 4; ++m) dst[m] = PG8_LD2(lds + PG8_SA(b, h) + aoff + m * 2048); } while (0)
; #define PG8_LDB(dst, b, h) do { _Pragma("unroll") for (int n = 0; n < 2; ++n) dst[n] = PG8_LD2(lds + PG8_SB(b, h) + boff + n * 2048); } while (0)
; #define PG8_WAIT_V(n) asm volatile("s_waitcnt vmcnt(" #n ")" ::: "memory")
; #define PG8_WAIT_L(n) asm volatile("s_waitcnt lgkmcnt(" #n ")" ::: "memory")
; #define PG8_BAR __builtin_amdgcn_s_barrier()
; #define PG8_SCHED __builtin_amdgcn_sched_barrier(0)
; template <class Epi, class Sched, bool ALIGN_EPI = false, bool SP2 = false, bool FP8 = false>
; __device__ __forceinline__ void gemm_phase(LAS unsigned char* lds, const Gemm g, const Sched& S, const Epi& E, int wbase) {
;     ...
;             PG8_LDB(B0, 0, 0); PG8_LDB(B1, 0, 1); PG8_SCHED; PG8_LDA(At, 0, 0); PG8_STAGE(PG8_SA(1, 1), rAc, a1 + hstep, voffA);
;             PG8_WAIT_V(8); PG8_WAIT_L(0); PG8_BAR; PG8_MMA(0, 0, At, B0); PG8_MMA(0, 1, At, B1); PG8_BAR; PG8_SCHED;
;             PG8_LDA(At, 0, 1); PG8_STAGE(PG8_SB(0, 0), rB2, b2, voffB); PG8_STAGE(PG8_SB(0, 1), rB2, b2 + hstep, voffB); PG8_STAGE(PG8_SA(0, 0), rA2, a2, voffA);
;             PG8_WAIT_V(8); PG8_WAIT_L(0); PG8_BAR; PG8_MMA(1, 0, At, B0); PG8_MMA(1, 1, At, B1); PG8_BAR; PG8_SCHED;
;             PG8_LDB(B0, 1, 0); PG8_LDB(B1, 1, 1); PG8_SCHED; PG8_LDA(At, 1, 0); PG8_STAGE(PG8_SA(0, 1), rA2, a2 + hstep, voffA);
;             PG8_WAIT_V(8); PG8_WAIT_L(0); PG8_BAR; PG8_MMA(0, 0, At, B0); PG8_MMA(0, 1, At, B1); PG8_BAR; PG8_SCHED;
;             PG8_LDA(At, 1, 1); PG8_STAGE(PG8_SB(1, 0), rB2, b3, voffB); PG8_STAGE(PG8_SB(1, 1), rB2, b3 + hstep, voffB); PG8_STAGE(PG8_SA(1, 0), rA2, a3, voffA);
;             PG8_WAIT_V(8); PG8_WAIT_L(0); PG8_BAR; PG8_MMA(1, 0, At, B0); PG8_MMA(1, 1, At, B1); PG8_BAR; PG8_SCHED;
	s_setprio 1
	v_mfma_f32_16x16x128_f8f6f4 v[140:143], v[0:7], v[8:15], v[140:143]
	v_mfma_f32_16x16x128_f8f6f4 v[128:131], v[16:23], v[8:15], v[128:131]
	v_mfma_f32_16x16x128_f8f6f4 v[108:111], v[0:7], v[24:31], v[108:111]
	v_mfma_f32_16x16x128_f8f6f4 v[104:107], v[16:23], v[24:31], v[104:107]
	v_mfma_f32_16x16x128_f8f6f4 v[92:95], v[0:7], v[32:39], v[168:171]
	v_mfma_f32_16x16x128_f8f6f4 v[88:91], v[16:23], v[32:39], v[190:193]
	v_mfma_f32_16x16x128_f8f6f4 v[76:79], v[0:7], v[40:47], v[210:213]
	v_mfma_f32_16x16x128_f8f6f4 v[72:75], v[16:23], v[40:47], v[214:217]
	v_mfma_f32_16x16x128_f8f6f4 v[116:119], v[120:127], v[8:15], v[116:119]
	v_mfma_f32_16x16x128_f8f6f4 v[112:115], v[132:139], v[8:15], v[112:115]
	v_mfma_f32_16x16x128_f8f6f4 v[100:103], v[120:127], v[24:31], v[100:103]
	v_mfma_f32_16x16x128_f8f6f4 v[96:99], v[132:139], v[24:31], v[96:99]
	v_mfma_f32_16x16x128_f8f6f4 v[84:87], v[120:127], v[32:39], v[160:163]
	v_mfma_f32_16x16x128_f8f6f4 v[80:83], v[132:139], v[32:39], v[164:167]
	v_mfma_f32_16x16x128_f8f6f4 v[68:71], v[120:127], v[40:47], v[182:185]
	v_mfma_f32_16x16x128_f8f6f4 v[64:67], v[132:139], v[40:47], v[186:189]
	s_setprio 0
	s_barrier
	s_mov_b32 m0, s56
	s_bitset1_b32 s55, 7
	buffer_load_dwordx4 v175, s[12:15], s55 offen lds
	s_mov_b32 m0, s57
	ds_read_b128 v[32:35], v181 offset:49152
	buffer_load_dwordx4 v177, s[12:15], s55 offen lds
	s_add_i32 s55, s55, s42
	s_mov_b32 m0, s65
	ds_read_b128 v[36:39], v181 offset:50176
	buffer_load_dwordx4 v175, s[12:15], s55 offen lds
	s_mov_b32 m0, s76
	ds_read_b128 v[144:147], v181 offset:51200
	buffer_load_dwordx4 v177, s[12:15], s55 offen lds
	s_mov_b32 m0, s58
	ds_read_b128 v[148:151], v181 offset:52224
	buffer_load_dwordx4 v174, s[36:39], s54 offen lds
	s_mov_b32 m0, s59
	ds_read_b128 v[152:155], v181 offset:53248
	buffer_load_dwordx4 v176, s[36:39], s54 offen lds
	ds_read_b128 v[156:159], v181 offset:54272
	ds_read_b128 v[160:163], v181 offset:55296
	ds_read_b128 v[164:167], v181 offset:56320
	s_waitcnt vmcnt(8)
	s_waitcnt lgkmcnt(0)
	s_barrier
	s_setprio 1
	v_mfma_f32_16x16x128_f8f6f4 v[60:63], v[0:7], v[32:39], v[60:63]
	v_mfma_f32_16x16x128_f8f6f4 v[56:59], v[16:23], v[32:39], v[56:59]
	v_mfma_f32_16x16x128_f8f6f4 v[44:47], v[0:7], v[144:151], v[194:197]
	v_mfma_f32_16x16x128_f8f6f4 v[40:43], v[16:23], v[144:151], v[198:201]
	v_mfma_f32_16x16x128_f8f6f4 v[28:31], v[0:7], v[152:159], v[202:205]
	v_mfma_f32_16x16x128_f8f6f4 v[24:27], v[16:23], v[152:159], v[206:209]
	v_mfma_f32_16x16x128_f8f6f4 v[12:15], v[0:7], v[160:167], v[218:221]
	v_mfma_f32_16x16x128_f8f6f4 v[8:11], v[16:23], v[160:167], v[226:229]
	v_mfma_f32_16x16x128_f8f6f4 v[52:55], v[120:127], v[32:39], v[52:55]
	v_mfma_f32_16x16x128_f8f6f4 v[48:51], v[132:139], v[32:39], v[48:51]
	v_mfma_f32_16x16x128_f8f6f4 v[36:39], v[120:127], v[144:151], v[230:233]
	v_mfma_f32_16x16x128_f8f6f4 v[32:35], v[132:139], v[144:151], v[234:237]
	v_mfma_f32_16x16x128_f8f6f4 v[20:23], v[120:127], v[152:159], v[238:241]
	v_mfma_f32_16x16x128_f8f6f4 v[16:19], v[132:139], v[152:159], v[242:245]
	v_mfma_f32_16x16x128_f8f6f4 v[4:7], v[120:127], v[160:167], v[246:249]
	v_mfma_f32_16x16x128_f8f6f4 v[0:3], v[132:139], v[160:167], v[250:253]
	s_setprio 0
	s_barrier
	s_add_i32 s61, s61, 2
	s_addk_i32 s4, 0x100
	s_addk_i32 s5, 0x100
	s_cmp_ge_i32 s61, s82
	s_cbranch_scc0 .LBB0_1990
	s_branch .Lzp_after_1990
.LBB0_1990:
	v_add_u32_e32 v136, 0x10000, v180
	v_add_u32_e32 v156, 0x14000, v180
	ds_read_b128 v[120:123], v136
	ds_read_b128 v[124:127], v136 offset:1024
	ds_read_b128 v[132:135], v136 offset:2048
	ds_read_b128 v[136:139], v136 offset:3072
	ds_read_b128 v[144:147], v156
	ds_read_b128 v[148:151], v156 offset:1024
	ds_read_b128 v[152:155], v156 offset:2048
	ds_read_b128 v[156:159], v156 offset:3072
	s_add_i32 s14, s4, 0x80
	s_cmp_eq_u32 s84, s61
	s_cselect_b32 s62, s2, s14
	s_cselect_b32 s55, s3, s5
	s_or_b32 s54, s62, 0x80
	s_add_i32 s14, s42, s4
	s_mov_b32 m0, s85
	ds_read_b128 v[160:163], v181
	ds_read_b128 v[164:167], v181 offset:1024
	ds_read_b128 v[182:185], v181 offset:2048
	ds_read_b128 v[186:189], v181 offset:3072
	ds_read_b128 v[194:197], v181 offset:4096
	ds_read_b128 v[198:201], v181 offset:5120
	ds_read_b128 v[202:205], v181 offset:6144
	ds_read_b128 v[206:209], v181 offset:7168
	buffer_load_dwordx4 v174, s[36:39], s14 offen lds
	s_mov_b32 m0, s8
	s_nop 0
	buffer_load_dwordx4 v176, s[36:39], s14 offen lds
	s_waitcnt vmcnt(8)
	s_waitcnt lgkmcnt(0)
	s_barrier
	s_setprio 1
	v_mfma_f32_16x16x128_f8f6f4 v[140:143], v[120:127], v[160:167], v[140:143]
	v_mfma_f32_16x16x128_f8f6f4 v[128:131], v[132:139], v[160:167], v[128:131]
	v_mfma_f32_16x16x128_f8f6f4 v[108:111], v[120:127], v[182:189], v[108:111]
	v_mfma_f32_16x16x128_f8f6f4 v[104:107], v[132:139], v[182:189], v[104:107]
	v_mfma_f32_16x16x128_f8f6f4 v[168:171], v[120:127], v[194:201], v[92:95]
	v_mfma_f32_16x16x128_f8f6f4 v[190:193], v[132:139], v[194:201], v[88:91]
	v_mfma_f32_16x16x128_f8f6f4 v[210:213], v[120:127], v[202:209], v[76:79]
	v_mfma_f32_16x16x128_f8f6f4 v[214:217], v[132:139], v[202:209], v[72:75]
	v_mfma_f32_16x16x128_f8f6f4 v[116:119], v[144:151], v[160:167], v[116:119]
	v_mfma_f32_16x16x128_f8f6f4 v[112:115], v[152:159], v[160:167], v[112:115]
	v_mfma_f32_16x16x128_f8f6f4 v[100:103], v[144:151], v[182:189], v[100:103]
	v_mfma_f32_16x16x128_f8f6f4 v[96:99], v[152:159], v[182:189], v[96:99]
	v_mfma_f32_16x16x128_f8f6f4 v[160:163], v[144:151], v[194:201], v[84:87]
	v_mfma_f32_16x16x128_f8f6f4 v[164:167], v[152:159], v[194:201], v[80:83]
	v_mfma_f32_16x16x128_f8f6f4 v[182:185], v[144:151], v[202:209], v[68:71]
	v_mfma_f32_16x16x128_f8f6f4 v[186:189], v[152:159], v[202:209], v[64:67]
	s_setprio 0
	s_barrier
; #define PG8_STAGE(bufoff, rs_, soff_, voff) do { _Pragma("unroll") for (int _i = 0; _i < 2; ++_i) \
;         __builtin_amdgcn_raw_ptr_buffer_load_lds(rs_, (LAS void*)(lds + (bufoff) + ldsw + _i * 8192), 16, (int)(voff)[_i], (int)(soff_), 0, 0); } while (0)
; #define PG8_LDA(dst, b, h) do { _Pragma("unroll") for (int m = 0; m < 4; ++m) dst[m] = PG8_LD2(lds + PG8_SA(b, h) + aoff + m * 2048); } while (0)
; #define PG8_LDB(dst, b, h) do { _Pragma("unroll") for (int n = 0; n < 2; ++n) dst[n] = PG8_LD2(lds + PG8_SB(b, h) + boff + n * 2048); } while (0)
; #define PG8_WAIT_V(n) asm volatile("s_waitcnt vmcnt(" #n ")" ::: "memory")
; #define PG8_WAIT_L(n) asm volatile("s_waitcnt lgkmcnt(" #n ")" ::: "memory")
; #define PG8_BAR __builtin_amdgcn_s_barrier()
; #define PG8_SCHED __builtin_amdgcn_sched_barrier(0)
; template <class Epi, class Sched, bool ALIGN_EPI = false, bool SP2 = false, bool FP8 = false>
; __device__ __forceinline__ void gemm_phase(LAS unsigned char* lds, const Gemm g, const Sched& S, const Epi& E, int wbase) {
;     ...
;             PG8_LDA(At, 0, 1); PG8_STAGE(PG8_SB(0, 0), rB2, b2, voffB); PG8_STAGE(PG8_SB(0, 1), rB2, b2 + hstep, voffB); PG8_STAGE(PG8_SA(0, 0), rA2, a2, voffA);
;             PG8_WAIT_V(8); PG8_WAIT_L(0); PG8_BAR; PG8_MMA(1, 0, At, B0); PG8_MMA(1, 1, At, B1); PG8_BAR; PG8_SCHED;
;             PG8_LDB(B0, 1, 0); PG8_LDB(B1, 1, 1); PG8_SCHED; PG8_LDA(At, 1, 0); PG8_STAGE(PG8_SA(0, 1), rA2, a2 + hstep, voffA);
;             PG8_WAIT_V(8); PG8_WAIT_L(0); PG8_BAR; PG8_MMA(0, 0, At, B0); PG8_MMA(0, 1, At, B1); PG8_BAR; PG8_SCHED;
;             PG8_LDA(At, 1, 1); PG8_STAGE(PG8_SB(1, 0), rB2, b3, voffB); PG8_STAGE(PG8_SB(1, 1), rB2, b3 + hstep, voffB); PG8_STAGE(PG8_SA(1, 0), rA2, a3, voffA);
;             PG8_WAIT_V(8); PG8_WAIT_L(0); PG8_BAR; PG8_MMA(1, 0, At, B0); PG8_MMA(1, 1, At, B1); PG8_BAR; PG8_SCHED;
	s_mov_b32 m0, s44
	s_mov_b32 s14, s38
	s_mov_b32 s15, s39
	s_nop 1
	buffer_load_dwordx4 v175, s[12:15], s55 offen lds
	s_mov_b32 m0, s45
	ds_read_b128 v[64:67], v181 offset:16384
	s_add_i32 s63, s55, s42
	buffer_load_dwordx4 v177, s[12:15], s55 offen lds
	s_mov_b32 m0, s46
	ds_read_b128 v[68:71], v181 offset:17408
	buffer_load_dwordx4 v175, s[12:15], s63 offen lds
	s_mov_b32 m0, s43
	ds_read_b128 v[72:75], v181 offset:18432
	buffer_load_dwordx4 v174, s[36:39], s62 offen lds
	s_mov_b32 m0, s48
	ds_read_b128 v[76:79], v181 offset:19456
	buffer_load_dwordx4 v176, s[36:39], s62 offen lds
	ds_read_b128 v[80:83], v181 offset:20480
	ds_read_b128 v[84:87], v181 offset:21504
	ds_read_b128 v[88:91], v181 offset:22528
	ds_read_b128 v[92:95], v181 offset:23552
	s_waitcnt vmcnt(7)
	s_waitcnt lgkmcnt(0)
	s_barrier
	s_setprio 1
	v_mfma_f32_16x16x128_f8f6f4 v[60:63], v[120:127], v[64:71], v[60:63]
	v_mfma_f32_16x16x128_f8f6f4 v[56:59], v[132:139], v[64:71], v[56:59]
	v_mfma_f32_16x16x128_f8f6f4 v[194:197], v[120:127], v[72:79], v[44:47]
	v_mfma_f32_16x16x128_f8f6f4 v[198:201], v[132:139], v[72:79], v[40:43]
	v_mfma_f32_16x16x128_f8f6f4 v[202:205], v[120:127], v[80:87], v[28:31]
	v_mfma_f32_16x16x128_f8f6f4 v[206:209], v[132:139], v[80:87], v[24:27]
	v_mfma_f32_16x16x128_f8f6f4 v[218:221], v[120:127], v[88:95], v[12:15]
	v_mfma_f32_16x16x128_f8f6f4 v[226:229], v[132:139], v[88:95], v[8:11]
	v_mfma_f32_16x16x128_f8f6f4 v[52:55], v[144:151], v[64:71], v[52:55]
	v_mfma_f32_16x16x128_f8f6f4 v[48:51], v[152:159], v[64:71], v[48:51]
	v_mfma_f32_16x16x128_f8f6f4 v[230:233], v[144:151], v[72:79], v[36:39]
	v_mfma_f32_16x16x128_f8f6f4 v[234:237], v[152:159], v[72:79], v[32:35]
	v_mfma_f32_16x16x128_f8f6f4 v[238:241], v[144:151], v[80:87], v[20:23]
	v_mfma_f32_16x16x128_f8f6f4 v[242:245], v[152:159], v[80:87], v[16:19]
	v_mfma_f32_16x16x128_f8f6f4 v[246:249], v[144:151], v[88:95], v[4:7]
	v_mfma_f32_16x16x128_f8f6f4 v[250:253], v[152:159], v[88:95], v[0:3]
	s_setprio 0
	s_barrier
	s_mov_b32 m0, s47
	s_nop 0
	buffer_load_dwordx4 v177, s[12:15], s63 offen lds
	v_add_u32_e32 v8, 0x18000, v180
	s_nop 3
	ds_read_b128 v[0:3], v8
	ds_read_b128 v[4:7], v8 offset:1024
	ds_read_b128 v[16:19], v8 offset:2048
	ds_read_b128 v[20:23], v8 offset:3072
	v_add_u32_e32 v8, 0x1c000, v180
	ds_read_b128 v[120:123], v8
	ds_read_b128 v[124:127], v8 offset:1024
	ds_read_b128 v[132:135], v8 offset:2048
	ds_read_b128 v[136:139], v8 offset:3072
	s_add_i32 s62, s62, s42
	s_mov_b32 m0, s52
	ds_read_b128 v[8:11], v181 offset:32768
	ds_read_b128 v[12:15], v181 offset:33792
	ds_read_b128 v[24:27], v181 offset:34816
	ds_read_b128 v[28:31], v181 offset:35840
	ds_read_b128 v[32:35], v181 offset:36864
	ds_read_b128 v[36:39], v181 offset:37888
	ds_read_b128 v[40:43], v181 offset:38912
	ds_read_b128 v[44:47], v181 offset:39936
	buffer_load_dwordx4 v174, s[36:39], s62 offen lds
	s_mov_b32 m0, s53
	s_nop 0
	buffer_load_dwordx4 v176, s[36:39], s62 offen lds
	s_waitcnt vmcnt(8)
	s_waitcnt lgkmcnt(0)
	s_barrier
	s_setprio 1
	v_mfma_f32_16x16x128_f8f6f4 v[140:143], v[0:7], v[8:15], v[140:143]
	v_mfma_f32_16x16x128_f8f6f4 v[128:131], v[16:23], v[8:15], v[128:131]
	v_mfma_f32_16x16x128_f8f6f4 v[108:111], v[0:7], v[24:31], v[108:111]
	v_mfma_f32_16x16x128_f8f6f4 v[104:107], v[16:23], v[24:31], v[104:107]
	v_mfma_f32_16x16x128_f8f6f4 v[92:95], v[0:7], v[32:39], v[168:171]
	v_mfma_f32_16x16x128_f8f6f4 v[88:91], v[16:23], v[32:39], v[190:193]
	v_mfma_f32_16x16x128_f8f6f4 v[76:79], v[0:7], v[40:47], v[210:213]
	v_mfma_f32_16x16x128_f8f6f4 v[72:75], v[16:23], v[40:47], v[214:217]
	v_mfma_f32_16x16x128_f8f6f4 v[116:119], v[120:127], v[8:15], v[116:119]
	v_mfma_f32_16x16x128_f8f6f4 v[112:115], v[132:139], v[8:15], v[112:115]
	v_mfma_f32_16x16x128_f8f6f4 v[100:103], v[120:127], v[24:31], v[100:103]
	v_mfma_f32_16x16x128_f8f6f4 v[96:99], v[132:139], v[24:31], v[96:99]
	v_mfma_f32_16x16x128_f8f6f4 v[84:87], v[120:127], v[32:39], v[160:163]
	v_mfma_f32_16x16x128_f8f6f4 v[80:83], v[132:139], v[32:39], v[164:167]
	v_mfma_f32_16x16x128_f8f6f4 v[68:71], v[120:127], v[40:47], v[182:185]
	v_mfma_f32_16x16x128_f8f6f4 v[64:67], v[132:139], v[40:47], v[186:189]
	s_setprio 0
	s_barrier
	s_mov_b32 m0, s56
	s_bitset1_b32 s55, 7
	buffer_load_dwordx4 v175, s[12:15], s55 offen lds
	s_mov_b32 m0, s57
	ds_read_b128 v[32:35], v181 offset:49152
	buffer_load_dwordx4 v177, s[12:15], s55 offen lds
	s_add_i32 s55, s55, s42
	s_mov_b32 m0, s65
	ds_read_b128 v[36:39], v181 offset:50176
	buffer_load_dwordx4 v175, s[12:15], s55 offen lds
	s_mov_b32 m0, s76
	ds_read_b128 v[144:147], v181 offset:51200
	buffer_load_dwordx4 v177, s[12:15], s55 offen lds
	s_mov_b32 m0, s58
	ds_read_b128 v[148:151], v181 offset:52224
	buffer_load_dwordx4 v174, s[36:39], s54 offen lds
	s_mov_b32 m0, s59
	ds_read_b128 v[152:155], v181 offset:53248
	buffer_load_dwordx4 v176, s[36:39], s54 offen lds
	ds_read_b128 v[156:159], v181 offset:54272
	ds_read_b128 v[160:163], v181 offset:55296
	ds_read_b128 v[164:167], v181 offset:56320
	s_waitcnt vmcnt(8)
	s_waitcnt lgkmcnt(0)
	s_barrier
	s_setprio 1
	v_mfma_f32_16x16x128_f8f6f4 v[60:63], v[0:7], v[32:39], v[60:63]
	v_mfma_f32_16x16x128_f8f6f4 v[56:59], v[16:23], v[32:39], v[56:59]
	v_mfma_f32_16x16x128_f8f6f4 v[44:47], v[0:7], v[144:151], v[194:197]
	v_mfma_f32_16x16x128_f8f6f4 v[40:43], v[16:23], v[144:151], v[198:201]
	v_mfma_f32_16x16x128_f8f6f4 v[28:31], v[0:7], v[152:159], v[202:205]
	v_mfma_f32_16x16x128_f8f6f4 v[24:27], v[16:23], v[152:159], v[206:209]
	v_mfma_f32_16x16x128_f8f6f4 v[12:15], v[0:7], v[160:167], v[218:221]
	v_mfma_f32_16x16x128_f8f6f4 v[8:11], v[16:23], v[160:167], v[226:229]
	v_mfma_f32_16x16x128_f8f6f4 v[52:55], v[120:127], v[32:39], v[52:55]
	v_mfma_f32_16x16x128_f8f6f4 v[48:51], v[132:139], v[32:39], v[48:51]
	v_mfma_f32_16x16x128_f8f6f4 v[36:39], v[120:127], v[144:151], v[230:233]
	v_mfma_f32_16x16x128_f8f6f4 v[32:35], v[132:139], v[144:151], v[234:237]
	v_mfma_f32_16x16x128_f8f6f4 v[20:23], v[120:127], v[152:159], v[238:241]
	v_mfma_f32_16x16x128_f8f6f4 v[16:19], v[132:139], v[152:159], v[242:245]
	v_mfma_f32_16x16x128_f8f6f4 v[4:7], v[120:127], v[160:167], v[246:249]
	v_mfma_f32_16x16x128_f8f6f4 v[0:3], v[132:139], v[160:167], v[250:253]
	s_setprio 0
	s_barrier
	s_add_i32 s61, s61, 2
	s_addk_i32 s4, 0x100
	s_addk_i32 s5, 0x100
	s_cmp_ge_i32 s61, s82
	s_cbranch_scc0 .LBB0_1990
